# baseline (speedup 1.0000x reference)
_Z7k_frontPKDF16_S0_PKfS2_S0_S2_S2_S2_PjPfS4_S4_S4_:
	s_mov_b32 s12, s3
	s_load_dwordx8 s[4:11], s[0:1], 0x0
	s_lshl_b32 s3, s2, 6
	s_ashr_i32 s13, s12, 31
	s_lshl_b64 s[14:15], s[12:13], 12
	s_ashr_i32 s16, s3, 31
	s_add_u32 s14, s14, s3
	s_addc_u32 s15, s15, s16
	s_lshl_b32 s16, s12, 22
	s_and_b32 s16, s16, 0x400000
	s_waitcnt lgkmcnt(0)
	s_add_u32 s16, s4, s16
	s_addc_u32 s17, s5, 0
	s_lshl_b32 s4, s12, 6
	s_and_b32 s4, s4, 0xffffff80
	s_ashr_i32 s5, s4, 31
	s_lshl_b64 s[4:5], s[4:5], 1
	s_add_u32 s4, s16, s4
	s_addc_u32 s5, s17, s5
	s_add_i32 s3, s3, -16
	v_lshrrev_b32_e32 v134, 4, v0
	v_lshlrev_b32_e32 v1, 4, v0
	v_mov_b32_e32 v91, 0
	v_or_b32_e32 v24, s3, v134
	v_and_b32_e32 v90, 0xf0, v1
	v_max_i32_e32 v2, 0, v24
	v_mov_b32_e32 v3, v91
	v_lshl_add_u64 v[18:19], s[4:5], 0, v[90:91]
	v_lshlrev_b64 v[2:3], 10, v[2:3]
	v_lshl_add_u64 v[10:11], v[18:19], 0, v[2:3]
	v_or_b32_e32 v2, 0x100, v0
	v_lshrrev_b32_e32 v135, 4, v2
	v_add_u32_e32 v25, s3, v135
	v_max_i32_e32 v2, 0, v25
	v_mov_b32_e32 v3, v91
	v_lshlrev_b64 v[2:3], 10, v[2:3]
	v_lshl_add_u64 v[12:13], v[18:19], 0, v[2:3]
	global_load_dwordx4 v[2:5], v[10:11], off
	global_load_dwordx4 v[6:9], v[12:13], off
	v_or_b32_e32 v10, 0x200, v0
	v_lshrrev_b32_e32 v136, 4, v10
	v_or_b32_e32 v14, 0x300, v0
	v_add_u32_e32 v30, s3, v136
	v_lshrrev_b32_e32 v137, 4, v14
	v_max_i32_e32 v10, 0, v30
	v_mov_b32_e32 v11, v91
	v_add_u32_e32 v31, s3, v137
	v_lshlrev_b64 v[10:11], 10, v[10:11]
	v_max_i32_e32 v14, 0, v31
	v_mov_b32_e32 v15, v91
	v_add_u32_e32 v32, 64, v24
	v_lshl_add_u64 v[10:11], v[18:19], 0, v[10:11]
	v_lshlrev_b64 v[14:15], 10, v[14:15]
	v_max_i32_e32 v20, 0, v32
	v_mov_b32_e32 v21, v91
	global_load_dwordx4 v[10:13], v[10:11], off
	v_lshl_add_u64 v[14:15], v[18:19], 0, v[14:15]
	v_lshlrev_b64 v[20:21], 10, v[20:21]
	global_load_dwordx4 v[14:17], v[14:15], off
	v_lshl_add_u64 v[18:19], v[18:19], 0, v[20:21]
	global_load_dwordx4 v[18:21], v[18:19], off
	v_lshrrev_b32_e32 v138, 2, v0
	v_and_b32_e32 v141, 48, v138
	v_and_b32_e32 v92, 0x3f0, v1
	v_mov_b32_e32 v23, v91
	v_lshl_or_b32 v22, v141, 10, v92
	s_movk_i32 s16, 0x2000
	v_lshl_add_u64 v[26:27], s[6:7], 0, v[22:23]
	v_add_co_u32_e32 v28, vcc, s16, v26
	global_load_dwordx4 v[74:77], v22, s[6:7]
	global_load_dwordx4 v[70:73], v22, s[6:7] offset:1024
	global_load_dwordx4 v[66:69], v22, s[6:7] offset:2048
	global_load_dwordx4 v[62:65], v22, s[6:7] offset:3072
	v_addc_co_u32_e32 v29, vcc, 0, v27, vcc
	v_cmp_lt_i32_e32 vcc, -1, v24
	global_load_dwordx4 v[50:53], v[28:29], off offset:-4096
	s_movk_i32 s3, 0x1000
	s_movk_i32 s17, 0x3000
	v_or_b32_e32 v139, 0x3c00, v1
	v_lshl_or_b32 v1, v138, 10, v139
	v_lshlrev_b32_e32 v33, 3, v0
	v_or_b32_e32 v90, 0xa500, v90
	v_and_b32_e32 v140, 15, v0
	v_and_b32_e32 v142, 48, v0
	s_movk_i32 s18, 0xc0
	v_lshlrev_b32_e32 v132, 6, v0
	v_lshlrev_b32_e32 v133, 5, v0
	s_waitcnt vmcnt(9)
	v_cndmask_b32_e32 v34, 0, v2, vcc
	v_cndmask_b32_e32 v35, 0, v3, vcc
	v_cndmask_b32_e32 v36, 0, v4, vcc
	v_cndmask_b32_e32 v37, 0, v5, vcc
	v_cmp_lt_i32_e32 vcc, -1, v25
	v_add_co_u32_e64 v2, s[4:5], s3, v26
	s_waitcnt vmcnt(8)
	v_cndmask_b32_e32 v46, 0, v6, vcc
	v_cndmask_b32_e32 v47, 0, v7, vcc
	v_cndmask_b32_e32 v48, 0, v8, vcc
	v_cndmask_b32_e32 v49, 0, v9, vcc
	v_cmp_lt_i32_e32 vcc, -1, v30
	v_addc_co_u32_e64 v3, s[4:5], 0, v27, s[4:5]
	global_load_dwordx4 v[78:81], v[2:3], off offset:1024
	global_load_dwordx4 v[82:85], v[2:3], off offset:2048
	global_load_dwordx4 v[86:89], v[2:3], off offset:3072
	s_movk_i32 s4, 0x110
	s_waitcnt vmcnt(10)
	v_cndmask_b32_e32 v94, 0, v10, vcc
	v_cndmask_b32_e32 v95, 0, v11, vcc
	v_cndmask_b32_e32 v96, 0, v12, vcc
	v_cndmask_b32_e32 v97, 0, v13, vcc
	v_cmp_lt_i32_e32 vcc, -1, v31
	v_mad_u32_u24 v106, v134, s4, v90
	v_mad_u32_u24 v130, v140, s4, v142
	s_waitcnt vmcnt(9)
	v_cndmask_b32_e32 v98, 0, v14, vcc
	v_cndmask_b32_e32 v99, 0, v15, vcc
	v_cndmask_b32_e32 v100, 0, v16, vcc
	v_cndmask_b32_e32 v101, 0, v17, vcc
	v_cmp_lt_i32_e32 vcc, -1, v32
	s_waitcnt vmcnt(8)
	s_nop 0
	v_cndmask_b32_e32 v102, 0, v18, vcc
	v_cndmask_b32_e32 v103, 0, v19, vcc
	v_cndmask_b32_e32 v104, 0, v20, vcc
	v_cndmask_b32_e32 v105, 0, v21, vcc
	v_add_co_u32_e32 v6, vcc, s17, v26
	global_load_dwordx4 v[58:61], v[28:29], off
	global_load_dwordx4 v[54:57], v[28:29], off offset:1024
	global_load_dwordx4 v[22:25], v[28:29], off offset:2048
	global_load_dwordx4 v[18:21], v[28:29], off offset:3072
	v_addc_co_u32_e32 v7, vcc, 0, v27, vcc
	global_load_dwordx4 v[14:17], v[6:7], off
	global_load_dwordx4 v[10:13], v[6:7], off offset:1024
	global_load_dwordx4 v[2:5], v[6:7], off offset:2048
	s_nop 0
	global_load_dwordx4 v[6:9], v1, s[6:7]
	v_and_b32_e32 v1, 0xf8, v33
	v_lshlrev_b32_e32 v26, 4, v1
	global_load_dwordx4 v[122:125], v26, s[8:9] offset:32
	global_load_dwordx4 v[38:41], v26, s[8:9] offset:48
	global_load_dwordx4 v[126:129], v26, s[8:9]
	global_load_dwordx4 v[42:45], v26, s[8:9] offset:16
	v_or_b32_e32 v30, 64, v26
	global_load_dwordx4 v[114:117], v30, s[8:9] offset:32
	global_load_dwordx4 v[26:29], v30, s[8:9] offset:48
	global_load_dwordx4 v[144:147], v30, s[8:9]
	s_nop 0
	global_load_dwordx4 v[30:33], v30, s[8:9] offset:16
	ds_write_b128 v106, v[34:37]
	v_mad_u32_u24 v34, v135, s4, v90
	ds_write_b128 v34, v[46:49]
	v_mad_u32_u24 v34, v136, s4, v90
	ds_write_b128 v34, v[94:97]
	v_mad_u32_u24 v34, v137, s4, v90
	v_lshlrev_b32_e32 v93, 2, v1
	ds_write_b128 v34, v[98:101]
	ds_write_b128 v106, v[102:105] offset:17408
	global_load_dwordx4 v[34:37], v93, s[10:11] offset:16
	global_load_dwordx4 v[46:49], v93, s[10:11]
	s_waitcnt lgkmcnt(0)
	s_barrier
	ds_read_b128 v[94:97], v130 offset:42240
	ds_read_b128 v[98:101], v130 offset:42304
	s_waitcnt vmcnt(25) lgkmcnt(1)
	v_mfma_f32_16x16x32_f16 a[0:3], v[74:77], v[94:97], 0
	ds_read_b128 v[102:105], v130 offset:42368
	ds_read_b128 v[106:109], v130 offset:42432
	v_and_b32_e32 v90, 12, v138
	v_and_or_b32 v90, v0, s18, v90
	s_waitcnt vmcnt(21)
	v_mfma_f32_16x16x32_f16 a[4:7], v[50:53], v[94:97], 0
	v_mul_u32_u24_e32 v93, 0x210, v140
	v_lshl_add_u32 v131, v90, 1, v93
	v_and_b32_e32 v93, 56, v138
	s_waitcnt vmcnt(17)
	v_mfma_f32_16x16x32_f16 a[8:11], v[58:61], v[94:97], 0
	v_mul_u32_u24_e32 v93, 0x210, v93
	v_lshl_add_u32 v93, v1, 1, v93
	s_load_dwordx8 s[4:11], s[0:1], 0x20
	s_waitcnt vmcnt(13)
	v_mfma_f32_16x16x32_f16 a[12:15], v[14:17], v[94:97], 0
	v_lshlrev_b32_e32 v90, 2, v0
	s_mov_b32 s18, 0xbfb8aa3b
	s_waitcnt lgkmcnt(0)
	v_mfma_f32_16x16x32_f16 a[0:3], v[70:73], v[98:101], a[0:3]
	v_mfma_f32_16x16x32_f16 a[4:7], v[78:81], v[98:101], a[4:7]
	v_mfma_f32_16x16x32_f16 a[8:11], v[54:57], v[98:101], a[8:11]
	s_waitcnt vmcnt(12)
	v_mfma_f32_16x16x32_f16 a[12:15], v[10:13], v[98:101], a[12:15]
	s_waitcnt vmcnt(9)
	v_mov_b32_e32 v98, v122
	s_waitcnt vmcnt(8)
	v_mov_b32_e32 v99, v38
	v_mov_b32_e32 v38, v123
	v_mfma_f32_16x16x32_f16 a[0:3], v[66:69], v[102:105], a[0:3]
	v_mov_b32_e32 v100, v124
	v_mov_b32_e32 v101, v40
	v_mov_b32_e32 v40, v125
	v_mfma_f32_16x16x32_f16 a[4:7], v[82:85], v[102:105], a[4:7]
	v_mfma_f32_16x16x32_f16 a[8:11], v[22:25], v[102:105], a[8:11]
	v_mfma_f32_16x16x32_f16 a[12:15], v[2:5], v[102:105], a[12:15]
	s_waitcnt vmcnt(7)
	v_mov_b32_e32 v102, v126
	s_waitcnt vmcnt(6)
	v_mov_b32_e32 v103, v42
	v_mov_b32_e32 v42, v127
	v_mfma_f32_16x16x32_f16 a[0:3], v[62:65], v[106:109], a[0:3]
	v_mov_b32_e32 v104, v128
	v_mov_b32_e32 v105, v44
	v_mov_b32_e32 v44, v129
	v_mfma_f32_16x16x32_f16 a[4:7], v[86:89], v[106:109], a[4:7]
	v_mfma_f32_16x16x32_f16 a[8:11], v[18:21], v[106:109], a[8:11]
	s_nop 2
	v_accvgpr_read_b32 v1, a0
	v_accvgpr_read_b32 v126, a1
	v_accvgpr_read_b32 v127, a2
	v_mfma_f32_16x16x32_f16 a[12:15], v[6:9], v[106:109], a[12:15]
	ds_read_b128 v[94:97], v130 offset:46592
	ds_read_b128 v[106:109], v130 offset:46656
	ds_read_b128 v[110:113], v130 offset:46720
	ds_read_b128 v[118:121], v130 offset:46784
	v_accvgpr_read_b32 v128, a3
	s_waitcnt lgkmcnt(3)
	v_mfma_f32_16x16x32_f16 a[16:19], v[74:77], v[94:97], 0
	v_cvt_pk_f16_f32 v127, v127, v128
	v_cvt_pk_f16_f32 v126, v1, v126
	v_accvgpr_read_b32 v1, a4
	v_mfma_f32_16x16x32_f16 a[20:23], v[50:53], v[94:97], 0
	v_accvgpr_read_b32 v128, a5
	v_accvgpr_read_b32 v129, a6
	v_accvgpr_read_b32 v143, a7
	v_mfma_f32_16x16x32_f16 a[24:27], v[58:61], v[94:97], 0
	v_cvt_pk_f16_f32 v129, v129, v143
	v_cvt_pk_f16_f32 v128, v1, v128
	ds_write2_b64 v131, v[126:127], v[128:129] offset1:4
	v_mfma_f32_16x16x32_f16 a[28:31], v[14:17], v[94:97], 0
	v_accvgpr_read_b32 v1, a8
	v_accvgpr_read_b32 v126, a9
	v_accvgpr_read_b32 v127, a10
	s_waitcnt lgkmcnt(3)
	v_mfma_f32_16x16x32_f16 a[16:19], v[70:73], v[106:109], a[16:19]
	v_accvgpr_read_b32 v128, a11
	ds_read_b128 v[122:125], v130 offset:51136
	v_cvt_pk_f16_f32 v127, v127, v128
	v_mfma_f32_16x16x32_f16 a[20:23], v[78:81], v[106:109], a[20:23]
	v_cvt_pk_f16_f32 v126, v1, v126
	v_accvgpr_read_b32 v1, a12
	v_accvgpr_read_b32 v128, a13
	v_mfma_f32_16x16x32_f16 a[24:27], v[54:57], v[106:109], a[24:27]
	v_accvgpr_read_b32 v129, a14
	v_accvgpr_read_b32 v143, a15
	v_cvt_pk_f16_f32 v129, v129, v143
	v_mfma_f32_16x16x32_f16 a[28:31], v[10:13], v[106:109], a[28:31]
	ds_read_b128 v[106:109], v130 offset:50944
	v_cvt_pk_f16_f32 v128, v1, v128
	ds_write2_b64 v131, v[126:127], v[128:129] offset0:8 offset1:12
	s_waitcnt lgkmcnt(5)
	v_mfma_f32_16x16x32_f16 a[16:19], v[66:69], v[110:113], a[16:19]
	s_waitcnt vmcnt(3)
	v_mov_b32_e32 v94, v144
	s_waitcnt vmcnt(2)
	v_mov_b32_e32 v95, v30
	v_mov_b32_e32 v30, v145
	v_mfma_f32_16x16x32_f16 a[20:23], v[82:85], v[110:113], a[20:23]
	v_mov_b32_e32 v96, v146
	v_mov_b32_e32 v97, v32
	v_mov_b32_e32 v32, v147
	v_mfma_f32_16x16x32_f16 a[24:27], v[22:25], v[110:113], a[24:27]
	v_mfma_f32_16x16x32_f16 a[28:31], v[2:5], v[110:113], a[28:31]
	ds_read_b128 v[110:113], v130 offset:51008
	s_waitcnt lgkmcnt(2)
	v_mfma_f32_16x16x32_f16 a[32:35], v[74:77], v[106:109], 0
	v_mfma_f32_16x16x32_f16 a[0:3], v[50:53], v[106:109], 0
	v_mfma_f32_16x16x32_f16 a[16:19], v[62:65], v[118:121], a[16:19]
	v_mfma_f32_16x16x32_f16 a[20:23], v[86:89], v[118:121], a[20:23]
	v_mfma_f32_16x16x32_f16 a[24:27], v[18:21], v[118:121], a[24:27]
	s_nop 5
	v_accvgpr_read_b32 v1, a16
	v_accvgpr_read_b32 v126, a17
	v_accvgpr_read_b32 v127, a18
	v_mfma_f32_16x16x32_f16 a[28:31], v[6:9], v[118:121], a[28:31]
	ds_read_b128 v[118:121], v130 offset:51072
	v_accvgpr_read_b32 v128, a19
	v_cvt_pk_f16_f32 v126, v1, v126
	v_mfma_f32_16x16x32_f16 a[4:7], v[58:61], v[106:109], 0
	v_accvgpr_read_b32 v1, a20
	v_cvt_pk_f16_f32 v127, v127, v128
	v_accvgpr_read_b32 v128, a25
	s_waitcnt lgkmcnt(1)
	v_mfma_f32_16x16x32_f16 a[32:35], v[70:73], v[110:113], a[32:35]
	v_accvgpr_read_b32 v129, a27
	v_accvgpr_read_b32 v143, a29
	v_accvgpr_read_b32 v144, a31
	v_mfma_f32_16x16x32_f16 a[8:11], v[14:17], v[106:109], 0
	v_accvgpr_read_b32 v106, a21
	v_accvgpr_read_b32 v107, a22
	v_accvgpr_read_b32 v108, a23
	v_mfma_f32_16x16x32_f16 a[0:3], v[78:81], v[110:113], a[0:3]
	v_mfma_f32_16x16x32_f16 a[4:7], v[54:57], v[110:113], a[4:7]
	s_waitcnt lgkmcnt(0)
	v_mfma_f32_16x16x32_f16 a[32:35], v[66:69], v[118:121], a[32:35]
	v_mfma_f32_16x16x32_f16 a[8:11], v[10:13], v[110:113], a[8:11]
	v_cvt_pk_f16_f32 v111, v107, v108
	v_cvt_pk_f16_f32 v110, v1, v106
	v_add_u32_e32 v1, 0x2000, v131
	v_mfma_f32_16x16x32_f16 a[0:3], v[82:85], v[118:121], a[0:3]
	ds_write2_b64 v1, v[126:127], v[110:111] offset0:32 offset1:36
	v_accvgpr_read_b32 v126, a24
	v_accvgpr_read_b32 v127, a26
	v_mfma_f32_16x16x32_f16 a[4:7], v[22:25], v[118:121], a[4:7]
	ds_read_b128 v[106:109], v130 offset:55296
	ds_read_b128 v[110:113], v130 offset:55360
	v_cvt_pk_f16_f32 v127, v127, v129
	v_mfma_f32_16x16x32_f16 a[32:35], v[62:65], v[122:125], a[32:35]
	v_cvt_pk_f16_f32 v126, v126, v128
	v_accvgpr_read_b32 v128, a28
	v_accvgpr_read_b32 v129, a30
	v_mfma_f32_16x16x32_f16 a[8:11], v[2:5], v[118:121], a[8:11]
	v_cvt_pk_f16_f32 v129, v129, v144
	v_cvt_pk_f16_f32 v128, v128, v143
	ds_write2_b64 v1, v[126:127], v[128:129] offset0:40 offset1:44
	v_mfma_f32_16x16x32_f16 a[0:3], v[86:89], v[122:125], a[0:3]
	v_accvgpr_read_b32 v1, a32
	v_accvgpr_read_b32 v126, a33
	v_accvgpr_read_b32 v127, a34
	v_mfma_f32_16x16x32_f16 a[4:7], v[18:21], v[122:125], a[4:7]
	v_accvgpr_read_b32 v128, a35
	v_cvt_pk_f16_f32 v127, v127, v128
	v_cvt_pk_f16_f32 v126, v1, v126
	v_mfma_f32_16x16x32_f16 a[8:11], v[6:9], v[122:125], a[8:11]
	v_accvgpr_read_b32 v1, a0
	v_accvgpr_read_b32 v128, a1
	v_accvgpr_read_b32 v129, a2
	v_accvgpr_read_b32 v143, a3
	v_cvt_pk_f16_f32 v129, v129, v143
	v_cvt_pk_f16_f32 v128, v1, v128
	v_add_u32_e32 v1, 0x4000, v131
	s_waitcnt lgkmcnt(2)
	v_mfma_f32_16x16x32_f16 a[12:15], v[74:77], v[106:109], 0
	ds_write2_b64 v1, v[126:127], v[128:129] offset0:64 offset1:68
	v_accvgpr_read_b32 v126, a4
	v_accvgpr_read_b32 v128, a5
	v_mfma_f32_16x16x32_f16 a[16:19], v[50:53], v[106:109], 0
	v_accvgpr_read_b32 v127, a6
	v_accvgpr_read_b32 v129, a7
	v_cvt_pk_f16_f32 v126, v126, v128
	v_mfma_f32_16x16x32_f16 a[20:23], v[58:61], v[106:109], 0
	v_accvgpr_read_b32 v128, a8
	v_cvt_pk_f16_f32 v127, v127, v129
	ds_read_b128 v[118:121], v130 offset:55424
	ds_read_b128 v[122:125], v130 offset:55488
	v_mfma_f32_16x16x32_f16 a[4:7], v[14:17], v[106:109], 0
	v_accvgpr_read_b32 v106, a9
	v_accvgpr_read_b32 v107, a10
	v_accvgpr_read_b32 v108, a11
	v_cvt_pk_f16_f32 v107, v107, v108
	v_cvt_pk_f16_f32 v106, v128, v106
	ds_write2_b64 v1, v[126:127], v[106:107] offset0:72 offset1:76
	ds_read_b128 v[106:109], v130 offset:59648
	s_waitcnt lgkmcnt(6)
	v_mfma_f32_16x16x32_f16 a[12:15], v[70:73], v[110:113], a[12:15]
	v_mfma_f32_16x16x32_f16 a[16:19], v[78:81], v[110:113], a[16:19]
	v_mfma_f32_16x16x32_f16 a[0:3], v[54:57], v[110:113], a[20:23]
	v_mfma_f32_16x16x32_f16 a[4:7], v[10:13], v[110:113], a[4:7]
	ds_read_b128 v[110:113], v130 offset:59712
	s_waitcnt lgkmcnt(4)
	v_mfma_f32_16x16x32_f16 a[12:15], v[66:69], v[118:121], a[12:15]
	s_waitcnt lgkmcnt(1)
	v_mfma_f32_16x16x32_f16 a[8:11], v[74:77], v[106:109], 0
	ds_read_b128 v[74:77], v130 offset:59776
	v_mfma_f32_16x16x32_f16 a[0:3], v[22:25], v[118:121], a[0:3]
	v_mfma_f32_16x16x32_f16 a[12:15], v[62:65], v[122:125], a[12:15]
	v_mfma_f32_16x16x32_f16 a[4:7], v[2:5], v[118:121], a[4:7]
	s_waitcnt lgkmcnt(1)
	v_mfma_f32_16x16x32_f16 a[8:11], v[70:73], v[110:113], a[8:11]
	ds_read_b128 v[70:73], v130 offset:59840
	s_nop 3
	v_accvgpr_read_b32 v1, a12
	v_mfma_f32_16x16x32_f16 a[0:3], v[18:21], v[122:125], a[0:3]
	v_mfma_f32_16x16x32_f16 a[16:19], v[82:85], v[118:121], a[16:19]
	v_accvgpr_read_b32 v118, a13
	v_accvgpr_read_b32 v119, a14
	v_accvgpr_read_b32 v120, a15
	v_mfma_f32_16x16x32_f16 a[4:7], v[6:9], v[122:125], a[4:7]
	v_cvt_pk_f16_f32 v119, v119, v120
	v_cvt_pk_f16_f32 v118, v1, v118
	s_waitcnt lgkmcnt(1)
	v_mfma_f32_16x16x32_f16 a[8:11], v[66:69], v[74:77], a[8:11]
	v_mfma_f32_16x16x32_f16 a[12:15], v[50:53], v[106:109], 0
	v_accvgpr_read_b32 v50, a0
	v_accvgpr_read_b32 v52, a1
	v_accvgpr_read_b32 v51, a2
	v_accvgpr_read_b32 v53, a3
	s_waitcnt lgkmcnt(0)
	v_mfma_f32_16x16x32_f16 a[8:11], v[62:65], v[70:73], a[8:11]
	v_cvt_pk_f16_f32 v51, v51, v53
	v_cvt_pk_f16_f32 v50, v50, v52
	v_accvgpr_read_b32 v52, a4
	v_mfma_f32_16x16x32_f16 a[12:15], v[78:81], v[110:113], a[12:15]
	v_accvgpr_read_b32 v62, a5
	v_accvgpr_read_b32 v53, a6
	v_accvgpr_read_b32 v63, a7
	v_mfma_f32_16x16x32_f16 a[4:7], v[58:61], v[106:109], 0
	v_cvt_pk_f16_f32 v53, v53, v63
	v_cvt_pk_f16_f32 v52, v52, v62
	v_mfma_f32_16x16x32_f16 a[0:3], v[82:85], v[74:77], a[12:15]
	v_mfma_f32_16x16x32_f16 a[4:7], v[54:57], v[110:113], a[4:7]
	v_mfma_f32_16x16x32_f16 a[16:19], v[86:89], v[122:125], a[16:19]
	v_mfma_f32_16x16x32_f16 a[0:3], v[86:89], v[70:73], a[0:3]
	v_mfma_f32_16x16x32_f16 a[4:7], v[22:25], v[74:77], a[4:7]
	s_nop 5
	v_accvgpr_read_b32 v1, a16
	v_accvgpr_read_b32 v120, a17
	v_accvgpr_read_b32 v66, a18
	v_accvgpr_read_b32 v67, a19
	v_cvt_pk_f16_f32 v67, v66, v67
	v_cvt_pk_f16_f32 v66, v1, v120
	v_add_u32_e32 v1, 0x6000, v131
	ds_write2_b64 v1, v[118:119], v[66:67] offset0:96 offset1:100
	ds_write2_b64 v1, v[50:51], v[52:53] offset0:104 offset1:108
	v_accvgpr_read_b32 v1, a8
	v_accvgpr_read_b32 v50, a9
	v_cvt_pk_f16_f32 v50, v1, v50
	v_accvgpr_read_b32 v1, a0
	v_accvgpr_read_b32 v22, a1
	v_mfma_f32_16x16x32_f16 a[4:7], v[18:21], v[70:73], a[4:7]
	v_accvgpr_read_b32 v18, a2
	v_accvgpr_read_b32 v19, a3
	v_accvgpr_read_b32 v51, a10
	v_mfma_f32_16x16x32_f16 a[0:3], v[14:17], v[106:109], 0
	v_accvgpr_read_b32 v52, a11
	v_cvt_pk_f16_f32 v51, v51, v52
	v_cvt_pk_f16_f32 v19, v18, v19
	v_mfma_f32_16x16x32_f16 a[0:3], v[10:13], v[110:113], a[0:3]
	v_accvgpr_read_b32 v10, a4
	v_accvgpr_read_b32 v11, a5
	v_accvgpr_read_b32 v12, a6
	v_mfma_f32_16x16x32_f16 a[0:3], v[2:5], v[74:77], a[0:3]
	v_accvgpr_read_b32 v2, a7
	v_cvt_pk_f16_f32 v18, v1, v22
	v_add_u32_e32 v1, 0x8000, v131
	v_mfma_f32_16x16x32_f16 a[0:3], v[6:9], v[70:73], a[0:3]
	v_cvt_pk_f16_f32 v3, v12, v2
	v_cvt_pk_f16_f32 v2, v10, v11
	ds_write2_b64 v1, v[50:51], v[18:19] offset0:128 offset1:132
	s_nop 4
	v_accvgpr_read_b32 v4, a0
	v_accvgpr_read_b32 v6, a1
	v_accvgpr_read_b32 v5, a2
	v_accvgpr_read_b32 v7, a3
	v_cvt_pk_f16_f32 v5, v5, v7
	v_cvt_pk_f16_f32 v4, v4, v6
	ds_write2_b64 v1, v[2:3], v[4:5] offset0:136 offset1:140
	global_load_dwordx4 v[2:5], v132, s[10:11] offset:48
	global_load_dwordx4 v[6:9], v132, s[10:11] offset:32
	global_load_dwordx4 v[10:13], v132, s[10:11] offset:16
	global_load_dwordx4 v[14:17], v132, s[10:11]
	global_load_dwordx4 v[18:21], v133, s[6:7] offset:16
	global_load_dwordx4 v[22:25], v133, s[6:7]
	global_load_dword v1, v90, s[8:9]
	s_waitcnt lgkmcnt(0)
	s_barrier
	ds_read_b128 v[50:53], v93 offset:6864
	ds_read_b128 v[82:85], v93 offset:7392
	ds_read_b128 v[106:109], v93 offset:7920
	ds_read_b128 v[118:121], v93 offset:8448
	ds_read_b128 v[62:65], v93 offset:8976
	ds_read_b128 v[70:73], v93 offset:9504
	ds_read_b128 v[78:81], v93 offset:10032
	ds_read_b128 v[74:77], v93 offset:10560
	s_waitcnt lgkmcnt(7)
	v_cvt_f32_f16_e32 v54, v50
	v_cvt_f32_f16_sdwa v55, v50 dst_sel:DWORD dst_unused:UNUSED_PAD src0_sel:WORD_1
	s_waitcnt lgkmcnt(6)
	v_cvt_f32_f16_e32 v122, v82
	v_cvt_f32_f16_sdwa v123, v82 dst_sel:DWORD dst_unused:UNUSED_PAD src0_sel:WORD_1
	s_waitcnt lgkmcnt(5)
	v_cvt_f32_f16_e32 v110, v106
	v_cvt_f32_f16_sdwa v111, v106 dst_sel:DWORD dst_unused:UNUSED_PAD src0_sel:WORD_1
	s_waitcnt lgkmcnt(4)
	v_cvt_f32_f16_e32 v86, v118
	v_cvt_f32_f16_sdwa v87, v118 dst_sel:DWORD dst_unused:UNUSED_PAD src0_sel:WORD_1
	s_waitcnt vmcnt(7)
	v_pk_fma_f32 v[54:55], v[102:103], v[54:55], v[46:47]
	v_cvt_f32_f16_e32 v126, v83
	v_pk_fma_f32 v[54:55], v[42:43], v[122:123], v[54:55]
	v_cvt_f32_f16_sdwa v127, v83 dst_sel:DWORD dst_unused:UNUSED_PAD src0_sel:WORD_1
	v_pk_fma_f32 v[54:55], v[104:105], v[110:111], v[54:55]
	v_cvt_f32_f16_e32 v112, v107
	v_pk_fma_f32 v[124:125], v[44:45], v[86:87], v[54:55]
	v_cvt_f32_f16_sdwa v55, v51 dst_sel:DWORD dst_unused:UNUSED_PAD src0_sel:WORD_1
	v_mul_f32_e32 v54, 0xbfb8aa3b, v125
	v_exp_f32_e32 v54, v54
	v_cvt_f32_f16_sdwa v113, v107 dst_sel:DWORD dst_unused:UNUSED_PAD src0_sel:WORD_1
	v_cvt_f32_f16_e32 v88, v119
	v_cvt_f32_f16_sdwa v89, v119 dst_sel:DWORD dst_unused:UNUSED_PAD src0_sel:WORD_1
	v_add_f32_e32 v56, 1.0, v54
	v_cvt_f32_f16_e32 v54, v51
	v_mul_f32_e32 v50, 0xbfb8aa3b, v124
	v_exp_f32_e32 v50, v50
	v_cvt_f32_f16_e32 v118, v52
	v_pk_fma_f32 v[54:55], v[98:99], v[54:55], v[48:49]
	v_cvt_f32_f16_sdwa v119, v52 dst_sel:DWORD dst_unused:UNUSED_PAD src0_sel:WORD_1
	v_pk_fma_f32 v[54:55], v[38:39], v[126:127], v[54:55]
	v_add_f32_e32 v50, 1.0, v50
	v_pk_fma_f32 v[54:55], v[100:101], v[112:113], v[54:55]
	v_rcp_f32_e32 v50, v50
	v_pk_fma_f32 v[82:83], v[40:41], v[88:89], v[54:55]
	v_cvt_f32_f16_e32 v144, v108
	v_mul_f32_e32 v51, 0xbfb8aa3b, v82
	v_exp_f32_e32 v54, v51
	v_mul_f32_e32 v51, 0xbfb8aa3b, v83
	v_exp_f32_e32 v55, v51
	v_rcp_f32_e32 v51, v56
	v_add_f32_e32 v54, 1.0, v54
	v_rcp_f32_e32 v106, v54
	v_add_f32_e32 v54, 1.0, v55
	v_rcp_f32_e32 v107, v54
	v_pk_mul_f32 v[50:51], v[124:125], v[50:51]
	v_cvt_f32_f16_e32 v124, v84
	v_cvt_f32_f16_sdwa v125, v84 dst_sel:DWORD dst_unused:UNUSED_PAD src0_sel:WORD_1
	v_cvt_f32_f16_sdwa v145, v108 dst_sel:DWORD dst_unused:UNUSED_PAD src0_sel:WORD_1
	v_pk_mul_f32 v[82:83], v[82:83], v[106:107]
	v_cvt_f32_f16_e32 v106, v120
	v_cvt_f32_f16_sdwa v107, v120 dst_sel:DWORD dst_unused:UNUSED_PAD src0_sel:WORD_1
	v_pk_fma_f32 v[118:119], v[94:95], v[118:119], v[34:35]
	v_cvt_pk_f16_f32 v50, v50, v51
	v_pk_fma_f32 v[118:119], v[30:31], v[124:125], v[118:119]
	v_cvt_f32_f16_e32 v146, v85
	v_pk_fma_f32 v[118:119], v[96:97], v[144:145], v[118:119]
	v_cvt_f32_f16_sdwa v147, v85 dst_sel:DWORD dst_unused:UNUSED_PAD src0_sel:WORD_1
	v_pk_fma_f32 v[118:119], v[32:33], v[106:107], v[118:119]
	v_cvt_f32_f16_e32 v108, v121
	v_mul_f32_e32 v51, 0xbfb8aa3b, v118
	v_exp_f32_e32 v52, v51
	v_mul_f32_e32 v51, 0xbfb8aa3b, v119
	v_exp_f32_e32 v84, v51
	v_cvt_pk_f16_f32 v51, v82, v83
	v_add_f32_e32 v52, 1.0, v52
	v_rcp_f32_e32 v128, v52
	v_add_f32_e32 v52, 1.0, v84
	v_rcp_f32_e32 v129, v52
	v_cvt_f32_f16_e32 v52, v53
	v_cvt_f32_f16_sdwa v53, v53 dst_sel:DWORD dst_unused:UNUSED_PAD src0_sel:WORD_1
	v_mov_b32_e32 v82, v114
	v_mov_b32_e32 v83, v26
	v_mov_b32_e32 v26, v115
	v_cvt_f32_f16_e32 v114, v109
	v_cvt_f32_f16_sdwa v115, v109 dst_sel:DWORD dst_unused:UNUSED_PAD src0_sel:WORD_1
	v_cvt_f32_f16_sdwa v109, v121 dst_sel:DWORD dst_unused:UNUSED_PAD src0_sel:WORD_1
	v_pk_fma_f32 v[52:53], v[82:83], v[52:53], v[36:37]
	v_mov_b32_e32 v84, v116
	v_pk_fma_f32 v[52:53], v[26:27], v[146:147], v[52:53]
	v_mov_b32_e32 v85, v28
	v_pk_fma_f32 v[52:53], v[84:85], v[114:115], v[52:53]
	v_mov_b32_e32 v28, v117
	v_pk_fma_f32 v[116:117], v[28:29], v[108:109], v[52:53]
	s_waitcnt lgkmcnt(3)
	v_cvt_f32_f16_e32 v132, v62
	v_mul_f32_e32 v52, 0xbfb8aa3b, v116
	v_exp_f32_e32 v120, v52
	v_mul_f32_e32 v52, 0xbfb8aa3b, v117
	v_exp_f32_e32 v121, v52
	v_cvt_f32_f16_sdwa v133, v62 dst_sel:DWORD dst_unused:UNUSED_PAD src0_sel:WORD_1
	v_pk_mul_f32 v[52:53], v[118:119], v[128:129]
	v_add_f32_e32 v118, 1.0, v120
	v_add_f32_e32 v119, 1.0, v121
	v_pk_fma_f32 v[120:121], v[102:103], v[122:123], v[46:47]
	v_rcp_f32_e32 v118, v118
	v_pk_fma_f32 v[120:121], v[42:43], v[110:111], v[120:121]
	v_rcp_f32_e32 v119, v119
	v_pk_fma_f32 v[120:121], v[104:105], v[86:87], v[120:121]
	v_cvt_f32_f16_e32 v130, v63
	v_pk_fma_f32 v[120:121], v[44:45], v[132:133], v[120:121]
	v_cvt_f32_f16_sdwa v131, v63 dst_sel:DWORD dst_unused:UNUSED_PAD src0_sel:WORD_1
	v_mul_f32_e32 v62, 0xbfb8aa3b, v120
	v_exp_f32_e32 v62, v62
	v_mul_f32_e32 v122, 0xbfb8aa3b, v121
	v_exp_f32_e32 v123, v122
	v_pk_mul_f32 v[116:117], v[116:117], v[118:119]
	v_add_f32_e32 v62, 1.0, v62
	v_rcp_f32_e32 v122, v62
	v_add_f32_e32 v62, 1.0, v123
	v_rcp_f32_e32 v123, v62
	v_pk_fma_f32 v[62:63], v[98:99], v[126:127], v[48:49]
	v_cvt_pk_f16_f32 v52, v52, v53
	v_pk_fma_f32 v[62:63], v[38:39], v[112:113], v[62:63]
	v_cvt_pk_f16_f32 v53, v116, v117
	v_pk_fma_f32 v[62:63], v[100:101], v[88:89], v[62:63]
	v_pk_mul_f32 v[116:117], v[120:121], v[122:123]
	v_pk_fma_f32 v[118:119], v[40:41], v[130:131], v[62:63]
	v_cvt_f32_f16_e32 v128, v64
	v_mul_f32_e32 v62, 0xbfb8aa3b, v118
	v_exp_f32_e32 v63, v62
	v_mul_f32_e32 v62, 0xbfb8aa3b, v119
	v_exp_f32_e32 v120, v62
	v_cvt_f32_f16_sdwa v129, v64 dst_sel:DWORD dst_unused:UNUSED_PAD src0_sel:WORD_1
	v_add_f32_e32 v63, 1.0, v63
	v_cvt_pk_f16_f32 v62, v116, v117
	v_rcp_f32_e32 v116, v63
	v_add_f32_e32 v63, 1.0, v120
	v_pk_fma_f32 v[120:121], v[94:95], v[124:125], v[34:35]
	v_rcp_f32_e32 v117, v63
	v_pk_fma_f32 v[120:121], v[30:31], v[144:145], v[120:121]
	v_cvt_f32_f16_e32 v126, v65
	v_pk_fma_f32 v[120:121], v[96:97], v[106:107], v[120:121]
	v_cvt_f32_f16_sdwa v127, v65 dst_sel:DWORD dst_unused:UNUSED_PAD src0_sel:WORD_1
	v_pk_fma_f32 v[120:121], v[32:33], v[128:129], v[120:121]
	v_pk_mul_f32 v[116:117], v[118:119], v[116:117]
	v_mul_f32_e32 v63, 0xbfb8aa3b, v120
	v_exp_f32_e32 v63, v63
	v_mul_f32_e32 v64, 0xbfb8aa3b, v121
	v_pk_fma_f32 v[118:119], v[82:83], v[146:147], v[36:37]
	v_exp_f32_e32 v122, v64
	v_pk_fma_f32 v[118:119], v[26:27], v[114:115], v[118:119]
	v_add_f32_e32 v63, 1.0, v63
	v_pk_fma_f32 v[118:119], v[84:85], v[108:109], v[118:119]
	v_rcp_f32_e32 v64, v63
	v_pk_fma_f32 v[118:119], v[28:29], v[126:127], v[118:119]
	v_add_f32_e32 v63, 1.0, v122
	v_mul_f32_e32 v65, 0xbfb8aa3b, v118
	v_exp_f32_e32 v122, v65
	v_mul_f32_e32 v65, 0xbfb8aa3b, v119
	v_exp_f32_e32 v123, v65
	v_rcp_f32_e32 v65, v63
	s_waitcnt lgkmcnt(2)
	v_cvt_f32_f16_e32 v124, v70
	v_cvt_f32_f16_sdwa v125, v70 dst_sel:DWORD dst_unused:UNUSED_PAD src0_sel:WORD_1
	v_add_f32_e32 v63, 1.0, v122
	v_pk_fma_f32 v[110:111], v[102:103], v[110:111], v[46:47]
	v_rcp_f32_e32 v122, v63
	v_add_f32_e32 v63, 1.0, v123
	v_pk_fma_f32 v[110:111], v[42:43], v[86:87], v[110:111]
	v_rcp_f32_e32 v123, v63
	v_pk_fma_f32 v[110:111], v[104:105], v[132:133], v[110:111]
	v_pk_mul_f32 v[64:65], v[120:121], v[64:65]
	v_pk_fma_f32 v[110:111], v[44:45], v[124:125], v[110:111]
	v_cvt_pk_f16_f32 v64, v64, v65
	v_mul_f32_e32 v65, 0xbfb8aa3b, v110
	v_exp_f32_e32 v70, v65
	v_mul_f32_e32 v65, 0xbfb8aa3b, v111
	v_cvt_pk_f16_f32 v63, v116, v117
	v_pk_mul_f32 v[116:117], v[118:119], v[122:123]
	v_exp_f32_e32 v118, v65
	v_add_f32_e32 v70, 1.0, v70
	v_cvt_pk_f16_f32 v65, v116, v117
	v_rcp_f32_e32 v116, v70
	v_add_f32_e32 v70, 1.0, v118
	v_cvt_f32_f16_e32 v122, v71
	v_cvt_f32_f16_sdwa v123, v71 dst_sel:DWORD dst_unused:UNUSED_PAD src0_sel:WORD_1
	v_rcp_f32_e32 v117, v70
	v_pk_fma_f32 v[70:71], v[98:99], v[112:113], v[48:49]
	v_cvt_f32_f16_e32 v120, v72
	v_pk_fma_f32 v[70:71], v[38:39], v[88:89], v[70:71]
	v_cvt_f32_f16_sdwa v121, v72 dst_sel:DWORD dst_unused:UNUSED_PAD src0_sel:WORD_1
	v_pk_fma_f32 v[70:71], v[100:101], v[130:131], v[70:71]
	v_pk_fma_f32 v[86:87], v[102:103], v[86:87], v[46:47]
	v_pk_fma_f32 v[112:113], v[40:41], v[122:123], v[70:71]
	v_pk_fma_f32 v[86:87], v[42:43], v[132:133], v[86:87]
	v_mul_f32_e32 v70, 0xbfb8aa3b, v112
	v_exp_f32_e32 v118, v70
	v_mul_f32_e32 v70, 0xbfb8aa3b, v113
	v_exp_f32_e32 v119, v70
	v_pk_mul_f32 v[70:71], v[110:111], v[116:117]
	v_pk_fma_f32 v[116:117], v[94:95], v[144:145], v[34:35]
	v_add_f32_e32 v110, 1.0, v118
	v_pk_fma_f32 v[116:117], v[30:31], v[106:107], v[116:117]
	v_add_f32_e32 v111, 1.0, v119
	v_pk_fma_f32 v[116:117], v[96:97], v[128:129], v[116:117]
	v_rcp_f32_e32 v110, v110
	v_pk_fma_f32 v[116:117], v[32:33], v[120:121], v[116:117]
	v_rcp_f32_e32 v111, v111
	v_mul_f32_e32 v72, 0xbfb8aa3b, v116
	v_exp_f32_e32 v72, v72
	v_mul_f32_e32 v118, 0xbfb8aa3b, v117
	v_exp_f32_e32 v119, v118
	v_pk_mul_f32 v[110:111], v[112:113], v[110:111]
	v_add_f32_e32 v72, 1.0, v72
	v_rcp_f32_e32 v118, v72
	v_add_f32_e32 v72, 1.0, v119
	v_rcp_f32_e32 v119, v72
	v_cvt_pk_f16_f32 v70, v70, v71
	v_cvt_pk_f16_f32 v71, v110, v111
	v_pk_fma_f32 v[86:87], v[104:105], v[124:125], v[86:87]
	v_pk_mul_f32 v[110:111], v[116:117], v[118:119]
	v_cvt_f32_f16_e32 v118, v73
	v_cvt_f32_f16_sdwa v119, v73 dst_sel:DWORD dst_unused:UNUSED_PAD src0_sel:WORD_1
	v_pk_fma_f32 v[72:73], v[82:83], v[114:115], v[36:37]
	s_waitcnt lgkmcnt(1)
	v_cvt_f32_f16_e32 v116, v78
	v_pk_fma_f32 v[72:73], v[26:27], v[108:109], v[72:73]
	v_cvt_f32_f16_sdwa v117, v78 dst_sel:DWORD dst_unused:UNUSED_PAD src0_sel:WORD_1
	v_pk_fma_f32 v[72:73], v[84:85], v[126:127], v[72:73]
	v_cvt_f32_f16_sdwa v115, v79 dst_sel:DWORD dst_unused:UNUSED_PAD src0_sel:WORD_1
	v_pk_fma_f32 v[112:113], v[28:29], v[118:119], v[72:73]
	v_pk_fma_f32 v[86:87], v[44:45], v[116:117], v[86:87]
	v_mul_f32_e32 v72, 0xbfb8aa3b, v112
	v_exp_f32_e32 v73, v72
	v_mul_f32_e32 v72, 0xbfb8aa3b, v113
	v_exp_f32_e32 v114, v72
	v_cvt_pk_f16_f32 v72, v110, v111
	v_add_f32_e32 v73, 1.0, v73
	v_rcp_f32_e32 v110, v73
	v_add_f32_e32 v73, 1.0, v114
	v_rcp_f32_e32 v111, v73
	v_mul_f32_e32 v73, 0xbfb8aa3b, v86
	v_exp_f32_e32 v73, v73
	v_mul_f32_e32 v78, 0xbfb8aa3b, v87
	v_exp_f32_e32 v114, v78
	v_pk_fma_f32 v[88:89], v[98:99], v[88:89], v[48:49]
	v_add_f32_e32 v73, 1.0, v73
	v_rcp_f32_e32 v78, v73
	v_add_f32_e32 v73, 1.0, v114
	v_cvt_f32_f16_e32 v114, v79
	v_pk_fma_f32 v[88:89], v[38:39], v[130:131], v[88:89]
	v_pk_mul_f32 v[110:111], v[112:113], v[110:111]
	v_pk_fma_f32 v[88:89], v[100:101], v[122:123], v[88:89]
	ds_read_b128 v[66:69], v93 offset:11088
	ds_read_b128 v[58:61], v93 offset:11616
	v_pk_fma_f32 v[88:89], v[40:41], v[114:115], v[88:89]
	ds_read_b128 v[54:57], v93 offset:12144
	v_mul_f32_e32 v79, 0xbfb8aa3b, v88
	v_exp_f32_e32 v112, v79
	v_mul_f32_e32 v79, 0xbfb8aa3b, v89
	v_exp_f32_e32 v113, v79
	v_rcp_f32_e32 v79, v73
	v_add_f32_e32 v73, 1.0, v112
	v_rcp_f32_e32 v112, v73
	v_add_f32_e32 v73, 1.0, v113
	v_rcp_f32_e32 v113, v73
	v_pk_mul_f32 v[78:79], v[86:87], v[78:79]
	v_cvt_pk_f16_f32 v73, v110, v111
	v_cvt_pk_f16_f32 v78, v78, v79
	v_pk_mul_f32 v[86:87], v[88:89], v[112:113]
	v_cvt_f32_f16_e32 v112, v80
	v_cvt_f32_f16_sdwa v113, v80 dst_sel:DWORD dst_unused:UNUSED_PAD src0_sel:WORD_1
	v_pk_fma_f32 v[88:89], v[94:95], v[106:107], v[34:35]
	v_cvt_f32_f16_e32 v110, v81
	v_pk_fma_f32 v[88:89], v[30:31], v[128:129], v[88:89]
	v_cvt_f32_f16_sdwa v111, v81 dst_sel:DWORD dst_unused:UNUSED_PAD src0_sel:WORD_1
	v_pk_fma_f32 v[88:89], v[96:97], v[120:121], v[88:89]
	v_pk_fma_f32 v[128:129], v[94:95], v[128:129], v[34:35]
	v_pk_fma_f32 v[88:89], v[32:33], v[112:113], v[88:89]
	v_pk_fma_f32 v[128:129], v[30:31], v[120:121], v[128:129]
	v_mul_f32_e32 v79, 0xbfb8aa3b, v88
	v_exp_f32_e32 v80, v79
	v_mul_f32_e32 v79, 0xbfb8aa3b, v89
	v_exp_f32_e32 v106, v79
	v_cvt_pk_f16_f32 v79, v86, v87
	v_add_f32_e32 v80, 1.0, v80
	v_rcp_f32_e32 v86, v80
	v_add_f32_e32 v80, 1.0, v106
	v_rcp_f32_e32 v87, v80
	v_pk_fma_f32 v[80:81], v[82:83], v[108:109], v[36:37]
	v_pk_fma_f32 v[128:129], v[96:97], v[112:113], v[128:129]
	v_pk_fma_f32 v[80:81], v[26:27], v[126:127], v[80:81]
	v_pk_fma_f32 v[126:127], v[82:83], v[126:127], v[36:37]
	v_pk_fma_f32 v[80:81], v[84:85], v[118:119], v[80:81]
	v_pk_fma_f32 v[126:127], v[26:27], v[118:119], v[126:127]
	v_pk_fma_f32 v[106:107], v[28:29], v[110:111], v[80:81]
	v_pk_fma_f32 v[126:127], v[84:85], v[110:111], v[126:127]
	v_mul_f32_e32 v80, 0xbfb8aa3b, v106
	v_exp_f32_e32 v108, v80
	v_mul_f32_e32 v80, 0xbfb8aa3b, v107
	v_exp_f32_e32 v109, v80
	v_pk_mul_f32 v[80:81], v[88:89], v[86:87]
	v_add_f32_e32 v86, 1.0, v108
	s_waitcnt lgkmcnt(3)
	v_cvt_f32_f16_e32 v108, v74
	v_add_f32_e32 v87, 1.0, v109
	v_cvt_f32_f16_sdwa v109, v74 dst_sel:DWORD dst_unused:UNUSED_PAD src0_sel:WORD_1
	v_pk_fma_f32 v[88:89], v[102:103], v[132:133], v[46:47]
	v_rcp_f32_e32 v86, v86
	v_pk_fma_f32 v[88:89], v[42:43], v[124:125], v[88:89]
	v_rcp_f32_e32 v87, v87
	v_pk_fma_f32 v[88:89], v[104:105], v[116:117], v[88:89]
	v_cvt_pk_f16_f32 v80, v80, v81
	v_pk_fma_f32 v[88:89], v[44:45], v[108:109], v[88:89]
	v_pk_mul_f32 v[86:87], v[106:107], v[86:87]
	v_mul_f32_e32 v74, 0xbfb8aa3b, v88
	v_exp_f32_e32 v74, v74
	v_mul_f32_e32 v132, 0xbfb8aa3b, v89
	v_exp_f32_e32 v133, v132
	v_cvt_f32_f16_e32 v106, v75
	v_add_f32_e32 v74, 1.0, v74
	v_rcp_f32_e32 v132, v74
	v_add_f32_e32 v74, 1.0, v133
	v_cvt_f32_f16_sdwa v107, v75 dst_sel:DWORD dst_unused:UNUSED_PAD src0_sel:WORD_1
	v_rcp_f32_e32 v133, v74
	v_pk_fma_f32 v[74:75], v[98:99], v[130:131], v[48:49]
	v_cvt_pk_f16_f32 v81, v86, v87
	v_pk_fma_f32 v[74:75], v[38:39], v[122:123], v[74:75]
	v_pk_mul_f32 v[86:87], v[88:89], v[132:133]
	v_pk_fma_f32 v[74:75], v[100:101], v[114:115], v[74:75]
	v_cvt_f32_f16_sdwa v89, v76 dst_sel:DWORD dst_unused:UNUSED_PAD src0_sel:WORD_1
	v_pk_fma_f32 v[130:131], v[40:41], v[106:107], v[74:75]
	v_pk_fma_f32 v[124:125], v[102:103], v[124:125], v[46:47]
	v_mul_f32_e32 v74, 0xbfb8aa3b, v130
	v_exp_f32_e32 v75, v74
	v_mul_f32_e32 v74, 0xbfb8aa3b, v131
	v_exp_f32_e32 v88, v74
	v_cvt_pk_f16_f32 v74, v86, v87
	v_add_f32_e32 v75, 1.0, v75
	v_rcp_f32_e32 v86, v75
	v_add_f32_e32 v75, 1.0, v88
	v_cvt_f32_f16_e32 v88, v76
	v_rcp_f32_e32 v87, v75
	v_pk_fma_f32 v[124:125], v[42:43], v[116:117], v[124:125]
	v_pk_fma_f32 v[120:121], v[94:95], v[120:121], v[34:35]
	v_pk_fma_f32 v[128:129], v[32:33], v[88:89], v[128:129]
	v_pk_mul_f32 v[130:131], v[130:131], v[86:87]
	v_mul_f32_e32 v75, 0xbfb8aa3b, v128
	v_cvt_f32_f16_e32 v86, v77
	v_cvt_f32_f16_sdwa v87, v77 dst_sel:DWORD dst_unused:UNUSED_PAD src0_sel:WORD_1
	v_exp_f32_e32 v75, v75
	v_mul_f32_e32 v76, 0xbfb8aa3b, v129
	v_exp_f32_e32 v132, v76
	v_pk_fma_f32 v[126:127], v[28:29], v[86:87], v[126:127]
	v_add_f32_e32 v75, 1.0, v75
	v_mul_f32_e32 v77, 0xbfb8aa3b, v126
	v_rcp_f32_e32 v76, v75
	v_add_f32_e32 v75, 1.0, v132
	v_exp_f32_e32 v132, v77
	v_mul_f32_e32 v77, 0xbfb8aa3b, v127
	v_exp_f32_e32 v133, v77
	v_rcp_f32_e32 v77, v75
	v_pk_fma_f32 v[124:125], v[104:105], v[108:109], v[124:125]
	v_add_f32_e32 v75, 1.0, v132
	v_rcp_f32_e32 v132, v75
	v_pk_mul_f32 v[76:77], v[128:129], v[76:77]
	s_waitcnt lgkmcnt(2)
	v_cvt_f32_f16_e32 v128, v66
	v_cvt_f32_f16_sdwa v129, v66 dst_sel:DWORD dst_unused:UNUSED_PAD src0_sel:WORD_1
	v_add_f32_e32 v75, 1.0, v133
	v_rcp_f32_e32 v133, v75
	v_cvt_pk_f16_f32 v76, v76, v77
	v_pk_fma_f32 v[124:125], v[44:45], v[128:129], v[124:125]
	v_cvt_pk_f16_f32 v75, v130, v131
	v_mul_f32_e32 v66, 0xbfb8aa3b, v124
	v_exp_f32_e32 v66, v66
	v_mul_f32_e32 v77, 0xbfb8aa3b, v125
	v_exp_f32_e32 v130, v77
	v_pk_mul_f32 v[126:127], v[126:127], v[132:133]
	v_add_f32_e32 v66, 1.0, v66
	v_cvt_pk_f16_f32 v77, v126, v127
	v_rcp_f32_e32 v126, v66
	v_add_f32_e32 v66, 1.0, v130
	v_cvt_f32_f16_e32 v130, v67
	v_cvt_f32_f16_sdwa v131, v67 dst_sel:DWORD dst_unused:UNUSED_PAD src0_sel:WORD_1
	v_rcp_f32_e32 v127, v66
	v_pk_fma_f32 v[66:67], v[98:99], v[122:123], v[48:49]
	v_pk_fma_f32 v[120:121], v[30:31], v[112:113], v[120:121]
	v_pk_fma_f32 v[66:67], v[38:39], v[114:115], v[66:67]
	v_pk_fma_f32 v[120:121], v[96:97], v[88:89], v[120:121]
	v_pk_fma_f32 v[66:67], v[100:101], v[106:107], v[66:67]
	v_pk_fma_f32 v[116:117], v[102:103], v[116:117], v[46:47]
	v_pk_fma_f32 v[122:123], v[40:41], v[130:131], v[66:67]
	v_pk_fma_f32 v[116:117], v[42:43], v[108:109], v[116:117]
	v_mul_f32_e32 v66, 0xbfb8aa3b, v122
	v_exp_f32_e32 v132, v66
	v_mul_f32_e32 v66, 0xbfb8aa3b, v123
	v_exp_f32_e32 v133, v66
	v_pk_mul_f32 v[66:67], v[124:125], v[126:127]
	v_cvt_f32_f16_e32 v126, v68
	v_cvt_f32_f16_sdwa v127, v68 dst_sel:DWORD dst_unused:UNUSED_PAD src0_sel:WORD_1
	v_add_f32_e32 v124, 1.0, v132
	v_add_f32_e32 v125, 1.0, v133
	v_rcp_f32_e32 v124, v124
	v_pk_fma_f32 v[120:121], v[32:33], v[126:127], v[120:121]
	v_rcp_f32_e32 v125, v125
	v_mul_f32_e32 v68, 0xbfb8aa3b, v120
	v_exp_f32_e32 v68, v68
	v_mul_f32_e32 v132, 0xbfb8aa3b, v121
	v_exp_f32_e32 v133, v132
	v_pk_mul_f32 v[122:123], v[122:123], v[124:125]
	v_add_f32_e32 v68, 1.0, v68
	v_rcp_f32_e32 v132, v68
	v_add_f32_e32 v68, 1.0, v133
	v_cvt_pk_f16_f32 v66, v66, v67
	v_cvt_pk_f16_f32 v67, v122, v123
	v_cvt_f32_f16_e32 v122, v69
	v_cvt_f32_f16_sdwa v123, v69 dst_sel:DWORD dst_unused:UNUSED_PAD src0_sel:WORD_1
	v_rcp_f32_e32 v133, v68
	v_pk_fma_f32 v[68:69], v[82:83], v[118:119], v[36:37]
	s_waitcnt lgkmcnt(1)
	v_cvt_f32_f16_sdwa v125, v58 dst_sel:DWORD dst_unused:UNUSED_PAD src0_sel:WORD_1
	v_pk_fma_f32 v[68:69], v[26:27], v[110:111], v[68:69]
	v_pk_mul_f32 v[120:121], v[120:121], v[132:133]
	v_pk_fma_f32 v[68:69], v[84:85], v[86:87], v[68:69]
	v_pk_fma_f32 v[116:117], v[104:105], v[128:129], v[116:117]
	v_pk_fma_f32 v[118:119], v[28:29], v[122:123], v[68:69]
	v_pk_fma_f32 v[114:115], v[98:99], v[114:115], v[48:49]
	v_mul_f32_e32 v68, 0xbfb8aa3b, v118
	v_exp_f32_e32 v69, v68
	v_mul_f32_e32 v68, 0xbfb8aa3b, v119
	v_exp_f32_e32 v124, v68
	v_cvt_pk_f16_f32 v68, v120, v121
	v_add_f32_e32 v69, 1.0, v69
	v_rcp_f32_e32 v120, v69
	v_add_f32_e32 v69, 1.0, v124
	v_rcp_f32_e32 v121, v69
	v_cvt_f32_f16_e32 v124, v58
	v_pk_fma_f32 v[114:115], v[38:39], v[106:107], v[114:115]
	v_pk_fma_f32 v[112:113], v[94:95], v[112:113], v[34:35]
	v_pk_mul_f32 v[118:119], v[118:119], v[120:121]
	v_pk_fma_f32 v[116:117], v[44:45], v[124:125], v[116:117]
	v_cvt_f32_f16_e32 v120, v59
	v_cvt_f32_f16_sdwa v121, v59 dst_sel:DWORD dst_unused:UNUSED_PAD src0_sel:WORD_1
	v_mul_f32_e32 v58, 0xbfb8aa3b, v116
	v_mul_f32_e32 v69, 0xbfb8aa3b, v117
	v_exp_f32_e32 v58, v58
	v_exp_f32_e32 v69, v69
	v_pk_fma_f32 v[114:115], v[100:101], v[130:131], v[114:115]
	v_pk_fma_f32 v[112:113], v[30:31], v[88:89], v[112:113]
	v_pk_fma_f32 v[114:115], v[40:41], v[120:121], v[114:115]
	v_add_f32_e32 v58, 1.0, v58
	v_mul_f32_e32 v59, 0xbfb8aa3b, v114
	v_add_f32_e32 v69, 1.0, v69
	v_exp_f32_e32 v132, v59
	v_mul_f32_e32 v59, 0xbfb8aa3b, v115
	v_rcp_f32_e32 v58, v58
	v_exp_f32_e32 v133, v59
	v_rcp_f32_e32 v59, v69
	v_pk_fma_f32 v[112:113], v[96:97], v[126:127], v[112:113]
	v_add_f32_e32 v69, 1.0, v132
	v_rcp_f32_e32 v132, v69
	v_pk_mul_f32 v[58:59], v[116:117], v[58:59]
	v_cvt_f32_f16_e32 v116, v60
	v_cvt_f32_f16_sdwa v117, v60 dst_sel:DWORD dst_unused:UNUSED_PAD src0_sel:WORD_1
	v_add_f32_e32 v69, 1.0, v133
	v_cvt_pk_f16_f32 v58, v58, v59
	v_rcp_f32_e32 v133, v69
	v_pk_fma_f32 v[112:113], v[32:33], v[116:117], v[112:113]
	v_cvt_pk_f16_f32 v69, v118, v119
	v_mul_f32_e32 v59, 0xbfb8aa3b, v112
	v_exp_f32_e32 v60, v59
	v_mul_f32_e32 v59, 0xbfb8aa3b, v113
	v_exp_f32_e32 v118, v59
	v_pk_mul_f32 v[114:115], v[114:115], v[132:133]
	v_add_f32_e32 v60, 1.0, v60
	v_cvt_pk_f16_f32 v59, v114, v115
	v_rcp_f32_e32 v114, v60
	v_add_f32_e32 v60, 1.0, v118
	v_cvt_f32_f16_e32 v118, v61
	v_cvt_f32_f16_sdwa v119, v61 dst_sel:DWORD dst_unused:UNUSED_PAD src0_sel:WORD_1
	v_rcp_f32_e32 v115, v60
	v_pk_fma_f32 v[60:61], v[82:83], v[110:111], v[36:37]
	v_pk_fma_f32 v[46:47], v[102:103], v[108:109], v[46:47]
	v_pk_fma_f32 v[60:61], v[26:27], v[86:87], v[60:61]
	v_pk_fma_f32 v[42:43], v[42:43], v[128:129], v[46:47]
	v_pk_fma_f32 v[60:61], v[84:85], v[122:123], v[60:61]
	v_pk_fma_f32 v[42:43], v[104:105], v[124:125], v[42:43]
	v_pk_fma_f32 v[110:111], v[28:29], v[118:119], v[60:61]
	v_pk_fma_f32 v[34:35], v[94:95], v[88:89], v[34:35]
	v_mul_f32_e32 v60, 0xbfb8aa3b, v110
	v_exp_f32_e32 v132, v60
	v_mul_f32_e32 v60, 0xbfb8aa3b, v111
	v_exp_f32_e32 v133, v60
	v_pk_mul_f32 v[60:61], v[112:113], v[114:115]
	s_waitcnt lgkmcnt(0)
	v_cvt_f32_f16_e32 v114, v54
	v_cvt_f32_f16_sdwa v115, v54 dst_sel:DWORD dst_unused:UNUSED_PAD src0_sel:WORD_1
	v_add_f32_e32 v112, 1.0, v132
	v_add_f32_e32 v113, 1.0, v133
	v_rcp_f32_e32 v112, v112
	v_pk_fma_f32 v[42:43], v[44:45], v[114:115], v[42:43]
	v_rcp_f32_e32 v113, v113
	v_mul_f32_e32 v44, 0xbfb8aa3b, v42
	v_mul_f32_e32 v45, 0xbfb8aa3b, v43
	v_exp_f32_e32 v44, v44
	v_exp_f32_e32 v45, v45
	v_pk_mul_f32 v[46:47], v[110:111], v[112:113]
	v_cvt_pk_f16_f32 v60, v60, v61
	v_add_f32_e32 v44, 1.0, v44
	v_add_f32_e32 v45, 1.0, v45
	v_rcp_f32_e32 v44, v44
	v_rcp_f32_e32 v45, v45
	v_cvt_pk_f16_f32 v61, v46, v47
	v_pk_fma_f32 v[46:47], v[98:99], v[106:107], v[48:49]
	v_pk_fma_f32 v[30:31], v[30:31], v[126:127], v[34:35]
	v_pk_mul_f32 v[42:43], v[42:43], v[44:45]
	v_cvt_f32_f16_e32 v44, v55
	v_cvt_f32_f16_sdwa v45, v55 dst_sel:DWORD dst_unused:UNUSED_PAD src0_sel:WORD_1
	v_pk_fma_f32 v[38:39], v[38:39], v[130:131], v[46:47]
	v_pk_fma_f32 v[30:31], v[96:97], v[116:117], v[30:31]
	v_pk_fma_f32 v[38:39], v[100:101], v[120:121], v[38:39]
	v_pk_fma_f32 v[36:37], v[82:83], v[86:87], v[36:37]
	v_pk_fma_f32 v[40:41], v[40:41], v[44:45], v[38:39]
	v_cvt_f32_f16_sdwa v45, v56 dst_sel:DWORD dst_unused:UNUSED_PAD src0_sel:WORD_1
	v_mul_f32_e32 v38, 0xbfb8aa3b, v40
	v_exp_f32_e32 v39, v38
	v_mul_f32_e32 v38, 0xbfb8aa3b, v41
	v_exp_f32_e32 v44, v38
	v_cvt_pk_f16_f32 v38, v42, v43
	v_add_f32_e32 v39, 1.0, v39
	v_rcp_f32_e32 v42, v39
	v_add_f32_e32 v39, 1.0, v44
	v_cvt_f32_f16_e32 v44, v56
	v_rcp_f32_e32 v43, v39
	v_pk_fma_f32 v[26:27], v[26:27], v[122:123], v[36:37]
	v_pk_fma_f32 v[30:31], v[32:33], v[44:45], v[30:31]
	v_pk_fma_f32 v[26:27], v[84:85], v[118:119], v[26:27]
	v_mul_f32_e32 v32, 0xbfb8aa3b, v30
	v_exp_f32_e32 v34, v32
	v_mul_f32_e32 v32, 0xbfb8aa3b, v31
	v_exp_f32_e32 v35, v32
	v_pk_mul_f32 v[32:33], v[40:41], v[42:43]
	v_cvt_f32_f16_e32 v40, v57
	v_cvt_f32_f16_sdwa v41, v57 dst_sel:DWORD dst_unused:UNUSED_PAD src0_sel:WORD_1
	v_add_f32_e32 v34, 1.0, v34
	v_add_f32_e32 v35, 1.0, v35
	v_rcp_f32_e32 v34, v34
	v_pk_fma_f32 v[26:27], v[28:29], v[40:41], v[26:27]
	v_rcp_f32_e32 v35, v35
	v_mul_f32_e32 v28, 0xbfb8aa3b, v26
	v_mul_f32_e32 v29, 0xbfb8aa3b, v27
	v_exp_f32_e32 v28, v28
	v_exp_f32_e32 v29, v29
	v_pk_mul_f32 v[30:31], v[30:31], v[34:35]
	v_cvt_pk_f16_f32 v39, v32, v33
	v_add_f32_e32 v28, 1.0, v28
	v_add_f32_e32 v29, 1.0, v29
	v_rcp_f32_e32 v28, v28
	v_rcp_f32_e32 v29, v29
	v_cvt_pk_f16_f32 v40, v30, v31
	s_barrier
	v_pk_mul_f32 v[26:27], v[26:27], v[28:29]
	v_or_b32_e32 v34, v141, v140
	v_cvt_pk_f16_f32 v41, v26, v27
	ds_write_b128 v93, v[50:53] offset:8448
	ds_write_b128 v93, v[62:65] offset:8976
	ds_write_b128 v93, v[70:73] offset:9504
	ds_write_b128 v93, v[78:81] offset:10032
	ds_write_b128 v93, v[74:77] offset:10560
	ds_write_b128 v93, v[66:69] offset:11088
	ds_write_b128 v93, v[58:61] offset:11616
	ds_write_b128 v93, v[38:41] offset:12144
	v_mov_b32_e32 v93, v91
	v_lshl_add_u64 v[58:59], s[4:5], 0, v[92:93]
	v_add_co_u32_e32 v60, vcc, s17, v58
	s_waitcnt lgkmcnt(0)
	s_nop 0
	v_addc_co_u32_e32 v61, vcc, 0, v59, vcc
	s_barrier
	global_load_dwordx4 v[26:29], v92, s[4:5]
	global_load_dwordx4 v[30:33], v[60:61], off offset:-4096
	s_movk_i32 s6, 0x210
	v_add_u32_e32 v34, 16, v34
	v_mad_u32_u24 v66, v34, s6, v142
	ds_read_b128 v[34:37], v66
	s_movk_i32 s6, 0x5000
	v_add_co_u32_e32 v62, vcc, s6, v58
	s_waitcnt vmcnt(1) lgkmcnt(0)
	v_mfma_f32_16x16x32_f16 a[0:3], v[34:37], v[26:29], 0
	v_addc_co_u32_e32 v63, vcc, 0, v59, vcc
	global_load_dwordx4 v[38:41], v[62:63], off offset:-4096
	global_load_dwordx4 v[42:45], v92, s[4:5] offset:1024
	v_add_co_u32_e32 v54, vcc, s16, v58
	global_load_dwordx4 v[26:29], v[60:61], off
	s_nop 0
	v_addc_co_u32_e32 v55, vcc, 0, v59, vcc
	s_waitcnt vmcnt(3)
	v_mfma_f32_16x16x32_f16 a[4:7], v[34:37], v[30:33], 0
	global_load_dwordx4 v[30:33], v[54:55], off offset:1024
	ds_read_b128 v[46:49], v66 offset:64
	s_movk_i32 s6, 0x4000
	v_add_co_u32_e32 v64, vcc, s6, v58
	global_load_dwordx4 v[50:53], v[62:63], off
	s_nop 0
	v_addc_co_u32_e32 v65, vcc, 0, v59, vcc
	s_waitcnt vmcnt(4)
	v_mfma_f32_16x16x32_f16 a[8:11], v[34:37], v[38:41], 0
	global_load_dwordx4 v[34:37], v[64:65], off offset:1024
	global_load_dwordx4 v[38:41], v[54:55], off offset:2048
	v_add_co_u32_e32 v58, vcc, s3, v58
	s_waitcnt vmcnt(5) lgkmcnt(0)
	v_mfma_f32_16x16x32_f16 a[0:3], v[46:49], v[42:45], a[0:3]
	v_addc_co_u32_e32 v59, vcc, 0, v59, vcc
	s_load_dwordx2 s[16:17], s[0:1], 0x60
	s_waitcnt vmcnt(3)
	v_mfma_f32_16x16x32_f16 a[4:7], v[46:49], v[30:33], a[4:7]
	global_load_dwordx4 v[30:33], v92, s[4:5] offset:2048
	global_load_dwordx4 v[42:45], v[54:55], off offset:3072
	s_mov_b32 s3, 4
	s_waitcnt vmcnt(3)
	v_mfma_f32_16x16x32_f16 a[8:11], v[46:49], v[34:37], a[8:11]
	ds_read_b128 v[34:37], v66 offset:128
	ds_read_b128 v[46:49], v66 offset:192
	global_load_dwordx4 v[54:57], v92, s[4:5] offset:3072
	s_waitcnt vmcnt(2) lgkmcnt(0)
	v_mfma_f32_16x16x32_f16 a[0:3], v[34:37], v[30:33], a[0:3]
	global_load_dwordx4 v[30:33], v[64:65], off offset:2048
	v_mfma_f32_16x16x32_f16 a[4:7], v[34:37], v[38:41], a[4:7]
	global_load_dwordx4 v[38:41], v[64:65], off offset:3072
	s_waitcnt vmcnt(3)
	v_mfma_f32_16x16x32_f16 a[4:7], v[46:49], v[42:45], a[4:7]
	global_load_dwordx4 v[42:45], v[60:61], off offset:1024
	s_waitcnt vmcnt(2)
	v_mfma_f32_16x16x32_f16 a[8:11], v[34:37], v[30:33], a[8:11]
	global_load_dwordx4 v[30:33], v[58:59], off
	global_load_dwordx4 v[34:37], v[58:59], off offset:1024
	v_mfma_f32_16x16x32_f16 a[0:3], v[46:49], v[54:57], a[0:3]
	s_waitcnt vmcnt(3)
	v_mfma_f32_16x16x32_f16 a[8:11], v[46:49], v[38:41], a[8:11]
	ds_read_b128 v[38:41], v66 offset:256
	ds_read_b128 v[46:49], v66 offset:320
	s_waitcnt vmcnt(1) lgkmcnt(1)
	v_mfma_f32_16x16x32_f16 a[0:3], v[38:41], v[30:33], a[0:3]
	global_load_dwordx4 v[30:33], v[62:63], off offset:1024
	v_mfma_f32_16x16x32_f16 a[4:7], v[38:41], v[26:29], a[4:7]
	global_load_dwordx4 v[26:29], v[58:59], off offset:2048
	v_mfma_f32_16x16x32_f16 a[8:11], v[38:41], v[50:53], a[8:11]
	global_load_dwordx4 v[38:41], v[60:61], off offset:2048
	s_waitcnt vmcnt(3) lgkmcnt(0)
	v_mfma_f32_16x16x32_f16 a[0:3], v[46:49], v[34:37], a[0:3]
	global_load_dwordx4 v[34:37], v[62:63], off offset:2048
	v_mfma_f32_16x16x32_f16 a[4:7], v[46:49], v[42:45], a[4:7]
	global_load_dwordx4 v[42:45], v[58:59], off offset:3072
	s_waitcnt vmcnt(4)
	v_mfma_f32_16x16x32_f16 a[8:11], v[46:49], v[30:33], a[8:11]
	ds_read_b128 v[30:33], v66 offset:384
	ds_read_b128 v[46:49], v66 offset:448
	s_waitcnt vmcnt(3) lgkmcnt(1)
	v_mfma_f32_16x16x32_f16 a[0:3], v[30:33], v[26:29], a[0:3]
	global_load_dwordx4 v[26:29], v139, s[4:5]
	s_load_dwordx8 s[4:11], s[0:1], 0x40
	s_movk_i32 s0, 0xd0
	s_waitcnt vmcnt(3)
	v_mfma_f32_16x16x32_f16 a[4:7], v[30:33], v[38:41], a[4:7]
	v_mov_b32_e32 v40, v91
	v_mov_b32_e32 v41, v91
	v_mov_b32_e32 v38, v91
	s_waitcnt vmcnt(2)
	v_mfma_f32_16x16x32_f16 a[8:11], v[30:33], v[34:37], a[8:11]
	global_load_dwordx4 v[30:33], v[62:63], off offset:3072
	v_lshlrev_b32_e32 v34, 2, v140
	v_or_b32_e32 v35, 0xfa00, v34
	s_waitcnt vmcnt(2) lgkmcnt(0)
	v_mfma_f32_16x16x32_f16 a[0:3], v[46:49], v[42:45], a[0:3]
	v_mov_b32_e32 v42, v91
	v_mov_b32_e32 v43, v91
	v_mov_b32_e32 v39, v91
	s_waitcnt vmcnt(1)
	v_mfma_f32_16x16x32_f16 a[4:7], v[46:49], v[26:29], a[4:7]
	v_bitop3_b32 v26, v138, 12, 48 bitop3:0xe0
	v_mad_u32_u24 v26, v26, s0, v35
	v_or_b32_e32 v28, s14, v134
	s_waitcnt vmcnt(0)
	v_mfma_f32_16x16x32_f16 a[8:11], v[46:49], v[30:33], a[8:11]
	ds_write_b32 v26, a0
	ds_write_b32 v26, a1 offset:208
	ds_write_b32 v26, a2 offset:416
	ds_write_b32 v26, a3 offset:624
	ds_write_b32 v26, a4 offset:64
	ds_write_b32 v26, a5 offset:272
	ds_write_b32 v26, a6 offset:480
	ds_write_b32 v26, a7 offset:688
	ds_write_b32 v26, a8 offset:128
	ds_write_b32 v26, a9 offset:336
	ds_write_b32 v26, a10 offset:544
	ds_write_b32 v26, a11 offset:752
	v_mad_u32_u24 v26, v134, s0, v35
	s_waitcnt lgkmcnt(0)
	s_barrier
	ds_read2_b32 v[26:27], v26 offset0:8 offset1:24
	v_mov_b32_e32 v29, s15
	v_lshlrev_b64 v[30:31], 6, v[28:29]
	v_or_b32_e32 v30, v30, v34
	v_lshl_add_u64 v[32:33], s[6:7], 0, v[30:31]
	s_waitcnt lgkmcnt(0)
	global_store_dword v[32:33], v26, off
	v_lshl_add_u64 v[30:31], s[8:9], 0, v[30:31]
	v_mad_u32_u24 v26, v135, s0, v35
	global_store_dword v[30:31], v27, off
	ds_read2_b32 v[26:27], v26 offset0:8 offset1:24
	v_or_b32_e32 v28, s14, v135
	v_lshlrev_b64 v[30:31], 6, v[28:29]
	v_or_b32_e32 v30, v30, v34
	v_lshl_add_u64 v[32:33], s[6:7], 0, v[30:31]
	s_waitcnt lgkmcnt(0)
	global_store_dword v[32:33], v26, off
	v_lshl_add_u64 v[30:31], s[8:9], 0, v[30:31]
	v_mad_u32_u24 v26, v136, s0, v35
	global_store_dword v[30:31], v27, off
	ds_read2_b32 v[26:27], v26 offset0:8 offset1:24
	v_or_b32_e32 v28, s14, v136
	v_lshlrev_b64 v[30:31], 6, v[28:29]
	v_or_b32_e32 v30, v30, v34
	v_lshl_add_u64 v[32:33], s[6:7], 0, v[30:31]
	s_waitcnt lgkmcnt(0)
	global_store_dword v[32:33], v26, off
	v_lshl_add_u64 v[30:31], s[8:9], 0, v[30:31]
	v_mad_u32_u24 v26, v137, s0, v35
	global_store_dword v[30:31], v27, off
	ds_read2_b32 v[30:31], v26 offset0:8 offset1:24
	v_or_b32_e32 v28, s14, v137
	v_lshlrev_b64 v[32:33], 6, v[28:29]
	ds_read_b128 v[26:29], v91 offset:64000
	v_or_b32_e32 v32, v32, v34
	v_lshl_add_u64 v[34:35], s[6:7], 0, v[32:33]
	v_lshl_add_u64 v[32:33], s[8:9], 0, v[32:33]
	s_waitcnt lgkmcnt(1)
	global_store_dword v[34:35], v30, off
	global_store_dword v[32:33], v31, off
	ds_read_b128 v[30:33], v91 offset:64016
	v_lshlrev_b32_e32 v46, 1, v0
	ds_read_u16 v48, v46 offset:8448
	s_waitcnt lgkmcnt(2)
	v_fma_f32 v26, v22, v26, v1
	v_fmac_f32_e32 v26, v24, v28
	v_mul_f32_e32 v28, v25, v29
	v_fmac_f32_e32 v28, v23, v27
	s_waitcnt lgkmcnt(1)
	v_fmac_f32_e32 v26, v18, v30
	v_fmac_f32_e32 v28, v19, v31
	v_fmac_f32_e32 v26, v20, v32
	v_fmac_f32_e32 v28, v21, v33
	v_add_f32_e32 v28, v26, v28
	v_mul_f32_e64 v26, |v28|, s18
	v_exp_f32_e32 v26, v26
	s_lshl_b64 s[0:1], s[14:15], 10
	s_add_u32 s0, s4, s0
	s_addc_u32 s1, s5, s1
	v_add_f32_e32 v26, 1.0, v26
	v_log_f32_e32 v29, v26
	v_max_f32_e32 v49, 0, v28
	v_lshl_add_u64 v[26:27], s[0:1], 0, v[90:91]
	v_mul_u32_u24_e32 v164, 12, v0
	v_mov_b32_e32 v165, 0
	v_lshl_add_u64 v[26:27], v[26:27], 0, v[164:165]
	s_mov_b32 s4, 0x3f317218
	v_fmac_f32_e32 v49, 0x3f317218, v29
	v_add_u32_e32 v47, 0x2310, v46
	s_mov_b64 s[0:1], 0
	s_mov_b32 s5, 0xfa20
	v_mov_b32_e32 v28, v91
	v_mov_b32_e32 v29, v91
	v_mov_b32_e32 v36, v91
	v_mov_b32_e32 v37, v91
	v_mov_b32_e32 v34, v91
	v_mov_b32_e32 v35, v91
	v_mov_b32_e32 v32, v91
	v_mov_b32_e32 v33, v91
	v_mov_b32_e32 v30, v91
	v_mov_b32_e32 v31, v91
.LBB1_1:
	v_cvt_f16_f32_e32 v49, v49
	s_cmpk_lg_u32 s0, 0xf000
	v_mov_b32_e32 v90, s5
	s_cselect_b32 s6, s3, 63
	ds_read_u16 v149, v47
	ds_read_u16 v150, v47 offset:528
	ds_read_u16 v151, v47 offset:1056
	ds_read_b128 v[50:53], v90 offset:176
	ds_read_b128 v[54:57], v90 offset:192
	ds_read_b128 v[58:61], v90
	ds_read_b128 v[62:65], v90 offset:16
	ds_read_b128 v[66:69], v90 offset:32
	ds_read_b128 v[70:73], v90 offset:48
	ds_read_b128 v[74:77], v90 offset:384
	ds_read_b128 v[78:81], v90 offset:400
	ds_read_b128 v[82:85], v90 offset:208
	ds_read_b128 v[86:89], v90 offset:224
	ds_read_b128 v[92:95], v90 offset:240
	ds_read_b128 v[96:99], v90 offset:256
	ds_read_b128 v[100:103], v90 offset:592
	ds_read_b128 v[104:107], v90 offset:608
	ds_read_b128 v[108:111], v90 offset:416
	ds_read_b128 v[112:115], v90 offset:432
	ds_read_b128 v[116:119], v90 offset:448
	ds_read_b128 v[120:123], v90 offset:464
	s_mul_i32 s7, s6, 0xd0
	s_waitcnt lgkmcnt(14)
	v_lshlrev_b32_e32 v140, 16, v48
	v_cvt_f32_f16_e32 v148, v48
	s_mulk_i32 s6, 0x210
	v_mov_b32_e32 v48, s7
	v_fma_f32 v50, v22, v50, v1
	v_mul_f32_e32 v51, v23, v51
	ds_read_b128 v[124:127], v90 offset:624
	ds_read_b128 v[128:131], v90 offset:640
	ds_read_b128 v[132:135], v90 offset:656
	ds_read_b128 v[136:139], v90 offset:672
	v_add_u32_e32 v152, s6, v46
	v_or_b32_e32 v164, v140, v49
	ds_read_b128 v[140:143], v48 offset:64000
	ds_read_b128 v[144:147], v48 offset:64016
	ds_read_u16 v48, v152 offset:8448
	s_waitcnt lgkmcnt(14)
	v_fma_f32 v74, v22, v74, v1
	v_mul_f32_e32 v75, v23, v75
	s_waitcnt lgkmcnt(12)
	v_fma_f32 v100, v22, v100, v1
	v_mul_f32_e32 v101, v23, v101
	v_pk_fma_f32 v[50:51], v[24:25], v[52:53], v[50:51]
	v_cvt_f32_f16_e32 v90, v49
	v_pk_fma_f32 v[52:53], v[24:25], v[76:77], v[74:75]
	v_pk_fma_f32 v[74:75], v[24:25], v[102:103], v[100:101]
	v_pk_fma_f32 v[50:51], v[18:19], v[54:55], v[50:51]
	v_pk_fma_f32 v[52:53], v[18:19], v[78:79], v[52:53]
	s_waitcnt lgkmcnt(11)
	v_pk_fma_f32 v[74:75], v[18:19], v[104:105], v[74:75]
	v_pk_fma_f32 v[50:51], v[20:21], v[56:57], v[50:51]
	v_pk_fma_f32 v[52:53], v[20:21], v[80:81], v[52:53]
	v_pk_fma_f32 v[74:75], v[20:21], v[106:107], v[74:75]
	s_waitcnt lgkmcnt(2)
	v_fma_f32 v80, v22, v140, v1
	v_mul_f32_e32 v81, v23, v141
	v_add_f32_e32 v49, v50, v51
	v_lshl_add_u64 v[44:45], v[26:27], 0, s[0:1]
	v_add_f32_e32 v52, v52, v53
	v_add_f32_e32 v53, v74, v75
	v_pk_fma_f32 v[50:51], v[24:25], v[142:143], v[80:81]
	v_mul_f32_e64 v74, |v49|, s18
	v_lshlrev_b32_e32 v158, 16, v149
	v_cvt_f32_f16_e32 v159, v149
	v_lshlrev_b32_e32 v160, 16, v150
	v_cvt_f32_f16_e32 v161, v150
	v_lshlrev_b32_e32 v162, 16, v151
	v_cvt_f32_f16_e32 v163, v151
	v_mul_f32_e32 v54, v90, v148
	v_pk_mul_f32 v[76:77], v[90:91], v[14:15] op_sel_hi:[0,1]
	v_pk_mul_f32 v[100:101], v[90:91], v[16:17] op_sel_hi:[0,1]
	v_pk_mul_f32 v[102:103], v[90:91], v[10:11] op_sel_hi:[0,1]
	v_pk_mul_f32 v[148:149], v[90:91], v[12:13] op_sel_hi:[0,1]
	v_pk_mul_f32 v[150:151], v[90:91], v[6:7] op_sel_hi:[0,1]
	v_pk_mul_f32 v[152:153], v[90:91], v[8:9] op_sel_hi:[0,1]
	v_pk_mul_f32 v[154:155], v[90:91], v[2:3] op_sel_hi:[0,1]
	v_pk_mul_f32 v[156:157], v[90:91], v[4:5] op_sel_hi:[0,1]
	v_mul_f32_e64 v80, |v53|, s18
	s_waitcnt lgkmcnt(1)
	v_pk_fma_f32 v[50:51], v[18:19], v[144:145], v[50:51]
	v_exp_f32_e32 v74, v74
	v_add_f32_e32 v55, v91, v90
	v_exp_f32_e32 v56, v76
	v_exp_f32_e32 v57, v77
	v_exp_f32_e32 v76, v100
	v_exp_f32_e32 v77, v101
	v_exp_f32_e32 v78, v102
	v_exp_f32_e32 v79, v103
	v_exp_f32_e32 v90, v148
	v_exp_f32_e32 v91, v149
	v_exp_f32_e32 v100, v150
	v_exp_f32_e32 v101, v151
	v_exp_f32_e32 v102, v152
	v_exp_f32_e32 v103, v153
	v_exp_f32_e32 v104, v154
	v_exp_f32_e32 v105, v155
	v_exp_f32_e32 v148, v156
	v_exp_f32_e32 v149, v157
	v_max_f32_e32 v75, 0, v49
	v_mul_f32_e64 v49, |v52|, s18
	v_exp_f32_e32 v80, v80
	v_pk_fma_f32 v[50:51], v[20:21], v[146:147], v[50:51]
	v_exp_f32_e32 v81, v49
	v_add_f32_e32 v49, v50, v51
	v_mul_f32_e64 v50, |v49|, s18
	v_exp_f32_e32 v50, v50
	v_add_f32_e32 v51, 1.0, v74
	v_pk_mul_f32 v[42:43], v[42:43], v[56:57]
	v_pk_mul_f32 v[40:41], v[40:41], v[76:77]
	v_pk_mul_f32 v[38:39], v[38:39], v[78:79]
	v_pk_mul_f32 v[36:37], v[36:37], v[90:91]
	v_pk_mul_f32 v[34:35], v[34:35], v[100:101]
	v_pk_mul_f32 v[32:33], v[32:33], v[102:103]
	v_pk_mul_f32 v[30:31], v[30:31], v[104:105]
	v_pk_mul_f32 v[28:29], v[28:29], v[148:149]
	v_add_f32_e32 v56, 1.0, v80
	v_log_f32_e32 v51, v51
	v_pk_fma_f32 v[42:43], v[54:55], v[58:59], v[42:43] op_sel_hi:[0,1,1]
	v_pk_fma_f32 v[40:41], v[54:55], v[60:61], v[40:41] op_sel_hi:[0,1,1]
	v_pk_fma_f32 v[38:39], v[54:55], v[62:63], v[38:39] op_sel_hi:[0,1,1]
	v_pk_fma_f32 v[36:37], v[54:55], v[64:65], v[36:37] op_sel_hi:[0,1,1]
	v_pk_fma_f32 v[34:35], v[54:55], v[66:67], v[34:35] op_sel_hi:[0,1,1]
	v_pk_fma_f32 v[32:33], v[54:55], v[68:69], v[32:33] op_sel_hi:[0,1,1]
	v_pk_fma_f32 v[30:31], v[54:55], v[70:71], v[30:31] op_sel_hi:[0,1,1]
	v_pk_fma_f32 v[28:29], v[54:55], v[72:73], v[28:29] op_sel_hi:[0,1,1]
	v_add_f32_e32 v54, 1.0, v81
	v_log_f32_e32 v56, v56
	v_log_f32_e32 v54, v54
	v_add_f32_e32 v50, 1.0, v50
	v_max_f32_e32 v53, 0, v53
	v_log_f32_e32 v57, v50
	v_fma_mixlo_f16 v50, v51, s4, v75
	v_max_f32_e32 v52, 0, v52
	v_fma_mixlo_f16 v53, v56, s4, v53
	v_or_b32_sdwa v165, v158, v50 dst_sel:DWORD dst_unused:UNUSED_PAD src0_sel:DWORD src1_sel:WORD_0
	v_cvt_f32_f16_e32 v50, v50
	v_fma_mixlo_f16 v51, v54, s4, v52
	v_cvt_f32_f16_e32 v52, v51
	v_max_f32_e32 v49, 0, v49
	v_or_b32_sdwa v166, v160, v51 dst_sel:DWORD dst_unused:UNUSED_PAD src0_sel:DWORD src1_sel:WORD_0
	v_or_b32_sdwa v167, v162, v53 dst_sel:DWORD dst_unused:UNUSED_PAD src0_sel:DWORD src1_sel:WORD_0
	v_cvt_f32_f16_e32 v54, v53
	global_store_dwordx4 v[44:45], v[164:167], off
	v_fmac_f32_e32 v49, 0x3f317218, v57
	v_pk_mul_f32 v[56:57], v[50:51], v[14:15] op_sel_hi:[0,1]
	v_pk_mul_f32 v[58:59], v[50:51], v[16:17] op_sel_hi:[0,1]
	v_pk_mul_f32 v[60:61], v[50:51], v[10:11] op_sel_hi:[0,1]
	v_pk_mul_f32 v[62:63], v[50:51], v[12:13] op_sel_hi:[0,1]
	v_pk_mul_f32 v[64:65], v[50:51], v[6:7] op_sel_hi:[0,1]
	v_pk_mul_f32 v[66:67], v[50:51], v[8:9] op_sel_hi:[0,1]
	v_pk_mul_f32 v[68:69], v[50:51], v[2:3] op_sel_hi:[0,1]
	v_pk_mul_f32 v[70:71], v[50:51], v[4:5] op_sel_hi:[0,1]
	v_exp_f32_e32 v56, v56
	v_exp_f32_e32 v57, v57
	v_exp_f32_e32 v58, v58
	v_exp_f32_e32 v59, v59
	v_exp_f32_e32 v60, v60
	v_exp_f32_e32 v61, v61
	v_exp_f32_e32 v62, v62
	v_exp_f32_e32 v63, v63
	v_exp_f32_e32 v64, v64
	v_exp_f32_e32 v65, v65
	v_exp_f32_e32 v66, v66
	v_exp_f32_e32 v67, v67
	v_exp_f32_e32 v68, v68
	v_exp_f32_e32 v69, v69
	v_exp_f32_e32 v70, v70
	v_exp_f32_e32 v71, v71
	v_pk_mul_f32 v[72:73], v[52:53], v[14:15] op_sel_hi:[0,1]
	v_pk_mul_f32 v[74:75], v[52:53], v[16:17] op_sel_hi:[0,1]
	v_pk_mul_f32 v[76:77], v[52:53], v[10:11] op_sel_hi:[0,1]
	v_pk_mul_f32 v[78:79], v[52:53], v[12:13] op_sel_hi:[0,1]
	v_pk_mul_f32 v[80:81], v[52:53], v[6:7] op_sel_hi:[0,1]
	v_pk_mul_f32 v[90:91], v[52:53], v[8:9] op_sel_hi:[0,1]
	v_pk_mul_f32 v[100:101], v[52:53], v[2:3] op_sel_hi:[0,1]
	v_pk_mul_f32 v[102:103], v[52:53], v[4:5] op_sel_hi:[0,1]
	v_exp_f32_e32 v72, v72
	v_exp_f32_e32 v73, v73
	v_exp_f32_e32 v74, v74
	v_exp_f32_e32 v75, v75
	v_exp_f32_e32 v76, v76
	v_exp_f32_e32 v77, v77
	v_exp_f32_e32 v78, v78
	v_exp_f32_e32 v79, v79
	v_exp_f32_e32 v80, v80
	v_exp_f32_e32 v81, v81
	v_exp_f32_e32 v154, v90
	v_exp_f32_e32 v155, v91
	v_exp_f32_e32 v100, v100
	v_exp_f32_e32 v101, v101
	v_exp_f32_e32 v102, v102
	v_exp_f32_e32 v103, v103
	v_add_f32_e32 v45, v55, v50
	v_pk_mul_f32 v[106:107], v[54:55], v[14:15] op_sel_hi:[0,1]
	v_pk_mul_f32 v[140:141], v[54:55], v[16:17] op_sel_hi:[0,1]
	v_pk_mul_f32 v[142:143], v[54:55], v[10:11] op_sel_hi:[0,1]
	v_pk_mul_f32 v[144:145], v[54:55], v[12:13] op_sel_hi:[0,1]
	v_pk_mul_f32 v[146:147], v[54:55], v[6:7] op_sel_hi:[0,1]
	v_pk_mul_f32 v[148:149], v[54:55], v[8:9] op_sel_hi:[0,1]
	v_pk_mul_f32 v[150:151], v[54:55], v[2:3] op_sel_hi:[0,1]
	v_pk_mul_f32 v[152:153], v[54:55], v[4:5] op_sel_hi:[0,1]
	v_mul_f32_e32 v44, v50, v159
	v_mul_f32_e32 v50, v52, v161
	v_add_f32_e32 v45, v45, v52
	v_exp_f32_e32 v52, v106
	v_exp_f32_e32 v53, v107
	v_exp_f32_e32 v106, v140
	v_exp_f32_e32 v107, v141
	v_exp_f32_e32 v140, v142
	v_exp_f32_e32 v141, v143
	v_exp_f32_e32 v142, v144
	v_exp_f32_e32 v143, v145
	v_exp_f32_e32 v144, v146
	v_exp_f32_e32 v145, v147
	v_exp_f32_e32 v146, v148
	v_exp_f32_e32 v147, v149
	v_exp_f32_e32 v148, v150
	v_exp_f32_e32 v149, v151
	v_exp_f32_e32 v150, v152
	v_exp_f32_e32 v151, v153
	v_pk_mul_f32 v[42:43], v[42:43], v[56:57]
	v_pk_mul_f32 v[40:41], v[40:41], v[58:59]
	v_pk_mul_f32 v[38:39], v[38:39], v[60:61]
	v_pk_mul_f32 v[36:37], v[36:37], v[62:63]
	v_pk_mul_f32 v[34:35], v[34:35], v[64:65]
	v_pk_mul_f32 v[32:33], v[32:33], v[66:67]
	v_pk_mul_f32 v[30:31], v[30:31], v[68:69]
	v_pk_mul_f32 v[28:29], v[28:29], v[70:71]
	v_pk_fma_f32 v[42:43], v[44:45], v[82:83], v[42:43] op_sel_hi:[0,1,1]
	v_pk_fma_f32 v[40:41], v[44:45], v[84:85], v[40:41] op_sel_hi:[0,1,1]
	v_pk_fma_f32 v[38:39], v[44:45], v[86:87], v[38:39] op_sel_hi:[0,1,1]
	v_pk_fma_f32 v[36:37], v[44:45], v[88:89], v[36:37] op_sel_hi:[0,1,1]
	v_pk_fma_f32 v[34:35], v[44:45], v[92:93], v[34:35] op_sel_hi:[0,1,1]
	v_pk_fma_f32 v[32:33], v[44:45], v[94:95], v[32:33] op_sel_hi:[0,1,1]
	v_pk_fma_f32 v[30:31], v[44:45], v[96:97], v[30:31] op_sel_hi:[0,1,1]
	v_pk_fma_f32 v[28:29], v[44:45], v[98:99], v[28:29] op_sel_hi:[0,1,1]
	v_pk_mul_f32 v[42:43], v[42:43], v[72:73]
	v_pk_mul_f32 v[40:41], v[40:41], v[74:75]
	v_pk_mul_f32 v[38:39], v[38:39], v[76:77]
	v_pk_mul_f32 v[36:37], v[36:37], v[78:79]
	v_pk_mul_f32 v[34:35], v[34:35], v[80:81]
	v_pk_mul_f32 v[32:33], v[32:33], v[154:155]
	v_pk_mul_f32 v[30:31], v[30:31], v[100:101]
	v_pk_mul_f32 v[28:29], v[28:29], v[102:103]
	s_add_u32 s0, s0, 0x1000
	v_pk_fma_f32 v[42:43], v[50:51], v[108:109], v[42:43] op_sel_hi:[0,1,1]
	v_pk_fma_f32 v[40:41], v[50:51], v[110:111], v[40:41] op_sel_hi:[0,1,1]
	v_pk_fma_f32 v[38:39], v[50:51], v[112:113], v[38:39] op_sel_hi:[0,1,1]
	v_pk_fma_f32 v[36:37], v[50:51], v[114:115], v[36:37] op_sel_hi:[0,1,1]
	v_pk_fma_f32 v[34:35], v[50:51], v[116:117], v[34:35] op_sel_hi:[0,1,1]
	v_pk_fma_f32 v[32:33], v[50:51], v[118:119], v[32:33] op_sel_hi:[0,1,1]
	v_pk_fma_f32 v[30:31], v[50:51], v[120:121], v[30:31] op_sel_hi:[0,1,1]
	v_pk_fma_f32 v[28:29], v[50:51], v[122:123], v[28:29] op_sel_hi:[0,1,1]
	s_addc_u32 s1, s1, 0
	s_add_i32 s3, s3, 4
	s_addk_i32 s5, 0x340
	v_mul_f32_e32 v104, v54, v163
	v_pk_mul_f32 v[42:43], v[42:43], v[52:53]
	v_pk_mul_f32 v[40:41], v[40:41], v[106:107]
	v_pk_mul_f32 v[38:39], v[38:39], v[140:141]
	v_pk_mul_f32 v[36:37], v[36:37], v[142:143]
	v_pk_mul_f32 v[34:35], v[34:35], v[144:145]
	v_pk_mul_f32 v[32:33], v[32:33], v[146:147]
	v_pk_mul_f32 v[30:31], v[30:31], v[148:149]
	v_pk_mul_f32 v[28:29], v[28:29], v[150:151]
	v_add_u32_e32 v47, 0x840, v47
	s_cmp_eq_u32 s0, 0x10000
	v_add_f32_e32 v91, v45, v54
	v_pk_fma_f32 v[42:43], v[104:105], v[124:125], v[42:43] op_sel_hi:[0,1,1]
	v_pk_fma_f32 v[40:41], v[104:105], v[126:127], v[40:41] op_sel_hi:[0,1,1]
	v_pk_fma_f32 v[38:39], v[104:105], v[128:129], v[38:39] op_sel_hi:[0,1,1]
	v_pk_fma_f32 v[36:37], v[104:105], v[130:131], v[36:37] op_sel_hi:[0,1,1]
	v_pk_fma_f32 v[34:35], v[104:105], v[132:133], v[34:35] op_sel_hi:[0,1,1]
	v_pk_fma_f32 v[32:33], v[104:105], v[134:135], v[32:33] op_sel_hi:[0,1,1]
	v_pk_fma_f32 v[30:31], v[104:105], v[136:137], v[30:31] op_sel_hi:[0,1,1]
	v_pk_fma_f32 v[28:29], v[104:105], v[138:139], v[28:29] op_sel_hi:[0,1,1]
	s_cbranch_scc0 .LBB1_1
	s_ashr_i32 s3, s2, 31
	s_lshl_b64 s[0:1], s[12:13], 10
	s_lshl_b64 s[4:5], s[2:3], 4
	s_add_u32 s0, s0, s4
	s_addc_u32 s1, s1, s5
	s_lshl_b64 s[0:1], s[0:1], 10
	s_add_u32 s0, s10, s0
	s_addc_u32 s1, s11, s1
	v_lshlrev_b32_e32 v0, 2, v0
	v_mov_b32_e32 v1, 0
	v_lshl_add_u64 v[2:3], s[0:1], 0, v[0:1]
	global_store_dword v0, v42, s[0:1]
	global_store_dword v0, v43, s[0:1] offset:1024
	global_store_dword v0, v40, s[0:1] offset:2048
	global_store_dword v0, v41, s[0:1] offset:3072
	s_movk_i32 s0, 0x1000
	v_add_co_u32_e32 v4, vcc, s0, v2
	s_movk_i32 s0, 0x2000
	s_nop 0
	v_addc_co_u32_e32 v5, vcc, 0, v3, vcc
	v_add_co_u32_e32 v6, vcc, s0, v2
	s_movk_i32 s0, 0x3000
	s_nop 0
	v_addc_co_u32_e32 v7, vcc, 0, v3, vcc
	v_add_co_u32_e32 v2, vcc, s0, v2
	s_lshl_b64 s[0:1], s[12:13], 16
	s_add_u32 s4, s16, s0
	s_addc_u32 s5, s17, s1
	s_lshl_b64 s[0:1], s[2:3], 10
	s_add_u32 s0, s4, s0
	v_addc_co_u32_e32 v3, vcc, 0, v3, vcc
	s_addc_u32 s1, s5, s1
	global_store_dword v[6:7], v38, off offset:-4096
	global_store_dword v[4:5], v39, off offset:1024
	global_store_dword v[4:5], v36, off offset:2048
	global_store_dword v[4:5], v37, off offset:3072
	global_store_dword v[6:7], v34, off
	global_store_dword v[6:7], v35, off offset:1024
	global_store_dword v[6:7], v32, off offset:2048
	global_store_dword v[6:7], v33, off offset:3072
	global_store_dword v[2:3], v30, off
	global_store_dword v[2:3], v31, off offset:1024
	global_store_dword v[2:3], v28, off offset:2048
	global_store_dword v[2:3], v29, off offset:3072
	global_store_dword v0, v91, s[0:1]
	s_endpgm

	.amdhsa_kernel _Z7k_frontPKDF16_S0_PKfS2_S0_S2_S2_S2_PjPfS4_S4_S4_
		.amdhsa_group_segment_fixed_size 77312
		.amdhsa_private_segment_fixed_size 0
		.amdhsa_kernarg_size 104
		.amdhsa_user_sgpr_count 2
		.amdhsa_user_sgpr_dispatch_ptr 0
		.amdhsa_user_sgpr_queue_ptr 0
		.amdhsa_user_sgpr_kernarg_segment_ptr 1
		.amdhsa_user_sgpr_dispatch_id 0
		.amdhsa_user_sgpr_kernarg_preload_length 0
		.amdhsa_user_sgpr_kernarg_preload_offset 0
		.amdhsa_user_sgpr_private_segment_size 0
		.amdhsa_uses_dynamic_stack 0
		.amdhsa_enable_private_segment 0
		.amdhsa_system_sgpr_workgroup_id_x 1
		.amdhsa_system_sgpr_workgroup_id_y 1
		.amdhsa_system_sgpr_workgroup_id_z 0
		.amdhsa_system_sgpr_workgroup_info 0
		.amdhsa_system_vgpr_workitem_id 0
		.amdhsa_next_free_vgpr 204
		.amdhsa_next_free_sgpr 96
		.amdhsa_accum_offset 168
		.amdhsa_reserve_vcc 1
		.amdhsa_float_round_mode_32 0
		.amdhsa_float_round_mode_16_64 0
		.amdhsa_float_denorm_mode_32 3
		.amdhsa_float_denorm_mode_16_64 3
		.amdhsa_dx10_clamp 1
		.amdhsa_ieee_mode 1
		.amdhsa_fp16_overflow 0
		.amdhsa_tg_split 0
		.amdhsa_exception_fp_ieee_invalid_op 0
		.amdhsa_exception_fp_denorm_src 0
		.amdhsa_exception_fp_ieee_div_zero 0
		.amdhsa_exception_fp_ieee_overflow 0
		.amdhsa_exception_fp_ieee_underflow 0
		.amdhsa_exception_fp_ieee_inexact 0
		.amdhsa_exception_int_div_zero 0
	.end_amdhsa_kernel

_Z7k_scan3PKjPKfS2_S2_S2_S2_PKDF16_S4_S4_7EpiArgs:
	s_mov_b32 s24, s3
	s_ashr_i32 s25, s3, 31
	s_lshl_b32 s20, s2, 6
	s_load_dwordx8 s[4:11], s[0:1], 0x0
	s_load_dwordx8 s[12:19], s[0:1], 0x20
	s_lshl_b64 s[22:23], s[24:25], 12
	s_ashr_i32 s21, s20, 31
	s_add_u32 s22, s22, s20
	s_addc_u32 s23, s23, s21
	s_lshl_b64 s[26:27], s[22:23], 6
	s_waitcnt lgkmcnt(0)
	s_add_u32 s6, s6, s26
	s_addc_u32 s7, s7, s27
	s_add_u32 s8, s8, s26
	s_addc_u32 s9, s9, s27
	s_lshl_b32 s3, s3, 22
	s_and_b32 s26, s3, 0x400000
	v_lshlrev_b32_e32 v1, 4, v0
	s_add_u32 s3, s16, s26
	global_load_dwordx4 v[108:111], v1, s[6:7]
	global_load_dwordx4 v[114:117], v1, s[8:9]
	s_addc_u32 s8, s17, 0
	s_lshl_b64 s[6:7], s[20:21], 10
	s_add_u32 s3, s3, s6
	s_addc_u32 s16, s8, s7
	s_lshl_b32 s6, s24, 6
	s_and_b32 s8, s6, 0xffffff80
	s_ashr_i32 s9, s8, 31
	s_lshl_b64 s[6:7], s[8:9], 1
	v_mov_b32_e32 v85, 0
	s_add_u32 s6, s3, s6
	s_addc_u32 s7, s16, s7
	v_and_b32_e32 v82, 0xf0, v1
	v_mov_b32_e32 v83, v85
	v_lshlrev_b32_e32 v8, 5, v0
	v_lshl_add_u64 v[2:3], s[6:7], 0, v[82:83]
	v_lshlrev_b32_e32 v83, 6, v0
	s_movk_i32 s3, 0x3e00
	v_mov_b32_e32 v6, 0x2000
	v_and_b32_e32 v4, 0x3c00, v83
	v_mov_b32_e32 v5, v85
	v_bitop3_b32 v6, v8, s3, v6 bitop3:0xc8
	v_lshl_add_u64 v[4:5], v[2:3], 0, v[4:5]
	v_lshlrev_b32_e32 v6, 1, v6
	v_mov_b32_e32 v7, v85
	v_lshl_add_u64 v[6:7], v[2:3], 0, v[6:7]
	global_load_dwordx4 v[118:121], v[4:5], off
	global_load_dwordx4 v[122:125], v[6:7], off
	s_movk_i32 s3, 0x5e00
	v_mov_b32_e32 v4, 0x4000
	v_bitop3_b32 v4, v8, s3, v4 bitop3:0xc8
	s_movk_i32 s3, 0x7e00
	v_mov_b32_e32 v6, 0x6000
	v_lshlrev_b32_e32 v4, 1, v4
	v_mov_b32_e32 v5, v85
	v_bitop3_b32 v6, v8, s3, v6 bitop3:0xc8
	v_lshl_add_u64 v[4:5], v[2:3], 0, v[4:5]
	v_lshlrev_b32_e32 v6, 1, v6
	v_mov_b32_e32 v7, v85
	v_lshl_add_u64 v[2:3], v[2:3], 0, v[6:7]
	global_load_dwordx4 v[126:129], v[4:5], off
	global_load_dwordx4 v[130:133], v[2:3], off
	v_lshlrev_b32_e32 v9, 3, v0
	v_lshrrev_b32_e32 v107, 6, v0
	v_lshlrev_b32_e32 v2, 13, v107
	v_and_b32_e32 v3, 0x1f8, v9
	v_or_b32_e32 v2, v2, v3
	v_lshlrev_b32_e32 v86, 1, v2
	v_or_b32_e32 v2, 0x10000, v86
	global_load_dwordx4 v[78:81], v2, s[18:19]
	global_load_dwordx4 v[74:77], v2, s[18:19] offset:1024
	global_load_dwordx4 v[70:73], v2, s[18:19] offset:2048
	global_load_dwordx4 v[66:69], v2, s[18:19] offset:3072
	v_or_b32_e32 v2, 0x11000, v86
	global_load_dwordx4 v[62:65], v2, s[18:19]
	global_load_dwordx4 v[58:61], v2, s[18:19] offset:1024
	global_load_dwordx4 v[54:57], v2, s[18:19] offset:2048
	global_load_dwordx4 v[50:53], v2, s[18:19] offset:3072
	v_or_b32_e32 v2, 0x12000, v86
	global_load_dwordx4 v[46:49], v2, s[18:19]
	global_load_dwordx4 v[42:45], v2, s[18:19] offset:1024
	global_load_dwordx4 v[38:41], v2, s[18:19] offset:2048
	global_load_dwordx4 v[34:37], v2, s[18:19] offset:3072
	v_or_b32_e32 v87, 0x13000, v86
	global_load_dwordx4 v[30:33], v87, s[18:19]
	global_load_dwordx4 v[26:29], v87, s[18:19] offset:1024
	global_load_dwordx4 v[22:25], v87, s[18:19] offset:2048
	global_load_dwordx4 v[18:21], v87, s[18:19] offset:3072
	global_load_dwordx4 v[2:5], v83, s[10:11] offset:48
	global_load_dwordx4 v[6:9], v83, s[10:11] offset:32
	global_load_dwordx4 v[10:13], v83, s[10:11] offset:16
	global_load_dwordx4 v[14:17], v83, s[10:11]
	s_ashr_i32 s3, s2, 31
	s_lshl_b64 s[6:7], s[24:25], 10
	s_lshl_b64 s[10:11], s[2:3], 4
	s_add_u32 s6, s6, s10
	s_addc_u32 s7, s7, s11
	s_lshl_b64 s[6:7], s[6:7], 10
	s_add_u32 s6, s14, s6
	v_lshlrev_b32_e32 v84, 2, v0
	s_addc_u32 s7, s15, s7
	v_lshl_add_u64 v[94:95], s[6:7], 0, v[84:85]
	s_movk_i32 s3, 0x1000
	v_add_co_u32_e32 v102, vcc, s3, v94
	s_movk_i32 s16, 0x2000
	s_nop 0
	v_addc_co_u32_e32 v103, vcc, 0, v95, vcc
	v_add_co_u32_e32 v96, vcc, s16, v94
	s_movk_i32 s3, 0x3000
	s_nop 0
	v_addc_co_u32_e32 v97, vcc, 0, v95, vcc
	s_lshl_b64 s[10:11], s[22:23], 10
	v_add_co_u32_e32 v104, vcc, s3, v94
	s_add_u32 s14, s4, s10
	global_load_dword v88, v[96:97], off offset:-4096
	global_load_dword v90, v[96:97], off
	global_load_dword v91, v[96:97], off offset:1024
	global_load_dword v92, v[96:97], off offset:2048
	global_load_dword v93, v[96:97], off offset:3072
	v_addc_co_u32_e32 v105, vcc, 0, v95, vcc
	global_load_dword v94, v84, s[6:7]
	global_load_dword v89, v[102:103], off offset:1024
	global_load_dword v96, v[102:103], off offset:2048
	global_load_dword v97, v[102:103], off offset:3072
	global_load_dword v98, v[104:105], off
	global_load_dword v99, v[104:105], off offset:1024
	global_load_dword v100, v[104:105], off offset:2048
	global_load_dword v101, v[104:105], off offset:3072
	s_addc_u32 s15, s5, s11
	global_load_dword v95, v84, s[6:7] offset:1024
	global_load_dword v102, v84, s[6:7] offset:2048
	global_load_dword v103, v84, s[6:7] offset:3072
	global_load_dword v87, v84, s[12:13]
	global_load_dword v113, v84, s[14:15]
	global_load_dword v112, v84, s[14:15] offset:1024
	v_or_b32_e32 v104, 0x8800, v82
	v_lshrrev_b32_e32 v82, 4, v0
	s_movk_i32 s3, 0x110
	s_waitcnt vmcnt(44)
	ds_write_b128 v1, v[108:111] offset:52224
	s_waitcnt vmcnt(43)
	ds_write_b128 v1, v[114:117] offset:56320
	v_mad_u32_u24 v1, v82, s3, v104
	v_and_b32_e32 v109, 15, v0
	s_mov_b32 s11, 0
	v_mul_u32_u24_e32 v111, 0x110, v82
	s_mov_b32 s12, 0
	s_waitcnt vmcnt(42)
	ds_write_b128 v1, v[118:121]
	v_or_b32_e32 v1, 0x100, v0
	v_lshrrev_b32_e32 v106, 4, v1
	v_mad_u32_u24 v1, v106, s3, v104
	s_waitcnt vmcnt(41)
	ds_write_b128 v1, v[122:125]
	v_or_b32_e32 v1, 0x200, v0
	v_lshrrev_b32_e32 v83, 4, v1
	v_mad_u32_u24 v1, v83, s3, v104
	v_mul_u32_u24_e32 v110, 0x110, v106
	v_mul_u32_u24_e32 v108, 0x110, v83
	s_waitcnt vmcnt(40)
	ds_write_b128 v1, v[126:129]
	v_or_b32_e32 v1, 0x300, v0
	v_lshrrev_b32_e32 v1, 4, v1
	v_mad_u32_u24 v104, v1, s3, v104
	s_waitcnt vmcnt(39)
	ds_write_b128 v104, v[130:133]
	v_lshrrev_b32_e32 v104, 1, v0
	v_and_b32_e32 v178, 24, v104
	v_lshlrev_b32_e32 v104, 1, v178
	v_mad_u32_u24 v179, v109, s3, v104
	s_waitcnt lgkmcnt(0)
	s_barrier
	ds_read_b128 v[114:117], v179 offset:34816
	ds_read_b128 v[118:121], v179 offset:34880
	s_waitcnt vmcnt(38) lgkmcnt(1)
	v_mfma_f32_16x16x32_f16 v[122:125], v[78:81], v[114:117], 0
	ds_read_b128 v[126:129], v179 offset:34944
	ds_read_b128 v[130:133], v179 offset:35008
	s_movk_i32 s3, 0x210
	v_lshl_add_u64 v[104:105], s[14:15], 0, v[84:85]
	v_mul_u32_u24_e32 v232, 12, v0
	v_mov_b32_e32 v233, 0
	v_lshl_add_u64 v[104:105], v[104:105], 0, v[232:233]
	s_waitcnt vmcnt(34)
	v_mfma_f32_16x16x32_f16 v[134:137], v[62:65], v[114:117], 0
	v_mul_u32_u24_e32 v85, 0x110, v1
	s_waitcnt vmcnt(30)
	v_mfma_f32_16x16x32_f16 v[138:141], v[46:49], v[114:117], 0
	s_waitcnt vmcnt(26)
	v_mfma_f32_16x16x32_f16 v[114:117], v[30:33], v[114:117], 0
	s_waitcnt lgkmcnt(2)
	v_mfma_f32_16x16x32_f16 v[122:125], v[74:77], v[118:121], v[122:125]
	v_mfma_f32_16x16x32_f16 v[134:137], v[58:61], v[118:121], v[134:137]
	v_mfma_f32_16x16x32_f16 v[138:141], v[42:45], v[118:121], v[138:141]
	s_waitcnt vmcnt(25)
	v_mfma_f32_16x16x32_f16 v[114:117], v[26:29], v[118:121], v[114:117]
	s_waitcnt lgkmcnt(1)
	v_mfma_f32_16x16x32_f16 v[122:125], v[70:73], v[126:129], v[122:125]
	v_mfma_f32_16x16x32_f16 v[134:137], v[54:57], v[126:129], v[134:137]
	v_mfma_f32_16x16x32_f16 v[138:141], v[38:41], v[126:129], v[138:141]
	s_waitcnt vmcnt(24)
	v_mfma_f32_16x16x32_f16 v[114:117], v[22:25], v[126:129], v[114:117]
	s_waitcnt lgkmcnt(0)
	v_mfma_f32_16x16x32_f16 v[122:125], v[66:69], v[130:133], v[122:125]
	v_mfma_f32_16x16x32_f16 v[134:137], v[50:53], v[130:133], v[134:137]
	v_mfma_f32_16x16x32_f16 v[138:141], v[34:37], v[130:133], v[138:141]
	s_nop 5
	v_cvt_pk_f16_f32 v121, v124, v125
	v_cvt_pk_f16_f32 v120, v122, v123
	s_waitcnt vmcnt(23)
	v_lshlrev_b32_e32 v228, 4, v0
	v_add_u32_e32 v229, 0x1000, v228
	v_add_u32_e32 v230, 0x2000, v228
	v_add_u32_e32 v231, 0x3000, v228
	global_load_dwordx4 v[180:183], v228, s[14:15]
	global_load_dwordx4 v[184:187], v229, s[14:15]
	global_load_dwordx4 v[188:191], v230, s[14:15]
	global_load_dwordx4 v[192:195], v231, s[14:15]
	v_mfma_f32_16x16x32_f16 v[116:119], v[18:21], v[130:133], v[114:117]
	ds_read_b128 v[126:129], v179 offset:39168
	ds_read_b128 v[130:133], v179 offset:39232
	ds_read_b128 v[146:149], v179 offset:39296
	ds_read_b128 v[150:153], v179 offset:39360
	v_and_b32_e32 v115, 0xc0, v0
	s_waitcnt lgkmcnt(3)
	v_mfma_f32_16x16x32_f16 v[142:145], v[78:81], v[126:129], 0
	v_lshl_or_b32 v115, v115, 1, v178
	v_mad_u32_u24 v115, v109, s3, v115
	v_lshrrev_b32_e32 v114, 2, v0
	v_mfma_f32_16x16x32_f16 v[154:157], v[62:65], v[126:129], 0
	s_mov_b32 s3, 0xcc00
	v_mfma_f32_16x16x32_f16 v[158:161], v[46:49], v[126:129], 0
	v_mfma_f32_16x16x32_f16 v[126:129], v[30:33], v[126:129], 0
	s_waitcnt lgkmcnt(2)
	v_mfma_f32_16x16x32_f16 v[142:145], v[74:77], v[130:133], v[142:145]
	v_mfma_f32_16x16x32_f16 v[154:157], v[58:61], v[130:133], v[154:157]
	v_mfma_f32_16x16x32_f16 v[158:161], v[42:45], v[130:133], v[158:161]
	v_mfma_f32_16x16x32_f16 v[126:129], v[26:29], v[130:133], v[126:129]
	s_waitcnt lgkmcnt(1)
	v_mfma_f32_16x16x32_f16 v[142:145], v[70:73], v[146:149], v[142:145]
	v_mfma_f32_16x16x32_f16 v[154:157], v[54:57], v[146:149], v[154:157]
	v_mfma_f32_16x16x32_f16 v[158:161], v[38:41], v[146:149], v[158:161]
	v_mfma_f32_16x16x32_f16 v[126:129], v[22:25], v[146:149], v[126:129]
	ds_read_b128 v[130:133], v179 offset:43520
	ds_read_b128 v[146:149], v179 offset:43584
	ds_read_b128 v[162:165], v179 offset:43648
	ds_read_b128 v[166:169], v179 offset:43712
	s_load_dwordx4 s[4:7], s[0:1], 0x40
	s_nop 0
	s_load_dwordx2 s[0:1], s[0:1], 0x88
	s_waitcnt lgkmcnt(0)
	v_mfma_f32_16x16x32_f16 v[142:145], v[66:69], v[150:153], v[142:145]
	v_mfma_f32_16x16x32_f16 v[154:157], v[50:53], v[150:153], v[154:157]
	v_mfma_f32_16x16x32_f16 v[158:161], v[34:37], v[150:153], v[158:161]
	v_mfma_f32_16x16x32_f16 v[126:129], v[18:21], v[150:153], v[126:129]
	v_mfma_f32_16x16x32_f16 v[150:153], v[78:81], v[130:133], 0
	v_mfma_f32_16x16x32_f16 v[170:173], v[62:65], v[130:133], 0
	v_mfma_f32_16x16x32_f16 v[174:177], v[46:49], v[130:133], 0
	v_mfma_f32_16x16x32_f16 v[130:133], v[30:33], v[130:133], 0
	v_mfma_f32_16x16x32_f16 v[150:153], v[74:77], v[146:149], v[150:153]
	v_mfma_f32_16x16x32_f16 v[170:173], v[58:61], v[146:149], v[170:173]
	v_mfma_f32_16x16x32_f16 v[174:177], v[42:45], v[146:149], v[174:177]
	v_mfma_f32_16x16x32_f16 v[130:133], v[26:29], v[146:149], v[130:133]
	ds_read_b128 v[146:149], v179 offset:47872
	v_mfma_f32_16x16x32_f16 v[150:153], v[70:73], v[162:165], v[150:153]
	v_mfma_f32_16x16x32_f16 v[170:173], v[54:57], v[162:165], v[170:173]
	v_mfma_f32_16x16x32_f16 v[174:177], v[38:41], v[162:165], v[174:177]
	v_mfma_f32_16x16x32_f16 v[130:133], v[22:25], v[162:165], v[130:133]
	ds_read_b128 v[162:165], v179 offset:47936
	s_waitcnt lgkmcnt(1)
	v_mfma_f32_16x16x32_f16 v[78:81], v[78:81], v[146:149], 0
	v_mfma_f32_16x16x32_f16 v[62:65], v[62:65], v[146:149], 0
	v_mfma_f32_16x16x32_f16 v[46:49], v[46:49], v[146:149], 0
	v_mfma_f32_16x16x32_f16 v[30:33], v[30:33], v[146:149], 0
	v_mfma_f32_16x16x32_f16 v[150:153], v[66:69], v[166:169], v[150:153]
	v_mfma_f32_16x16x32_f16 v[170:173], v[50:53], v[166:169], v[170:173]
	v_mfma_f32_16x16x32_f16 v[174:177], v[34:37], v[166:169], v[174:177]
	v_mfma_f32_16x16x32_f16 v[130:133], v[18:21], v[166:169], v[130:133]
	ds_read_b128 v[166:169], v179 offset:48000
	s_waitcnt lgkmcnt(1)
	v_mfma_f32_16x16x32_f16 v[74:77], v[74:77], v[162:165], v[78:81]
	v_mfma_f32_16x16x32_f16 v[58:61], v[58:61], v[162:165], v[62:65]
	s_nop 1
	ds_read_b128 v[78:81], v179 offset:48064
	v_mfma_f32_16x16x32_f16 v[42:45], v[42:45], v[162:165], v[46:49]
	v_cvt_pk_f16_f32 v63, v144, v145
	v_cvt_pk_f16_f32 v62, v142, v143
	v_cvt_pk_f16_f32 v65, v156, v157
	v_mfma_f32_16x16x32_f16 v[26:29], v[26:29], v[162:165], v[30:33]
	v_cvt_pk_f16_f32 v64, v154, v155
	v_cvt_pk_f16_f32 v47, v172, v173
	v_cvt_pk_f16_f32 v46, v170, v171
	s_waitcnt lgkmcnt(1)
	v_mfma_f32_16x16x32_f16 v[70:73], v[70:73], v[166:169], v[74:77]
	v_add_u32_e32 v32, 0x6000, v115
	v_mfma_f32_16x16x32_f16 v[54:57], v[54:57], v[166:169], v[58:61]
	s_nop 0
	v_cvt_pk_f16_f32 v75, v136, v137
	v_cvt_pk_f16_f32 v74, v134, v135
	ds_write2_b64 v115, v[120:121], v[74:75] offset1:4
	v_mfma_f32_16x16x32_f16 v[38:41], v[38:41], v[166:169], v[42:45]
	v_add_u32_e32 v58, 0x2000, v115
	ds_write2_b64 v58, v[62:63], v[64:65] offset0:32 offset1:36
	v_mfma_f32_16x16x32_f16 v[22:25], v[22:25], v[166:169], v[26:29]
	v_add_u32_e32 v44, 0x4000, v115
	v_cvt_pk_f16_f32 v43, v176, v177
	v_cvt_pk_f16_f32 v42, v174, v175
	s_waitcnt lgkmcnt(2)
	v_mfma_f32_16x16x32_f16 v[66:69], v[66:69], v[78:81], v[70:73]
	v_mfma_f32_16x16x32_f16 v[50:53], v[50:53], v[78:81], v[54:57]
	s_nop 1
	v_cvt_pk_f16_f32 v71, v140, v141
	v_cvt_pk_f16_f32 v70, v138, v139
	v_cvt_pk_f16_f32 v73, v118, v119
	v_mfma_f32_16x16x32_f16 v[34:37], v[34:37], v[78:81], v[38:41]
	v_cvt_pk_f16_f32 v55, v160, v161
	v_cvt_pk_f16_f32 v54, v158, v159
	v_cvt_pk_f16_f32 v57, v128, v129
	v_mfma_f32_16x16x32_f16 v[18:21], v[18:21], v[78:81], v[22:25]
	v_cvt_pk_f16_f32 v56, v126, v127
	v_cvt_pk_f16_f32 v39, v132, v133
	v_cvt_pk_f16_f32 v38, v130, v131
	v_cvt_pk_f16_f32 v72, v116, v117
	ds_write2_b64 v58, v[54:55], v[56:57] offset0:40 offset1:44
	v_cvt_pk_f16_f32 v55, v152, v153
	v_cvt_pk_f16_f32 v54, v150, v151
	ds_write2_b64 v44, v[42:43], v[38:39] offset0:72 offset1:76
	v_cvt_pk_f16_f32 v39, v68, v69
	v_cvt_pk_f16_f32 v38, v66, v67
	v_cvt_pk_f16_f32 v31, v52, v53
	v_cvt_pk_f16_f32 v30, v50, v51
	v_cvt_pk_f16_f32 v27, v36, v37
	v_cvt_pk_f16_f32 v26, v34, v35
	v_cvt_pk_f16_f32 v21, v20, v21
	v_cvt_pk_f16_f32 v20, v18, v19
	v_lshlrev_b32_e32 v19, 1, v0
	ds_write2_b64 v115, v[70:71], v[72:73] offset0:8 offset1:12
	ds_write2_b64 v44, v[54:55], v[46:47] offset0:64 offset1:68
	ds_write2_b64 v32, v[38:39], v[30:31] offset0:96 offset1:100
	ds_write2_b64 v32, v[26:27], v[20:21] offset0:104 offset1:108
	s_waitcnt lgkmcnt(0)
	s_barrier
	v_mov_b32_e32 v57, 0xcc00
	ds_read_b128 v[116:119], v57 offset:0
	ds_read_b128 v[120:123], v57 offset:16
	ds_read_b128 v[124:127], v57 offset:32
	ds_read_b128 v[128:131], v57 offset:48
	ds_read_b128 v[132:135], v57 offset:4096
	ds_read_b128 v[136:139], v57 offset:4112
	ds_read_b128 v[140:143], v57 offset:4128
	ds_read_b128 v[144:147], v57 offset:4144
	ds_read_u16 v52, v19
	s_mov_b32 s10, 0x5000
	s_mov_b32 s11, 0
	v_lshl_add_u64 v[58:59], v[104:105], 0, s[10:11]
	s_mov_b32 s10, 0x2000
	v_lshl_add_u64 v[50:51], v[58:59], 0, s[10:11]
	s_mov_b32 s10, 0x4000
	s_waitcnt vmcnt(3)
	v_cvt_f32_f16_e32 v46, v180
	v_fma_mix_f32 v44, v180, v180, 0 op_sel:[0,1,0] op_sel_hi:[1,1,0]
	v_pk_mul_f32 v[20:21], v[46:47], v[14:15] op_sel_hi:[0,1]
	v_pk_mul_f32 v[22:23], v[46:47], v[16:17] op_sel_hi:[0,1]
	v_pk_mul_f32 v[24:25], v[46:47], v[10:11] op_sel_hi:[0,1]
	v_pk_mul_f32 v[26:27], v[46:47], v[12:13] op_sel_hi:[0,1]
	v_pk_mul_f32 v[28:29], v[46:47], v[6:7] op_sel_hi:[0,1]
	v_pk_mul_f32 v[30:31], v[46:47], v[8:9] op_sel_hi:[0,1]
	v_pk_mul_f32 v[32:33], v[46:47], v[2:3] op_sel_hi:[0,1]
	v_pk_mul_f32 v[34:35], v[46:47], v[4:5] op_sel_hi:[0,1]
	v_exp_f32_e32 v20, v20
	v_exp_f32_e32 v21, v21
	v_exp_f32_e32 v22, v22
	v_exp_f32_e32 v23, v23
	v_exp_f32_e32 v24, v24
	v_exp_f32_e32 v25, v25
	v_exp_f32_e32 v26, v26
	v_exp_f32_e32 v27, v27
	v_exp_f32_e32 v28, v28
	v_exp_f32_e32 v29, v29
	v_exp_f32_e32 v30, v30
	v_exp_f32_e32 v31, v31
	v_exp_f32_e32 v32, v32
	v_exp_f32_e32 v33, v33
	v_exp_f32_e32 v34, v34
	v_exp_f32_e32 v35, v35
	s_mov_b32 s12, 0
.Lsc3_loop:
	s_waitcnt lgkmcnt(0)
	ds_read_b128 v[196:199], v57 offset:64
	ds_read_b128 v[200:203], v57 offset:80
	ds_read_b128 v[204:207], v57 offset:96
	ds_read_b128 v[208:211], v57 offset:112
	ds_read_b128 v[212:215], v57 offset:4160
	ds_read_b128 v[216:219], v57 offset:4176
	ds_read_b128 v[220:223], v57 offset:4192
	ds_read_b128 v[224:227], v57 offset:4208
	v_cvt_f32_f16_e32 v46, v181
	v_cvt_f32_f16_e32 v53, v52
	ds_read_u16 v52, v19 offset:528
	v_pk_mul_f32 v[94:95], v[94:95], v[20:21]
	v_pk_mul_f32 v[20:21], v[46:47], v[14:15] op_sel_hi:[0,1]
	v_mul_f32_e32 v55, 0xbfb8aa3b, v53
	v_pk_mul_f32 v[102:103], v[102:103], v[22:23]
	v_exp_f32_e32 v20, v20
	v_pk_mul_f32 v[22:23], v[46:47], v[16:17] op_sel_hi:[0,1]
	v_pk_fma_f32 v[94:95], v[44:45], v[116:117], v[94:95] op_sel_hi:[0,1,1]
	v_exp_f32_e32 v21, v21
	v_pk_mul_f32 v[48:49], v[94:95], v[132:133]
	v_pk_mul_f32 v[88:89], v[88:89], v[24:25]
	v_exp_f32_e32 v22, v22
	v_pk_mul_f32 v[24:25], v[46:47], v[10:11] op_sel_hi:[0,1]
	v_pk_fma_f32 v[102:103], v[44:45], v[118:119], v[102:103] op_sel_hi:[0,1,1]
	v_exp_f32_e32 v23, v23
	v_pk_fma_f32 v[48:49], v[102:103], v[134:135], v[48:49]
	v_exp_f32_e32 v55, v55
	v_pk_mul_f32 v[96:97], v[96:97], v[26:27]
	v_exp_f32_e32 v24, v24
	v_pk_mul_f32 v[26:27], v[46:47], v[12:13] op_sel_hi:[0,1]
	v_pk_fma_f32 v[88:89], v[44:45], v[120:121], v[88:89] op_sel_hi:[0,1,1]
	v_exp_f32_e32 v25, v25
	v_pk_fma_f32 v[48:49], v[88:89], v[136:137], v[48:49]
	v_pk_mul_f32 v[90:91], v[90:91], v[28:29]
	v_exp_f32_e32 v26, v26
	v_pk_mul_f32 v[28:29], v[46:47], v[6:7] op_sel_hi:[0,1]
	v_pk_fma_f32 v[96:97], v[44:45], v[122:123], v[96:97] op_sel_hi:[0,1,1]
	v_exp_f32_e32 v27, v27
	v_pk_fma_f32 v[48:49], v[96:97], v[138:139], v[48:49]
	v_add_f32_e32 v55, 1.0, v55
	v_pk_mul_f32 v[92:93], v[92:93], v[30:31]
	v_exp_f32_e32 v28, v28
	v_pk_mul_f32 v[30:31], v[46:47], v[8:9] op_sel_hi:[0,1]
	v_pk_fma_f32 v[90:91], v[44:45], v[124:125], v[90:91] op_sel_hi:[0,1,1]
	v_exp_f32_e32 v29, v29
	v_pk_fma_f32 v[48:49], v[90:91], v[140:141], v[48:49]
	v_pk_mul_f32 v[98:99], v[98:99], v[32:33]
	v_exp_f32_e32 v30, v30
	v_pk_mul_f32 v[32:33], v[46:47], v[2:3] op_sel_hi:[0,1]
	v_pk_fma_f32 v[92:93], v[44:45], v[126:127], v[92:93] op_sel_hi:[0,1,1]
	v_exp_f32_e32 v31, v31
	v_pk_fma_f32 v[48:49], v[92:93], v[142:143], v[48:49]
	v_rcp_f32_e32 v55, v55
	v_pk_mul_f32 v[100:101], v[100:101], v[34:35]
	v_exp_f32_e32 v32, v32
	v_pk_mul_f32 v[34:35], v[46:47], v[4:5] op_sel_hi:[0,1]
	v_pk_fma_f32 v[98:99], v[44:45], v[128:129], v[98:99] op_sel_hi:[0,1,1]
	v_exp_f32_e32 v33, v33
	v_pk_fma_f32 v[48:49], v[98:99], v[144:145], v[48:49]
	v_exp_f32_e32 v34, v34
	v_pk_fma_f32 v[100:101], v[44:45], v[130:131], v[100:101] op_sel_hi:[0,1,1]
	v_exp_f32_e32 v35, v35
	v_pk_fma_f32 v[48:49], v[100:101], v[146:147], v[48:49]
	v_add_f32_e32 v54, v48, v49
	v_fma_mix_f32 v54, v87, v180, v54 op_sel:[0,1,0] op_sel_hi:[0,1,0]
	v_mul_f32_e32 v54, v54, v53
	v_fma_mix_f32 v44, v181, v181, 0 op_sel:[0,1,0] op_sel_hi:[1,1,0]
	v_fma_mixlo_f16 v56, v54, v55, 0
	ds_write_b16 v19, v56
	v_add_u32_e32 v19, 0x210, v19
	s_waitcnt lgkmcnt(1)
	ds_read_b128 v[116:119], v57 offset:128
	ds_read_b128 v[120:123], v57 offset:144
	ds_read_b128 v[124:127], v57 offset:160
	ds_read_b128 v[128:131], v57 offset:176
	ds_read_b128 v[132:135], v57 offset:4224
	ds_read_b128 v[136:139], v57 offset:4240
	ds_read_b128 v[140:143], v57 offset:4256
	ds_read_b128 v[144:147], v57 offset:4272
	v_cvt_f32_f16_e32 v46, v182
	v_cvt_f32_f16_e32 v53, v52
	ds_read_u16 v52, v19 offset:528
	v_pk_mul_f32 v[94:95], v[94:95], v[20:21]
	v_pk_mul_f32 v[20:21], v[46:47], v[14:15] op_sel_hi:[0,1]
	v_mul_f32_e32 v55, 0xbfb8aa3b, v53
	v_pk_mul_f32 v[102:103], v[102:103], v[22:23]
	v_exp_f32_e32 v20, v20
	v_pk_mul_f32 v[22:23], v[46:47], v[16:17] op_sel_hi:[0,1]
	v_pk_fma_f32 v[94:95], v[44:45], v[196:197], v[94:95] op_sel_hi:[0,1,1]
	v_exp_f32_e32 v21, v21
	v_pk_mul_f32 v[48:49], v[94:95], v[212:213]
	v_pk_mul_f32 v[88:89], v[88:89], v[24:25]
	v_exp_f32_e32 v22, v22
	v_pk_mul_f32 v[24:25], v[46:47], v[10:11] op_sel_hi:[0,1]
	v_pk_fma_f32 v[102:103], v[44:45], v[198:199], v[102:103] op_sel_hi:[0,1,1]
	v_exp_f32_e32 v23, v23
	v_pk_fma_f32 v[48:49], v[102:103], v[214:215], v[48:49]
	v_exp_f32_e32 v55, v55
	v_pk_mul_f32 v[96:97], v[96:97], v[26:27]
	v_exp_f32_e32 v24, v24
	v_pk_mul_f32 v[26:27], v[46:47], v[12:13] op_sel_hi:[0,1]
	v_pk_fma_f32 v[88:89], v[44:45], v[200:201], v[88:89] op_sel_hi:[0,1,1]
	v_exp_f32_e32 v25, v25
	v_pk_fma_f32 v[48:49], v[88:89], v[216:217], v[48:49]
	v_pk_mul_f32 v[90:91], v[90:91], v[28:29]
	v_exp_f32_e32 v26, v26
	v_pk_mul_f32 v[28:29], v[46:47], v[6:7] op_sel_hi:[0,1]
	v_pk_fma_f32 v[96:97], v[44:45], v[202:203], v[96:97] op_sel_hi:[0,1,1]
	v_exp_f32_e32 v27, v27
	v_pk_fma_f32 v[48:49], v[96:97], v[218:219], v[48:49]
	v_add_f32_e32 v55, 1.0, v55
	v_pk_mul_f32 v[92:93], v[92:93], v[30:31]
	v_exp_f32_e32 v28, v28
	v_pk_mul_f32 v[30:31], v[46:47], v[8:9] op_sel_hi:[0,1]
	v_pk_fma_f32 v[90:91], v[44:45], v[204:205], v[90:91] op_sel_hi:[0,1,1]
	v_exp_f32_e32 v29, v29
	v_pk_fma_f32 v[48:49], v[90:91], v[220:221], v[48:49]
	v_pk_mul_f32 v[98:99], v[98:99], v[32:33]
	v_exp_f32_e32 v30, v30
	v_pk_mul_f32 v[32:33], v[46:47], v[2:3] op_sel_hi:[0,1]
	v_pk_fma_f32 v[92:93], v[44:45], v[206:207], v[92:93] op_sel_hi:[0,1,1]
	v_exp_f32_e32 v31, v31
	v_pk_fma_f32 v[48:49], v[92:93], v[222:223], v[48:49]
	v_rcp_f32_e32 v55, v55
	v_pk_mul_f32 v[100:101], v[100:101], v[34:35]
	v_exp_f32_e32 v32, v32
	v_pk_mul_f32 v[34:35], v[46:47], v[4:5] op_sel_hi:[0,1]
	v_pk_fma_f32 v[98:99], v[44:45], v[208:209], v[98:99] op_sel_hi:[0,1,1]
	v_exp_f32_e32 v33, v33
	v_pk_fma_f32 v[48:49], v[98:99], v[224:225], v[48:49]
	v_exp_f32_e32 v34, v34
	v_pk_fma_f32 v[100:101], v[44:45], v[210:211], v[100:101] op_sel_hi:[0,1,1]
	v_exp_f32_e32 v35, v35
	v_pk_fma_f32 v[48:49], v[100:101], v[226:227], v[48:49]
	v_add_f32_e32 v54, v48, v49
	v_fma_mix_f32 v54, v87, v181, v54 op_sel:[0,1,0] op_sel_hi:[0,1,0]
	v_mul_f32_e32 v54, v54, v53
	v_fma_mix_f32 v44, v182, v182, 0 op_sel:[0,1,0] op_sel_hi:[1,1,0]
	v_fma_mixlo_f16 v56, v54, v55, 0
	ds_write_b16 v19, v56
	v_add_u32_e32 v19, 0x210, v19
	s_waitcnt lgkmcnt(1)
	ds_read_b128 v[196:199], v57 offset:192
	ds_read_b128 v[200:203], v57 offset:208
	ds_read_b128 v[204:207], v57 offset:224
	ds_read_b128 v[208:211], v57 offset:240
	ds_read_b128 v[212:215], v57 offset:4288
	ds_read_b128 v[216:219], v57 offset:4304
	ds_read_b128 v[220:223], v57 offset:4320
	ds_read_b128 v[224:227], v57 offset:4336
	v_cvt_f32_f16_e32 v46, v183
	v_cvt_f32_f16_e32 v53, v52
	ds_read_u16 v52, v19 offset:528
	v_pk_mul_f32 v[94:95], v[94:95], v[20:21]
	v_pk_mul_f32 v[20:21], v[46:47], v[14:15] op_sel_hi:[0,1]
	v_mul_f32_e32 v55, 0xbfb8aa3b, v53
	v_pk_mul_f32 v[102:103], v[102:103], v[22:23]
	v_exp_f32_e32 v20, v20
	v_pk_mul_f32 v[22:23], v[46:47], v[16:17] op_sel_hi:[0,1]
	v_pk_fma_f32 v[94:95], v[44:45], v[116:117], v[94:95] op_sel_hi:[0,1,1]
	v_exp_f32_e32 v21, v21
	v_pk_mul_f32 v[48:49], v[94:95], v[132:133]
	v_pk_mul_f32 v[88:89], v[88:89], v[24:25]
	v_exp_f32_e32 v22, v22
	v_pk_mul_f32 v[24:25], v[46:47], v[10:11] op_sel_hi:[0,1]
	v_pk_fma_f32 v[102:103], v[44:45], v[118:119], v[102:103] op_sel_hi:[0,1,1]
	v_exp_f32_e32 v23, v23
	v_pk_fma_f32 v[48:49], v[102:103], v[134:135], v[48:49]
	v_exp_f32_e32 v55, v55
	v_pk_mul_f32 v[96:97], v[96:97], v[26:27]
	v_exp_f32_e32 v24, v24
	v_pk_mul_f32 v[26:27], v[46:47], v[12:13] op_sel_hi:[0,1]
	v_pk_fma_f32 v[88:89], v[44:45], v[120:121], v[88:89] op_sel_hi:[0,1,1]
	v_exp_f32_e32 v25, v25
	v_pk_fma_f32 v[48:49], v[88:89], v[136:137], v[48:49]
	v_pk_mul_f32 v[90:91], v[90:91], v[28:29]
	v_exp_f32_e32 v26, v26
	v_pk_mul_f32 v[28:29], v[46:47], v[6:7] op_sel_hi:[0,1]
	v_pk_fma_f32 v[96:97], v[44:45], v[122:123], v[96:97] op_sel_hi:[0,1,1]
	v_exp_f32_e32 v27, v27
	v_pk_fma_f32 v[48:49], v[96:97], v[138:139], v[48:49]
	v_add_f32_e32 v55, 1.0, v55
	v_pk_mul_f32 v[92:93], v[92:93], v[30:31]
	v_exp_f32_e32 v28, v28
	v_pk_mul_f32 v[30:31], v[46:47], v[8:9] op_sel_hi:[0,1]
	v_pk_fma_f32 v[90:91], v[44:45], v[124:125], v[90:91] op_sel_hi:[0,1,1]
	v_exp_f32_e32 v29, v29
	v_pk_fma_f32 v[48:49], v[90:91], v[140:141], v[48:49]
	v_pk_mul_f32 v[98:99], v[98:99], v[32:33]
	v_exp_f32_e32 v30, v30
	v_pk_mul_f32 v[32:33], v[46:47], v[2:3] op_sel_hi:[0,1]
	v_pk_fma_f32 v[92:93], v[44:45], v[126:127], v[92:93] op_sel_hi:[0,1,1]
	v_exp_f32_e32 v31, v31
	v_pk_fma_f32 v[48:49], v[92:93], v[142:143], v[48:49]
	v_rcp_f32_e32 v55, v55
	v_pk_mul_f32 v[100:101], v[100:101], v[34:35]
	v_exp_f32_e32 v32, v32
	v_pk_mul_f32 v[34:35], v[46:47], v[4:5] op_sel_hi:[0,1]
	v_pk_fma_f32 v[98:99], v[44:45], v[128:129], v[98:99] op_sel_hi:[0,1,1]
	v_exp_f32_e32 v33, v33
	v_pk_fma_f32 v[48:49], v[98:99], v[144:145], v[48:49]
	v_exp_f32_e32 v34, v34
	v_pk_fma_f32 v[100:101], v[44:45], v[130:131], v[100:101] op_sel_hi:[0,1,1]
	v_exp_f32_e32 v35, v35
	v_pk_fma_f32 v[48:49], v[100:101], v[146:147], v[48:49]
	v_add_f32_e32 v54, v48, v49
	v_fma_mix_f32 v54, v87, v182, v54 op_sel:[0,1,0] op_sel_hi:[0,1,0]
	v_mul_f32_e32 v54, v54, v53
	v_fma_mix_f32 v44, v183, v183, 0 op_sel:[0,1,0] op_sel_hi:[1,1,0]
	v_fma_mixlo_f16 v56, v54, v55, 0
	ds_write_b16 v19, v56
	v_add_u32_e32 v19, 0x210, v19
	s_waitcnt lgkmcnt(1)
	ds_read_b128 v[116:119], v57 offset:256
	ds_read_b128 v[120:123], v57 offset:272
	ds_read_b128 v[124:127], v57 offset:288
	ds_read_b128 v[128:131], v57 offset:304
	ds_read_b128 v[132:135], v57 offset:4352
	ds_read_b128 v[136:139], v57 offset:4368
	ds_read_b128 v[140:143], v57 offset:4384
	ds_read_b128 v[144:147], v57 offset:4400
	s_waitcnt vmcnt(2)
	v_cvt_f32_f16_e32 v46, v184
	v_cvt_f32_f16_e32 v53, v52
	ds_read_u16 v52, v19 offset:528
	v_pk_mul_f32 v[94:95], v[94:95], v[20:21]
	v_pk_mul_f32 v[20:21], v[46:47], v[14:15] op_sel_hi:[0,1]
	v_mul_f32_e32 v55, 0xbfb8aa3b, v53
	v_pk_mul_f32 v[102:103], v[102:103], v[22:23]
	v_exp_f32_e32 v20, v20
	v_pk_mul_f32 v[22:23], v[46:47], v[16:17] op_sel_hi:[0,1]
	v_pk_fma_f32 v[94:95], v[44:45], v[196:197], v[94:95] op_sel_hi:[0,1,1]
	v_exp_f32_e32 v21, v21
	v_pk_mul_f32 v[48:49], v[94:95], v[212:213]
	v_pk_mul_f32 v[88:89], v[88:89], v[24:25]
	v_exp_f32_e32 v22, v22
	v_pk_mul_f32 v[24:25], v[46:47], v[10:11] op_sel_hi:[0,1]
	v_pk_fma_f32 v[102:103], v[44:45], v[198:199], v[102:103] op_sel_hi:[0,1,1]
	v_exp_f32_e32 v23, v23
	v_pk_fma_f32 v[48:49], v[102:103], v[214:215], v[48:49]
	v_exp_f32_e32 v55, v55
	v_pk_mul_f32 v[96:97], v[96:97], v[26:27]
	v_exp_f32_e32 v24, v24
	v_pk_mul_f32 v[26:27], v[46:47], v[12:13] op_sel_hi:[0,1]
	v_pk_fma_f32 v[88:89], v[44:45], v[200:201], v[88:89] op_sel_hi:[0,1,1]
	v_exp_f32_e32 v25, v25
	v_pk_fma_f32 v[48:49], v[88:89], v[216:217], v[48:49]
	v_pk_mul_f32 v[90:91], v[90:91], v[28:29]
	v_exp_f32_e32 v26, v26
	v_pk_mul_f32 v[28:29], v[46:47], v[6:7] op_sel_hi:[0,1]
	v_pk_fma_f32 v[96:97], v[44:45], v[202:203], v[96:97] op_sel_hi:[0,1,1]
	v_exp_f32_e32 v27, v27
	v_pk_fma_f32 v[48:49], v[96:97], v[218:219], v[48:49]
	v_add_f32_e32 v55, 1.0, v55
	v_pk_mul_f32 v[92:93], v[92:93], v[30:31]
	v_exp_f32_e32 v28, v28
	v_pk_mul_f32 v[30:31], v[46:47], v[8:9] op_sel_hi:[0,1]
	v_pk_fma_f32 v[90:91], v[44:45], v[204:205], v[90:91] op_sel_hi:[0,1,1]
	v_exp_f32_e32 v29, v29
	v_pk_fma_f32 v[48:49], v[90:91], v[220:221], v[48:49]
	v_pk_mul_f32 v[98:99], v[98:99], v[32:33]
	v_exp_f32_e32 v30, v30
	v_pk_mul_f32 v[32:33], v[46:47], v[2:3] op_sel_hi:[0,1]
	v_pk_fma_f32 v[92:93], v[44:45], v[206:207], v[92:93] op_sel_hi:[0,1,1]
	v_exp_f32_e32 v31, v31
	v_pk_fma_f32 v[48:49], v[92:93], v[222:223], v[48:49]
	v_rcp_f32_e32 v55, v55
	v_pk_mul_f32 v[100:101], v[100:101], v[34:35]
	v_exp_f32_e32 v32, v32
	v_pk_mul_f32 v[34:35], v[46:47], v[4:5] op_sel_hi:[0,1]
	v_pk_fma_f32 v[98:99], v[44:45], v[208:209], v[98:99] op_sel_hi:[0,1,1]
	v_exp_f32_e32 v33, v33
	v_pk_fma_f32 v[48:49], v[98:99], v[224:225], v[48:49]
	v_exp_f32_e32 v34, v34
	v_pk_fma_f32 v[100:101], v[44:45], v[210:211], v[100:101] op_sel_hi:[0,1,1]
	v_exp_f32_e32 v35, v35
	v_pk_fma_f32 v[48:49], v[100:101], v[226:227], v[48:49]
	v_add_f32_e32 v54, v48, v49
	v_fma_mix_f32 v54, v87, v183, v54 op_sel:[0,1,0] op_sel_hi:[0,1,0]
	v_mul_f32_e32 v54, v54, v53
	v_fma_mix_f32 v44, v184, v184, 0 op_sel:[0,1,0] op_sel_hi:[1,1,0]
	global_load_dwordx4 v[180:183], v[58:59], off offset:-4096
	v_fma_mixlo_f16 v56, v54, v55, 0
	ds_write_b16 v19, v56
	v_add_u32_e32 v19, 0x210, v19
	s_waitcnt lgkmcnt(1)
	ds_read_b128 v[196:199], v57 offset:320
	ds_read_b128 v[200:203], v57 offset:336
	ds_read_b128 v[204:207], v57 offset:352
	ds_read_b128 v[208:211], v57 offset:368
	ds_read_b128 v[212:215], v57 offset:4416
	ds_read_b128 v[216:219], v57 offset:4432
	ds_read_b128 v[220:223], v57 offset:4448
	ds_read_b128 v[224:227], v57 offset:4464
	v_cvt_f32_f16_e32 v46, v185
	v_cvt_f32_f16_e32 v53, v52
	ds_read_u16 v52, v19 offset:528
	v_pk_mul_f32 v[94:95], v[94:95], v[20:21]
	v_pk_mul_f32 v[20:21], v[46:47], v[14:15] op_sel_hi:[0,1]
	v_mul_f32_e32 v55, 0xbfb8aa3b, v53
	v_pk_mul_f32 v[102:103], v[102:103], v[22:23]
	v_exp_f32_e32 v20, v20
	v_pk_mul_f32 v[22:23], v[46:47], v[16:17] op_sel_hi:[0,1]
	v_pk_fma_f32 v[94:95], v[44:45], v[116:117], v[94:95] op_sel_hi:[0,1,1]
	v_exp_f32_e32 v21, v21
	v_pk_mul_f32 v[48:49], v[94:95], v[132:133]
	v_pk_mul_f32 v[88:89], v[88:89], v[24:25]
	v_exp_f32_e32 v22, v22
	v_pk_mul_f32 v[24:25], v[46:47], v[10:11] op_sel_hi:[0,1]
	v_pk_fma_f32 v[102:103], v[44:45], v[118:119], v[102:103] op_sel_hi:[0,1,1]
	v_exp_f32_e32 v23, v23
	v_pk_fma_f32 v[48:49], v[102:103], v[134:135], v[48:49]
	v_exp_f32_e32 v55, v55
	v_pk_mul_f32 v[96:97], v[96:97], v[26:27]
	v_exp_f32_e32 v24, v24
	v_pk_mul_f32 v[26:27], v[46:47], v[12:13] op_sel_hi:[0,1]
	v_pk_fma_f32 v[88:89], v[44:45], v[120:121], v[88:89] op_sel_hi:[0,1,1]
	v_exp_f32_e32 v25, v25
	v_pk_fma_f32 v[48:49], v[88:89], v[136:137], v[48:49]
	v_pk_mul_f32 v[90:91], v[90:91], v[28:29]
	v_exp_f32_e32 v26, v26
	v_pk_mul_f32 v[28:29], v[46:47], v[6:7] op_sel_hi:[0,1]
	v_pk_fma_f32 v[96:97], v[44:45], v[122:123], v[96:97] op_sel_hi:[0,1,1]
	v_exp_f32_e32 v27, v27
	v_pk_fma_f32 v[48:49], v[96:97], v[138:139], v[48:49]
	v_add_f32_e32 v55, 1.0, v55
	v_pk_mul_f32 v[92:93], v[92:93], v[30:31]
	v_exp_f32_e32 v28, v28
	v_pk_mul_f32 v[30:31], v[46:47], v[8:9] op_sel_hi:[0,1]
	v_pk_fma_f32 v[90:91], v[44:45], v[124:125], v[90:91] op_sel_hi:[0,1,1]
	v_exp_f32_e32 v29, v29
	v_pk_fma_f32 v[48:49], v[90:91], v[140:141], v[48:49]
	v_pk_mul_f32 v[98:99], v[98:99], v[32:33]
	v_exp_f32_e32 v30, v30
	v_pk_mul_f32 v[32:33], v[46:47], v[2:3] op_sel_hi:[0,1]
	v_pk_fma_f32 v[92:93], v[44:45], v[126:127], v[92:93] op_sel_hi:[0,1,1]
	v_exp_f32_e32 v31, v31
	v_pk_fma_f32 v[48:49], v[92:93], v[142:143], v[48:49]
	v_rcp_f32_e32 v55, v55
	v_pk_mul_f32 v[100:101], v[100:101], v[34:35]
	v_exp_f32_e32 v32, v32
	v_pk_mul_f32 v[34:35], v[46:47], v[4:5] op_sel_hi:[0,1]
	v_pk_fma_f32 v[98:99], v[44:45], v[128:129], v[98:99] op_sel_hi:[0,1,1]
	v_exp_f32_e32 v33, v33
	v_pk_fma_f32 v[48:49], v[98:99], v[144:145], v[48:49]
	v_exp_f32_e32 v34, v34
	v_pk_fma_f32 v[100:101], v[44:45], v[130:131], v[100:101] op_sel_hi:[0,1,1]
	v_exp_f32_e32 v35, v35
	v_pk_fma_f32 v[48:49], v[100:101], v[146:147], v[48:49]
	v_add_f32_e32 v54, v48, v49
	v_fma_mix_f32 v54, v87, v184, v54 op_sel:[0,1,0] op_sel_hi:[0,1,0]
	v_mul_f32_e32 v54, v54, v53
	v_fma_mix_f32 v44, v185, v185, 0 op_sel:[0,1,0] op_sel_hi:[1,1,0]
	v_fma_mixlo_f16 v56, v54, v55, 0
	ds_write_b16 v19, v56
	v_add_u32_e32 v19, 0x210, v19
	s_waitcnt lgkmcnt(1)
	ds_read_b128 v[116:119], v57 offset:384
	ds_read_b128 v[120:123], v57 offset:400
	ds_read_b128 v[124:127], v57 offset:416
	ds_read_b128 v[128:131], v57 offset:432
	ds_read_b128 v[132:135], v57 offset:4480
	ds_read_b128 v[136:139], v57 offset:4496
	ds_read_b128 v[140:143], v57 offset:4512
	ds_read_b128 v[144:147], v57 offset:4528
	v_cvt_f32_f16_e32 v46, v186
	v_cvt_f32_f16_e32 v53, v52
	ds_read_u16 v52, v19 offset:528
	v_pk_mul_f32 v[94:95], v[94:95], v[20:21]
	v_pk_mul_f32 v[20:21], v[46:47], v[14:15] op_sel_hi:[0,1]
	v_mul_f32_e32 v55, 0xbfb8aa3b, v53
	v_pk_mul_f32 v[102:103], v[102:103], v[22:23]
	v_exp_f32_e32 v20, v20
	v_pk_mul_f32 v[22:23], v[46:47], v[16:17] op_sel_hi:[0,1]
	v_pk_fma_f32 v[94:95], v[44:45], v[196:197], v[94:95] op_sel_hi:[0,1,1]
	v_exp_f32_e32 v21, v21
	v_pk_mul_f32 v[48:49], v[94:95], v[212:213]
	v_pk_mul_f32 v[88:89], v[88:89], v[24:25]
	v_exp_f32_e32 v22, v22
	v_pk_mul_f32 v[24:25], v[46:47], v[10:11] op_sel_hi:[0,1]
	v_pk_fma_f32 v[102:103], v[44:45], v[198:199], v[102:103] op_sel_hi:[0,1,1]
	v_exp_f32_e32 v23, v23
	v_pk_fma_f32 v[48:49], v[102:103], v[214:215], v[48:49]
	v_exp_f32_e32 v55, v55
	v_pk_mul_f32 v[96:97], v[96:97], v[26:27]
	v_exp_f32_e32 v24, v24
	v_pk_mul_f32 v[26:27], v[46:47], v[12:13] op_sel_hi:[0,1]
	v_pk_fma_f32 v[88:89], v[44:45], v[200:201], v[88:89] op_sel_hi:[0,1,1]
	v_exp_f32_e32 v25, v25
	v_pk_fma_f32 v[48:49], v[88:89], v[216:217], v[48:49]
	v_pk_mul_f32 v[90:91], v[90:91], v[28:29]
	v_exp_f32_e32 v26, v26
	v_pk_mul_f32 v[28:29], v[46:47], v[6:7] op_sel_hi:[0,1]
	v_pk_fma_f32 v[96:97], v[44:45], v[202:203], v[96:97] op_sel_hi:[0,1,1]
	v_exp_f32_e32 v27, v27
	v_pk_fma_f32 v[48:49], v[96:97], v[218:219], v[48:49]
	v_add_f32_e32 v55, 1.0, v55
	v_pk_mul_f32 v[92:93], v[92:93], v[30:31]
	v_exp_f32_e32 v28, v28
	v_pk_mul_f32 v[30:31], v[46:47], v[8:9] op_sel_hi:[0,1]
	v_pk_fma_f32 v[90:91], v[44:45], v[204:205], v[90:91] op_sel_hi:[0,1,1]
	v_exp_f32_e32 v29, v29
	v_pk_fma_f32 v[48:49], v[90:91], v[220:221], v[48:49]
	v_pk_mul_f32 v[98:99], v[98:99], v[32:33]
	v_exp_f32_e32 v30, v30
	v_pk_mul_f32 v[32:33], v[46:47], v[2:3] op_sel_hi:[0,1]
	v_pk_fma_f32 v[92:93], v[44:45], v[206:207], v[92:93] op_sel_hi:[0,1,1]
	v_exp_f32_e32 v31, v31
	v_pk_fma_f32 v[48:49], v[92:93], v[222:223], v[48:49]
	v_rcp_f32_e32 v55, v55
	v_pk_mul_f32 v[100:101], v[100:101], v[34:35]
	v_exp_f32_e32 v32, v32
	v_pk_mul_f32 v[34:35], v[46:47], v[4:5] op_sel_hi:[0,1]
	v_pk_fma_f32 v[98:99], v[44:45], v[208:209], v[98:99] op_sel_hi:[0,1,1]
	v_exp_f32_e32 v33, v33
	v_pk_fma_f32 v[48:49], v[98:99], v[224:225], v[48:49]
	v_exp_f32_e32 v34, v34
	v_pk_fma_f32 v[100:101], v[44:45], v[210:211], v[100:101] op_sel_hi:[0,1,1]
	v_exp_f32_e32 v35, v35
	v_pk_fma_f32 v[48:49], v[100:101], v[226:227], v[48:49]
	v_add_f32_e32 v54, v48, v49
	v_fma_mix_f32 v54, v87, v185, v54 op_sel:[0,1,0] op_sel_hi:[0,1,0]
	v_mul_f32_e32 v54, v54, v53
	v_fma_mix_f32 v44, v186, v186, 0 op_sel:[0,1,0] op_sel_hi:[1,1,0]
	v_fma_mixlo_f16 v56, v54, v55, 0
	ds_write_b16 v19, v56
	v_add_u32_e32 v19, 0x210, v19
	s_waitcnt lgkmcnt(1)
	ds_read_b128 v[196:199], v57 offset:448
	ds_read_b128 v[200:203], v57 offset:464
	ds_read_b128 v[204:207], v57 offset:480
	ds_read_b128 v[208:211], v57 offset:496
	ds_read_b128 v[212:215], v57 offset:4544
	ds_read_b128 v[216:219], v57 offset:4560
	ds_read_b128 v[220:223], v57 offset:4576
	ds_read_b128 v[224:227], v57 offset:4592
	v_cvt_f32_f16_e32 v46, v187
	v_cvt_f32_f16_e32 v53, v52
	ds_read_u16 v52, v19 offset:528
	v_pk_mul_f32 v[94:95], v[94:95], v[20:21]
	v_pk_mul_f32 v[20:21], v[46:47], v[14:15] op_sel_hi:[0,1]
	v_mul_f32_e32 v55, 0xbfb8aa3b, v53
	v_pk_mul_f32 v[102:103], v[102:103], v[22:23]
	v_exp_f32_e32 v20, v20
	v_pk_mul_f32 v[22:23], v[46:47], v[16:17] op_sel_hi:[0,1]
	v_pk_fma_f32 v[94:95], v[44:45], v[116:117], v[94:95] op_sel_hi:[0,1,1]
	v_exp_f32_e32 v21, v21
	v_pk_mul_f32 v[48:49], v[94:95], v[132:133]
	v_pk_mul_f32 v[88:89], v[88:89], v[24:25]
	v_exp_f32_e32 v22, v22
	v_pk_mul_f32 v[24:25], v[46:47], v[10:11] op_sel_hi:[0,1]
	v_pk_fma_f32 v[102:103], v[44:45], v[118:119], v[102:103] op_sel_hi:[0,1,1]
	v_exp_f32_e32 v23, v23
	v_pk_fma_f32 v[48:49], v[102:103], v[134:135], v[48:49]
	v_exp_f32_e32 v55, v55
	v_pk_mul_f32 v[96:97], v[96:97], v[26:27]
	v_exp_f32_e32 v24, v24
	v_pk_mul_f32 v[26:27], v[46:47], v[12:13] op_sel_hi:[0,1]
	v_pk_fma_f32 v[88:89], v[44:45], v[120:121], v[88:89] op_sel_hi:[0,1,1]
	v_exp_f32_e32 v25, v25
	v_pk_fma_f32 v[48:49], v[88:89], v[136:137], v[48:49]
	v_pk_mul_f32 v[90:91], v[90:91], v[28:29]
	v_exp_f32_e32 v26, v26
	v_pk_mul_f32 v[28:29], v[46:47], v[6:7] op_sel_hi:[0,1]
	v_pk_fma_f32 v[96:97], v[44:45], v[122:123], v[96:97] op_sel_hi:[0,1,1]
	v_exp_f32_e32 v27, v27
	v_pk_fma_f32 v[48:49], v[96:97], v[138:139], v[48:49]
	v_add_f32_e32 v55, 1.0, v55
	v_pk_mul_f32 v[92:93], v[92:93], v[30:31]
	v_exp_f32_e32 v28, v28
	v_pk_mul_f32 v[30:31], v[46:47], v[8:9] op_sel_hi:[0,1]
	v_pk_fma_f32 v[90:91], v[44:45], v[124:125], v[90:91] op_sel_hi:[0,1,1]
	v_exp_f32_e32 v29, v29
	v_pk_fma_f32 v[48:49], v[90:91], v[140:141], v[48:49]
	v_pk_mul_f32 v[98:99], v[98:99], v[32:33]
	v_exp_f32_e32 v30, v30
	v_pk_mul_f32 v[32:33], v[46:47], v[2:3] op_sel_hi:[0,1]
	v_pk_fma_f32 v[92:93], v[44:45], v[126:127], v[92:93] op_sel_hi:[0,1,1]
	v_exp_f32_e32 v31, v31
	v_pk_fma_f32 v[48:49], v[92:93], v[142:143], v[48:49]
	v_rcp_f32_e32 v55, v55
	v_pk_mul_f32 v[100:101], v[100:101], v[34:35]
	v_exp_f32_e32 v32, v32
	v_pk_mul_f32 v[34:35], v[46:47], v[4:5] op_sel_hi:[0,1]
	v_pk_fma_f32 v[98:99], v[44:45], v[128:129], v[98:99] op_sel_hi:[0,1,1]
	v_exp_f32_e32 v33, v33
	v_pk_fma_f32 v[48:49], v[98:99], v[144:145], v[48:49]
	v_exp_f32_e32 v34, v34
	v_pk_fma_f32 v[100:101], v[44:45], v[130:131], v[100:101] op_sel_hi:[0,1,1]
	v_exp_f32_e32 v35, v35
	v_pk_fma_f32 v[48:49], v[100:101], v[146:147], v[48:49]
	v_add_f32_e32 v54, v48, v49
	v_fma_mix_f32 v54, v87, v186, v54 op_sel:[0,1,0] op_sel_hi:[0,1,0]
	v_mul_f32_e32 v54, v54, v53
	v_fma_mix_f32 v44, v187, v187, 0 op_sel:[0,1,0] op_sel_hi:[1,1,0]
	v_fma_mixlo_f16 v56, v54, v55, 0
	ds_write_b16 v19, v56
	v_add_u32_e32 v19, 0x210, v19
	s_waitcnt lgkmcnt(1)
	ds_read_b128 v[116:119], v57 offset:512
	ds_read_b128 v[120:123], v57 offset:528
	ds_read_b128 v[124:127], v57 offset:544
	ds_read_b128 v[128:131], v57 offset:560
	ds_read_b128 v[132:135], v57 offset:4608
	ds_read_b128 v[136:139], v57 offset:4624
	ds_read_b128 v[140:143], v57 offset:4640
	ds_read_b128 v[144:147], v57 offset:4656
	s_waitcnt vmcnt(2)
	v_cvt_f32_f16_e32 v46, v188
	v_cvt_f32_f16_e32 v53, v52
	ds_read_u16 v52, v19 offset:528
	v_pk_mul_f32 v[94:95], v[94:95], v[20:21]
	v_pk_mul_f32 v[20:21], v[46:47], v[14:15] op_sel_hi:[0,1]
	v_mul_f32_e32 v55, 0xbfb8aa3b, v53
	v_pk_mul_f32 v[102:103], v[102:103], v[22:23]
	v_exp_f32_e32 v20, v20
	v_pk_mul_f32 v[22:23], v[46:47], v[16:17] op_sel_hi:[0,1]
	v_pk_fma_f32 v[94:95], v[44:45], v[196:197], v[94:95] op_sel_hi:[0,1,1]
	v_exp_f32_e32 v21, v21
	v_pk_mul_f32 v[48:49], v[94:95], v[212:213]
	v_pk_mul_f32 v[88:89], v[88:89], v[24:25]
	v_exp_f32_e32 v22, v22
	v_pk_mul_f32 v[24:25], v[46:47], v[10:11] op_sel_hi:[0,1]
	v_pk_fma_f32 v[102:103], v[44:45], v[198:199], v[102:103] op_sel_hi:[0,1,1]
	v_exp_f32_e32 v23, v23
	v_pk_fma_f32 v[48:49], v[102:103], v[214:215], v[48:49]
	v_exp_f32_e32 v55, v55
	v_pk_mul_f32 v[96:97], v[96:97], v[26:27]
	v_exp_f32_e32 v24, v24
	v_pk_mul_f32 v[26:27], v[46:47], v[12:13] op_sel_hi:[0,1]
	v_pk_fma_f32 v[88:89], v[44:45], v[200:201], v[88:89] op_sel_hi:[0,1,1]
	v_exp_f32_e32 v25, v25
	v_pk_fma_f32 v[48:49], v[88:89], v[216:217], v[48:49]
	v_pk_mul_f32 v[90:91], v[90:91], v[28:29]
	v_exp_f32_e32 v26, v26
	v_pk_mul_f32 v[28:29], v[46:47], v[6:7] op_sel_hi:[0,1]
	v_pk_fma_f32 v[96:97], v[44:45], v[202:203], v[96:97] op_sel_hi:[0,1,1]
	v_exp_f32_e32 v27, v27
	v_pk_fma_f32 v[48:49], v[96:97], v[218:219], v[48:49]
	v_add_f32_e32 v55, 1.0, v55
	v_pk_mul_f32 v[92:93], v[92:93], v[30:31]
	v_exp_f32_e32 v28, v28
	v_pk_mul_f32 v[30:31], v[46:47], v[8:9] op_sel_hi:[0,1]
	v_pk_fma_f32 v[90:91], v[44:45], v[204:205], v[90:91] op_sel_hi:[0,1,1]
	v_exp_f32_e32 v29, v29
	v_pk_fma_f32 v[48:49], v[90:91], v[220:221], v[48:49]
	v_pk_mul_f32 v[98:99], v[98:99], v[32:33]
	v_exp_f32_e32 v30, v30
	v_pk_mul_f32 v[32:33], v[46:47], v[2:3] op_sel_hi:[0,1]
	v_pk_fma_f32 v[92:93], v[44:45], v[206:207], v[92:93] op_sel_hi:[0,1,1]
	v_exp_f32_e32 v31, v31
	v_pk_fma_f32 v[48:49], v[92:93], v[222:223], v[48:49]
	v_rcp_f32_e32 v55, v55
	v_pk_mul_f32 v[100:101], v[100:101], v[34:35]
	v_exp_f32_e32 v32, v32
	v_pk_mul_f32 v[34:35], v[46:47], v[4:5] op_sel_hi:[0,1]
	v_pk_fma_f32 v[98:99], v[44:45], v[208:209], v[98:99] op_sel_hi:[0,1,1]
	v_exp_f32_e32 v33, v33
	v_pk_fma_f32 v[48:49], v[98:99], v[224:225], v[48:49]
	v_exp_f32_e32 v34, v34
	v_pk_fma_f32 v[100:101], v[44:45], v[210:211], v[100:101] op_sel_hi:[0,1,1]
	v_exp_f32_e32 v35, v35
	v_pk_fma_f32 v[48:49], v[100:101], v[226:227], v[48:49]
	v_add_f32_e32 v54, v48, v49
	v_fma_mix_f32 v54, v87, v187, v54 op_sel:[0,1,0] op_sel_hi:[0,1,0]
	v_mul_f32_e32 v54, v54, v53
	v_fma_mix_f32 v44, v188, v188, 0 op_sel:[0,1,0] op_sel_hi:[1,1,0]
	global_load_dwordx4 v[184:187], v[58:59], off
	v_fma_mixlo_f16 v56, v54, v55, 0
	ds_write_b16 v19, v56
	v_add_u32_e32 v19, 0x210, v19
	s_waitcnt lgkmcnt(1)
	ds_read_b128 v[196:199], v57 offset:576
	ds_read_b128 v[200:203], v57 offset:592
	ds_read_b128 v[204:207], v57 offset:608
	ds_read_b128 v[208:211], v57 offset:624
	ds_read_b128 v[212:215], v57 offset:4672
	ds_read_b128 v[216:219], v57 offset:4688
	ds_read_b128 v[220:223], v57 offset:4704
	ds_read_b128 v[224:227], v57 offset:4720
	v_cvt_f32_f16_e32 v46, v189
	v_cvt_f32_f16_e32 v53, v52
	ds_read_u16 v52, v19 offset:528
	v_pk_mul_f32 v[94:95], v[94:95], v[20:21]
	v_pk_mul_f32 v[20:21], v[46:47], v[14:15] op_sel_hi:[0,1]
	v_mul_f32_e32 v55, 0xbfb8aa3b, v53
	v_pk_mul_f32 v[102:103], v[102:103], v[22:23]
	v_exp_f32_e32 v20, v20
	v_pk_mul_f32 v[22:23], v[46:47], v[16:17] op_sel_hi:[0,1]
	v_pk_fma_f32 v[94:95], v[44:45], v[116:117], v[94:95] op_sel_hi:[0,1,1]
	v_exp_f32_e32 v21, v21
	v_pk_mul_f32 v[48:49], v[94:95], v[132:133]
	v_pk_mul_f32 v[88:89], v[88:89], v[24:25]
	v_exp_f32_e32 v22, v22
	v_pk_mul_f32 v[24:25], v[46:47], v[10:11] op_sel_hi:[0,1]
	v_pk_fma_f32 v[102:103], v[44:45], v[118:119], v[102:103] op_sel_hi:[0,1,1]
	v_exp_f32_e32 v23, v23
	v_pk_fma_f32 v[48:49], v[102:103], v[134:135], v[48:49]
	v_exp_f32_e32 v55, v55
	v_pk_mul_f32 v[96:97], v[96:97], v[26:27]
	v_exp_f32_e32 v24, v24
	v_pk_mul_f32 v[26:27], v[46:47], v[12:13] op_sel_hi:[0,1]
	v_pk_fma_f32 v[88:89], v[44:45], v[120:121], v[88:89] op_sel_hi:[0,1,1]
	v_exp_f32_e32 v25, v25
	v_pk_fma_f32 v[48:49], v[88:89], v[136:137], v[48:49]
	v_pk_mul_f32 v[90:91], v[90:91], v[28:29]
	v_exp_f32_e32 v26, v26
	v_pk_mul_f32 v[28:29], v[46:47], v[6:7] op_sel_hi:[0,1]
	v_pk_fma_f32 v[96:97], v[44:45], v[122:123], v[96:97] op_sel_hi:[0,1,1]
	v_exp_f32_e32 v27, v27
	v_pk_fma_f32 v[48:49], v[96:97], v[138:139], v[48:49]
	v_add_f32_e32 v55, 1.0, v55
	v_pk_mul_f32 v[92:93], v[92:93], v[30:31]
	v_exp_f32_e32 v28, v28
	v_pk_mul_f32 v[30:31], v[46:47], v[8:9] op_sel_hi:[0,1]
	v_pk_fma_f32 v[90:91], v[44:45], v[124:125], v[90:91] op_sel_hi:[0,1,1]
	v_exp_f32_e32 v29, v29
	v_pk_fma_f32 v[48:49], v[90:91], v[140:141], v[48:49]
	v_pk_mul_f32 v[98:99], v[98:99], v[32:33]
	v_exp_f32_e32 v30, v30
	v_pk_mul_f32 v[32:33], v[46:47], v[2:3] op_sel_hi:[0,1]
	v_pk_fma_f32 v[92:93], v[44:45], v[126:127], v[92:93] op_sel_hi:[0,1,1]
	v_exp_f32_e32 v31, v31
	v_pk_fma_f32 v[48:49], v[92:93], v[142:143], v[48:49]
	v_rcp_f32_e32 v55, v55
	v_pk_mul_f32 v[100:101], v[100:101], v[34:35]
	v_exp_f32_e32 v32, v32
	v_pk_mul_f32 v[34:35], v[46:47], v[4:5] op_sel_hi:[0,1]
	v_pk_fma_f32 v[98:99], v[44:45], v[128:129], v[98:99] op_sel_hi:[0,1,1]
	v_exp_f32_e32 v33, v33
	v_pk_fma_f32 v[48:49], v[98:99], v[144:145], v[48:49]
	v_exp_f32_e32 v34, v34
	v_pk_fma_f32 v[100:101], v[44:45], v[130:131], v[100:101] op_sel_hi:[0,1,1]
	v_exp_f32_e32 v35, v35
	v_pk_fma_f32 v[48:49], v[100:101], v[146:147], v[48:49]
	v_add_f32_e32 v54, v48, v49
	v_fma_mix_f32 v54, v87, v188, v54 op_sel:[0,1,0] op_sel_hi:[0,1,0]
	v_mul_f32_e32 v54, v54, v53
	v_fma_mix_f32 v44, v189, v189, 0 op_sel:[0,1,0] op_sel_hi:[1,1,0]
	v_fma_mixlo_f16 v56, v54, v55, 0
	ds_write_b16 v19, v56
	v_add_u32_e32 v19, 0x210, v19
	s_waitcnt lgkmcnt(1)
	ds_read_b128 v[116:119], v57 offset:640
	ds_read_b128 v[120:123], v57 offset:656
	ds_read_b128 v[124:127], v57 offset:672
	ds_read_b128 v[128:131], v57 offset:688
	ds_read_b128 v[132:135], v57 offset:4736
	ds_read_b128 v[136:139], v57 offset:4752
	ds_read_b128 v[140:143], v57 offset:4768
	ds_read_b128 v[144:147], v57 offset:4784
	v_cvt_f32_f16_e32 v46, v190
	v_cvt_f32_f16_e32 v53, v52
	ds_read_u16 v52, v19 offset:528
	v_pk_mul_f32 v[94:95], v[94:95], v[20:21]
	v_pk_mul_f32 v[20:21], v[46:47], v[14:15] op_sel_hi:[0,1]
	v_mul_f32_e32 v55, 0xbfb8aa3b, v53
	v_pk_mul_f32 v[102:103], v[102:103], v[22:23]
	v_exp_f32_e32 v20, v20
	v_pk_mul_f32 v[22:23], v[46:47], v[16:17] op_sel_hi:[0,1]
	v_pk_fma_f32 v[94:95], v[44:45], v[196:197], v[94:95] op_sel_hi:[0,1,1]
	v_exp_f32_e32 v21, v21
	v_pk_mul_f32 v[48:49], v[94:95], v[212:213]
	v_pk_mul_f32 v[88:89], v[88:89], v[24:25]
	v_exp_f32_e32 v22, v22
	v_pk_mul_f32 v[24:25], v[46:47], v[10:11] op_sel_hi:[0,1]
	v_pk_fma_f32 v[102:103], v[44:45], v[198:199], v[102:103] op_sel_hi:[0,1,1]
	v_exp_f32_e32 v23, v23
	v_pk_fma_f32 v[48:49], v[102:103], v[214:215], v[48:49]
	v_exp_f32_e32 v55, v55
	v_pk_mul_f32 v[96:97], v[96:97], v[26:27]
	v_exp_f32_e32 v24, v24
	v_pk_mul_f32 v[26:27], v[46:47], v[12:13] op_sel_hi:[0,1]
	v_pk_fma_f32 v[88:89], v[44:45], v[200:201], v[88:89] op_sel_hi:[0,1,1]
	v_exp_f32_e32 v25, v25
	v_pk_fma_f32 v[48:49], v[88:89], v[216:217], v[48:49]
	v_pk_mul_f32 v[90:91], v[90:91], v[28:29]
	v_exp_f32_e32 v26, v26
	v_pk_mul_f32 v[28:29], v[46:47], v[6:7] op_sel_hi:[0,1]
	v_pk_fma_f32 v[96:97], v[44:45], v[202:203], v[96:97] op_sel_hi:[0,1,1]
	v_exp_f32_e32 v27, v27
	v_pk_fma_f32 v[48:49], v[96:97], v[218:219], v[48:49]
	v_add_f32_e32 v55, 1.0, v55
	v_pk_mul_f32 v[92:93], v[92:93], v[30:31]
	v_exp_f32_e32 v28, v28
	v_pk_mul_f32 v[30:31], v[46:47], v[8:9] op_sel_hi:[0,1]
	v_pk_fma_f32 v[90:91], v[44:45], v[204:205], v[90:91] op_sel_hi:[0,1,1]
	v_exp_f32_e32 v29, v29
	v_pk_fma_f32 v[48:49], v[90:91], v[220:221], v[48:49]
	v_pk_mul_f32 v[98:99], v[98:99], v[32:33]
	v_exp_f32_e32 v30, v30
	v_pk_mul_f32 v[32:33], v[46:47], v[2:3] op_sel_hi:[0,1]
	v_pk_fma_f32 v[92:93], v[44:45], v[206:207], v[92:93] op_sel_hi:[0,1,1]
	v_exp_f32_e32 v31, v31
	v_pk_fma_f32 v[48:49], v[92:93], v[222:223], v[48:49]
	v_rcp_f32_e32 v55, v55
	v_pk_mul_f32 v[100:101], v[100:101], v[34:35]
	v_exp_f32_e32 v32, v32
	v_pk_mul_f32 v[34:35], v[46:47], v[4:5] op_sel_hi:[0,1]
	v_pk_fma_f32 v[98:99], v[44:45], v[208:209], v[98:99] op_sel_hi:[0,1,1]
	v_exp_f32_e32 v33, v33
	v_pk_fma_f32 v[48:49], v[98:99], v[224:225], v[48:49]
	v_exp_f32_e32 v34, v34
	v_pk_fma_f32 v[100:101], v[44:45], v[210:211], v[100:101] op_sel_hi:[0,1,1]
	v_exp_f32_e32 v35, v35
	v_pk_fma_f32 v[48:49], v[100:101], v[226:227], v[48:49]
	v_add_f32_e32 v54, v48, v49
	v_fma_mix_f32 v54, v87, v189, v54 op_sel:[0,1,0] op_sel_hi:[0,1,0]
	v_mul_f32_e32 v54, v54, v53
	v_fma_mix_f32 v44, v190, v190, 0 op_sel:[0,1,0] op_sel_hi:[1,1,0]
	v_fma_mixlo_f16 v56, v54, v55, 0
	ds_write_b16 v19, v56
	v_add_u32_e32 v19, 0x210, v19
	s_waitcnt lgkmcnt(1)
	ds_read_b128 v[196:199], v57 offset:704
	ds_read_b128 v[200:203], v57 offset:720
	ds_read_b128 v[204:207], v57 offset:736
	ds_read_b128 v[208:211], v57 offset:752
	ds_read_b128 v[212:215], v57 offset:4800
	ds_read_b128 v[216:219], v57 offset:4816
	ds_read_b128 v[220:223], v57 offset:4832
	ds_read_b128 v[224:227], v57 offset:4848
	v_cvt_f32_f16_e32 v46, v191
	v_cvt_f32_f16_e32 v53, v52
	ds_read_u16 v52, v19 offset:528
	v_pk_mul_f32 v[94:95], v[94:95], v[20:21]
	v_pk_mul_f32 v[20:21], v[46:47], v[14:15] op_sel_hi:[0,1]
	v_mul_f32_e32 v55, 0xbfb8aa3b, v53
	v_pk_mul_f32 v[102:103], v[102:103], v[22:23]
	v_exp_f32_e32 v20, v20
	v_pk_mul_f32 v[22:23], v[46:47], v[16:17] op_sel_hi:[0,1]
	v_pk_fma_f32 v[94:95], v[44:45], v[116:117], v[94:95] op_sel_hi:[0,1,1]
	v_exp_f32_e32 v21, v21
	v_pk_mul_f32 v[48:49], v[94:95], v[132:133]
	v_pk_mul_f32 v[88:89], v[88:89], v[24:25]
	v_exp_f32_e32 v22, v22
	v_pk_mul_f32 v[24:25], v[46:47], v[10:11] op_sel_hi:[0,1]
	v_pk_fma_f32 v[102:103], v[44:45], v[118:119], v[102:103] op_sel_hi:[0,1,1]
	v_exp_f32_e32 v23, v23
	v_pk_fma_f32 v[48:49], v[102:103], v[134:135], v[48:49]
	v_exp_f32_e32 v55, v55
	v_pk_mul_f32 v[96:97], v[96:97], v[26:27]
	v_exp_f32_e32 v24, v24
	v_pk_mul_f32 v[26:27], v[46:47], v[12:13] op_sel_hi:[0,1]
	v_pk_fma_f32 v[88:89], v[44:45], v[120:121], v[88:89] op_sel_hi:[0,1,1]
	v_exp_f32_e32 v25, v25
	v_pk_fma_f32 v[48:49], v[88:89], v[136:137], v[48:49]
	v_pk_mul_f32 v[90:91], v[90:91], v[28:29]
	v_exp_f32_e32 v26, v26
	v_pk_mul_f32 v[28:29], v[46:47], v[6:7] op_sel_hi:[0,1]
	v_pk_fma_f32 v[96:97], v[44:45], v[122:123], v[96:97] op_sel_hi:[0,1,1]
	v_exp_f32_e32 v27, v27
	v_pk_fma_f32 v[48:49], v[96:97], v[138:139], v[48:49]
	v_add_f32_e32 v55, 1.0, v55
	v_pk_mul_f32 v[92:93], v[92:93], v[30:31]
	v_exp_f32_e32 v28, v28
	v_pk_mul_f32 v[30:31], v[46:47], v[8:9] op_sel_hi:[0,1]
	v_pk_fma_f32 v[90:91], v[44:45], v[124:125], v[90:91] op_sel_hi:[0,1,1]
	v_exp_f32_e32 v29, v29
	v_pk_fma_f32 v[48:49], v[90:91], v[140:141], v[48:49]
	v_pk_mul_f32 v[98:99], v[98:99], v[32:33]
	v_exp_f32_e32 v30, v30
	v_pk_mul_f32 v[32:33], v[46:47], v[2:3] op_sel_hi:[0,1]
	v_pk_fma_f32 v[92:93], v[44:45], v[126:127], v[92:93] op_sel_hi:[0,1,1]
	v_exp_f32_e32 v31, v31
	v_pk_fma_f32 v[48:49], v[92:93], v[142:143], v[48:49]
	v_rcp_f32_e32 v55, v55
	v_pk_mul_f32 v[100:101], v[100:101], v[34:35]
	v_exp_f32_e32 v32, v32
	v_pk_mul_f32 v[34:35], v[46:47], v[4:5] op_sel_hi:[0,1]
	v_pk_fma_f32 v[98:99], v[44:45], v[128:129], v[98:99] op_sel_hi:[0,1,1]
	v_exp_f32_e32 v33, v33
	v_pk_fma_f32 v[48:49], v[98:99], v[144:145], v[48:49]
	v_exp_f32_e32 v34, v34
	v_pk_fma_f32 v[100:101], v[44:45], v[130:131], v[100:101] op_sel_hi:[0,1,1]
	v_exp_f32_e32 v35, v35
	v_pk_fma_f32 v[48:49], v[100:101], v[146:147], v[48:49]
	v_add_f32_e32 v54, v48, v49
	v_fma_mix_f32 v54, v87, v190, v54 op_sel:[0,1,0] op_sel_hi:[0,1,0]
	v_mul_f32_e32 v54, v54, v53
	v_fma_mix_f32 v44, v191, v191, 0 op_sel:[0,1,0] op_sel_hi:[1,1,0]
	v_fma_mixlo_f16 v56, v54, v55, 0
	ds_write_b16 v19, v56
	v_add_u32_e32 v19, 0x210, v19
	s_waitcnt lgkmcnt(1)
	ds_read_b128 v[116:119], v57 offset:768
	ds_read_b128 v[120:123], v57 offset:784
	ds_read_b128 v[124:127], v57 offset:800
	ds_read_b128 v[128:131], v57 offset:816
	ds_read_b128 v[132:135], v57 offset:4864
	ds_read_b128 v[136:139], v57 offset:4880
	ds_read_b128 v[140:143], v57 offset:4896
	ds_read_b128 v[144:147], v57 offset:4912
	s_waitcnt vmcnt(2)
	v_cvt_f32_f16_e32 v46, v192
	v_cvt_f32_f16_e32 v53, v52
	ds_read_u16 v52, v19 offset:528
	v_pk_mul_f32 v[94:95], v[94:95], v[20:21]
	v_pk_mul_f32 v[20:21], v[46:47], v[14:15] op_sel_hi:[0,1]
	v_mul_f32_e32 v55, 0xbfb8aa3b, v53
	v_pk_mul_f32 v[102:103], v[102:103], v[22:23]
	v_exp_f32_e32 v20, v20
	v_pk_mul_f32 v[22:23], v[46:47], v[16:17] op_sel_hi:[0,1]
	v_pk_fma_f32 v[94:95], v[44:45], v[196:197], v[94:95] op_sel_hi:[0,1,1]
	v_exp_f32_e32 v21, v21
	v_pk_mul_f32 v[48:49], v[94:95], v[212:213]
	v_pk_mul_f32 v[88:89], v[88:89], v[24:25]
	v_exp_f32_e32 v22, v22
	v_pk_mul_f32 v[24:25], v[46:47], v[10:11] op_sel_hi:[0,1]
	v_pk_fma_f32 v[102:103], v[44:45], v[198:199], v[102:103] op_sel_hi:[0,1,1]
	v_exp_f32_e32 v23, v23
	v_pk_fma_f32 v[48:49], v[102:103], v[214:215], v[48:49]
	v_exp_f32_e32 v55, v55
	v_pk_mul_f32 v[96:97], v[96:97], v[26:27]
	v_exp_f32_e32 v24, v24
	v_pk_mul_f32 v[26:27], v[46:47], v[12:13] op_sel_hi:[0,1]
	v_pk_fma_f32 v[88:89], v[44:45], v[200:201], v[88:89] op_sel_hi:[0,1,1]
	v_exp_f32_e32 v25, v25
	v_pk_fma_f32 v[48:49], v[88:89], v[216:217], v[48:49]
	v_pk_mul_f32 v[90:91], v[90:91], v[28:29]
	v_exp_f32_e32 v26, v26
	v_pk_mul_f32 v[28:29], v[46:47], v[6:7] op_sel_hi:[0,1]
	v_pk_fma_f32 v[96:97], v[44:45], v[202:203], v[96:97] op_sel_hi:[0,1,1]
	v_exp_f32_e32 v27, v27
	v_pk_fma_f32 v[48:49], v[96:97], v[218:219], v[48:49]
	v_add_f32_e32 v55, 1.0, v55
	v_pk_mul_f32 v[92:93], v[92:93], v[30:31]
	v_exp_f32_e32 v28, v28
	v_pk_mul_f32 v[30:31], v[46:47], v[8:9] op_sel_hi:[0,1]
	v_pk_fma_f32 v[90:91], v[44:45], v[204:205], v[90:91] op_sel_hi:[0,1,1]
	v_exp_f32_e32 v29, v29
	v_pk_fma_f32 v[48:49], v[90:91], v[220:221], v[48:49]
	v_pk_mul_f32 v[98:99], v[98:99], v[32:33]
	v_exp_f32_e32 v30, v30
	v_pk_mul_f32 v[32:33], v[46:47], v[2:3] op_sel_hi:[0,1]
	v_pk_fma_f32 v[92:93], v[44:45], v[206:207], v[92:93] op_sel_hi:[0,1,1]
	v_exp_f32_e32 v31, v31
	v_pk_fma_f32 v[48:49], v[92:93], v[222:223], v[48:49]
	v_rcp_f32_e32 v55, v55
	v_pk_mul_f32 v[100:101], v[100:101], v[34:35]
	v_exp_f32_e32 v32, v32
	v_pk_mul_f32 v[34:35], v[46:47], v[4:5] op_sel_hi:[0,1]
	v_pk_fma_f32 v[98:99], v[44:45], v[208:209], v[98:99] op_sel_hi:[0,1,1]
	v_exp_f32_e32 v33, v33
	v_pk_fma_f32 v[48:49], v[98:99], v[224:225], v[48:49]
	v_exp_f32_e32 v34, v34
	v_pk_fma_f32 v[100:101], v[44:45], v[210:211], v[100:101] op_sel_hi:[0,1,1]
	v_exp_f32_e32 v35, v35
	v_pk_fma_f32 v[48:49], v[100:101], v[226:227], v[48:49]
	v_add_f32_e32 v54, v48, v49
	v_fma_mix_f32 v54, v87, v191, v54 op_sel:[0,1,0] op_sel_hi:[0,1,0]
	v_mul_f32_e32 v54, v54, v53
	v_fma_mix_f32 v44, v192, v192, 0 op_sel:[0,1,0] op_sel_hi:[1,1,0]
	global_load_dwordx4 v[188:191], v[50:51], off offset:-4096
	v_fma_mixlo_f16 v56, v54, v55, 0
	ds_write_b16 v19, v56
	v_add_u32_e32 v19, 0x210, v19
	s_waitcnt lgkmcnt(1)
	ds_read_b128 v[196:199], v57 offset:832
	ds_read_b128 v[200:203], v57 offset:848
	ds_read_b128 v[204:207], v57 offset:864
	ds_read_b128 v[208:211], v57 offset:880
	ds_read_b128 v[212:215], v57 offset:4928
	ds_read_b128 v[216:219], v57 offset:4944
	ds_read_b128 v[220:223], v57 offset:4960
	ds_read_b128 v[224:227], v57 offset:4976
	v_cvt_f32_f16_e32 v46, v193
	v_cvt_f32_f16_e32 v53, v52
	ds_read_u16 v52, v19 offset:528
	v_pk_mul_f32 v[94:95], v[94:95], v[20:21]
	v_pk_mul_f32 v[20:21], v[46:47], v[14:15] op_sel_hi:[0,1]
	v_mul_f32_e32 v55, 0xbfb8aa3b, v53
	v_pk_mul_f32 v[102:103], v[102:103], v[22:23]
	v_exp_f32_e32 v20, v20
	v_pk_mul_f32 v[22:23], v[46:47], v[16:17] op_sel_hi:[0,1]
	v_pk_fma_f32 v[94:95], v[44:45], v[116:117], v[94:95] op_sel_hi:[0,1,1]
	v_exp_f32_e32 v21, v21
	v_pk_mul_f32 v[48:49], v[94:95], v[132:133]
	v_pk_mul_f32 v[88:89], v[88:89], v[24:25]
	v_exp_f32_e32 v22, v22
	v_pk_mul_f32 v[24:25], v[46:47], v[10:11] op_sel_hi:[0,1]
	v_pk_fma_f32 v[102:103], v[44:45], v[118:119], v[102:103] op_sel_hi:[0,1,1]
	v_exp_f32_e32 v23, v23
	v_pk_fma_f32 v[48:49], v[102:103], v[134:135], v[48:49]
	v_exp_f32_e32 v55, v55
	v_pk_mul_f32 v[96:97], v[96:97], v[26:27]
	v_exp_f32_e32 v24, v24
	v_pk_mul_f32 v[26:27], v[46:47], v[12:13] op_sel_hi:[0,1]
	v_pk_fma_f32 v[88:89], v[44:45], v[120:121], v[88:89] op_sel_hi:[0,1,1]
	v_exp_f32_e32 v25, v25
	v_pk_fma_f32 v[48:49], v[88:89], v[136:137], v[48:49]
	v_pk_mul_f32 v[90:91], v[90:91], v[28:29]
	v_exp_f32_e32 v26, v26
	v_pk_mul_f32 v[28:29], v[46:47], v[6:7] op_sel_hi:[0,1]
	v_pk_fma_f32 v[96:97], v[44:45], v[122:123], v[96:97] op_sel_hi:[0,1,1]
	v_exp_f32_e32 v27, v27
	v_pk_fma_f32 v[48:49], v[96:97], v[138:139], v[48:49]
	v_add_f32_e32 v55, 1.0, v55
	v_pk_mul_f32 v[92:93], v[92:93], v[30:31]
	v_exp_f32_e32 v28, v28
	v_pk_mul_f32 v[30:31], v[46:47], v[8:9] op_sel_hi:[0,1]
	v_pk_fma_f32 v[90:91], v[44:45], v[124:125], v[90:91] op_sel_hi:[0,1,1]
	v_exp_f32_e32 v29, v29
	v_pk_fma_f32 v[48:49], v[90:91], v[140:141], v[48:49]
	v_pk_mul_f32 v[98:99], v[98:99], v[32:33]
	v_exp_f32_e32 v30, v30
	v_pk_mul_f32 v[32:33], v[46:47], v[2:3] op_sel_hi:[0,1]
	v_pk_fma_f32 v[92:93], v[44:45], v[126:127], v[92:93] op_sel_hi:[0,1,1]
	v_exp_f32_e32 v31, v31
	v_pk_fma_f32 v[48:49], v[92:93], v[142:143], v[48:49]
	v_rcp_f32_e32 v55, v55
	v_pk_mul_f32 v[100:101], v[100:101], v[34:35]
	v_exp_f32_e32 v32, v32
	v_pk_mul_f32 v[34:35], v[46:47], v[4:5] op_sel_hi:[0,1]
	v_pk_fma_f32 v[98:99], v[44:45], v[128:129], v[98:99] op_sel_hi:[0,1,1]
	v_exp_f32_e32 v33, v33
	v_pk_fma_f32 v[48:49], v[98:99], v[144:145], v[48:49]
	v_exp_f32_e32 v34, v34
	v_pk_fma_f32 v[100:101], v[44:45], v[130:131], v[100:101] op_sel_hi:[0,1,1]
	v_exp_f32_e32 v35, v35
	v_pk_fma_f32 v[48:49], v[100:101], v[146:147], v[48:49]
	v_add_f32_e32 v54, v48, v49
	v_fma_mix_f32 v54, v87, v192, v54 op_sel:[0,1,0] op_sel_hi:[0,1,0]
	v_mul_f32_e32 v54, v54, v53
	v_fma_mix_f32 v44, v193, v193, 0 op_sel:[0,1,0] op_sel_hi:[1,1,0]
	v_fma_mixlo_f16 v56, v54, v55, 0
	ds_write_b16 v19, v56
	v_add_u32_e32 v19, 0x210, v19
	s_waitcnt lgkmcnt(1)
	ds_read_b128 v[116:119], v57 offset:896
	ds_read_b128 v[120:123], v57 offset:912
	ds_read_b128 v[124:127], v57 offset:928
	ds_read_b128 v[128:131], v57 offset:944
	ds_read_b128 v[132:135], v57 offset:4992
	ds_read_b128 v[136:139], v57 offset:5008
	ds_read_b128 v[140:143], v57 offset:5024
	ds_read_b128 v[144:147], v57 offset:5040
	v_cvt_f32_f16_e32 v46, v194
	v_cvt_f32_f16_e32 v53, v52
	ds_read_u16 v52, v19 offset:528
	v_pk_mul_f32 v[94:95], v[94:95], v[20:21]
	v_pk_mul_f32 v[20:21], v[46:47], v[14:15] op_sel_hi:[0,1]
	v_mul_f32_e32 v55, 0xbfb8aa3b, v53
	v_pk_mul_f32 v[102:103], v[102:103], v[22:23]
	v_exp_f32_e32 v20, v20
	v_pk_mul_f32 v[22:23], v[46:47], v[16:17] op_sel_hi:[0,1]
	v_pk_fma_f32 v[94:95], v[44:45], v[196:197], v[94:95] op_sel_hi:[0,1,1]
	v_exp_f32_e32 v21, v21
	v_pk_mul_f32 v[48:49], v[94:95], v[212:213]
	v_pk_mul_f32 v[88:89], v[88:89], v[24:25]
	v_exp_f32_e32 v22, v22
	v_pk_mul_f32 v[24:25], v[46:47], v[10:11] op_sel_hi:[0,1]
	v_pk_fma_f32 v[102:103], v[44:45], v[198:199], v[102:103] op_sel_hi:[0,1,1]
	v_exp_f32_e32 v23, v23
	v_pk_fma_f32 v[48:49], v[102:103], v[214:215], v[48:49]
	v_exp_f32_e32 v55, v55
	v_pk_mul_f32 v[96:97], v[96:97], v[26:27]
	v_exp_f32_e32 v24, v24
	v_pk_mul_f32 v[26:27], v[46:47], v[12:13] op_sel_hi:[0,1]
	v_pk_fma_f32 v[88:89], v[44:45], v[200:201], v[88:89] op_sel_hi:[0,1,1]
	v_exp_f32_e32 v25, v25
	v_pk_fma_f32 v[48:49], v[88:89], v[216:217], v[48:49]
	v_pk_mul_f32 v[90:91], v[90:91], v[28:29]
	v_exp_f32_e32 v26, v26
	v_pk_mul_f32 v[28:29], v[46:47], v[6:7] op_sel_hi:[0,1]
	v_pk_fma_f32 v[96:97], v[44:45], v[202:203], v[96:97] op_sel_hi:[0,1,1]
	v_exp_f32_e32 v27, v27
	v_pk_fma_f32 v[48:49], v[96:97], v[218:219], v[48:49]
	v_add_f32_e32 v55, 1.0, v55
	v_pk_mul_f32 v[92:93], v[92:93], v[30:31]
	v_exp_f32_e32 v28, v28
	v_pk_mul_f32 v[30:31], v[46:47], v[8:9] op_sel_hi:[0,1]
	v_pk_fma_f32 v[90:91], v[44:45], v[204:205], v[90:91] op_sel_hi:[0,1,1]
	v_exp_f32_e32 v29, v29
	v_pk_fma_f32 v[48:49], v[90:91], v[220:221], v[48:49]
	v_pk_mul_f32 v[98:99], v[98:99], v[32:33]
	v_exp_f32_e32 v30, v30
	v_pk_mul_f32 v[32:33], v[46:47], v[2:3] op_sel_hi:[0,1]
	v_pk_fma_f32 v[92:93], v[44:45], v[206:207], v[92:93] op_sel_hi:[0,1,1]
	v_exp_f32_e32 v31, v31
	v_pk_fma_f32 v[48:49], v[92:93], v[222:223], v[48:49]
	v_rcp_f32_e32 v55, v55
	v_pk_mul_f32 v[100:101], v[100:101], v[34:35]
	v_exp_f32_e32 v32, v32
	v_pk_mul_f32 v[34:35], v[46:47], v[4:5] op_sel_hi:[0,1]
	v_pk_fma_f32 v[98:99], v[44:45], v[208:209], v[98:99] op_sel_hi:[0,1,1]
	v_exp_f32_e32 v33, v33
	v_pk_fma_f32 v[48:49], v[98:99], v[224:225], v[48:49]
	v_exp_f32_e32 v34, v34
	v_pk_fma_f32 v[100:101], v[44:45], v[210:211], v[100:101] op_sel_hi:[0,1,1]
	v_exp_f32_e32 v35, v35
	v_pk_fma_f32 v[48:49], v[100:101], v[226:227], v[48:49]
	v_add_f32_e32 v54, v48, v49
	v_fma_mix_f32 v54, v87, v193, v54 op_sel:[0,1,0] op_sel_hi:[0,1,0]
	v_mul_f32_e32 v54, v54, v53
	v_fma_mix_f32 v44, v194, v194, 0 op_sel:[0,1,0] op_sel_hi:[1,1,0]
	v_fma_mixlo_f16 v56, v54, v55, 0
	ds_write_b16 v19, v56
	v_add_u32_e32 v19, 0x210, v19
	s_waitcnt lgkmcnt(1)
	ds_read_b128 v[196:199], v57 offset:960
	ds_read_b128 v[200:203], v57 offset:976
	ds_read_b128 v[204:207], v57 offset:992
	ds_read_b128 v[208:211], v57 offset:1008
	ds_read_b128 v[212:215], v57 offset:5056
	ds_read_b128 v[216:219], v57 offset:5072
	ds_read_b128 v[220:223], v57 offset:5088
	ds_read_b128 v[224:227], v57 offset:5104
	v_cvt_f32_f16_e32 v46, v195
	v_cvt_f32_f16_e32 v53, v52
	ds_read_u16 v52, v19 offset:528
	v_pk_mul_f32 v[94:95], v[94:95], v[20:21]
	v_pk_mul_f32 v[20:21], v[46:47], v[14:15] op_sel_hi:[0,1]
	v_mul_f32_e32 v55, 0xbfb8aa3b, v53
	v_pk_mul_f32 v[102:103], v[102:103], v[22:23]
	v_exp_f32_e32 v20, v20
	v_pk_mul_f32 v[22:23], v[46:47], v[16:17] op_sel_hi:[0,1]
	v_pk_fma_f32 v[94:95], v[44:45], v[116:117], v[94:95] op_sel_hi:[0,1,1]
	v_exp_f32_e32 v21, v21
	v_pk_mul_f32 v[48:49], v[94:95], v[132:133]
	v_pk_mul_f32 v[88:89], v[88:89], v[24:25]
	v_exp_f32_e32 v22, v22
	v_pk_mul_f32 v[24:25], v[46:47], v[10:11] op_sel_hi:[0,1]
	v_pk_fma_f32 v[102:103], v[44:45], v[118:119], v[102:103] op_sel_hi:[0,1,1]
	v_exp_f32_e32 v23, v23
	v_pk_fma_f32 v[48:49], v[102:103], v[134:135], v[48:49]
	v_exp_f32_e32 v55, v55
	v_pk_mul_f32 v[96:97], v[96:97], v[26:27]
	v_exp_f32_e32 v24, v24
	v_pk_mul_f32 v[26:27], v[46:47], v[12:13] op_sel_hi:[0,1]
	v_pk_fma_f32 v[88:89], v[44:45], v[120:121], v[88:89] op_sel_hi:[0,1,1]
	v_exp_f32_e32 v25, v25
	v_pk_fma_f32 v[48:49], v[88:89], v[136:137], v[48:49]
	v_pk_mul_f32 v[90:91], v[90:91], v[28:29]
	v_exp_f32_e32 v26, v26
	v_pk_mul_f32 v[28:29], v[46:47], v[6:7] op_sel_hi:[0,1]
	v_pk_fma_f32 v[96:97], v[44:45], v[122:123], v[96:97] op_sel_hi:[0,1,1]
	v_exp_f32_e32 v27, v27
	v_pk_fma_f32 v[48:49], v[96:97], v[138:139], v[48:49]
	v_add_f32_e32 v55, 1.0, v55
	v_pk_mul_f32 v[92:93], v[92:93], v[30:31]
	v_exp_f32_e32 v28, v28
	v_pk_mul_f32 v[30:31], v[46:47], v[8:9] op_sel_hi:[0,1]
	v_pk_fma_f32 v[90:91], v[44:45], v[124:125], v[90:91] op_sel_hi:[0,1,1]
	v_exp_f32_e32 v29, v29
	v_pk_fma_f32 v[48:49], v[90:91], v[140:141], v[48:49]
	v_pk_mul_f32 v[98:99], v[98:99], v[32:33]
	v_exp_f32_e32 v30, v30
	v_pk_mul_f32 v[32:33], v[46:47], v[2:3] op_sel_hi:[0,1]
	v_pk_fma_f32 v[92:93], v[44:45], v[126:127], v[92:93] op_sel_hi:[0,1,1]
	v_exp_f32_e32 v31, v31
	v_pk_fma_f32 v[48:49], v[92:93], v[142:143], v[48:49]
	v_rcp_f32_e32 v55, v55
	v_pk_mul_f32 v[100:101], v[100:101], v[34:35]
	v_exp_f32_e32 v32, v32
	v_pk_mul_f32 v[34:35], v[46:47], v[4:5] op_sel_hi:[0,1]
	v_pk_fma_f32 v[98:99], v[44:45], v[128:129], v[98:99] op_sel_hi:[0,1,1]
	v_exp_f32_e32 v33, v33
	v_pk_fma_f32 v[48:49], v[98:99], v[144:145], v[48:49]
	v_exp_f32_e32 v34, v34
	v_pk_fma_f32 v[100:101], v[44:45], v[130:131], v[100:101] op_sel_hi:[0,1,1]
	v_exp_f32_e32 v35, v35
	v_pk_fma_f32 v[48:49], v[100:101], v[146:147], v[48:49]
	v_add_f32_e32 v54, v48, v49
	v_fma_mix_f32 v54, v87, v194, v54 op_sel:[0,1,0] op_sel_hi:[0,1,0]
	v_mul_f32_e32 v54, v54, v53
	v_fma_mix_f32 v44, v195, v195, 0 op_sel:[0,1,0] op_sel_hi:[1,1,0]
	v_fma_mixlo_f16 v56, v54, v55, 0
	ds_write_b16 v19, v56
	v_add_u32_e32 v19, 0x210, v19
	s_waitcnt lgkmcnt(1)
	ds_read_b128 v[116:119], v57 offset:1024
	ds_read_b128 v[120:123], v57 offset:1040
	ds_read_b128 v[124:127], v57 offset:1056
	ds_read_b128 v[128:131], v57 offset:1072
	ds_read_b128 v[132:135], v57 offset:5120
	ds_read_b128 v[136:139], v57 offset:5136
	ds_read_b128 v[140:143], v57 offset:5152
	ds_read_b128 v[144:147], v57 offset:5168
	s_waitcnt vmcnt(2)
	v_cvt_f32_f16_e32 v46, v180
	v_cvt_f32_f16_e32 v53, v52
	ds_read_u16 v52, v19 offset:528
	v_pk_mul_f32 v[94:95], v[94:95], v[20:21]
	v_pk_mul_f32 v[20:21], v[46:47], v[14:15] op_sel_hi:[0,1]
	v_mul_f32_e32 v55, 0xbfb8aa3b, v53
	v_pk_mul_f32 v[102:103], v[102:103], v[22:23]
	v_exp_f32_e32 v20, v20
	v_pk_mul_f32 v[22:23], v[46:47], v[16:17] op_sel_hi:[0,1]
	v_pk_fma_f32 v[94:95], v[44:45], v[196:197], v[94:95] op_sel_hi:[0,1,1]
	v_exp_f32_e32 v21, v21
	v_pk_mul_f32 v[48:49], v[94:95], v[212:213]
	v_pk_mul_f32 v[88:89], v[88:89], v[24:25]
	v_exp_f32_e32 v22, v22
	v_pk_mul_f32 v[24:25], v[46:47], v[10:11] op_sel_hi:[0,1]
	v_pk_fma_f32 v[102:103], v[44:45], v[198:199], v[102:103] op_sel_hi:[0,1,1]
	v_exp_f32_e32 v23, v23
	v_pk_fma_f32 v[48:49], v[102:103], v[214:215], v[48:49]
	v_exp_f32_e32 v55, v55
	v_pk_mul_f32 v[96:97], v[96:97], v[26:27]
	v_exp_f32_e32 v24, v24
	v_pk_mul_f32 v[26:27], v[46:47], v[12:13] op_sel_hi:[0,1]
	v_pk_fma_f32 v[88:89], v[44:45], v[200:201], v[88:89] op_sel_hi:[0,1,1]
	v_exp_f32_e32 v25, v25
	v_pk_fma_f32 v[48:49], v[88:89], v[216:217], v[48:49]
	v_pk_mul_f32 v[90:91], v[90:91], v[28:29]
	v_exp_f32_e32 v26, v26
	v_pk_mul_f32 v[28:29], v[46:47], v[6:7] op_sel_hi:[0,1]
	v_pk_fma_f32 v[96:97], v[44:45], v[202:203], v[96:97] op_sel_hi:[0,1,1]
	v_exp_f32_e32 v27, v27
	v_pk_fma_f32 v[48:49], v[96:97], v[218:219], v[48:49]
	v_add_f32_e32 v55, 1.0, v55
	v_pk_mul_f32 v[92:93], v[92:93], v[30:31]
	v_exp_f32_e32 v28, v28
	v_pk_mul_f32 v[30:31], v[46:47], v[8:9] op_sel_hi:[0,1]
	v_pk_fma_f32 v[90:91], v[44:45], v[204:205], v[90:91] op_sel_hi:[0,1,1]
	v_exp_f32_e32 v29, v29
	v_pk_fma_f32 v[48:49], v[90:91], v[220:221], v[48:49]
	v_pk_mul_f32 v[98:99], v[98:99], v[32:33]
	v_exp_f32_e32 v30, v30
	v_pk_mul_f32 v[32:33], v[46:47], v[2:3] op_sel_hi:[0,1]
	v_pk_fma_f32 v[92:93], v[44:45], v[206:207], v[92:93] op_sel_hi:[0,1,1]
	v_exp_f32_e32 v31, v31
	v_pk_fma_f32 v[48:49], v[92:93], v[222:223], v[48:49]
	v_rcp_f32_e32 v55, v55
	v_pk_mul_f32 v[100:101], v[100:101], v[34:35]
	v_exp_f32_e32 v32, v32
	v_pk_mul_f32 v[34:35], v[46:47], v[4:5] op_sel_hi:[0,1]
	v_pk_fma_f32 v[98:99], v[44:45], v[208:209], v[98:99] op_sel_hi:[0,1,1]
	v_exp_f32_e32 v33, v33
	v_pk_fma_f32 v[48:49], v[98:99], v[224:225], v[48:49]
	v_exp_f32_e32 v34, v34
	v_pk_fma_f32 v[100:101], v[44:45], v[210:211], v[100:101] op_sel_hi:[0,1,1]
	v_exp_f32_e32 v35, v35
	v_pk_fma_f32 v[48:49], v[100:101], v[226:227], v[48:49]
	v_add_f32_e32 v54, v48, v49
	v_fma_mix_f32 v54, v87, v195, v54 op_sel:[0,1,0] op_sel_hi:[0,1,0]
	v_mul_f32_e32 v54, v54, v53
	v_fma_mix_f32 v44, v180, v180, 0 op_sel:[0,1,0] op_sel_hi:[1,1,0]
	global_load_dwordx4 v[192:195], v[50:51], off
	v_fma_mixlo_f16 v56, v54, v55, 0
	ds_write_b16 v19, v56
	v_add_u32_e32 v19, 0x210, v19
	v_add_u32_e32 v57, 0x400, v57
	v_lshl_add_u64 v[58:59], v[58:59], 0, s[10:11]
	v_lshl_add_u64 v[50:51], v[50:51], 0, s[10:11]
	s_add_i32 s12, s12, 1
	s_cmp_eq_u32 s12, 4
	s_cbranch_scc0 .Lsc3_loop
	global_load_dwordx4 v[18:21], v86, s[4:5]
	global_load_dwordx4 v[34:37], v86, s[4:5] offset:1024
	global_load_dwordx4 v[38:41], v86, s[4:5] offset:2048
	global_load_dwordx4 v[42:45], v86, s[4:5] offset:3072
	v_mov_b32_e32 v87, 0
	v_and_b32_e32 v112, 31, v0
	v_lshl_add_u64 v[2:3], s[4:5], 0, v[86:87]
	v_and_b32_e32 v5, 8, v114
	v_mul_u32_u24_e32 v6, 0x210, v112
	v_add_co_u32_e32 v4, vcc, 0x1000, v2
	v_lshl_add_u32 v113, v5, 1, v6
	s_nop 0
	v_addc_co_u32_e32 v5, vcc, 0, v3, vcc
	global_load_dwordx4 v[46:49], v[4:5], off
	global_load_dwordx4 v[50:53], v[4:5], off offset:1024
	global_load_dwordx4 v[54:57], v[4:5], off offset:2048
	global_load_dwordx4 v[58:61], v[4:5], off offset:3072
	v_add_co_u32_e32 v6, vcc, 0x2000, v2
	s_movk_i32 s4, 0x110
	s_nop 0
	v_addc_co_u32_e32 v7, vcc, 0, v3, vcc
	global_load_dwordx4 v[62:65], v[6:7], off
	global_load_dwordx4 v[66:69], v[6:7], off offset:1024
	global_load_dwordx4 v[70:73], v[6:7], off offset:2048
	global_load_dwordx4 v[74:77], v[6:7], off offset:3072
	v_add_co_u32_e32 v2, vcc, 0x3000, v2
	s_lshl_b32 s2, s2, 12
	s_nop 0
	v_addc_co_u32_e32 v3, vcc, 0, v3, vcc
	global_load_dwordx4 v[78:81], v[2:3], off
	global_load_dwordx4 v[86:89], v[2:3], off offset:1024
	global_load_dwordx4 v[90:93], v[2:3], off offset:2048
	global_load_dwordx4 v[94:97], v[2:3], off offset:3072
	s_waitcnt lgkmcnt(0)
	s_barrier
	ds_read_b128 v[2:5], v113
	ds_read_b128 v[98:101], v113 offset:32
	ds_read_b128 v[22:25], v113 offset:16896
	ds_read_b128 v[102:105], v113 offset:16928
	s_and_b32 s2, s2, 0xf000
	s_add_u32 s0, s0, s2
	s_addc_u32 s1, s1, 0
	s_add_u32 s2, s6, s26
	s_addc_u32 s3, s7, 0
	v_cmp_eq_u32_e32 vcc, 0, v109
	s_waitcnt vmcnt(15) lgkmcnt(3)
	v_mfma_f32_32x32x16_f16 v[2:17], v[18:21], v[2:5], 0
	s_waitcnt lgkmcnt(1)
	v_mfma_f32_32x32x16_f16 v[18:33], v[18:21], v[22:25], 0
	s_waitcnt vmcnt(14)
	v_mfma_f32_32x32x16_f16 v[2:17], v[34:37], v[98:101], v[2:17]
	s_waitcnt lgkmcnt(0)
	v_mfma_f32_32x32x16_f16 v[18:33], v[34:37], v[102:105], v[18:33]
	ds_read_b128 v[34:37], v113 offset:64
	ds_read_b128 v[98:101], v113 offset:96
	s_waitcnt vmcnt(13) lgkmcnt(1)
	v_mfma_f32_32x32x16_f16 v[2:17], v[38:41], v[34:37], v[2:17]
	ds_read_b128 v[34:37], v113 offset:16960
	ds_read_b128 v[102:105], v113 offset:16992
	s_waitcnt lgkmcnt(1)
	v_mfma_f32_32x32x16_f16 v[18:33], v[38:41], v[34:37], v[18:33]
	ds_read_b128 v[34:37], v113 offset:128
	ds_read_b128 v[38:41], v113 offset:160
	s_waitcnt vmcnt(12)
	v_mfma_f32_32x32x16_f16 v[2:17], v[42:45], v[98:101], v[2:17]
	s_waitcnt lgkmcnt(2)
	v_mfma_f32_32x32x16_f16 v[18:33], v[42:45], v[102:105], v[18:33]
	s_waitcnt vmcnt(11) lgkmcnt(1)
	v_mfma_f32_32x32x16_f16 v[2:17], v[46:49], v[34:37], v[2:17]
	ds_read_b128 v[34:37], v113 offset:17024
	ds_read_b128 v[42:45], v113 offset:17056
	s_waitcnt lgkmcnt(1)
	v_mfma_f32_32x32x16_f16 v[18:33], v[46:49], v[34:37], v[18:33]
	s_waitcnt vmcnt(10)
	v_mfma_f32_32x32x16_f16 v[2:17], v[50:53], v[38:41], v[2:17]
	ds_read_b128 v[34:37], v113 offset:192
	ds_read_b128 v[38:41], v113 offset:224
	s_waitcnt lgkmcnt(2)
	v_mfma_f32_32x32x16_f16 v[18:33], v[50:53], v[42:45], v[18:33]
	s_waitcnt vmcnt(9) lgkmcnt(1)
	v_mfma_f32_32x32x16_f16 v[2:17], v[54:57], v[34:37], v[2:17]
	ds_read_b128 v[34:37], v113 offset:17088
	ds_read_b128 v[42:45], v113 offset:17120
	s_waitcnt lgkmcnt(1)
	v_mfma_f32_32x32x16_f16 v[18:33], v[54:57], v[34:37], v[18:33]
	s_waitcnt vmcnt(8)
	v_mfma_f32_32x32x16_f16 v[2:17], v[58:61], v[38:41], v[2:17]
	ds_read_b128 v[34:37], v113 offset:256
	ds_read_b128 v[38:41], v113 offset:288
	s_waitcnt lgkmcnt(2)
	v_mfma_f32_32x32x16_f16 v[18:33], v[58:61], v[42:45], v[18:33]
	s_waitcnt vmcnt(7) lgkmcnt(1)
	v_mfma_f32_32x32x16_f16 v[2:17], v[62:65], v[34:37], v[2:17]
	ds_read_b128 v[34:37], v113 offset:17152
	ds_read_b128 v[42:45], v113 offset:17184
	s_waitcnt lgkmcnt(1)
	v_mfma_f32_32x32x16_f16 v[18:33], v[62:65], v[34:37], v[18:33]
	s_waitcnt vmcnt(6)
	v_mfma_f32_32x32x16_f16 v[2:17], v[66:69], v[38:41], v[2:17]
	ds_read_b128 v[34:37], v113 offset:320
	ds_read_b128 v[38:41], v113 offset:352
	s_waitcnt lgkmcnt(2)
	v_mfma_f32_32x32x16_f16 v[18:33], v[66:69], v[42:45], v[18:33]
	s_waitcnt vmcnt(5) lgkmcnt(1)
	v_mfma_f32_32x32x16_f16 v[2:17], v[70:73], v[34:37], v[2:17]
	ds_read_b128 v[34:37], v113 offset:17216
	ds_read_b128 v[42:45], v113 offset:17248
	s_waitcnt lgkmcnt(1)
	v_mfma_f32_32x32x16_f16 v[18:33], v[70:73], v[34:37], v[18:33]
	s_waitcnt vmcnt(4)
	v_mfma_f32_32x32x16_f16 v[2:17], v[74:77], v[38:41], v[2:17]
	ds_read_b128 v[34:37], v113 offset:384
	ds_read_b128 v[38:41], v113 offset:416
	s_waitcnt lgkmcnt(2)
	v_mfma_f32_32x32x16_f16 v[18:33], v[74:77], v[42:45], v[18:33]
	s_waitcnt vmcnt(3) lgkmcnt(1)
	v_mfma_f32_32x32x16_f16 v[2:17], v[78:81], v[34:37], v[2:17]
	ds_read_b128 v[34:37], v113 offset:17280
	ds_read_b128 v[42:45], v113 offset:17312
	s_waitcnt lgkmcnt(1)
	v_mfma_f32_32x32x16_f16 v[18:33], v[78:81], v[34:37], v[18:33]
	s_waitcnt vmcnt(2)
	v_mfma_f32_32x32x16_f16 v[2:17], v[86:89], v[38:41], v[2:17]
	ds_read_b128 v[34:37], v113 offset:448
	ds_read_b128 v[38:41], v113 offset:480
	s_waitcnt lgkmcnt(2)
	v_mfma_f32_32x32x16_f16 v[18:33], v[86:89], v[42:45], v[18:33]
	s_waitcnt vmcnt(1) lgkmcnt(1)
	v_mfma_f32_32x32x16_f16 v[2:17], v[90:93], v[34:37], v[2:17]
	ds_read_b128 v[34:37], v113 offset:17344
	ds_read_b128 v[42:45], v113 offset:17376
	s_waitcnt lgkmcnt(0)
	s_barrier
	v_mfma_f32_32x32x16_f16 v[18:33], v[90:93], v[34:37], v[18:33]
	v_lshrrev_b32_e32 v34, 3, v0
	v_and_b32_e32 v34, 4, v34
	v_lshl_or_b32 v34, v107, 5, v34
	v_mul_u32_u24_e32 v34, 0x110, v34
	v_lshl_add_u32 v34, v112, 2, v34
	s_waitcnt vmcnt(0)
	v_mfma_f32_32x32x16_f16 v[2:17], v[94:97], v[38:41], v[2:17]
	v_mfma_f32_32x32x16_f16 v[18:33], v[94:97], v[42:45], v[18:33]
	s_nop 11
	ds_write2_b32 v34, v2, v18 offset1:32
	ds_write2_b32 v34, v3, v19 offset0:68 offset1:100
	ds_write2_b32 v34, v4, v20 offset0:136 offset1:168
	ds_write2_b32 v34, v5, v21 offset0:204 offset1:236
	v_add_u32_e32 v2, 0x800, v34
	ds_write2_b32 v2, v6, v22 offset0:32 offset1:64
	ds_write2_b32 v2, v7, v23 offset0:100 offset1:132
	ds_write2_b32 v2, v8, v24 offset0:168 offset1:200
	v_add_u32_e32 v2, 0xa00, v34
	ds_write2_b32 v2, v9, v25 offset0:108 offset1:140
	v_add_u32_e32 v2, 0x1000, v34
	ds_write2_b32 v2, v10, v26 offset0:64 offset1:96
	ds_write2_b32 v2, v11, v27 offset0:132 offset1:164
	ds_write2_b32 v2, v12, v28 offset0:200 offset1:232
	v_add_u32_e32 v2, 0x1400, v34
	ds_write2_b32 v2, v13, v29 offset0:12 offset1:44
	v_add_u32_e32 v2, 0x1800, v34
	v_and_b32_e32 v5, 60, v84
	v_mov_b32_e32 v8, 0x8800
	ds_write2_b32 v2, v14, v30 offset0:96 offset1:128
	ds_write2_b32 v2, v15, v31 offset0:164 offset1:196
	v_add_u32_e32 v2, 0x1a00, v34
	v_lshlrev_b32_e32 v6, 2, v5
	v_lshl_or_b32 v8, v82, 1, v8
	ds_write2_b32 v2, v16, v32 offset0:104 offset1:136
	v_add_u32_e32 v2, 0x1c00, v34
	v_add_u32_e32 v7, v6, v111
	v_mad_u32_u24 v9, v5, s4, v8
	ds_write2_b32 v2, v17, v33 offset0:44 offset1:76
	s_waitcnt lgkmcnt(0)
	s_barrier
	ds_read_b128 v[10:13], v7
	ds_read_u16 v14, v9
	ds_read_u16 v15, v9 offset:272
	ds_read_u16 v16, v9 offset:544
	ds_read_u16 v9, v9 offset:816
	v_or_b32_e32 v2, s20, v5
	v_mul_u32_u24_e32 v7, 0x110, v5
	s_waitcnt lgkmcnt(3)
	v_cvt_f32_f16_e32 v5, v14
	s_waitcnt lgkmcnt(2)
	v_cvt_f32_f16_e32 v14, v15
	s_waitcnt lgkmcnt(1)
	v_cvt_f32_f16_e32 v15, v16
	s_waitcnt lgkmcnt(0)
	v_cvt_f32_f16_e32 v9, v9
	v_or_b32_e32 v4, s8, v82
	v_ashrrev_i32_e32 v3, 31, v2
	v_add_f32_e32 v16, v10, v5
	v_ashrrev_i32_e32 v5, 31, v4
	v_lshl_add_u64 v[2:3], v[2:3], 1, s[2:3]
	v_add_f32_e32 v14, v11, v14
	v_add_f32_e32 v15, v12, v15
	v_add_f32_e32 v9, v13, v9
	v_lshlrev_b64 v[12:13], 13, v[4:5]
	v_cvt_pk_f16_f32 v11, v15, v9
	v_cvt_pk_f16_f32 v10, v16, v14
	v_lshl_add_u64 v[12:13], v[2:3], 0, v[12:13]
	global_store_dwordx2 v[12:13], v[10:11], off
	v_mul_f32_e32 v11, v14, v14
	v_add_f32_e32 v10, v16, v14
	v_fmac_f32_e32 v11, v16, v16
	v_add_f32_e32 v10, v15, v10
	v_fmac_f32_e32 v11, v15, v15
	v_add_f32_e32 v10, v9, v10
	v_fmac_f32_e32 v11, v9, v9
	s_nop 0
	v_add_f32_dpp v9, v10, v10 quad_perm:[1,0,3,2] row_mask:0xf bank_mask:0xf bound_ctrl:1
	v_add_f32_dpp v11, v11, v11 quad_perm:[1,0,3,2] row_mask:0xf bank_mask:0xf bound_ctrl:1
	s_nop 0
	v_add_f32_dpp v9, v9, v9 quad_perm:[2,3,0,1] row_mask:0xf bank_mask:0xf bound_ctrl:1
	v_add_f32_dpp v11, v11, v11 quad_perm:[2,3,0,1] row_mask:0xf bank_mask:0xf bound_ctrl:1
	s_nop 0
	v_add_f32_dpp v9, v9, v9 row_half_mirror row_mask:0xf bank_mask:0xf bound_ctrl:1
	v_add_f32_dpp v11, v11, v11 row_half_mirror row_mask:0xf bank_mask:0xf bound_ctrl:1
	s_nop 0
	v_mov_b32_dpp v10, v9 row_mirror row_mask:0xf bank_mask:0xf bound_ctrl:1
	v_mov_b32_dpp v12, v11 row_mirror row_mask:0xf bank_mask:0xf bound_ctrl:1
	s_and_saveexec_b64 s[2:3], vcc
	s_cbranch_execz .LBB3_4
	v_lshl_add_u64 v[4:5], v[4:5], 2, s[0:1]
	v_add_f32_e32 v9, v9, v10
	v_add_f32_e32 v11, v11, v12
	global_atomic_add_f32 v[4:5], v9, off
	global_atomic_add_f32 v[4:5], v11, off offset:2048

	.amdhsa_kernel _Z7k_scan3PKjPKfS2_S2_S2_S2_PKDF16_S4_S4_7EpiArgs
		.amdhsa_group_segment_fixed_size 60416
		.amdhsa_private_segment_fixed_size 0
		.amdhsa_kernarg_size 144
		.amdhsa_user_sgpr_count 2
		.amdhsa_user_sgpr_dispatch_ptr 0
		.amdhsa_user_sgpr_queue_ptr 0
		.amdhsa_user_sgpr_kernarg_segment_ptr 1
		.amdhsa_user_sgpr_dispatch_id 0
		.amdhsa_user_sgpr_kernarg_preload_length 0
		.amdhsa_user_sgpr_kernarg_preload_offset 0
		.amdhsa_user_sgpr_private_segment_size 0
		.amdhsa_uses_dynamic_stack 0
		.amdhsa_enable_private_segment 0
		.amdhsa_system_sgpr_workgroup_id_x 1
		.amdhsa_system_sgpr_workgroup_id_y 1
		.amdhsa_system_sgpr_workgroup_id_z 0
		.amdhsa_system_sgpr_workgroup_info 0
		.amdhsa_system_vgpr_workitem_id 0
		.amdhsa_next_free_vgpr 236
		.amdhsa_next_free_sgpr 96
		.amdhsa_accum_offset 236
		.amdhsa_reserve_vcc 1
		.amdhsa_float_round_mode_32 0
		.amdhsa_float_round_mode_16_64 0
		.amdhsa_float_denorm_mode_32 3
		.amdhsa_float_denorm_mode_16_64 3
		.amdhsa_dx10_clamp 1
		.amdhsa_ieee_mode 1
		.amdhsa_fp16_overflow 0
		.amdhsa_tg_split 0
		.amdhsa_exception_fp_ieee_invalid_op 0
		.amdhsa_exception_fp_denorm_src 0
		.amdhsa_exception_fp_ieee_div_zero 0
		.amdhsa_exception_fp_ieee_overflow 0
		.amdhsa_exception_fp_ieee_underflow 0
		.amdhsa_exception_fp_ieee_inexact 0
		.amdhsa_exception_int_div_zero 0
	.end_amdhsa_kernel

.LBB4_16:
	s_or_b64 exec, exec, s[0:1]
	v_or_b32_e32 v1, 0x800, v10
	v_and_b32_e32 v10, 56, v10
	v_lshrrev_b32_e32 v11, 3, v0
	v_lshlrev_b32_e32 v10, 2, v10
	s_movk_i32 s0, 0x120
	s_waitcnt vmcnt(1)
	v_cvt_f32_f16_sdwa v12, v6 dst_sel:DWORD dst_unused:UNUSED_PAD src0_sel:WORD_1
	v_cvt_f32_f16_e32 v6, v6
	v_lshrrev_b32_e32 v1, 6, v1
	v_mad_u32_u24 v11, v11, s0, v10
	v_cvt_f32_f16_sdwa v13, v7 dst_sel:DWORD dst_unused:UNUSED_PAD src0_sel:WORD_1
	v_cvt_f32_f16_e32 v7, v7
	v_mad_u32_u24 v1, v1, s0, v10
	s_mul_i32 s0, s2, 49
	v_cvt_f32_f16_sdwa v14, v8 dst_sel:DWORD dst_unused:UNUSED_PAD src0_sel:WORD_1
	v_cvt_f32_f16_e32 v8, v8
	s_ashr_i32 s1, s0, 31
	v_cvt_f32_f16_sdwa v15, v9 dst_sel:DWORD dst_unused:UNUSED_PAD src0_sel:WORD_1
	v_cvt_f32_f16_e32 v9, v9
	s_lshl_b64 s[0:1], s[0:1], 2
	ds_write2_b32 v11, v6, v12 offset0:219 offset1:220
	ds_write2_b32 v11, v7, v13 offset0:221 offset1:222
	ds_write2_b32 v11, v8, v14 offset0:223 offset1:224
	ds_write2_b32 v11, v9, v15 offset0:225 offset1:226
	s_waitcnt vmcnt(0)
	v_cvt_f32_f16_sdwa v6, v2 dst_sel:DWORD dst_unused:UNUSED_PAD src0_sel:WORD_1
	v_cvt_f32_f16_e32 v2, v2
	s_waitcnt lgkmcnt(0)
	s_add_u32 s56, s8, s0
	v_cvt_f32_f16_sdwa v7, v3 dst_sel:DWORD dst_unused:UNUSED_PAD src0_sel:WORD_1
	v_cvt_f32_f16_e32 v3, v3
	s_addc_u32 s57, s9, s1
	v_lshrrev_b32_e32 v50, 5, v0
	s_lshl_b64 s[0:1], s[2:3], 2
	v_cvt_f32_f16_sdwa v8, v4 dst_sel:DWORD dst_unused:UNUSED_PAD src0_sel:WORD_1
	v_cvt_f32_f16_e32 v4, v4
	v_and_b32_e32 v51, 31, v0
	v_mul_u32_u24_e32 v0, 0x900, v50
	s_add_u32 s0, s10, s0
	v_cvt_f32_f16_sdwa v9, v5 dst_sel:DWORD dst_unused:UNUSED_PAD src0_sel:WORD_1
	v_cvt_f32_f16_e32 v5, v5
	v_lshl_or_b32 v52, v51, 3, v0
	s_addc_u32 s1, s11, s1
	ds_write2_b32 v1, v2, v6 offset0:219 offset1:220
	ds_write2_b32 v1, v3, v7 offset0:221 offset1:222
	ds_write2_b32 v1, v4, v8 offset0:223 offset1:224
	ds_write2_b32 v1, v5, v9 offset0:225 offset1:226
	s_waitcnt lgkmcnt(0)
	s_barrier
	ds_read2_b64 v[8:11], v52 offset1:1
	ds_read2_b64 v[54:57], v52 offset0:2 offset1:3
	s_load_dword s64, s[0:1], 0x0
	ds_read2_b64 v[24:27], v52 offset0:36 offset1:37
	ds_read2_b64 v[16:19], v52 offset0:38 offset1:39
	s_load_dword s76, s[56:57], 0x58
	s_load_dwordx2 s[42:43], s[56:57], 0x58
	s_load_dwordx2 s[36:37], s[56:57], 0x5c
	s_load_dwordx2 s[44:45], s[56:57], 0x50
	s_load_dwordx4 s[16:19], s[56:57], 0x0
	s_load_dword s66, s[56:57], 0x8
	s_load_dwordx2 s[20:21], s[56:57], 0xc
	s_load_dwordx2 s[62:63], s[56:57], 0x10
	s_load_dwordx2 s[60:61], s[56:57], 0x14
	s_load_dwordx2 s[58:59], s[56:57], 0x18
	s_load_dwordx2 s[52:53], s[56:57], 0x1c
	s_load_dwordx2 s[54:55], s[56:57], 0x20
	s_load_dwordx2 s[50:51], s[56:57], 0x24
	s_load_dwordx2 s[46:47], s[56:57], 0x28
	s_load_dwordx2 s[48:49], s[56:57], 0x2c
	s_load_dwordx8 s[8:15], s[56:57], 0x30
	ds_read2_b64 v[44:47], v52 offset0:72 offset1:73
	ds_read2_b64 v[40:43], v52 offset0:74 offset1:75
	ds_read2_b64 v[36:39], v52 offset0:108 offset1:109
	ds_read2_b64 v[32:35], v52 offset0:110 offset1:111
	s_load_dwordx2 s[40:41], s[56:57], 0x60
	s_load_dwordx2 s[38:39], s[56:57], 0x64
	s_load_dword s22, s[56:57], 0xa0
	s_load_dwordx2 s[34:35], s[56:57], 0x98
	s_load_dwordx4 s[24:27], s[56:57], 0x88
	s_load_dwordx8 s[0:7], s[56:57], 0x68
	s_waitcnt lgkmcnt(0)
	v_mov_b64_e32 v[48:49], s[64:65]
	v_pk_fma_f32 v[12:13], v[8:9], s[16:17], v[48:49] op_sel_hi:[1,0,0]
	v_pk_mov_b32 v[8:9], v[8:9], v[10:11] op_sel:[1,0]
	v_pk_mov_b32 v[58:59], v[44:45], v[46:47] op_sel:[1,0]
	v_pk_fma_f32 v[8:9], v[8:9], s[16:17], v[12:13] op_sel:[0,1,0]
	s_mov_b32 s64, s11
	v_pk_fma_f32 v[8:9], v[10:11], s[66:67], v[8:9] op_sel_hi:[1,0,1]
	v_pk_mov_b32 v[10:11], v[10:11], v[54:55] op_sel:[1,0]
	s_mov_b32 s68, s13
	v_pk_fma_f32 v[8:9], v[10:11], s[18:19], v[8:9] op_sel:[0,1,0]
	v_pk_mov_b32 v[10:11], v[54:55], v[56:57] op_sel:[1,0]
	v_pk_fma_f32 v[8:9], v[54:55], s[20:21], v[8:9] op_sel:[0,1,0]
	ds_read2_b64 v[28:31], v52 offset0:144 offset1:145
	ds_read2_b64 v[20:23], v52 offset0:146 offset1:147
	ds_read2_b64 v[4:7], v52 offset0:180 offset1:181
	ds_read2_b64 v[0:3], v52 offset0:182 offset1:183
	v_pk_fma_f32 v[54:55], v[10:11], s[62:63], v[8:9] op_sel:[0,1,0]
	s_mov_b32 s70, s3
	v_pk_fma_f32 v[54:55], v[56:57], s[60:61], v[54:55] op_sel:[0,1,0]
	v_pk_mov_b32 v[56:57], v[24:25], v[26:27] op_sel:[1,0]
	v_pk_fma_f32 v[54:55], v[24:25], s[58:59], v[54:55] op_sel:[0,1,0]
	v_pk_fma_f32 v[24:25], v[24:25], s[16:17], v[48:49] op_sel_hi:[1,0,0]
	v_pk_fma_f32 v[54:55], v[56:57], s[52:53], v[54:55] op_sel:[0,1,0]
	v_pk_fma_f32 v[24:25], v[56:57], s[16:17], v[24:25] op_sel:[0,1,0]
	v_pk_fma_f32 v[54:55], v[26:27], s[54:55], v[54:55] op_sel:[0,1,0]
	v_pk_mov_b32 v[56:57], v[26:27], v[16:17] op_sel:[1,0]
	v_pk_fma_f32 v[24:25], v[26:27], s[66:67], v[24:25] op_sel_hi:[1,0,1]
	v_pk_fma_f32 v[54:55], v[56:57], s[50:51], v[54:55] op_sel:[0,1,0]
	v_pk_fma_f32 v[24:25], v[56:57], s[18:19], v[24:25] op_sel:[0,1,0]
	v_pk_fma_f32 v[54:55], v[16:17], s[46:47], v[54:55] op_sel:[0,1,0]
	v_pk_mov_b32 v[26:27], v[16:17], v[18:19] op_sel:[1,0]
	v_pk_fma_f32 v[16:17], v[16:17], s[20:21], v[24:25] op_sel:[0,1,0]
	v_pk_fma_f32 v[54:55], v[26:27], s[48:49], v[54:55] op_sel:[0,1,0]
	v_pk_fma_f32 v[16:17], v[26:27], s[62:63], v[16:17] op_sel:[0,1,0]
	v_pk_fma_f32 v[54:55], v[18:19], s[8:9], v[54:55] op_sel:[0,1,0]
	v_pk_fma_f32 v[16:17], v[18:19], s[60:61], v[16:17] op_sel:[0,1,0]
	v_pk_fma_f32 v[54:55], v[44:45], s[10:11], v[54:55] op_sel_hi:[1,0,1]
	v_pk_fma_f32 v[16:17], v[44:45], s[58:59], v[16:17] op_sel:[0,1,0]
	v_pk_fma_f32 v[54:55], v[58:59], s[64:65], v[54:55] op_sel_hi:[1,0,1]
	v_pk_fma_f32 v[56:57], v[58:59], s[52:53], v[16:17] op_sel:[0,1,0]
	v_pk_fma_f32 v[16:17], v[44:45], s[16:17], v[48:49] op_sel_hi:[1,0,0]
	v_pk_fma_f32 v[54:55], v[46:47], s[12:13], v[54:55] op_sel_hi:[1,0,1]
	v_pk_fma_f32 v[44:45], v[58:59], s[16:17], v[16:17] op_sel:[0,1,0]
	v_pk_fma_f32 v[56:57], v[46:47], s[54:55], v[56:57] op_sel:[0,1,0]
	v_pk_fma_f32 v[44:45], v[46:47], s[66:67], v[44:45] op_sel_hi:[1,0,1]
	v_pk_mov_b32 v[46:47], v[46:47], v[40:41] op_sel:[1,0]
	v_pk_mov_b32 v[58:59], v[40:41], v[42:43] op_sel:[1,0]
	v_pk_fma_f32 v[54:55], v[46:47], s[68:69], v[54:55] op_sel_hi:[1,0,1]
	v_pk_fma_f32 v[56:57], v[46:47], s[50:51], v[56:57] op_sel:[0,1,0]
	v_pk_fma_f32 v[44:45], v[46:47], s[18:19], v[44:45] op_sel:[0,1,0]
	v_pk_fma_f32 v[54:55], v[40:41], s[14:15], v[54:55] op_sel_hi:[1,0,1]
	s_mov_b32 s66, s15
	v_pk_fma_f32 v[56:57], v[40:41], s[46:47], v[56:57] op_sel:[0,1,0]
	v_pk_fma_f32 v[40:41], v[40:41], s[20:21], v[44:45] op_sel:[0,1,0]
	v_pk_fma_f32 v[54:55], v[58:59], s[66:67], v[54:55] op_sel_hi:[1,0,1]
	v_pk_fma_f32 v[40:41], v[58:59], s[62:63], v[40:41] op_sel:[0,1,0]
	v_pk_fma_f32 v[54:55], v[42:43], s[44:45], v[54:55] op_sel_hi:[1,0,1]
	v_pk_fma_f32 v[40:41], v[42:43], s[60:61], v[40:41] op_sel:[0,1,0]
	v_pk_fma_f32 v[54:55], v[36:37], s[44:45], v[54:55] op_sel:[0,1,0]
	v_pk_mov_b32 v[46:47], v[36:37], v[38:39] op_sel:[1,0]
	v_pk_fma_f32 v[40:41], v[36:37], s[58:59], v[40:41] op_sel:[0,1,0]
	v_pk_fma_f32 v[54:55], v[46:47], s[76:77], v[54:55] op_sel_hi:[1,0,1]
	v_pk_fma_f32 v[40:41], v[46:47], s[52:53], v[40:41] op_sel:[0,1,0]
	v_pk_fma_f32 v[54:55], v[38:39], s[42:43], v[54:55] op_sel:[0,1,0]
	v_pk_mov_b32 v[44:45], v[38:39], v[32:33] op_sel:[1,0]
	v_pk_fma_f32 v[40:41], v[38:39], s[54:55], v[40:41] op_sel:[0,1,0]
	v_pk_fma_f32 v[56:57], v[58:59], s[48:49], v[56:57] op_sel:[0,1,0]
	v_pk_fma_f32 v[54:55], v[44:45], s[36:37], v[54:55] op_sel:[0,1,0]
	v_pk_fma_f32 v[40:41], v[44:45], s[50:51], v[40:41] op_sel:[0,1,0]
	v_pk_fma_f32 v[54:55], v[32:33], s[40:41], v[54:55] op_sel:[0,1,0]
	v_pk_fma_f32 v[56:57], v[42:43], s[8:9], v[56:57] op_sel:[0,1,0]
	v_pk_mov_b32 v[42:43], v[32:33], v[34:35] op_sel:[1,0]
	v_pk_fma_f32 v[40:41], v[32:33], s[46:47], v[40:41] op_sel:[0,1,0]
	v_pk_fma_f32 v[54:55], v[42:43], s[38:39], v[54:55] op_sel:[0,1,0]
	v_pk_fma_f32 v[40:41], v[42:43], s[48:49], v[40:41] op_sel:[0,1,0]
	v_pk_fma_f32 v[54:55], v[34:35], s[0:1], v[54:55] op_sel:[0,1,0]
	v_pk_fma_f32 v[56:57], v[36:37], s[10:11], v[56:57] op_sel_hi:[1,0,1]
	v_pk_fma_f32 v[36:37], v[36:37], s[16:17], v[48:49] op_sel_hi:[1,0,0]
	v_pk_fma_f32 v[40:41], v[34:35], s[8:9], v[40:41] op_sel:[0,1,0]
	s_waitcnt lgkmcnt(3)
	v_pk_fma_f32 v[54:55], v[28:29], s[2:3], v[54:55] op_sel_hi:[1,0,1]
	v_pk_fma_f32 v[56:57], v[46:47], s[64:65], v[56:57] op_sel_hi:[1,0,1]
	v_pk_fma_f32 v[36:37], v[46:47], s[16:17], v[36:37] op_sel:[0,1,0]
	v_pk_mov_b32 v[46:47], v[28:29], v[30:31] op_sel:[1,0]
	v_pk_fma_f32 v[40:41], v[28:29], s[10:11], v[40:41] op_sel_hi:[1,0,1]
	v_pk_fma_f32 v[54:55], v[46:47], s[70:71], v[54:55] op_sel_hi:[1,0,1]
	v_pk_fma_f32 v[40:41], v[46:47], s[64:65], v[40:41] op_sel_hi:[1,0,1]
	v_pk_fma_f32 v[54:55], v[30:31], s[4:5], v[54:55] op_sel_hi:[1,0,1]
	v_pk_fma_f32 v[56:57], v[38:39], s[12:13], v[56:57] op_sel_hi:[1,0,1]
	s_waitcnt lgkmcnt(2)
	v_pk_mov_b32 v[58:59], v[30:31], v[20:21] op_sel:[1,0]
	s_mov_b32 s72, s5
	v_pk_fma_f32 v[40:41], v[30:31], s[12:13], v[40:41] op_sel_hi:[1,0,1]
	v_pk_fma_f32 v[36:37], v[38:39], s[18:19], v[36:37] op_sel_hi:[1,0,1]
	v_pk_fma_f32 v[38:39], v[58:59], s[72:73], v[54:55] op_sel_hi:[1,0,1]
	v_pk_fma_f32 v[56:57], v[44:45], s[68:69], v[56:57] op_sel_hi:[1,0,1]
	v_pk_fma_f32 v[40:41], v[58:59], s[68:69], v[40:41] op_sel_hi:[1,0,1]
	v_pk_fma_f32 v[38:39], v[20:21], s[6:7], v[38:39] op_sel_hi:[1,0,1]
	v_pk_mov_b32 v[54:55], v[20:21], v[22:23] op_sel:[1,0]
	s_mov_b32 s74, s7
	v_pk_fma_f32 v[56:57], v[32:33], s[14:15], v[56:57] op_sel_hi:[1,0,1]
	v_pk_fma_f32 v[40:41], v[20:21], s[14:15], v[40:41] op_sel_hi:[1,0,1]
	v_pk_fma_f32 v[38:39], v[54:55], s[74:75], v[38:39] op_sel_hi:[1,0,1]
	v_pk_fma_f32 v[56:57], v[42:43], s[66:67], v[56:57] op_sel_hi:[1,0,1]
	v_pk_fma_f32 v[40:41], v[54:55], s[66:67], v[40:41] op_sel_hi:[1,0,1]
	v_pk_fma_f32 v[38:39], v[22:23], s[24:25], v[38:39] op_sel_hi:[1,0,1]
	v_pk_fma_f32 v[56:57], v[34:35], s[44:45], v[56:57] op_sel_hi:[1,0,1]
	v_pk_fma_f32 v[40:41], v[22:23], s[44:45], v[40:41] op_sel_hi:[1,0,1]
	s_waitcnt lgkmcnt(1)
	v_pk_fma_f32 v[38:39], v[4:5], s[24:25], v[38:39] op_sel:[0,1,0]
	v_pk_fma_f32 v[36:37], v[44:45], s[20:21], v[36:37] op_sel_hi:[1,0,1]
	v_pk_mov_b32 v[44:45], v[4:5], v[6:7] op_sel:[1,0]
	v_pk_fma_f32 v[56:57], v[28:29], s[44:45], v[56:57] op_sel:[0,1,0]
	v_pk_fma_f32 v[40:41], v[4:5], s[44:45], v[40:41] op_sel:[0,1,0]
	v_pk_fma_f32 v[38:39], v[44:45], s[26:27], v[38:39] op_sel_hi:[1,0,1]
	v_pk_fma_f32 v[56:57], v[46:47], s[76:77], v[56:57] op_sel_hi:[1,0,1]
	v_pk_fma_f32 v[60:61], v[44:45], s[76:77], v[40:41] op_sel_hi:[1,0,1]
	s_mov_b32 s76, s27
	v_pk_fma_f32 v[38:39], v[6:7], s[76:77], v[38:39] op_sel_hi:[1,0,1]
	v_pk_fma_f32 v[32:33], v[32:33], s[62:63], v[36:37] op_sel_hi:[1,0,1]
	s_waitcnt lgkmcnt(0)
	v_pk_mov_b32 v[36:37], v[6:7], v[0:1] op_sel:[1,0]
	v_pk_fma_f32 v[32:33], v[42:43], s[60:61], v[32:33] op_sel_hi:[1,0,1]
	v_pk_fma_f32 v[38:39], v[36:37], s[34:35], v[38:39] op_sel_hi:[1,0,1]
	v_pk_fma_f32 v[40:41], v[34:35], s[58:59], v[32:33] op_sel_hi:[1,0,1]
	v_pk_fma_f32 v[38:39], v[0:1], s[34:35], v[38:39] op_sel:[0,1,0]
	v_pk_mov_b32 v[34:35], v[0:1], v[2:3] op_sel:[1,0]
	ds_read2_b64 v[12:15], v52 offset0:216 offset1:217
	ds_read2_b64 v[8:11], v52 offset0:218 offset1:219
	v_pk_fma_f32 v[32:33], v[34:35], s[22:23], v[38:39] op_sel_hi:[1,0,1]
	v_pk_fma_f32 v[38:39], v[28:29], s[52:53], v[40:41] op_sel_hi:[1,0,1]
	v_pk_fma_f32 v[28:29], v[28:29], s[16:17], v[48:49] op_sel_hi:[1,0,0]
	v_pk_fma_f32 v[40:41], v[30:31], s[42:43], v[56:57] op_sel:[0,1,0]
	v_pk_fma_f32 v[38:39], v[46:47], s[54:55], v[38:39] op_sel_hi:[1,0,1]
	v_pk_fma_f32 v[28:29], v[46:47], s[16:17], v[28:29] op_sel:[0,1,0]
	v_pk_fma_f32 v[40:41], v[58:59], s[36:37], v[40:41] op_sel:[0,1,0]
	v_pk_fma_f32 v[42:43], v[30:31], s[50:51], v[38:39] op_sel_hi:[1,0,1]
	v_pk_fma_f32 v[28:29], v[30:31], s[18:19], v[28:29] op_sel_hi:[1,0,1]
	v_pk_fma_f32 v[40:41], v[20:21], s[40:41], v[40:41] op_sel:[0,1,0]
	v_pk_fma_f32 v[42:43], v[58:59], s[46:47], v[42:43] op_sel_hi:[1,0,1]
	v_pk_fma_f32 v[40:41], v[54:55], s[38:39], v[40:41] op_sel:[0,1,0]
	v_pk_fma_f32 v[28:29], v[58:59], s[20:21], v[28:29] op_sel_hi:[1,0,1]
	v_pk_fma_f32 v[40:41], v[22:23], s[0:1], v[40:41] op_sel:[0,1,0]
	v_pk_fma_f32 v[42:43], v[20:21], s[48:49], v[42:43] op_sel_hi:[1,0,1]
	v_pk_fma_f32 v[20:21], v[20:21], s[62:63], v[28:29] op_sel_hi:[1,0,1]
	v_pk_fma_f32 v[40:41], v[4:5], s[2:3], v[40:41] op_sel_hi:[1,0,1]
	v_pk_fma_f32 v[42:43], v[54:55], s[8:9], v[42:43] op_sel_hi:[1,0,1]
	v_pk_fma_f32 v[20:21], v[54:55], s[60:61], v[20:21] op_sel_hi:[1,0,1]
	v_pk_fma_f32 v[54:55], v[6:7], s[42:43], v[60:61] op_sel:[0,1,0]
	v_pk_fma_f32 v[40:41], v[44:45], s[70:71], v[40:41] op_sel_hi:[1,0,1]
	v_pk_fma_f32 v[54:55], v[36:37], s[36:37], v[54:55] op_sel:[0,1,0]
	v_pk_fma_f32 v[40:41], v[6:7], s[4:5], v[40:41] op_sel_hi:[1,0,1]
	v_pk_fma_f32 v[54:55], v[0:1], s[40:41], v[54:55] op_sel:[0,1,0]
	v_pk_fma_f32 v[40:41], v[36:37], s[72:73], v[40:41] op_sel_hi:[1,0,1]
	v_pk_fma_f32 v[54:55], v[34:35], s[38:39], v[54:55] op_sel:[0,1,0]
	v_pk_fma_f32 v[40:41], v[0:1], s[6:7], v[40:41] op_sel_hi:[1,0,1]
	v_pk_fma_f32 v[54:55], v[2:3], s[0:1], v[54:55] op_sel:[0,1,0]
	s_waitcnt lgkmcnt(1)
	v_pk_mov_b32 v[46:47], v[12:13], v[14:15] op_sel:[1,0]
	v_pk_fma_f32 v[40:41], v[34:35], s[74:75], v[40:41] op_sel_hi:[1,0,1]
	v_pk_fma_f32 v[54:55], v[12:13], s[2:3], v[54:55] op_sel_hi:[1,0,1]
	v_pk_fma_f32 v[40:41], v[2:3], s[24:25], v[40:41] op_sel_hi:[1,0,1]
	v_pk_fma_f32 v[54:55], v[46:47], s[70:71], v[54:55] op_sel_hi:[1,0,1]
	s_waitcnt lgkmcnt(0)
	v_pk_mov_b32 v[38:39], v[14:15], v[8:9] op_sel:[1,0]
	v_pk_fma_f32 v[40:41], v[12:13], s[24:25], v[40:41] op_sel:[0,1,0]
	v_pk_fma_f32 v[54:55], v[14:15], s[4:5], v[54:55] op_sel_hi:[1,0,1]
	ds_read2_b64 v[24:27], v52 offset0:252 offset1:253
	ds_read2_b64 v[16:19], v52 offset0:254 offset1:255
	v_pk_fma_f32 v[40:41], v[46:47], s[26:27], v[40:41] op_sel_hi:[1,0,1]
	v_pk_fma_f32 v[54:55], v[38:39], s[72:73], v[54:55] op_sel_hi:[1,0,1]
	v_pk_mov_b32 v[30:31], v[8:9], v[10:11] op_sel:[1,0]
	v_pk_fma_f32 v[40:41], v[14:15], s[76:77], v[40:41] op_sel_hi:[1,0,1]
	v_pk_fma_f32 v[54:55], v[8:9], s[6:7], v[54:55] op_sel_hi:[1,0,1]
	v_pk_fma_f32 v[40:41], v[38:39], s[34:35], v[40:41] op_sel_hi:[1,0,1]
	v_pk_fma_f32 v[54:55], v[30:31], s[74:75], v[54:55] op_sel_hi:[1,0,1]
	v_pk_fma_f32 v[40:41], v[8:9], s[34:35], v[40:41] op_sel:[0,1,0]
	v_pk_fma_f32 v[54:55], v[10:11], s[24:25], v[54:55] op_sel_hi:[1,0,1]
	v_pk_fma_f32 v[56:57], v[30:31], s[22:23], v[40:41] op_sel_hi:[1,0,1]
	s_waitcnt lgkmcnt(1)
	v_pk_mov_b32 v[40:41], v[24:25], v[26:27] op_sel:[1,0]
	v_pk_fma_f32 v[42:43], v[22:23], s[8:9], v[42:43] op_sel:[0,1,0]
	v_pk_fma_f32 v[22:23], v[22:23], s[58:59], v[20:21] op_sel_hi:[1,0,1]
	v_pk_fma_f32 v[54:55], v[24:25], s[24:25], v[54:55] op_sel:[0,1,0]
	v_pk_fma_f32 v[42:43], v[4:5], s[10:11], v[42:43] op_sel_hi:[1,0,1]
	v_pk_fma_f32 v[54:55], v[40:41], s[26:27], v[54:55] op_sel_hi:[1,0,1]
	v_pk_fma_f32 v[22:23], v[4:5], s[52:53], v[22:23] op_sel_hi:[1,0,1]
	v_pk_fma_f32 v[4:5], v[4:5], s[16:17], v[48:49] op_sel_hi:[1,0,0]
	s_waitcnt lgkmcnt(0)
	v_pk_mov_b32 v[28:29], v[26:27], v[16:17] op_sel:[1,0]
	v_pk_fma_f32 v[54:55], v[26:27], s[76:77], v[54:55] op_sel_hi:[1,0,1]
	v_pk_fma_f32 v[42:43], v[44:45], s[64:65], v[42:43] op_sel_hi:[1,0,1]
	v_pk_fma_f32 v[22:23], v[44:45], s[54:55], v[22:23] op_sel_hi:[1,0,1]
	v_pk_fma_f32 v[4:5], v[44:45], s[16:17], v[4:5] op_sel:[0,1,0]
	v_pk_fma_f32 v[44:45], v[12:13], s[16:17], v[48:49] op_sel_hi:[1,0,0]
	v_pk_fma_f32 v[54:55], v[28:29], s[34:35], v[54:55] op_sel_hi:[1,0,1]
	v_pk_fma_f32 v[44:45], v[46:47], s[16:17], v[44:45] op_sel:[0,1,0]
	v_pk_mov_b32 v[20:21], v[16:17], v[18:19] op_sel:[1,0]
	v_pk_fma_f32 v[54:55], v[16:17], s[34:35], v[54:55] op_sel:[0,1,0]
	v_pk_fma_f32 v[44:45], v[14:15], s[18:19], v[44:45] op_sel_hi:[1,0,1]
	v_pk_fma_f32 v[58:59], v[20:21], s[22:23], v[54:55] op_sel_hi:[1,0,1]
	v_pk_fma_f32 v[54:55], v[38:39], s[20:21], v[44:45] op_sel_hi:[1,0,1]
	v_pk_fma_f32 v[44:45], v[24:25], s[16:17], v[48:49] op_sel_hi:[1,0,0]
	v_pk_fma_f32 v[4:5], v[6:7], s[18:19], v[4:5] op_sel_hi:[1,0,1]
	v_pk_fma_f32 v[44:45], v[40:41], s[16:17], v[44:45] op_sel:[0,1,0]
	v_pk_fma_f32 v[4:5], v[36:37], s[20:21], v[4:5] op_sel_hi:[1,0,1]
	v_pk_fma_f32 v[44:45], v[26:27], s[18:19], v[44:45] op_sel_hi:[1,0,1]
	v_pk_fma_f32 v[42:43], v[6:7], s[12:13], v[42:43] op_sel_hi:[1,0,1]
	v_pk_fma_f32 v[48:49], v[28:29], s[20:21], v[44:45] op_sel_hi:[1,0,1]
	s_load_dwordx8 s[16:23], s[56:57], 0xa0
	v_pk_fma_f32 v[6:7], v[6:7], s[50:51], v[22:23] op_sel_hi:[1,0,1]
	v_pk_fma_f32 v[22:23], v[36:37], s[68:69], v[42:43] op_sel_hi:[1,0,1]
	v_pk_fma_f32 v[6:7], v[36:37], s[46:47], v[6:7] op_sel_hi:[1,0,1]
	v_pk_fma_f32 v[22:23], v[0:1], s[14:15], v[22:23] op_sel_hi:[1,0,1]
	v_pk_fma_f32 v[6:7], v[0:1], s[48:49], v[6:7] op_sel_hi:[1,0,1]
	v_pk_fma_f32 v[0:1], v[0:1], s[62:63], v[4:5] op_sel_hi:[1,0,1]
	v_pk_fma_f32 v[22:23], v[34:35], s[66:67], v[22:23] op_sel_hi:[1,0,1]
	v_pk_fma_f32 v[6:7], v[34:35], s[8:9], v[6:7] op_sel_hi:[1,0,1]
	v_pk_fma_f32 v[0:1], v[34:35], s[60:61], v[0:1] op_sel_hi:[1,0,1]
	s_waitcnt lgkmcnt(0)
	v_pk_fma_f32 v[4:5], v[2:3], s[16:17], v[32:33] op_sel:[0,1,0]
	s_load_dword s78, s[56:57], 0xc0
	v_pk_fma_f32 v[22:23], v[2:3], s[44:45], v[22:23] op_sel_hi:[1,0,1]
	v_pk_fma_f32 v[6:7], v[2:3], s[8:9], v[6:7] op_sel:[0,1,0]
	v_pk_fma_f32 v[0:1], v[2:3], s[58:59], v[0:1] op_sel_hi:[1,0,1]
	v_pk_fma_f32 v[2:3], v[12:13], s[18:19], v[4:5] op_sel_hi:[1,0,1]
	s_mov_b32 s56, s19
	v_pk_fma_f32 v[2:3], v[46:47], s[56:57], v[2:3] op_sel_hi:[1,0,1]
	v_pk_fma_f32 v[4:5], v[8:9], s[62:63], v[54:55] op_sel_hi:[1,0,1]
	v_pk_fma_f32 v[54:55], v[14:15], s[20:21], v[2:3] op_sel_hi:[1,0,1]
	v_pk_fma_f32 v[2:3], v[12:13], s[44:45], v[22:23] op_sel:[0,1,0]
	v_pk_fma_f32 v[0:1], v[12:13], s[52:53], v[0:1] op_sel_hi:[1,0,1]
	v_pk_fma_f32 v[2:3], v[46:47], s[42:43], v[2:3] op_sel_hi:[1,0,1]
	v_pk_fma_f32 v[32:33], v[16:17], s[62:63], v[48:49] op_sel_hi:[1,0,1]
	v_pk_fma_f32 v[22:23], v[14:15], s[36:37], v[2:3] op_sel_hi:[1,0,1]
	v_pk_fma_f32 v[2:3], v[12:13], s[10:11], v[6:7] op_sel_hi:[1,0,1]
	v_pk_fma_f32 v[0:1], v[46:47], s[54:55], v[0:1] op_sel_hi:[1,0,1]
	v_pk_fma_f32 v[2:3], v[46:47], s[64:65], v[2:3] op_sel_hi:[1,0,1]
	v_pk_fma_f32 v[12:13], v[14:15], s[50:51], v[0:1] op_sel_hi:[1,0,1]
	v_pk_fma_f32 v[60:61], v[14:15], s[12:13], v[2:3] op_sel_hi:[1,0,1]
	v_pk_fma_f32 v[4:5], v[30:31], s[60:61], v[4:5] op_sel_hi:[1,0,1]
	v_pk_fma_f32 v[6:7], v[20:21], s[60:61], v[32:33] op_sel_hi:[1,0,1]
	s_mov_b32 s60, s21
	v_pk_fma_f32 v[14:15], v[38:39], s[60:61], v[54:55] op_sel_hi:[1,0,1]
	v_pk_fma_f32 v[22:23], v[38:39], s[40:41], v[22:23] op_sel_hi:[1,0,1]
	v_pk_fma_f32 v[32:33], v[38:39], s[68:69], v[60:61] op_sel_hi:[1,0,1]
	v_pk_fma_f32 v[12:13], v[38:39], s[46:47], v[12:13] op_sel_hi:[1,0,1]
	v_add_u32_e32 v44, 0x900, v52
	v_add_u32_e32 v45, 0x910, v52
	v_add_u32_e32 v53, 0xa20, v52
	v_add_u32_e32 v62, 0xa30, v52
	v_pk_fma_f32 v[14:15], v[8:9], s[22:23], v[14:15] op_sel_hi:[1,0,1]
	v_pk_fma_f32 v[22:23], v[8:9], s[38:39], v[22:23] op_sel_hi:[1,0,1]
	v_pk_fma_f32 v[32:33], v[8:9], s[14:15], v[32:33] op_sel_hi:[1,0,1]
	v_pk_fma_f32 v[8:9], v[8:9], s[48:49], v[12:13] op_sel_hi:[1,0,1]
	ds_read2_b64 v[34:37], v44 offset1:1
	ds_read2_b64 v[42:45], v45 offset1:1
	ds_read2_b64 v[0:3], v53 offset1:1
	ds_read2_b64 v[46:49], v62 offset1:1
	v_pk_fma_f32 v[4:5], v[10:11], s[58:59], v[4:5] op_sel_hi:[1,0,1]
	v_pk_fma_f32 v[62:63], v[18:19], s[58:59], v[6:7] op_sel_hi:[1,0,1]
	s_mov_b32 s58, s23
	v_pk_fma_f32 v[22:23], v[30:31], s[0:1], v[22:23] op_sel_hi:[1,0,1]
	v_pk_fma_f32 v[32:33], v[30:31], s[66:67], v[32:33] op_sel_hi:[1,0,1]
	v_pk_fma_f32 v[8:9], v[30:31], s[8:9], v[8:9] op_sel_hi:[1,0,1]
	v_pk_fma_f32 v[6:7], v[30:31], s[58:59], v[14:15] op_sel_hi:[1,0,1]
	v_pk_fma_f32 v[14:15], v[10:11], s[16:17], v[56:57] op_sel:[0,1,0]
	v_pk_fma_f32 v[22:23], v[10:11], s[0:1], v[22:23] op_sel:[0,1,0]
	v_pk_fma_f32 v[60:61], v[10:11], s[44:45], v[32:33] op_sel_hi:[1,0,1]
	v_pk_fma_f32 v[8:9], v[10:11], s[8:9], v[8:9] op_sel:[0,1,0]
	s_waitcnt lgkmcnt(0)
	v_pk_fma_f32 v[6:7], v[10:11], s[78:79], v[6:7] op_sel_hi:[1,0,1]
	v_pk_fma_f32 v[10:11], v[24:25], s[18:19], v[14:15] op_sel_hi:[1,0,1]
	v_pk_fma_f32 v[12:13], v[24:25], s[2:3], v[22:23] op_sel_hi:[1,0,1]
	v_pk_fma_f32 v[14:15], v[24:25], s[44:45], v[60:61] op_sel:[0,1,0]
	v_pk_fma_f32 v[8:9], v[24:25], s[10:11], v[8:9] op_sel_hi:[1,0,1]
	v_pk_fma_f32 v[4:5], v[24:25], s[52:53], v[4:5] op_sel_hi:[1,0,1]
	v_pk_fma_f32 v[12:13], v[40:41], s[70:71], v[12:13] op_sel_hi:[1,0,1]
	v_pk_fma_f32 v[14:15], v[40:41], s[42:43], v[14:15] op_sel_hi:[1,0,1]
	v_pk_fma_f32 v[8:9], v[40:41], s[64:65], v[8:9] op_sel_hi:[1,0,1]
	v_pk_fma_f32 v[4:5], v[40:41], s[54:55], v[4:5] op_sel_hi:[1,0,1]
	v_pk_fma_f32 v[10:11], v[40:41], s[56:57], v[10:11] op_sel_hi:[1,0,1]
	v_pk_fma_f32 v[12:13], v[26:27], s[4:5], v[12:13] op_sel_hi:[1,0,1]
	v_pk_fma_f32 v[14:15], v[26:27], s[36:37], v[14:15] op_sel_hi:[1,0,1]
	v_pk_fma_f32 v[8:9], v[26:27], s[12:13], v[8:9] op_sel_hi:[1,0,1]
	v_pk_fma_f32 v[4:5], v[26:27], s[50:51], v[4:5] op_sel_hi:[1,0,1]
	v_pk_fma_f32 v[10:11], v[26:27], s[20:21], v[10:11] op_sel_hi:[1,0,1]
	v_pk_fma_f32 v[12:13], v[28:29], s[72:73], v[12:13] op_sel_hi:[1,0,1]
	v_pk_fma_f32 v[14:15], v[28:29], s[40:41], v[14:15] op_sel_hi:[1,0,1]
	v_pk_fma_f32 v[8:9], v[28:29], s[68:69], v[8:9] op_sel_hi:[1,0,1]
	v_pk_fma_f32 v[4:5], v[28:29], s[46:47], v[4:5] op_sel_hi:[1,0,1]
	v_pk_fma_f32 v[10:11], v[28:29], s[60:61], v[10:11] op_sel_hi:[1,0,1]
	v_pk_fma_f32 v[12:13], v[16:17], s[6:7], v[12:13] op_sel_hi:[1,0,1]
	v_pk_fma_f32 v[14:15], v[16:17], s[38:39], v[14:15] op_sel_hi:[1,0,1]
	v_pk_fma_f32 v[8:9], v[16:17], s[14:15], v[8:9] op_sel_hi:[1,0,1]
	v_pk_fma_f32 v[4:5], v[16:17], s[48:49], v[4:5] op_sel_hi:[1,0,1]
	v_pk_fma_f32 v[10:11], v[16:17], s[22:23], v[10:11] op_sel_hi:[1,0,1]
	v_pk_fma_f32 v[12:13], v[20:21], s[74:75], v[12:13] op_sel_hi:[1,0,1]
	v_pk_fma_f32 v[14:15], v[20:21], s[0:1], v[14:15] op_sel_hi:[1,0,1]
	v_pk_fma_f32 v[8:9], v[20:21], s[66:67], v[8:9] op_sel_hi:[1,0,1]
	v_pk_fma_f32 v[4:5], v[20:21], s[8:9], v[4:5] op_sel_hi:[1,0,1]
	v_pk_fma_f32 v[10:11], v[20:21], s[58:59], v[10:11] op_sel_hi:[1,0,1]
	v_pk_fma_f32 v[26:27], v[18:19], s[16:17], v[58:59] op_sel:[0,1,0]
	v_pk_fma_f32 v[12:13], v[18:19], s[24:25], v[12:13] op_sel_hi:[1,0,1]
	v_pk_fma_f32 v[14:15], v[18:19], s[0:1], v[14:15] op_sel:[0,1,0]
	v_pk_fma_f32 v[8:9], v[18:19], s[44:45], v[8:9] op_sel_hi:[1,0,1]
	v_pk_fma_f32 v[4:5], v[18:19], s[8:9], v[4:5] op_sel:[0,1,0]
	v_add_u32_e32 v53, 0xb40, v52
	v_pk_fma_f32 v[10:11], v[18:19], s[78:79], v[10:11] op_sel_hi:[1,0,1]
	v_pk_fma_f32 v[26:27], v[34:35], s[18:19], v[26:27] op_sel_hi:[1,0,1]
	v_pk_mov_b32 v[16:17], v[34:35], v[36:37] op_sel:[1,0]
	v_pk_fma_f32 v[12:13], v[34:35], s[24:25], v[12:13] op_sel:[0,1,0]
	v_pk_fma_f32 v[14:15], v[34:35], s[2:3], v[14:15] op_sel_hi:[1,0,1]
	v_pk_fma_f32 v[8:9], v[34:35], s[44:45], v[8:9] op_sel:[0,1,0]
	v_pk_fma_f32 v[4:5], v[34:35], s[10:11], v[4:5] op_sel_hi:[1,0,1]
	v_pk_fma_f32 v[18:19], v[34:35], s[52:53], v[62:63] op_sel_hi:[1,0,1]
	v_add_u32_e32 v64, 0xb50, v52
	ds_read2_b64 v[30:33], v53 offset1:1
	ds_read2_b64 v[54:57], v64 offset1:1
	v_add_u32_e32 v38, 0xc60, v52
	v_add_u32_e32 v39, 0xc70, v52
	v_add_u32_e32 v53, 0xd80, v52
	v_add_u32_e32 v28, 0xd90, v52
	v_pk_fma_f32 v[58:59], v[16:17], s[56:57], v[26:27] op_sel_hi:[1,0,1]
	v_pk_fma_f32 v[12:13], v[16:17], s[26:27], v[12:13] op_sel_hi:[1,0,1]
	v_pk_fma_f32 v[14:15], v[16:17], s[70:71], v[14:15] op_sel_hi:[1,0,1]
	v_pk_fma_f32 v[8:9], v[16:17], s[42:43], v[8:9] op_sel_hi:[1,0,1]
	v_pk_fma_f32 v[4:5], v[16:17], s[64:65], v[4:5] op_sel_hi:[1,0,1]
	v_pk_fma_f32 v[16:17], v[16:17], s[54:55], v[18:19] op_sel_hi:[1,0,1]
	ds_read2_b64 v[22:25], v38 offset1:1
	ds_read2_b64 v[38:41], v39 offset1:1
	ds_read2_b64 v[18:21], v53 offset1:1
	ds_read2_b64 v[26:29], v28 offset1:1
	v_add_u32_e32 v60, 0xea0, v52
	v_add_u32_e32 v61, 0xeb0, v52
	v_pk_fma_f32 v[34:35], v[36:37], s[20:21], v[58:59] op_sel_hi:[1,0,1]
	v_pk_fma_f32 v[52:53], v[36:37], s[76:77], v[12:13] op_sel_hi:[1,0,1]
	v_pk_fma_f32 v[14:15], v[36:37], s[4:5], v[14:15] op_sel_hi:[1,0,1]
	v_pk_fma_f32 v[8:9], v[36:37], s[36:37], v[8:9] op_sel_hi:[1,0,1]
	v_pk_fma_f32 v[4:5], v[36:37], s[12:13], v[4:5] op_sel_hi:[1,0,1]
	v_pk_fma_f32 v[16:17], v[36:37], s[50:51], v[16:17] op_sel_hi:[1,0,1]
	v_pk_mov_b32 v[36:37], v[36:37], v[42:43] op_sel:[1,0]
	v_pk_mov_b32 v[58:59], v[0:1], v[2:3] op_sel:[1,0]
	v_pk_fma_f32 v[14:15], v[36:37], s[72:73], v[14:15] op_sel_hi:[1,0,1]
	v_pk_fma_f32 v[12:13], v[36:37], s[60:61], v[34:35] op_sel_hi:[1,0,1]
	v_pk_mov_b32 v[34:35], v[42:43], v[44:45] op_sel:[1,0]
	v_pk_fma_f32 v[52:53], v[36:37], s[34:35], v[52:53] op_sel_hi:[1,0,1]
	v_pk_fma_f32 v[14:15], v[42:43], s[6:7], v[14:15] op_sel_hi:[1,0,1]
	v_pk_fma_f32 v[8:9], v[36:37], s[40:41], v[8:9] op_sel_hi:[1,0,1]
	v_pk_fma_f32 v[4:5], v[36:37], s[68:69], v[4:5] op_sel_hi:[1,0,1]
	v_pk_fma_f32 v[16:17], v[36:37], s[46:47], v[16:17] op_sel_hi:[1,0,1]
	v_pk_fma_f32 v[52:53], v[42:43], s[34:35], v[52:53] op_sel:[0,1,0]
	v_pk_fma_f32 v[14:15], v[34:35], s[74:75], v[14:15] op_sel_hi:[1,0,1]
	v_pk_fma_f32 v[8:9], v[42:43], s[38:39], v[8:9] op_sel_hi:[1,0,1]
	v_pk_fma_f32 v[4:5], v[42:43], s[14:15], v[4:5] op_sel_hi:[1,0,1]
	v_pk_fma_f32 v[16:17], v[42:43], s[48:49], v[16:17] op_sel_hi:[1,0,1]
	v_pk_fma_f32 v[52:53], v[34:35], s[16:17], v[52:53] op_sel_hi:[1,0,1]
	v_pk_fma_f32 v[14:15], v[44:45], s[24:25], v[14:15] op_sel_hi:[1,0,1]
	v_pk_fma_f32 v[8:9], v[34:35], s[0:1], v[8:9] op_sel_hi:[1,0,1]
	v_pk_fma_f32 v[4:5], v[34:35], s[66:67], v[4:5] op_sel_hi:[1,0,1]
	v_pk_fma_f32 v[16:17], v[34:35], s[8:9], v[16:17] op_sel_hi:[1,0,1]
	v_pk_fma_f32 v[52:53], v[44:45], s[16:17], v[52:53] op_sel:[0,1,0]
	v_pk_fma_f32 v[8:9], v[44:45], s[0:1], v[8:9] op_sel:[0,1,0]
	v_pk_fma_f32 v[4:5], v[44:45], s[44:45], v[4:5] op_sel_hi:[1,0,1]
	v_pk_fma_f32 v[16:17], v[44:45], s[8:9], v[16:17] op_sel:[0,1,0]
	v_pk_fma_f32 v[14:15], v[0:1], s[24:25], v[14:15] op_sel:[0,1,0]
	v_pk_fma_f32 v[52:53], v[0:1], s[18:19], v[52:53] op_sel_hi:[1,0,1]
	v_pk_fma_f32 v[14:15], v[58:59], s[26:27], v[14:15] op_sel_hi:[1,0,1]
	v_pk_fma_f32 v[8:9], v[0:1], s[2:3], v[8:9] op_sel_hi:[1,0,1]
	v_pk_fma_f32 v[4:5], v[0:1], s[44:45], v[4:5] op_sel:[0,1,0]
	v_pk_fma_f32 v[0:1], v[0:1], s[10:11], v[16:17] op_sel_hi:[1,0,1]
	v_pk_fma_f32 v[52:53], v[58:59], s[56:57], v[52:53] op_sel_hi:[1,0,1]
	v_pk_fma_f32 v[8:9], v[58:59], s[70:71], v[8:9] op_sel_hi:[1,0,1]
	v_pk_fma_f32 v[4:5], v[58:59], s[42:43], v[4:5] op_sel_hi:[1,0,1]
	v_pk_fma_f32 v[0:1], v[58:59], s[64:65], v[0:1] op_sel_hi:[1,0,1]
	v_pk_mov_b32 v[58:59], v[2:3], v[46:47] op_sel:[1,0]
	v_pk_fma_f32 v[14:15], v[2:3], s[76:77], v[14:15] op_sel_hi:[1,0,1]
	v_pk_fma_f32 v[52:53], v[2:3], s[20:21], v[52:53] op_sel_hi:[1,0,1]
	v_pk_fma_f32 v[14:15], v[58:59], s[34:35], v[14:15] op_sel_hi:[1,0,1]
	v_pk_fma_f32 v[8:9], v[2:3], s[4:5], v[8:9] op_sel_hi:[1,0,1]
	v_pk_fma_f32 v[4:5], v[2:3], s[36:37], v[4:5] op_sel_hi:[1,0,1]
	v_pk_fma_f32 v[0:1], v[2:3], s[12:13], v[0:1] op_sel_hi:[1,0,1]
	v_pk_mov_b32 v[2:3], v[46:47], v[48:49] op_sel:[1,0]
	v_pk_fma_f32 v[14:15], v[46:47], s[34:35], v[14:15] op_sel:[0,1,0]
	v_pk_fma_f32 v[16:17], v[58:59], s[60:61], v[52:53] op_sel_hi:[1,0,1]
	v_pk_fma_f32 v[14:15], v[2:3], s[16:17], v[14:15] op_sel_hi:[1,0,1]
	s_waitcnt lgkmcnt(5)
	v_pk_mov_b32 v[52:53], v[30:31], v[32:33] op_sel:[1,0]
	v_pk_fma_f32 v[14:15], v[48:49], s[16:17], v[14:15] op_sel:[0,1,0]
	v_pk_fma_f32 v[8:9], v[58:59], s[72:73], v[8:9] op_sel_hi:[1,0,1]
	v_pk_fma_f32 v[14:15], v[30:31], s[18:19], v[14:15] op_sel_hi:[1,0,1]
	v_pk_fma_f32 v[4:5], v[58:59], s[40:41], v[4:5] op_sel_hi:[1,0,1]
	v_pk_fma_f32 v[14:15], v[52:53], s[56:57], v[14:15] op_sel_hi:[1,0,1]
	v_pk_fma_f32 v[0:1], v[58:59], s[68:69], v[0:1] op_sel_hi:[1,0,1]
	v_pk_fma_f32 v[14:15], v[32:33], s[20:21], v[14:15] op_sel_hi:[1,0,1]
	s_waitcnt lgkmcnt(4)
	v_pk_mov_b32 v[58:59], v[32:33], v[54:55] op_sel:[1,0]
	v_pk_fma_f32 v[12:13], v[42:43], s[22:23], v[12:13] op_sel_hi:[1,0,1]
	v_pk_fma_f32 v[14:15], v[58:59], s[60:61], v[14:15] op_sel_hi:[1,0,1]
	v_pk_fma_f32 v[12:13], v[34:35], s[58:59], v[12:13] op_sel_hi:[1,0,1]
	v_pk_fma_f32 v[16:17], v[46:47], s[22:23], v[16:17] op_sel_hi:[1,0,1]
	v_pk_fma_f32 v[14:15], v[54:55], s[22:23], v[14:15] op_sel_hi:[1,0,1]
	v_pk_fma_f32 v[8:9], v[46:47], s[6:7], v[8:9] op_sel_hi:[1,0,1]
	v_pk_fma_f32 v[4:5], v[46:47], s[38:39], v[4:5] op_sel_hi:[1,0,1]
	v_pk_fma_f32 v[0:1], v[46:47], s[14:15], v[0:1] op_sel_hi:[1,0,1]
	v_pk_mov_b32 v[46:47], v[54:55], v[56:57] op_sel:[1,0]
	v_pk_fma_f32 v[12:13], v[44:45], s[78:79], v[12:13] op_sel_hi:[1,0,1]
	ds_read2_b64 v[34:37], v60 offset1:1
	ds_read2_b64 v[42:45], v61 offset1:1
	v_pk_fma_f32 v[16:17], v[2:3], s[58:59], v[16:17] op_sel_hi:[1,0,1]
	v_pk_fma_f32 v[60:61], v[2:3], s[74:75], v[8:9] op_sel_hi:[1,0,1]
	v_pk_fma_f32 v[4:5], v[2:3], s[0:1], v[4:5] op_sel_hi:[1,0,1]
	v_pk_fma_f32 v[0:1], v[2:3], s[66:67], v[0:1] op_sel_hi:[1,0,1]
	v_pk_fma_f32 v[2:3], v[46:47], s[58:59], v[14:15] op_sel_hi:[1,0,1]
	v_pk_fma_f32 v[0:1], v[48:49], s[44:45], v[0:1] op_sel_hi:[1,0,1]
	v_pk_fma_f32 v[8:9], v[56:57], s[78:79], v[2:3] op_sel_hi:[1,0,1]
	v_pk_fma_f32 v[2:3], v[48:49], s[24:25], v[60:61] op_sel_hi:[1,0,1]
	v_pk_fma_f32 v[0:1], v[30:31], s[44:45], v[0:1] op_sel:[0,1,0]
	v_pk_fma_f32 v[2:3], v[30:31], s[24:25], v[2:3] op_sel:[0,1,0]
	v_pk_fma_f32 v[0:1], v[52:53], s[42:43], v[0:1] op_sel_hi:[1,0,1]
	v_pk_fma_f32 v[2:3], v[52:53], s[26:27], v[2:3] op_sel_hi:[1,0,1]
	v_pk_fma_f32 v[0:1], v[32:33], s[36:37], v[0:1] op_sel_hi:[1,0,1]
	v_pk_fma_f32 v[2:3], v[32:33], s[76:77], v[2:3] op_sel_hi:[1,0,1]
	v_pk_fma_f32 v[0:1], v[58:59], s[40:41], v[0:1] op_sel_hi:[1,0,1]
	v_pk_fma_f32 v[2:3], v[58:59], s[34:35], v[2:3] op_sel_hi:[1,0,1]
	v_pk_fma_f32 v[0:1], v[54:55], s[38:39], v[0:1] op_sel_hi:[1,0,1]
	v_pk_fma_f32 v[2:3], v[54:55], s[34:35], v[2:3] op_sel:[0,1,0]
	s_waitcnt lgkmcnt(5)
	v_pk_mov_b32 v[14:15], v[22:23], v[24:25] op_sel:[1,0]
	v_pk_fma_f32 v[2:3], v[46:47], s[16:17], v[2:3] op_sel_hi:[1,0,1]
	v_pk_fma_f32 v[0:1], v[46:47], s[0:1], v[0:1] op_sel_hi:[1,0,1]
	v_pk_fma_f32 v[2:3], v[56:57], s[16:17], v[2:3] op_sel:[0,1,0]
	v_pk_fma_f32 v[0:1], v[56:57], s[0:1], v[0:1] op_sel:[0,1,0]
	v_pk_fma_f32 v[2:3], v[22:23], s[18:19], v[2:3] op_sel_hi:[1,0,1]
	v_pk_fma_f32 v[16:17], v[48:49], s[78:79], v[16:17] op_sel_hi:[1,0,1]
	v_pk_fma_f32 v[2:3], v[14:15], s[56:57], v[2:3] op_sel_hi:[1,0,1]
	v_pk_fma_f32 v[4:5], v[48:49], s[0:1], v[4:5] op_sel:[0,1,0]
	v_pk_fma_f32 v[2:3], v[24:25], s[20:21], v[2:3] op_sel_hi:[1,0,1]
	s_waitcnt lgkmcnt(4)
	v_pk_mov_b32 v[48:49], v[24:25], v[38:39] op_sel:[1,0]
	v_pk_fma_f32 v[0:1], v[22:23], s[2:3], v[0:1] op_sel_hi:[1,0,1]
	v_pk_fma_f32 v[2:3], v[48:49], s[60:61], v[2:3] op_sel_hi:[1,0,1]
	v_pk_fma_f32 v[0:1], v[14:15], s[70:71], v[0:1] op_sel_hi:[1,0,1]
	v_pk_fma_f32 v[2:3], v[38:39], s[22:23], v[2:3] op_sel_hi:[1,0,1]
	v_pk_fma_f32 v[4:5], v[30:31], s[2:3], v[4:5] op_sel_hi:[1,0,1]
	v_pk_mov_b32 v[30:31], v[38:39], v[40:41] op_sel:[1,0]
	v_pk_fma_f32 v[0:1], v[24:25], s[4:5], v[0:1] op_sel_hi:[1,0,1]
	v_pk_fma_f32 v[60:61], v[52:53], s[70:71], v[4:5] op_sel_hi:[1,0,1]
	v_pk_fma_f32 v[2:3], v[30:31], s[58:59], v[2:3] op_sel_hi:[1,0,1]
	v_pk_fma_f32 v[0:1], v[48:49], s[72:73], v[0:1] op_sel_hi:[1,0,1]
	v_pk_fma_f32 v[4:5], v[40:41], s[78:79], v[2:3] op_sel_hi:[1,0,1]
	v_pk_fma_f32 v[2:3], v[32:33], s[4:5], v[60:61] op_sel_hi:[1,0,1]
	v_pk_fma_f32 v[0:1], v[38:39], s[6:7], v[0:1] op_sel_hi:[1,0,1]
	v_pk_fma_f32 v[2:3], v[58:59], s[72:73], v[2:3] op_sel_hi:[1,0,1]
	v_pk_fma_f32 v[0:1], v[30:31], s[74:75], v[0:1] op_sel_hi:[1,0,1]
	v_pk_fma_f32 v[2:3], v[54:55], s[6:7], v[2:3] op_sel_hi:[1,0,1]
	v_pk_fma_f32 v[0:1], v[40:41], s[24:25], v[0:1] op_sel_hi:[1,0,1]
	v_pk_fma_f32 v[2:3], v[46:47], s[74:75], v[2:3] op_sel_hi:[1,0,1]
	s_waitcnt lgkmcnt(3)
	v_pk_mov_b32 v[32:33], v[18:19], v[20:21] op_sel:[1,0]
	v_pk_fma_f32 v[0:1], v[18:19], s[24:25], v[0:1] op_sel:[0,1,0]
	v_pk_fma_f32 v[2:3], v[56:57], s[24:25], v[2:3] op_sel_hi:[1,0,1]
	v_pk_fma_f32 v[0:1], v[32:33], s[26:27], v[0:1] op_sel_hi:[1,0,1]
	v_pk_fma_f32 v[2:3], v[22:23], s[24:25], v[2:3] op_sel:[0,1,0]
	s_waitcnt lgkmcnt(2)
	v_pk_mov_b32 v[52:53], v[20:21], v[26:27] op_sel:[1,0]
	v_pk_fma_f32 v[0:1], v[20:21], s[76:77], v[0:1] op_sel_hi:[1,0,1]
	v_pk_fma_f32 v[2:3], v[14:15], s[26:27], v[2:3] op_sel_hi:[1,0,1]
	v_pk_fma_f32 v[0:1], v[52:53], s[34:35], v[0:1] op_sel_hi:[1,0,1]
	v_pk_fma_f32 v[2:3], v[24:25], s[76:77], v[2:3] op_sel_hi:[1,0,1]
	v_pk_mov_b32 v[58:59], v[26:27], v[28:29] op_sel:[1,0]
	v_pk_fma_f32 v[0:1], v[26:27], s[34:35], v[0:1] op_sel:[0,1,0]
	v_pk_fma_f32 v[2:3], v[48:49], s[34:35], v[2:3] op_sel_hi:[1,0,1]
	v_pk_fma_f32 v[0:1], v[58:59], s[16:17], v[0:1] op_sel_hi:[1,0,1]
	v_pk_fma_f32 v[2:3], v[38:39], s[34:35], v[2:3] op_sel:[0,1,0]
	v_pk_fma_f32 v[0:1], v[28:29], s[16:17], v[0:1] op_sel:[0,1,0]
	v_pk_fma_f32 v[2:3], v[30:31], s[16:17], v[2:3] op_sel_hi:[1,0,1]
	s_waitcnt lgkmcnt(1)
	v_pk_fma_f32 v[0:1], v[34:35], s[18:19], v[0:1] op_sel_hi:[1,0,1]
	v_pk_mov_b32 v[14:15], v[34:35], v[36:37] op_sel:[1,0]
	v_pk_fma_f32 v[2:3], v[40:41], s[16:17], v[2:3] op_sel:[0,1,0]
	v_pk_fma_f32 v[0:1], v[14:15], s[56:57], v[0:1] op_sel_hi:[1,0,1]
	v_pk_fma_f32 v[2:3], v[18:19], s[18:19], v[2:3] op_sel_hi:[1,0,1]
	v_pk_fma_f32 v[0:1], v[36:37], s[20:21], v[0:1] op_sel_hi:[1,0,1]
	s_waitcnt lgkmcnt(0)
	v_pk_mov_b32 v[14:15], v[36:37], v[42:43] op_sel:[1,0]
	s_add_u32 s0, s30, s28
	v_pk_fma_f32 v[2:3], v[32:33], s[56:57], v[2:3] op_sel_hi:[1,0,1]
	v_pk_fma_f32 v[0:1], v[14:15], s[60:61], v[0:1] op_sel_hi:[1,0,1]
	s_addc_u32 s1, s31, s29
	v_lshlrev_b32_e32 v18, 2, v51
	v_mov_b32_e32 v19, 0
	v_pk_fma_f32 v[2:3], v[20:21], s[20:21], v[2:3] op_sel_hi:[1,0,1]
	v_pk_fma_f32 v[0:1], v[42:43], s[22:23], v[0:1] op_sel_hi:[1,0,1]
	v_pk_mov_b32 v[14:15], v[42:43], v[44:45] op_sel:[1,0]
	v_lshl_add_u64 v[20:21], s[0:1], 0, v[18:19]
	s_mov_b32 s1, 0x3f3504f3
	v_pk_fma_f32 v[0:1], v[14:15], s[58:59], v[0:1] op_sel_hi:[1,0,1]
	v_mul_f32_e64 v14, |v6|, s1
	s_mov_b32 s3, 0x3ea7ba05
	v_fma_f32 v15, v14, s3, 1.0
	v_mul_f32_e32 v14, v14, v14
	v_mul_f32_e32 v14, 0xbfb8aa3b, v14
	v_mul_f32_e64 v18, |v7|, s1
	v_exp_f32_e32 v24, v14
	v_fma_f32 v14, v18, s3, 1.0
	v_rcp_f32_e32 v22, v15
	v_rcp_f32_e32 v23, v14
	s_mov_b32 s2, 0xbfba00e3
	v_pk_fma_f32 v[2:3], v[52:53], s[60:61], v[2:3] op_sel_hi:[1,0,1]
	s_mov_b32 s0, 0x3f87dc22
	v_mov_b64_e32 v[14:15], s[2:3]
	v_mul_f32_e32 v18, v18, v18
	v_pk_fma_f32 v[2:3], v[26:27], s[22:23], v[2:3] op_sel_hi:[1,0,1]
	v_pk_fma_f32 v[26:27], v[22:23], s[0:1], v[14:15] op_sel_hi:[1,0,0]
	s_mov_b32 s2, 0x3fb5f0e3
	v_mul_f32_e32 v18, 0xbfb8aa3b, v18
	v_pk_fma_f32 v[26:27], v[22:23], v[26:27], s[2:3] op_sel_hi:[1,1,0]
	v_exp_f32_e32 v25, v18
	s_mov_b32 s4, 0xbe91a98e
	v_pk_fma_f32 v[26:27], v[22:23], v[26:27], s[4:5] op_sel_hi:[1,1,0]
	s_mov_b32 s6, 0x3e827906
	v_pk_fma_f32 v[26:27], v[22:23], v[26:27], s[6:7] op_sel_hi:[1,1,0]
	v_cmp_gt_f32_e32 vcc, 0, v7
	v_pk_mul_f32 v[22:23], v[22:23], v[26:27]
	v_lshlrev_b32_e32 v18, 10, v50
	v_pk_fma_f32 v[22:23], v[24:25], v[22:23], 1.0 op_sel_hi:[1,1,0] neg_lo:[1,0,0] neg_hi:[1,0,0]
	v_pk_fma_f32 v[2:3], v[58:59], s[58:59], v[2:3] op_sel_hi:[1,0,1]
	v_cndmask_b32_e64 v23, v23, -v23, vcc
	v_cmp_gt_f32_e32 vcc, 0, v6
	v_pk_mul_f32 v[6:7], v[6:7], 0.5 op_sel_hi:[1,0]
	v_pk_fma_f32 v[2:3], v[28:29], s[78:79], v[2:3] op_sel_hi:[1,0,1]
	v_cndmask_b32_e64 v22, v22, -v22, vcc
	v_pk_add_f32 v[22:23], v[22:23], 1.0 op_sel_hi:[1,0]
	v_cmp_gt_f32_e32 vcc, 0, v11
	v_pk_mul_f32 v[6:7], v[6:7], v[22:23]
	v_pk_fma_f32 v[0:1], v[44:45], s[78:79], v[0:1] op_sel_hi:[1,0,1]
	v_cvt_pk_f16_f32 v22, v6, v7
	v_lshl_add_u64 v[6:7], v[20:21], 0, v[18:19]
	v_mul_f32_e64 v20, |v10|, s1
	v_mul_f32_e64 v21, |v11|, s1
	v_fma_f32 v18, v20, s3, 1.0
	v_fma_f32 v19, v21, s3, 1.0
	v_rcp_f32_e32 v18, v18
	v_rcp_f32_e32 v19, v19
	v_mul_f32_e32 v20, v20, v20
	v_mul_f32_e32 v21, v21, v21
	global_store_dword v[6:7], v22, off
	v_mul_f32_e32 v20, 0xbfb8aa3b, v20
	v_pk_fma_f32 v[22:23], v[18:19], s[0:1], v[14:15] op_sel_hi:[1,0,0]
	v_mul_f32_e32 v21, 0xbfb8aa3b, v21
	v_exp_f32_e32 v20, v20
	v_pk_fma_f32 v[22:23], v[18:19], v[22:23], s[2:3] op_sel_hi:[1,1,0]
	v_exp_f32_e32 v21, v21
	v_pk_fma_f32 v[22:23], v[18:19], v[22:23], s[4:5] op_sel_hi:[1,1,0]
	s_nop 0
	v_pk_fma_f32 v[22:23], v[18:19], v[22:23], s[6:7] op_sel_hi:[1,1,0]
	s_nop 0
	v_pk_mul_f32 v[18:19], v[18:19], v[22:23]
	s_nop 0
	v_pk_fma_f32 v[18:19], v[20:21], v[18:19], 1.0 op_sel_hi:[1,1,0] neg_lo:[1,0,0] neg_hi:[1,0,0]
	s_nop 0
	v_cndmask_b32_e64 v19, v19, -v19, vcc
	v_cmp_gt_f32_e32 vcc, 0, v10
	v_pk_mul_f32 v[10:11], v[10:11], 0.5 op_sel_hi:[1,0]
	s_nop 0
	v_cndmask_b32_e64 v18, v18, -v18, vcc
	v_pk_add_f32 v[18:19], v[18:19], 1.0 op_sel_hi:[1,0]
	v_cmp_gt_f32_e32 vcc, 0, v13
	v_pk_mul_f32 v[10:11], v[10:11], v[18:19]
	v_mul_f32_e64 v18, |v12|, s1
	v_cvt_pk_f16_f32 v10, v10, v11
	v_mul_f32_e64 v19, |v13|, s1
	global_store_dword v[6:7], v10, off offset:128
	v_fma_f32 v10, v18, s3, 1.0
	v_fma_f32 v11, v19, s3, 1.0
	v_rcp_f32_e32 v10, v10
	v_rcp_f32_e32 v11, v11
	v_mul_f32_e32 v18, v18, v18
	v_mul_f32_e32 v19, v19, v19
	v_mul_f32_e32 v18, 0xbfb8aa3b, v18
	v_pk_fma_f32 v[20:21], v[10:11], s[0:1], v[14:15] op_sel_hi:[1,0,0]
	v_mul_f32_e32 v19, 0xbfb8aa3b, v19
	v_exp_f32_e32 v18, v18
	v_pk_fma_f32 v[20:21], v[10:11], v[20:21], s[2:3] op_sel_hi:[1,1,0]
	v_exp_f32_e32 v19, v19
	v_pk_fma_f32 v[20:21], v[10:11], v[20:21], s[4:5] op_sel_hi:[1,1,0]
	s_nop 0
	v_pk_fma_f32 v[20:21], v[10:11], v[20:21], s[6:7] op_sel_hi:[1,1,0]
	s_nop 0
	v_pk_mul_f32 v[10:11], v[10:11], v[20:21]
	s_nop 0
	v_pk_fma_f32 v[10:11], v[18:19], v[10:11], 1.0 op_sel_hi:[1,1,0] neg_lo:[1,0,0] neg_hi:[1,0,0]
	s_nop 0
	v_cndmask_b32_e64 v11, v11, -v11, vcc
	v_cmp_gt_f32_e32 vcc, 0, v12
	v_pk_mul_f32 v[12:13], v[12:13], 0.5 op_sel_hi:[1,0]
	s_nop 0
	v_cndmask_b32_e64 v10, v10, -v10, vcc
	v_pk_add_f32 v[10:11], v[10:11], 1.0 op_sel_hi:[1,0]
	v_cmp_gt_f32_e32 vcc, 0, v17
	v_pk_mul_f32 v[10:11], v[12:13], v[10:11]
	v_mul_f32_e64 v12, |v16|, s1
	v_cvt_pk_f16_f32 v10, v10, v11
	v_mul_f32_e64 v13, |v17|, s1
	global_store_dword v[6:7], v10, off offset:256
	v_fma_f32 v10, v12, s3, 1.0
	v_fma_f32 v11, v13, s3, 1.0
	v_rcp_f32_e32 v10, v10
	v_rcp_f32_e32 v11, v11
	v_mul_f32_e32 v12, v12, v12
	v_mul_f32_e32 v13, v13, v13
	v_mul_f32_e32 v12, 0xbfb8aa3b, v12
	v_pk_fma_f32 v[18:19], v[10:11], s[0:1], v[14:15] op_sel_hi:[1,0,0]
	v_mul_f32_e32 v13, 0xbfb8aa3b, v13
	v_exp_f32_e32 v12, v12
	v_pk_fma_f32 v[18:19], v[10:11], v[18:19], s[2:3] op_sel_hi:[1,1,0]
	v_exp_f32_e32 v13, v13
	v_pk_fma_f32 v[18:19], v[10:11], v[18:19], s[4:5] op_sel_hi:[1,1,0]
	s_nop 0
	v_pk_fma_f32 v[18:19], v[10:11], v[18:19], s[6:7] op_sel_hi:[1,1,0]
	s_nop 0
	v_pk_mul_f32 v[10:11], v[10:11], v[18:19]
	s_nop 0
	v_pk_fma_f32 v[10:11], v[12:13], v[10:11], 1.0 op_sel_hi:[1,1,0] neg_lo:[1,0,0] neg_hi:[1,0,0]
	v_pk_mul_f32 v[12:13], v[16:17], 0.5 op_sel_hi:[1,0]
	v_cndmask_b32_e64 v11, v11, -v11, vcc
	v_cmp_gt_f32_e32 vcc, 0, v16
	s_nop 1
	v_cndmask_b32_e64 v10, v10, -v10, vcc
	v_pk_add_f32 v[10:11], v[10:11], 1.0 op_sel_hi:[1,0]
	v_cmp_gt_f32_e32 vcc, 0, v9
	v_pk_mul_f32 v[10:11], v[12:13], v[10:11]
	v_mul_f32_e64 v12, |v8|, s1
	v_cvt_pk_f16_f32 v10, v10, v11
	v_mul_f32_e64 v13, |v9|, s1
	global_store_dword v[6:7], v10, off offset:384
	v_fma_f32 v10, v12, s3, 1.0
	v_fma_f32 v11, v13, s3, 1.0
	v_rcp_f32_e32 v10, v10
	v_rcp_f32_e32 v11, v11
	v_mul_f32_e32 v12, v12, v12
	v_mul_f32_e32 v13, v13, v13
	v_mul_f32_e32 v12, 0xbfb8aa3b, v12
	v_pk_fma_f32 v[16:17], v[10:11], s[0:1], v[14:15] op_sel_hi:[1,0,0]
	v_mul_f32_e32 v13, 0xbfb8aa3b, v13
	v_exp_f32_e32 v12, v12
	v_pk_fma_f32 v[16:17], v[10:11], v[16:17], s[2:3] op_sel_hi:[1,1,0]
	v_exp_f32_e32 v13, v13
	v_pk_fma_f32 v[16:17], v[10:11], v[16:17], s[4:5] op_sel_hi:[1,1,0]
	s_nop 0
	v_pk_fma_f32 v[16:17], v[10:11], v[16:17], s[6:7] op_sel_hi:[1,1,0]
	s_nop 0
	v_pk_mul_f32 v[10:11], v[10:11], v[16:17]
	s_nop 0
	v_pk_fma_f32 v[10:11], v[12:13], v[10:11], 1.0 op_sel_hi:[1,1,0] neg_lo:[1,0,0] neg_hi:[1,0,0]
	s_nop 0
	v_cndmask_b32_e64 v11, v11, -v11, vcc
	v_cmp_gt_f32_e32 vcc, 0, v8
	v_pk_mul_f32 v[8:9], v[8:9], 0.5 op_sel_hi:[1,0]
	s_nop 0
	v_cndmask_b32_e64 v10, v10, -v10, vcc
	v_pk_add_f32 v[10:11], v[10:11], 1.0 op_sel_hi:[1,0]
	v_cmp_gt_f32_e32 vcc, 0, v5
	v_pk_mul_f32 v[8:9], v[8:9], v[10:11]
	v_mul_f32_e64 v10, |v4|, s1
	v_cvt_pk_f16_f32 v8, v8, v9
	v_mul_f32_e64 v11, |v5|, s1
	global_store_dword v[6:7], v8, off offset:512
	v_fma_f32 v8, v10, s3, 1.0
	v_fma_f32 v9, v11, s3, 1.0
	v_rcp_f32_e32 v8, v8
	v_rcp_f32_e32 v9, v9
	v_mul_f32_e32 v10, v10, v10
	v_mul_f32_e32 v11, v11, v11
	v_mul_f32_e32 v10, 0xbfb8aa3b, v10
	v_pk_fma_f32 v[12:13], v[8:9], s[0:1], v[14:15] op_sel_hi:[1,0,0]
	v_mul_f32_e32 v11, 0xbfb8aa3b, v11
	v_exp_f32_e32 v10, v10
	v_pk_fma_f32 v[12:13], v[8:9], v[12:13], s[2:3] op_sel_hi:[1,1,0]
	v_exp_f32_e32 v11, v11
	v_pk_fma_f32 v[12:13], v[8:9], v[12:13], s[4:5] op_sel_hi:[1,1,0]
	s_nop 0
	v_pk_fma_f32 v[12:13], v[8:9], v[12:13], s[6:7] op_sel_hi:[1,1,0]
	s_nop 0
	v_pk_mul_f32 v[8:9], v[8:9], v[12:13]
	s_nop 0
	v_pk_fma_f32 v[8:9], v[10:11], v[8:9], 1.0 op_sel_hi:[1,1,0] neg_lo:[1,0,0] neg_hi:[1,0,0]
	s_nop 0
	v_cndmask_b32_e64 v9, v9, -v9, vcc
	v_cmp_gt_f32_e32 vcc, 0, v4
	v_pk_mul_f32 v[4:5], v[4:5], 0.5 op_sel_hi:[1,0]
	s_nop 0
	v_cndmask_b32_e64 v8, v8, -v8, vcc
	v_pk_add_f32 v[8:9], v[8:9], 1.0 op_sel_hi:[1,0]
	v_cmp_gt_f32_e32 vcc, 0, v3
	v_pk_mul_f32 v[4:5], v[4:5], v[8:9]
	v_mul_f32_e64 v8, |v2|, s1
	v_cvt_pk_f16_f32 v4, v4, v5
	v_mul_f32_e64 v9, |v3|, s1
	global_store_dword v[6:7], v4, off offset:640
	v_fma_f32 v4, v8, s3, 1.0
	v_fma_f32 v5, v9, s3, 1.0
	v_rcp_f32_e32 v4, v4
	v_rcp_f32_e32 v5, v5
	v_mul_f32_e32 v8, v8, v8
	v_mul_f32_e32 v9, v9, v9
	v_mul_f32_e32 v8, 0xbfb8aa3b, v8
	v_pk_fma_f32 v[10:11], v[4:5], s[0:1], v[14:15] op_sel_hi:[1,0,0]
	v_mul_f32_e32 v9, 0xbfb8aa3b, v9
	v_exp_f32_e32 v8, v8
	v_pk_fma_f32 v[10:11], v[4:5], v[10:11], s[2:3] op_sel_hi:[1,1,0]
	v_exp_f32_e32 v9, v9
	v_pk_fma_f32 v[10:11], v[4:5], v[10:11], s[4:5] op_sel_hi:[1,1,0]
	s_nop 0
	v_pk_fma_f32 v[10:11], v[4:5], v[10:11], s[6:7] op_sel_hi:[1,1,0]
	s_nop 0
	v_pk_mul_f32 v[4:5], v[4:5], v[10:11]
	s_nop 0
	v_pk_fma_f32 v[4:5], v[8:9], v[4:5], 1.0 op_sel_hi:[1,1,0] neg_lo:[1,0,0] neg_hi:[1,0,0]
	s_nop 0
	v_cndmask_b32_e64 v5, v5, -v5, vcc
	v_cmp_gt_f32_e32 vcc, 0, v2
	v_pk_mul_f32 v[2:3], v[2:3], 0.5 op_sel_hi:[1,0]
	s_nop 0
	v_cndmask_b32_e64 v4, v4, -v4, vcc
	v_pk_add_f32 v[4:5], v[4:5], 1.0 op_sel_hi:[1,0]
	v_cmp_gt_f32_e32 vcc, 0, v1
	v_pk_mul_f32 v[2:3], v[2:3], v[4:5]
	v_mul_f32_e64 v4, |v0|, s1
	v_cvt_pk_f16_f32 v2, v2, v3
	v_mul_f32_e64 v5, |v1|, s1
	global_store_dword v[6:7], v2, off offset:768
	v_fma_f32 v2, v4, s3, 1.0
	v_fma_f32 v3, v5, s3, 1.0
	v_rcp_f32_e32 v2, v2
	v_rcp_f32_e32 v3, v3
	v_mul_f32_e32 v4, v4, v4
	v_mul_f32_e32 v5, v5, v5
	v_mul_f32_e32 v4, 0xbfb8aa3b, v4
	v_pk_fma_f32 v[8:9], v[2:3], s[0:1], v[14:15] op_sel_hi:[1,0,0]
	v_mul_f32_e32 v5, 0xbfb8aa3b, v5
	v_exp_f32_e32 v4, v4
	v_pk_fma_f32 v[8:9], v[2:3], v[8:9], s[2:3] op_sel_hi:[1,1,0]
	v_exp_f32_e32 v5, v5
	v_pk_fma_f32 v[8:9], v[2:3], v[8:9], s[4:5] op_sel_hi:[1,1,0]
	s_nop 0
	v_pk_fma_f32 v[8:9], v[2:3], v[8:9], s[6:7] op_sel_hi:[1,1,0]
	s_nop 0
	v_pk_mul_f32 v[2:3], v[2:3], v[8:9]
	s_nop 0
	v_pk_fma_f32 v[2:3], v[4:5], v[2:3], 1.0 op_sel_hi:[1,1,0] neg_lo:[1,0,0] neg_hi:[1,0,0]
	s_nop 0
	v_cndmask_b32_e64 v3, v3, -v3, vcc
	v_cmp_gt_f32_e32 vcc, 0, v0
	v_pk_mul_f32 v[0:1], v[0:1], 0.5 op_sel_hi:[1,0]
	s_nop 0
	v_cndmask_b32_e64 v2, v2, -v2, vcc
	v_pk_add_f32 v[2:3], v[2:3], 1.0 op_sel_hi:[1,0]
	s_nop 0
	v_pk_mul_f32 v[0:1], v[0:1], v[2:3]
	s_nop 0
	v_cvt_pk_f16_f32 v0, v0, v1
	global_store_dword v[6:7], v0, off offset:896
	s_endpgm
	.p2alignl 8, 3212836864

_Z9k_gemm_tlILi2ELb1EEvPKDF16_6TlArgs:
	s_load_dwordx4 s[12:15], s[0:1], 0x0
	s_load_dwordx8 s[4:11], s[0:1], 0x18
	v_lshrrev_b32_e32 v99, 6, v0
	s_lshr_b32 s16, s2, 6
	s_lshl_b32 s2, s2, 6
	s_mov_b32 s17, 0
	s_and_b32 s2, s2, 0xfc0
	v_lshl_or_b32 v86, s3, 2, v99
	v_mov_b32_e32 v87, 0
	s_lshl_b64 s[18:19], s[16:17], 21
	v_lshlrev_b64 v[2:3], 15, v[86:87]
	s_or_b32 s18, s18, s2
	s_waitcnt lgkmcnt(0)
	v_lshl_add_u64 v[2:3], s[12:13], 0, v[2:3]
	v_lshlrev_b32_e32 v1, 4, v0
	s_lshl_b64 s[12:13], s[18:19], 1
	v_and_b32_e32 v86, 0x3f0, v1
	s_add_u32 s12, s14, s12
	v_lshl_add_u64 v[88:89], v[2:3], 0, v[86:87]
	v_lshrrev_b32_e32 v100, 3, v0
	s_addc_u32 s13, s15, s13
	v_and_b32_e32 v86, 0x70, v1
	v_or_b32_e32 v98, 0x100, v0
	v_lshl_add_u64 v[2:3], s[12:13], 0, v[86:87]
	v_lshrrev_b32_e32 v101, 3, v98
	v_lshlrev_b32_e32 v86, 13, v100
	v_lshl_add_u64 v[92:93], v[2:3], 0, v[86:87]
	v_lshlrev_b32_e32 v86, 13, v101
	v_or_b32_e32 v107, 64, v100
	v_lshl_add_u64 v[90:91], v[2:3], 0, v[86:87]
	v_lshlrev_b32_e32 v86, 13, v107
	v_or_b32_e32 v106, 64, v101
	v_lshl_add_u64 v[6:7], v[2:3], 0, v[86:87]
	v_lshlrev_b32_e32 v86, 13, v106
	v_lshl_add_u64 v[8:9], v[2:3], 0, v[86:87]
	v_lshlrev_b32_e32 v86, 2, v0
	s_movk_i32 s20, 0x1000
	v_lshl_add_u64 v[2:3], s[4:5], 0, v[86:87]
	v_add_co_u32_e32 v4, vcc, s20, v2
	s_movk_i32 s12, 0x2000
	s_nop 0
	v_addc_co_u32_e32 v5, vcc, 0, v3, vcc
	v_add_co_u32_e32 v18, vcc, s12, v2
	s_movk_i32 s12, 0x3000
	s_nop 0
	v_addc_co_u32_e32 v19, vcc, 0, v3, vcc
	v_add_co_u32_e32 v20, vcc, s12, v2
	s_movk_i32 s12, 0x4000
	s_nop 0
	v_addc_co_u32_e32 v21, vcc, 0, v3, vcc
	v_add_co_u32_e32 v48, vcc, s12, v2
	s_movk_i32 s12, 0x5000
	s_nop 0
	v_addc_co_u32_e32 v49, vcc, 0, v3, vcc
	v_add_co_u32_e32 v50, vcc, s12, v2
	s_movk_i32 s12, 0x6000
	s_nop 0
	v_addc_co_u32_e32 v51, vcc, 0, v3, vcc
	v_add_co_u32_e32 v52, vcc, s12, v2
	s_movk_i32 s12, 0x7000
	s_nop 0
	v_addc_co_u32_e32 v53, vcc, 0, v3, vcc
	v_add_co_u32_e32 v54, vcc, s12, v2
	s_mov_b32 s12, 0x8000
	s_nop 0
	v_addc_co_u32_e32 v55, vcc, 0, v3, vcc
	global_load_dword v11, v86, s[4:5]
	global_load_dword v10, v86, s[4:5] offset:2048
	v_or_b32_e32 v1, 0x400, v0
	v_add_co_u32_e32 v56, vcc, s12, v2
	v_lshlrev_b32_e32 v15, 2, v1
	s_nop 0
	v_addc_co_u32_e32 v57, vcc, 0, v3, vcc
	s_mov_b32 s12, 0x9000
	global_load_dword v13, v15, s[4:5]
	global_load_dword v12, v[4:5], off offset:2048
	global_load_dword v14, v[18:19], off offset:2048
	v_add_co_u32_e32 v58, vcc, s12, v2
	s_mov_b32 s12, 0xa000
	s_nop 0
	v_addc_co_u32_e32 v59, vcc, 0, v3, vcc
	v_add_co_u32_e32 v60, vcc, s12, v2
	global_load_dword v15, v[20:21], off offset:-4096
	global_load_dword v17, v[20:21], off
	global_load_dword v16, v[20:21], off offset:2048
	global_load_dword v23, v[50:51], off offset:-4096
	global_load_dword v25, v[50:51], off
	v_addc_co_u32_e32 v61, vcc, 0, v3, vcc
	s_mov_b32 s12, 0xb000
	global_load_dword v24, v[50:51], off offset:2048
	global_load_dword v27, v[54:55], off offset:-4096
	global_load_dword v29, v[54:55], off
	global_load_dword v28, v[54:55], off offset:2048
	global_load_dword v22, v[48:49], off offset:2048
	global_load_dword v26, v[52:53], off offset:2048
	global_load_dword v30, v[56:57], off offset:2048
	v_add_co_u32_e32 v62, vcc, s12, v2
	s_mov_b32 s12, 0xc000
	s_nop 0
	v_addc_co_u32_e32 v63, vcc, 0, v3, vcc
	v_add_co_u32_e32 v64, vcc, s12, v2
	s_mov_b32 s12, 0xd000
	s_nop 0
	v_addc_co_u32_e32 v65, vcc, 0, v3, vcc
	v_add_co_u32_e32 v66, vcc, s12, v2
	global_load_dword v32, v[60:61], off offset:2048
	global_load_dword v31, v[58:59], off offset:-4096
	global_load_dword v35, v[58:59], off
	global_load_dword v34, v[58:59], off offset:2048
	global_load_dword v33, v[62:63], off offset:-4096
	global_load_dword v37, v[62:63], off
	v_addc_co_u32_e32 v67, vcc, 0, v3, vcc
	s_mov_b32 s12, 0xe000
	v_add_co_u32_e32 v46, vcc, s12, v2
	s_mov_b32 s12, 0xf000
	s_nop 0
	v_addc_co_u32_e32 v47, vcc, 0, v3, vcc
	v_add_co_u32_e32 v68, vcc, s12, v2
	s_load_dwordx4 s[12:15], s[0:1], 0x40
	s_nop 0
	v_addc_co_u32_e32 v69, vcc, 0, v3, vcc
	global_load_dword v36, v[62:63], off offset:2048
	global_load_dword v41, v[66:67], off offset:-4096
	global_load_dword v39, v[66:67], off
	global_load_dword v38, v[66:67], off offset:2048
	global_load_dword v43, v[68:69], off offset:-4096
	global_load_dword v40, v[64:65], off offset:2048
	global_load_dword v42, v[46:47], off offset:2048
	global_load_dword v45, v[68:69], off
	global_load_dword v44, v[68:69], off offset:2048
	global_load_dword v120, v86, s[6:7]
	global_load_dword v75, v86, s[4:5] offset:1024
	global_load_dword v76, v[20:21], off offset:3072
	global_load_dword v77, v[20:21], off offset:1024
	global_load_dword v74, v86, s[4:5] offset:3072
	global_load_dword v78, v[4:5], off offset:3072
	global_load_dword v80, v[18:19], off offset:3072
	global_load_dword v83, v[48:49], off offset:1024
	global_load_dword v81, v[18:19], off offset:1024
	global_load_dword v79, v[4:5], off offset:1024
	global_load_dword v84, v[54:55], off offset:3072
	global_load_dword v85, v[54:55], off offset:1024
	global_load_dword v94, v[50:51], off offset:3072
	global_load_dword v95, v[50:51], off offset:1024
	global_load_dword v82, v[48:49], off offset:3072
	global_load_dword v96, v[52:53], off offset:3072
	global_load_dword v102, v[56:57], off offset:3072
	global_load_dword v103, v[56:57], off offset:1024
	global_load_dword v97, v[52:53], off offset:1024
	global_load_dword v105, v[62:63], off offset:1024
	global_load_dword v108, v[58:59], off offset:3072
	global_load_dword v109, v[58:59], off offset:1024
	global_load_dword v110, v[60:61], off offset:3072
	global_load_dword v112, v[64:65], off offset:3072
	global_load_dword v115, v[46:47], off offset:1024
	global_load_dword v113, v[64:65], off offset:1024
	global_load_dword v111, v[60:61], off offset:1024
	global_load_dword v116, v[66:67], off offset:3072
	global_load_dword v117, v[66:67], off offset:1024
	global_load_dword v104, v[62:63], off offset:3072
	global_load_dword v121, v86, s[8:9]
	global_load_dword v122, v86, s[6:7] offset:1024
	global_load_dword v123, v86, s[8:9] offset:1024
	global_load_dword v114, v[46:47], off offset:3072
	global_load_dword v118, v[68:69], off offset:3072
	global_load_dword v119, v[68:69], off offset:1024
	global_load_dwordx4 v[18:21], v[88:89], off
	global_load_dwordx4 v[62:65], v[88:89], off offset:1024
	global_load_dwordx4 v[54:57], v[88:89], off offset:2048
	global_load_dwordx4 v[50:53], v[88:89], off offset:3072
	global_load_dwordx4 v[70:73], v[92:93], off
	global_load_dwordx4 v[2:5], v[90:91], off
	s_mov_b32 s4, 0x39000000
	s_cmp_eq_u32 s3, 0
	s_waitcnt vmcnt(62)
	v_pk_add_f32 v[10:11], v[10:11], 0 op_sel_hi:[1,0]
	s_nop 0
	v_pk_add_f32 v[10:11], v[10:11], v[12:13]
	s_nop 0
	v_pk_add_f32 v[10:11], v[10:11], v[14:15]
	s_nop 0
	v_pk_add_f32 v[10:11], v[10:11], v[16:17]
	s_waitcnt vmcnt(59)
	v_pk_add_f32 v[10:11], v[10:11], v[22:23]
	s_nop 0
	v_pk_add_f32 v[10:11], v[10:11], v[24:25]
	s_waitcnt vmcnt(1)
	v_cvt_f32_f16_e32 v22, v72
	v_pk_add_f32 v[10:11], v[10:11], v[26:27]
	v_cvt_f32_f16_sdwa v23, v72 dst_sel:DWORD dst_unused:UNUSED_PAD src0_sel:WORD_1
	v_pk_add_f32 v[10:11], v[10:11], v[28:29]
	v_cvt_f32_f16_e32 v24, v73
	v_pk_add_f32 v[10:11], v[10:11], v[30:31]
	v_cvt_f32_f16_sdwa v25, v73 dst_sel:DWORD dst_unused:UNUSED_PAD src0_sel:WORD_1
	v_pk_add_f32 v[10:11], v[10:11], v[34:35]
	s_nop 0
	v_pk_add_f32 v[10:11], v[10:11], v[32:33]
	s_nop 0
	v_pk_add_f32 v[10:11], v[10:11], v[36:37]
	s_nop 0
	v_pk_add_f32 v[10:11], v[10:11], v[40:41]
	s_nop 0
	v_pk_add_f32 v[10:11], v[10:11], v[38:39]
	s_nop 0
	v_pk_add_f32 v[10:11], v[10:11], v[42:43]
	s_nop 0
	v_pk_add_f32 v[10:11], v[10:11], v[44:45]
	s_nop 0
	v_pk_mul_f32 v[10:11], v[10:11], s[4:5] op_sel_hi:[1,0]
	s_mov_b32 s5, 0xf800000
	v_fma_f32 v10, -v11, v11, v10
	v_cmp_ngt_f32_e32 vcc, 0, v10
	s_nop 1
	v_cndmask_b32_e32 v10, 0, v10, vcc
	v_add_f32_e32 v10, 0x3727c5ac, v10
	v_mul_f32_e32 v12, 0x4f800000, v10
	v_cmp_gt_f32_e32 vcc, s5, v10
	s_nop 1
	v_cndmask_b32_e32 v10, v10, v12, vcc
	v_add_co_u32_e64 v12, s[0:1], s20, v88
	v_sqrt_f32_e32 v14, v10
	s_nop 0
	v_addc_co_u32_e64 v13, s[0:1], 0, v89, s[0:1]
	global_load_dwordx4 v[46:49], v[12:13], off
	global_load_dwordx4 v[38:41], v[12:13], off offset:1024
	global_load_dwordx4 v[42:45], v[12:13], off offset:2048
	global_load_dwordx4 v[34:37], v[12:13], off offset:3072
	global_load_dwordx4 v[66:69], v[6:7], off
	global_load_dwordx4 v[58:61], v[8:9], off
	v_add_u32_e32 v15, -1, v14
	v_fma_f32 v16, -v15, v14, v10
	v_cmp_ge_f32_e64 s[0:1], 0, v16
	v_add_u32_e32 v16, 1, v14
	s_nop 0
	v_cndmask_b32_e64 v15, v14, v15, s[0:1]
	v_fma_f32 v14, -v16, v14, v10
	v_cmp_lt_f32_e64 s[0:1], 0, v14
	s_nop 1
	v_cndmask_b32_e64 v14, v15, v16, s[0:1]
	v_mul_f32_e32 v15, 0x37800000, v14
	v_cndmask_b32_e32 v14, v14, v15, vcc
	v_mov_b32_e32 v15, 0x260
	v_cmp_class_f32_e32 vcc, v10, v15
	s_nop 1
	v_cndmask_b32_e32 v10, v14, v10, vcc
	v_div_scale_f32 v14, s[0:1], v10, v10, v120
	v_rcp_f32_e32 v16, v14
	v_div_scale_f32 v8, vcc, v120, v10, v120
	v_fma_f32 v6, -v14, v16, 1.0
	v_fmac_f32_e32 v16, v6, v16
	v_pk_add_f32 v[6:7], v[74:75], 0 op_sel_hi:[1,0]
	v_mul_f32_e32 v9, v8, v16
	v_pk_add_f32 v[6:7], v[6:7], v[78:79]
	v_fma_f32 v13, -v14, v9, v8
	v_pk_add_f32 v[6:7], v[6:7], v[80:81]
	v_fmac_f32_e32 v9, v13, v16
	v_pk_add_f32 v[6:7], v[6:7], v[76:77]
	v_fma_f32 v8, -v14, v9, v8
	v_pk_add_f32 v[6:7], v[6:7], v[82:83]
	v_div_fmas_f32 v8, v8, v16, v9
	v_pk_add_f32 v[6:7], v[6:7], v[94:95]
	v_div_fixup_f32 v8, v8, v10, v120
	v_pk_add_f32 v[6:7], v[6:7], v[96:97]
	v_fma_f32 v9, -v11, v8, v121
	v_pk_add_f32 v[6:7], v[6:7], v[84:85]
	s_nop 0
	v_pk_add_f32 v[6:7], v[6:7], v[102:103]
	s_nop 0
	v_pk_add_f32 v[6:7], v[6:7], v[108:109]
	s_nop 0
	v_pk_add_f32 v[6:7], v[6:7], v[110:111]
	s_nop 0
	v_pk_add_f32 v[6:7], v[6:7], v[104:105]
	s_nop 0
	v_pk_add_f32 v[6:7], v[6:7], v[112:113]
	s_nop 0
	v_pk_add_f32 v[6:7], v[6:7], v[116:117]
	s_nop 0
	v_pk_add_f32 v[6:7], v[6:7], v[114:115]
	s_nop 0
	v_pk_add_f32 v[6:7], v[6:7], v[118:119]
	s_nop 0
	v_pk_mul_f32 v[6:7], v[6:7], s[4:5] op_sel_hi:[1,0]
	s_nop 0
	v_fma_f32 v6, -v7, v7, v6
	v_cmp_ngt_f32_e64 s[0:1], 0, v6
	s_nop 1
	v_cndmask_b32_e64 v6, 0, v6, s[0:1]
	v_add_f32_e32 v6, 0x3727c5ac, v6
	v_mul_f32_e32 v12, 0x4f800000, v6
	v_cmp_gt_f32_e64 s[0:1], s5, v6
	s_nop 1
	v_cndmask_b32_e64 v6, v6, v12, s[0:1]
	v_sqrt_f32_e32 v12, v6
	s_nop 0
	v_add_u32_e32 v13, -1, v12
	v_fma_f32 v14, -v13, v12, v6
	v_cmp_ge_f32_e64 s[4:5], 0, v14
	v_add_u32_e32 v14, 1, v12
	s_nop 0
	v_cndmask_b32_e64 v13, v12, v13, s[4:5]
	v_fma_f32 v12, -v14, v12, v6
	v_cmp_lt_f32_e64 s[4:5], 0, v12
	s_nop 1
	v_cndmask_b32_e64 v12, v13, v14, s[4:5]
	v_mul_f32_e32 v13, 0x37800000, v12
	v_cndmask_b32_e64 v12, v12, v13, s[0:1]
	v_cmp_class_f32_e64 s[0:1], v6, v15
	s_cselect_b64 s[4:5], -1, 0
	v_lshlrev_b32_e32 v15, 2, v100
	v_cndmask_b32_e64 v6, v12, v6, s[0:1]
	v_div_scale_f32 v12, s[0:1], v6, v6, v122
	v_rcp_f32_e32 v13, v12
	s_lshl_b64 s[0:1], s[18:19], 2
	s_waitcnt lgkmcnt(0)
	s_add_u32 s0, s14, s0
	s_addc_u32 s1, s15, s1
	v_fma_f32 v10, -v12, v13, 1.0
	v_fmac_f32_e32 v13, v10, v13
	v_div_scale_f32 v10, vcc, v122, v6, v122
	v_mul_f32_e32 v11, v10, v13
	v_fma_f32 v14, -v12, v11, v10
	v_fmac_f32_e32 v11, v14, v13
	v_fma_f32 v10, -v12, v11, v10
	v_div_fmas_f32 v10, v10, v13, v11
	v_div_fixup_f32 v6, v10, v6, v122
	ds_write2st64_b32 v86, v8, v6 offset0:136 offset1:140
	v_fma_f32 v6, -v7, v6, v123
	ds_write2st64_b32 v86, v9, v6 offset0:144 offset1:148
	s_waitcnt lgkmcnt(0)
	s_barrier
	v_and_b32_e32 v14, 7, v0
	ds_read2st64_b32 v[8:9], v15 offset0:136 offset1:144
	v_lshlrev_b32_e32 v6, 5, v14
	v_mov_b32_e32 v7, v87
	v_lshl_add_u64 v[94:95], s[0:1], 0, v[6:7]
	v_cvt_f32_f16_e32 v6, v70
	v_cvt_f32_f16_sdwa v7, v70 dst_sel:DWORD dst_unused:UNUSED_PAD src0_sel:WORD_1
	v_cvt_f32_f16_e32 v12, v71
	v_cvt_f32_f16_sdwa v13, v71 dst_sel:DWORD dst_unused:UNUSED_PAD src0_sel:WORD_1
	s_waitcnt lgkmcnt(0)
	v_mov_b32_e32 v16, v9
	s_cmp_lg_u32 s3, 0
	v_pk_fma_f32 v[10:11], v[8:9], v[6:7], v[16:17] op_sel_hi:[0,1,0]
	v_pk_fma_f32 v[12:13], v[8:9], v[12:13], v[16:17] op_sel_hi:[0,1,0]
	v_pk_fma_f32 v[6:7], v[8:9], v[22:23], v[16:17] op_sel_hi:[0,1,0]
	v_pk_fma_f32 v[8:9], v[8:9], v[24:25], v[16:17] op_sel_hi:[0,1,0]
	s_cmp_lg_u32 s3, 0
	s_cbranch_scc1 .LBB5_2
	v_lshlrev_b32_e32 v16, 14, v100
	v_mov_b32_e32 v17, v87
	v_lshl_add_u64 v[16:17], v[94:95], 0, v[16:17]
	global_store_dwordx4 v[16:17], v[10:13], off nt
	global_store_dwordx4 v[16:17], v[6:9], off offset:16 nt
.LBB5_2:
	v_lshlrev_b32_e32 v108, 4, v14
	s_movk_i32 s6, 0x90
	v_cvt_pk_f16_f32 v10, v10, v11
	v_cvt_pk_f16_f32 v11, v12, v13
	v_cvt_pk_f16_f32 v12, v6, v7
	v_cvt_pk_f16_f32 v13, v8, v9
	v_mad_u32_u24 v6, v100, s6, v108
	v_lshlrev_b32_e32 v78, 2, v101
	ds_write_b128 v6, v[10:13]
	ds_read2st64_b32 v[10:11], v78 offset0:136 offset1:144
	s_waitcnt vmcnt(6)
	v_cvt_f32_f16_sdwa v7, v2 dst_sel:DWORD dst_unused:UNUSED_PAD src0_sel:WORD_1
	v_cvt_f32_f16_e32 v6, v2
	v_cvt_f32_f16_sdwa v9, v3 dst_sel:DWORD dst_unused:UNUSED_PAD src0_sel:WORD_1
	v_cvt_f32_f16_e32 v8, v3
	v_cvt_f32_f16_sdwa v3, v4 dst_sel:DWORD dst_unused:UNUSED_PAD src0_sel:WORD_1
	v_cvt_f32_f16_e32 v2, v4
	v_cvt_f32_f16_sdwa v13, v5 dst_sel:DWORD dst_unused:UNUSED_PAD src0_sel:WORD_1
	v_cvt_f32_f16_e32 v12, v5
	s_waitcnt lgkmcnt(0)
	v_mov_b32_e32 v4, v11
	v_pk_fma_f32 v[6:7], v[10:11], v[6:7], v[4:5] op_sel_hi:[0,1,0]
	v_pk_fma_f32 v[8:9], v[10:11], v[8:9], v[4:5] op_sel_hi:[0,1,0]
	v_pk_fma_f32 v[2:3], v[10:11], v[2:3], v[4:5] op_sel_hi:[0,1,0]
	v_cndmask_b32_e64 v5, 0, 1, s[4:5]
	v_or_b32_e32 v102, 0x8800, v15
	v_or_b32_e32 v103, 0x9000, v15
	v_cmp_ne_u32_e64 s[0:1], 1, v5
	s_andn2_b64 vcc, exec, s[4:5]
	v_pk_fma_f32 v[4:5], v[10:11], v[12:13], v[4:5] op_sel_hi:[0,1,0]
	s_cmp_lg_u32 s3, 0
	s_cbranch_scc1 .LBB5_4
	v_lshlrev_b32_e32 v10, 14, v101
	v_mov_b32_e32 v11, 0
	v_lshl_add_u64 v[10:11], v[94:95], 0, v[10:11]
	global_store_dwordx4 v[10:11], v[6:9], off nt
	global_store_dwordx4 v[10:11], v[2:5], off offset:16 nt
.LBB5_4:
	v_lshrrev_b32_e32 v10, 2, v0
	v_and_b32_e32 v11, 16, v0
	v_and_b32_e32 v10, 11, v10
	v_cvt_pk_f16_f32 v6, v6, v7
	v_cvt_pk_f16_f32 v7, v8, v9
	v_cvt_pk_f16_f32 v8, v2, v3
	v_cvt_pk_f16_f32 v9, v4, v5
	v_mad_u32_u24 v2, v101, s6, v108
	v_lshlrev_b32_e32 v3, 3, v0
	ds_write_b128 v2, v[6:9]
	v_mul_u32_u24_e32 v2, 0x90, v10
	v_and_b32_e32 v3, 24, v3
	v_lshlrev_b32_e32 v4, 1, v11
	v_add3_u32 v87, v2, v3, v4
	s_waitcnt lgkmcnt(0)
	s_barrier
	ds_read_b64_tr_b16 v[2:3], v87
	ds_read_b64_tr_b16 v[4:5], v87 offset:576
	ds_read_b64_tr_b16 v[24:25], v87 offset:640
	ds_read_b64_tr_b16 v[70:71], v87 offset:2304
	ds_read_b64_tr_b16 v[74:75], v87 offset:2368
	ds_read_b64_tr_b16 v[22:23], v87 offset:64
	ds_read_b32 v84, v103 offset:256
	s_waitcnt lgkmcnt(5)
	v_mfma_f32_32x32x16_f16 v[2:17], v[18:21], v[2:5], 0
	ds_read_b64_tr_b16 v[72:73], v87 offset:2880
	ds_read_b64_tr_b16 v[76:77], v87 offset:2944
	ds_read_b64_tr_b16 v[80:81], v87 offset:4608
	ds_read_b64_tr_b16 v[110:111], v87 offset:4672
	ds_read_b64_tr_b16 v[82:83], v87 offset:5184
	s_mov_b32 s4, 0x100000
	v_or_b32_e32 v104, 0x8800, v78
	v_or_b32_e32 v105, 0x9000, v78
	v_mul_u32_u24_e32 v109, 0x90, v100
	s_waitcnt lgkmcnt(6)
	v_mfma_f32_32x32x16_f16 v[18:33], v[18:21], v[22:25], 0
	s_waitcnt lgkmcnt(4)
	v_mfma_f32_32x32x16_f16 v[2:17], v[62:65], v[70:73], v[2:17]
	s_waitcnt lgkmcnt(3)
	v_mfma_f32_32x32x16_f16 v[18:33], v[62:65], v[74:77], v[18:33]
	v_add_co_u32_e32 v64, vcc, s4, v92
	ds_read_b64_tr_b16 v[112:113], v87 offset:5248
	ds_read_b64_tr_b16 v[62:63], v87 offset:6912
	ds_read_b64_tr_b16 v[114:115], v87 offset:6976
	v_addc_co_u32_e32 v65, vcc, 0, v93, vcc
	s_waitcnt lgkmcnt(3)
	v_mfma_f32_32x32x16_f16 v[2:17], v[54:57], v[80:83], v[2:17]
	v_add_co_u32_e32 v80, vcc, s4, v90
	s_movk_i32 s4, 0x2000
	s_nop 0
	v_addc_co_u32_e32 v81, vcc, 0, v91, vcc
	global_load_dwordx4 v[70:73], v[64:65], off
	global_load_dwordx4 v[74:77], v[80:81], off
	v_add_co_u32_e32 v96, vcc, s4, v88
	s_waitcnt lgkmcnt(2)
	v_mfma_f32_32x32x16_f16 v[18:33], v[54:57], v[110:113], v[18:33]
	ds_read_b32 v54, v102 offset:256
	ds_read_b64_tr_b16 v[64:65], v87 offset:7488
	ds_read_b64_tr_b16 v[116:117], v87 offset:7552
	s_waitcnt vmcnt(3)
	v_cvt_f32_f16_sdwa v57, v66 dst_sel:DWORD dst_unused:UNUSED_PAD src0_sel:WORD_1
	v_cvt_f32_f16_e32 v56, v66
	v_addc_co_u32_e32 v97, vcc, 0, v89, vcc
	s_and_b64 vcc, exec, s[0:1]
	s_waitcnt lgkmcnt(1)
	v_mfma_f32_32x32x16_f16 v[2:17], v[50:53], v[62:65], v[2:17]
	v_fma_f32 v78, v54, v56, v84
	v_fma_f32 v79, v54, v57, v84
	v_cvt_f32_f16_sdwa v57, v69 dst_sel:DWORD dst_unused:UNUSED_PAD src0_sel:WORD_1
	v_cvt_f32_f16_e32 v56, v69
	s_waitcnt lgkmcnt(0)
	v_mfma_f32_32x32x16_f16 v[18:33], v[50:53], v[114:117], v[18:33]
	v_cvt_f32_f16_sdwa v51, v67 dst_sel:DWORD dst_unused:UNUSED_PAD src0_sel:WORD_1
	v_cvt_f32_f16_e32 v50, v67
	v_cvt_f32_f16_sdwa v53, v68 dst_sel:DWORD dst_unused:UNUSED_PAD src0_sel:WORD_1
	v_cvt_f32_f16_e32 v52, v68
	v_fma_f32 v80, v54, v50, v84
	v_fma_f32 v81, v54, v51, v84
	v_pk_fma_f32 v[82:83], v[54:55], v[52:53], v[84:85] op_sel_hi:[0,1,0]
	v_pk_fma_f32 v[84:85], v[54:55], v[56:57], v[84:85] op_sel_hi:[0,1,0]
	s_cmp_lg_u32 s3, 0
	s_cbranch_scc1 .LBB5_6
	v_lshlrev_b32_e32 v50, 14, v107
	v_mov_b32_e32 v51, 0
	v_lshl_add_u64 v[50:51], v[94:95], 0, v[50:51]
	global_store_dwordx4 v[50:51], v[78:81], off nt
	global_store_dwordx4 v[50:51], v[82:85], off offset:16 nt
.LBB5_6:
	global_load_dwordx4 v[66:69], v[96:97], off
	global_load_dwordx4 v[62:65], v[96:97], off offset:1024
	global_load_dwordx4 v[54:57], v[96:97], off offset:2048
	s_nop 0
	global_load_dwordx4 v[50:53], v[96:97], off offset:3072
	v_cvt_pk_f16_f32 v78, v78, v79
	v_cvt_pk_f16_f32 v79, v80, v81
	v_cvt_pk_f16_f32 v80, v82, v83
	ds_read_b32 v82, v104 offset:256
	ds_read_b32 v110, v105 offset:256
	v_cvt_pk_f16_f32 v81, v84, v85
	v_add_u32_e32 v107, v108, v109
	s_waitcnt vmcnt(6)
	v_cvt_f32_f16_sdwa v113, v58 dst_sel:DWORD dst_unused:UNUSED_PAD src0_sel:WORD_1
	v_cvt_f32_f16_e32 v112, v58
	ds_write_b128 v107, v[78:81] offset:9216
	v_cvt_f32_f16_sdwa v81, v59 dst_sel:DWORD dst_unused:UNUSED_PAD src0_sel:WORD_1
	v_cvt_f32_f16_e32 v80, v59
	v_cvt_f32_f16_sdwa v59, v60 dst_sel:DWORD dst_unused:UNUSED_PAD src0_sel:WORD_1
	v_cvt_f32_f16_e32 v58, v60
	v_cvt_f32_f16_sdwa v85, v61 dst_sel:DWORD dst_unused:UNUSED_PAD src0_sel:WORD_1
	v_cvt_f32_f16_e32 v84, v61
	v_mul_u32_u24_e32 v96, 0x90, v101
	s_waitcnt lgkmcnt(1)
	v_pk_fma_f32 v[78:79], v[82:83], v[112:113], v[110:111] op_sel_hi:[0,1,0]
	v_pk_fma_f32 v[80:81], v[82:83], v[80:81], v[110:111] op_sel_hi:[0,1,0]
	v_pk_fma_f32 v[58:59], v[82:83], v[58:59], v[110:111] op_sel_hi:[0,1,0]
	s_and_b64 vcc, exec, s[0:1]
	v_pk_fma_f32 v[60:61], v[82:83], v[84:85], v[110:111] op_sel_hi:[0,1,0]
	s_cmp_lg_u32 s3, 0
	s_cbranch_scc1 .LBB5_8
	v_lshlrev_b32_e32 v82, 14, v106
	v_mov_b32_e32 v83, 0
	v_lshl_add_u64 v[82:83], v[94:95], 0, v[82:83]
	global_store_dwordx4 v[82:83], v[78:81], off nt
	global_store_dwordx4 v[82:83], v[58:61], off offset:16 nt
.LBB5_8:
	s_nop 0
	v_cvt_pk_f16_f32 v78, v78, v79
	v_cvt_pk_f16_f32 v79, v80, v81
	v_cvt_pk_f16_f32 v80, v58, v59
	v_cvt_pk_f16_f32 v81, v60, v61
	v_add_u32_e32 v106, v108, v96
	ds_write_b128 v106, v[78:81] offset:9216
	s_waitcnt lgkmcnt(0)
	s_barrier
	ds_read_b64_tr_b16 v[58:59], v87 offset:9216
	ds_read_b64_tr_b16 v[60:61], v87 offset:9792
	ds_read_b64_tr_b16 v[80:81], v87 offset:9856
	ds_read_b64_tr_b16 v[82:83], v87 offset:11520
	ds_read_b64_tr_b16 v[108:109], v87 offset:11584
	ds_read_b64_tr_b16 v[78:79], v87 offset:9280
	ds_read_b32 v112, v103 offset:512
	s_waitcnt lgkmcnt(5)
	v_mfma_f32_32x32x16_f16 v[2:17], v[46:49], v[58:61], v[2:17]
	ds_read_b64_tr_b16 v[84:85], v87 offset:12096
	v_add_co_u32_e32 v96, vcc, 0x3000, v88
	s_mov_b64 s[4:5], vcc
	s_waitcnt lgkmcnt(2)
	v_mfma_f32_32x32x16_f16 v[18:33], v[46:49], v[78:81], v[18:33]
	ds_read_b64_tr_b16 v[110:111], v87 offset:12160
	ds_read_b64_tr_b16 v[46:47], v87 offset:13824
	ds_read_b64_tr_b16 v[58:59], v87 offset:13888
	ds_read_b64_tr_b16 v[48:49], v87 offset:14400
	s_waitcnt lgkmcnt(4)
	v_mfma_f32_32x32x16_f16 v[2:17], v[38:41], v[82:85], v[2:17]
	v_add_co_u32_e32 v84, vcc, 0x180000, v92
	s_nop 1
	v_addc_co_u32_e32 v85, vcc, 0, v93, vcc
	v_add_co_u32_e32 v114, vcc, 0x180000, v90
	s_waitcnt lgkmcnt(3)
	v_mfma_f32_32x32x16_f16 v[18:33], v[38:41], v[108:111], v[18:33]
	v_addc_co_u32_e32 v115, vcc, 0, v91, vcc
	ds_read_b64_tr_b16 v[60:61], v87 offset:14464
	ds_read_b64_tr_b16 v[82:83], v87 offset:16128
	ds_read_b64_tr_b16 v[108:109], v87 offset:16192
	global_load_dwordx4 v[38:41], v[84:85], off
	global_load_dwordx4 v[78:81], v[114:115], off
	v_addc_co_u32_e64 v97, vcc, 0, v89, s[4:5]
	s_and_b64 vcc, exec, s[0:1]
	s_waitcnt lgkmcnt(3)
	v_mfma_f32_32x32x16_f16 v[2:17], v[42:45], v[46:49], v[2:17]
	ds_read_b32 v48, v102 offset:512
	ds_read_b64_tr_b16 v[84:85], v87 offset:16704
	ds_read_b64_tr_b16 v[110:111], v87 offset:16768
	s_waitcnt vmcnt(7)
	v_cvt_f32_f16_sdwa v47, v72 dst_sel:DWORD dst_unused:UNUSED_PAD src0_sel:WORD_1
	v_cvt_f32_f16_e32 v46, v72
	s_waitcnt lgkmcnt(2)
	v_pk_fma_f32 v[46:47], v[48:49], v[46:47], v[112:113] op_sel_hi:[0,1,0]
	v_mfma_f32_32x32x16_f16 v[18:33], v[42:45], v[58:61], v[18:33]
	v_cvt_f32_f16_sdwa v43, v70 dst_sel:DWORD dst_unused:UNUSED_PAD src0_sel:WORD_1
	v_cvt_f32_f16_e32 v42, v70
	v_cvt_f32_f16_sdwa v45, v71 dst_sel:DWORD dst_unused:UNUSED_PAD src0_sel:WORD_1
	v_cvt_f32_f16_e32 v44, v71
	s_waitcnt lgkmcnt(1)
	v_mfma_f32_32x32x16_f16 v[2:17], v[34:37], v[82:85], v[2:17]
	v_fma_f32 v82, v48, v42, v112
	v_fma_f32 v83, v48, v43, v112
	v_cvt_f32_f16_sdwa v43, v73 dst_sel:DWORD dst_unused:UNUSED_PAD src0_sel:WORD_1
	v_cvt_f32_f16_e32 v42, v73
	v_fma_f32 v84, v48, v44, v112
	v_fma_f32 v85, v48, v45, v112
	v_pk_fma_f32 v[48:49], v[48:49], v[42:43], v[112:113] op_sel_hi:[0,1,0]
	s_waitcnt lgkmcnt(0)
	v_mfma_f32_32x32x16_f16 v[18:33], v[34:37], v[108:111], v[18:33]
	s_cmp_lg_u32 s3, 1
	s_cbranch_scc1 .LBB5_10
	v_mov_b32_e32 v34, 0x200000
	v_lshl_or_b32 v34, v100, 14, v34
	v_mov_b32_e32 v35, 0
	v_lshl_add_u64 v[34:35], v[94:95], 0, v[34:35]
	global_store_dwordx4 v[34:35], v[82:85], off nt
	global_store_dwordx4 v[34:35], v[46:49], off offset:16 nt
.LBB5_10:
	global_load_dwordx4 v[70:73], v[96:97], off
	global_load_dwordx4 v[58:61], v[96:97], off offset:1024
	global_load_dwordx4 v[42:45], v[96:97], off offset:2048
	s_nop 0
	global_load_dwordx4 v[34:37], v[96:97], off offset:3072
	v_cvt_pk_f16_f32 v82, v82, v83
	v_cvt_pk_f16_f32 v83, v84, v85
	ds_read_b32 v96, v104 offset:512
	ds_read_b32 v108, v105 offset:512
	v_cvt_pk_f16_f32 v84, v46, v47
	v_cvt_pk_f16_f32 v85, v48, v49
	s_waitcnt vmcnt(10)
	v_cvt_f32_f16_sdwa v111, v74 dst_sel:DWORD dst_unused:UNUSED_PAD src0_sel:WORD_1
	v_cvt_f32_f16_e32 v110, v74
	ds_write_b128 v107, v[82:85]
	v_cvt_f32_f16_sdwa v49, v75 dst_sel:DWORD dst_unused:UNUSED_PAD src0_sel:WORD_1
	v_cvt_f32_f16_e32 v48, v75
	v_cvt_f32_f16_sdwa v75, v76 dst_sel:DWORD dst_unused:UNUSED_PAD src0_sel:WORD_1
	v_cvt_f32_f16_e32 v74, v76
	v_cvt_f32_f16_sdwa v83, v77 dst_sel:DWORD dst_unused:UNUSED_PAD src0_sel:WORD_1
	v_cvt_f32_f16_e32 v82, v77
	s_waitcnt lgkmcnt(1)
	v_pk_fma_f32 v[46:47], v[96:97], v[110:111], v[108:109] op_sel_hi:[0,1,0]
	v_pk_fma_f32 v[48:49], v[96:97], v[48:49], v[108:109] op_sel_hi:[0,1,0]
	v_pk_fma_f32 v[74:75], v[96:97], v[74:75], v[108:109] op_sel_hi:[0,1,0]
	s_and_b64 vcc, exec, s[0:1]
	v_pk_fma_f32 v[76:77], v[96:97], v[82:83], v[108:109] op_sel_hi:[0,1,0]
	s_cmp_lg_u32 s3, 1
	s_cbranch_scc1 .LBB5_12
	v_mov_b32_e32 v82, 0x200000
	v_lshl_or_b32 v82, v101, 14, v82
	v_mov_b32_e32 v83, 0
	v_lshl_add_u64 v[82:83], v[94:95], 0, v[82:83]
	global_store_dwordx4 v[82:83], v[46:49], off nt
	global_store_dwordx4 v[82:83], v[74:77], off offset:16 nt
.LBB5_12:
	s_nop 0
	v_cvt_pk_f16_f32 v46, v46, v47
	v_cvt_pk_f16_f32 v47, v48, v49
	v_cvt_pk_f16_f32 v48, v74, v75
	v_cvt_pk_f16_f32 v49, v76, v77
	ds_write_b128 v106, v[46:49]
	s_waitcnt lgkmcnt(0)
	s_barrier
	ds_read_b64_tr_b16 v[46:47], v87
	ds_read_b64_tr_b16 v[48:49], v87 offset:576
	ds_read_b64_tr_b16 v[76:77], v87 offset:640
	ds_read_b64_tr_b16 v[82:83], v87 offset:2304
	ds_read_b64_tr_b16 v[108:109], v87 offset:2368
	ds_read_b64_tr_b16 v[74:75], v87 offset:64
	ds_read_b32 v116, v103 offset:768
	s_waitcnt vmcnt(9) lgkmcnt(5)
	v_mfma_f32_32x32x16_f16 v[2:17], v[66:69], v[46:49], v[2:17]
	ds_read_b64_tr_b16 v[84:85], v87 offset:2880
	v_add_co_u32_e32 v96, vcc, 0x4000, v88
	s_mov_b64 s[4:5], vcc
	ds_read_b64_tr_b16 v[110:111], v87 offset:2944
	ds_read_b64_tr_b16 v[46:47], v87 offset:4608
	ds_read_b64_tr_b16 v[112:113], v87 offset:4672
	ds_read_b64_tr_b16 v[48:49], v87 offset:5184
	s_waitcnt lgkmcnt(6)
	v_mfma_f32_32x32x16_f16 v[18:33], v[66:69], v[74:77], v[18:33]
	s_waitcnt vmcnt(8) lgkmcnt(4)
	v_mfma_f32_32x32x16_f16 v[2:17], v[62:65], v[82:85], v[2:17]
	v_add_co_u32_e32 v82, vcc, 0x200000, v92
	s_nop 1
	v_addc_co_u32_e32 v83, vcc, 0, v93, vcc
	v_add_co_u32_e32 v84, vcc, 0x200000, v90
	s_waitcnt lgkmcnt(3)
	v_mfma_f32_32x32x16_f16 v[18:33], v[62:65], v[108:111], v[18:33]
	v_addc_co_u32_e32 v85, vcc, 0, v91, vcc
	ds_read_b64_tr_b16 v[114:115], v87 offset:5248
	ds_read_b64_tr_b16 v[62:63], v87 offset:6912
	ds_read_b64_tr_b16 v[108:109], v87 offset:6976
	global_load_dwordx4 v[74:77], v[82:83], off
	global_load_dwordx4 v[66:69], v[84:85], off
	v_addc_co_u32_e64 v97, vcc, 0, v89, s[4:5]
	s_and_b64 vcc, exec, s[0:1]
	s_waitcnt vmcnt(9) lgkmcnt(3)
	v_mfma_f32_32x32x16_f16 v[2:17], v[54:57], v[46:49], v[2:17]
	ds_read_b32 v46, v102 offset:768
	ds_read_b64_tr_b16 v[64:65], v87 offset:7488
	ds_read_b64_tr_b16 v[110:111], v87 offset:7552
	s_waitcnt vmcnt(7)
	v_cvt_f32_f16_sdwa v49, v38 dst_sel:DWORD dst_unused:UNUSED_PAD src0_sel:WORD_1
	v_cvt_f32_f16_e32 v48, v38
	v_cvt_f32_f16_e32 v38, v40
	s_waitcnt lgkmcnt(2)
	v_pk_fma_f32 v[82:83], v[46:47], v[48:49], v[116:117] op_sel_hi:[0,1,0]
	v_mfma_f32_32x32x16_f16 v[18:33], v[54:57], v[112:115], v[18:33]
	v_cvt_f32_f16_sdwa v55, v39 dst_sel:DWORD dst_unused:UNUSED_PAD src0_sel:WORD_1
	v_cvt_f32_f16_e32 v54, v39
	v_cvt_f32_f16_sdwa v39, v40 dst_sel:DWORD dst_unused:UNUSED_PAD src0_sel:WORD_1
	v_fma_f32 v84, v46, v54, v116
	v_fma_f32 v85, v46, v55, v116
	v_pk_fma_f32 v[54:55], v[46:47], v[38:39], v[116:117] op_sel_hi:[0,1,0]
	s_waitcnt lgkmcnt(1)
	v_mfma_f32_32x32x16_f16 v[2:17], v[50:53], v[62:65], v[2:17]
	v_cvt_f32_f16_sdwa v39, v41 dst_sel:DWORD dst_unused:UNUSED_PAD src0_sel:WORD_1
	v_cvt_f32_f16_e32 v38, v41
	v_fma_f32 v56, v46, v38, v116
	v_fma_f32 v57, v46, v39, v116
	s_waitcnt lgkmcnt(0)
	v_mfma_f32_32x32x16_f16 v[18:33], v[50:53], v[108:111], v[18:33]
	s_cmp_lg_u32 s3, 1
	s_cbranch_scc1 .LBB5_14
	v_mov_b32_e32 v38, 0x300000
	v_lshl_or_b32 v38, v100, 14, v38
	v_mov_b32_e32 v39, 0
	v_lshl_add_u64 v[38:39], v[94:95], 0, v[38:39]
	global_store_dwordx4 v[38:39], v[82:85], off nt
	global_store_dwordx4 v[38:39], v[54:57], off offset:16 nt
.LBB5_14:
	global_load_dwordx4 v[62:65], v[96:97], off
	global_load_dwordx4 v[50:53], v[96:97], off offset:1024
	global_load_dwordx4 v[46:49], v[96:97], off offset:2048
	s_nop 0
	global_load_dwordx4 v[38:41], v[96:97], off offset:3072
	v_cvt_pk_f16_f32 v82, v82, v83
	v_cvt_pk_f16_f32 v83, v84, v85
	ds_read_b32 v96, v104 offset:768
	ds_read_b32 v108, v105 offset:768
	v_cvt_pk_f16_f32 v84, v54, v55
	v_cvt_pk_f16_f32 v85, v56, v57
	s_waitcnt vmcnt(10)
	v_cvt_f32_f16_sdwa v111, v78 dst_sel:DWORD dst_unused:UNUSED_PAD src0_sel:WORD_1
	v_cvt_f32_f16_e32 v110, v78
	ds_write_b128 v107, v[82:85] offset:9216
	v_cvt_f32_f16_sdwa v57, v79 dst_sel:DWORD dst_unused:UNUSED_PAD src0_sel:WORD_1
	v_cvt_f32_f16_e32 v56, v79
	v_cvt_f32_f16_sdwa v79, v80 dst_sel:DWORD dst_unused:UNUSED_PAD src0_sel:WORD_1
	v_cvt_f32_f16_e32 v78, v80
	v_cvt_f32_f16_sdwa v83, v81 dst_sel:DWORD dst_unused:UNUSED_PAD src0_sel:WORD_1
	v_cvt_f32_f16_e32 v82, v81
	s_waitcnt lgkmcnt(1)
	v_pk_fma_f32 v[54:55], v[96:97], v[110:111], v[108:109] op_sel_hi:[0,1,0]
	v_pk_fma_f32 v[56:57], v[96:97], v[56:57], v[108:109] op_sel_hi:[0,1,0]
	v_pk_fma_f32 v[78:79], v[96:97], v[78:79], v[108:109] op_sel_hi:[0,1,0]
	s_and_b64 vcc, exec, s[0:1]
	v_pk_fma_f32 v[80:81], v[96:97], v[82:83], v[108:109] op_sel_hi:[0,1,0]
	s_cmp_lg_u32 s3, 1
	s_cbranch_scc1 .LBB5_16
	v_mov_b32_e32 v82, 0x300000
	v_lshl_or_b32 v82, v101, 14, v82
	v_mov_b32_e32 v83, 0
	v_lshl_add_u64 v[82:83], v[94:95], 0, v[82:83]
	global_store_dwordx4 v[82:83], v[54:57], off nt
	global_store_dwordx4 v[82:83], v[78:81], off offset:16 nt
.LBB5_16:
	s_nop 0
	v_cvt_pk_f16_f32 v54, v54, v55
	v_cvt_pk_f16_f32 v55, v56, v57
	v_cvt_pk_f16_f32 v56, v78, v79
	v_cvt_pk_f16_f32 v57, v80, v81
	ds_write_b128 v106, v[54:57] offset:9216
	s_waitcnt lgkmcnt(0)
	s_barrier
	ds_read_b64_tr_b16 v[54:55], v87 offset:9216
	ds_read_b64_tr_b16 v[56:57], v87 offset:9792
	ds_read_b64_tr_b16 v[80:81], v87 offset:9856
	ds_read_b64_tr_b16 v[82:83], v87 offset:11520
	ds_read_b64_tr_b16 v[108:109], v87 offset:11584
	ds_read_b64_tr_b16 v[78:79], v87 offset:9280
	ds_read_b32 v116, v103 offset:1024
	s_waitcnt vmcnt(9) lgkmcnt(5)
	v_mfma_f32_32x32x16_f16 v[2:17], v[70:73], v[54:57], v[2:17]
	ds_read_b64_tr_b16 v[84:85], v87 offset:12096
	v_add_co_u32_e32 v96, vcc, 0x5000, v88
	s_mov_b64 s[4:5], vcc
	ds_read_b64_tr_b16 v[110:111], v87 offset:12160
	ds_read_b64_tr_b16 v[54:55], v87 offset:13824
	ds_read_b64_tr_b16 v[112:113], v87 offset:13888
	ds_read_b64_tr_b16 v[56:57], v87 offset:14400
	s_waitcnt lgkmcnt(6)
	v_mfma_f32_32x32x16_f16 v[18:33], v[70:73], v[78:81], v[18:33]
	s_waitcnt vmcnt(8) lgkmcnt(4)
	v_mfma_f32_32x32x16_f16 v[2:17], v[58:61], v[82:85], v[2:17]
	v_add_co_u32_e32 v82, vcc, 0x280000, v92
	s_nop 1
	v_addc_co_u32_e32 v83, vcc, 0, v93, vcc
	v_add_co_u32_e32 v84, vcc, 0x280000, v90
	s_waitcnt lgkmcnt(3)
	v_mfma_f32_32x32x16_f16 v[18:33], v[58:61], v[108:111], v[18:33]
	v_addc_co_u32_e32 v85, vcc, 0, v91, vcc
	ds_read_b64_tr_b16 v[114:115], v87 offset:14464
	ds_read_b64_tr_b16 v[58:59], v87 offset:16128
	ds_read_b64_tr_b16 v[108:109], v87 offset:16192
	global_load_dwordx4 v[78:81], v[82:83], off
	global_load_dwordx4 v[70:73], v[84:85], off
	v_addc_co_u32_e64 v97, vcc, 0, v89, s[4:5]
	s_and_b64 vcc, exec, s[0:1]
	s_waitcnt vmcnt(9) lgkmcnt(3)
	v_mfma_f32_32x32x16_f16 v[2:17], v[42:45], v[54:57], v[2:17]
	ds_read_b32 v54, v102 offset:1024
	ds_read_b64_tr_b16 v[60:61], v87 offset:16704
	ds_read_b64_tr_b16 v[110:111], v87 offset:16768
	s_waitcnt vmcnt(7)
	v_cvt_f32_f16_sdwa v57, v76 dst_sel:DWORD dst_unused:UNUSED_PAD src0_sel:WORD_1
	v_cvt_f32_f16_e32 v56, v76
	s_waitcnt lgkmcnt(5)
	v_mfma_f32_32x32x16_f16 v[18:33], v[42:45], v[112:115], v[18:33]
	v_cvt_f32_f16_sdwa v43, v74 dst_sel:DWORD dst_unused:UNUSED_PAD src0_sel:WORD_1
	v_cvt_f32_f16_e32 v42, v74
	v_cvt_f32_f16_sdwa v45, v75 dst_sel:DWORD dst_unused:UNUSED_PAD src0_sel:WORD_1
	v_cvt_f32_f16_e32 v44, v75
	s_waitcnt lgkmcnt(2)
	v_pk_fma_f32 v[74:75], v[54:55], v[56:57], v[116:117] op_sel_hi:[0,1,0]
	v_pk_fma_f32 v[82:83], v[54:55], v[42:43], v[116:117] op_sel_hi:[0,1,0]
	v_cvt_f32_f16_sdwa v43, v77 dst_sel:DWORD dst_unused:UNUSED_PAD src0_sel:WORD_1
	s_waitcnt lgkmcnt(1)
	v_mfma_f32_32x32x16_f16 v[2:17], v[34:37], v[58:61], v[2:17]
	v_cvt_f32_f16_e32 v42, v77
	v_fma_f32 v84, v54, v44, v116
	v_fma_f32 v85, v54, v45, v116
	v_fma_f32 v76, v54, v42, v116
	v_fma_f32 v77, v54, v43, v116
	s_waitcnt lgkmcnt(0)
	v_mfma_f32_32x32x16_f16 v[18:33], v[34:37], v[108:111], v[18:33]
	s_cmp_lg_u32 s3, 2
	s_cbranch_scc1 .LBB5_18
	v_mov_b32_e32 v34, 0x400000
	v_lshl_or_b32 v34, v100, 14, v34
	v_mov_b32_e32 v35, 0
	v_lshl_add_u64 v[34:35], v[94:95], 0, v[34:35]
	global_store_dwordx4 v[34:35], v[82:85], off nt
	global_store_dwordx4 v[34:35], v[74:77], off offset:16 nt
.LBB5_18:
	global_load_dwordx4 v[58:61], v[96:97], off
	global_load_dwordx4 v[54:57], v[96:97], off offset:1024
	global_load_dwordx4 v[42:45], v[96:97], off offset:2048
	s_nop 0
	global_load_dwordx4 v[34:37], v[96:97], off offset:3072
	v_cvt_pk_f16_f32 v82, v82, v83
	v_cvt_pk_f16_f32 v83, v84, v85
	ds_read_b32 v96, v104 offset:1024
	ds_read_b32 v108, v105 offset:1024
	v_cvt_pk_f16_f32 v84, v74, v75
	v_cvt_pk_f16_f32 v85, v76, v77
	s_waitcnt vmcnt(10)
	v_cvt_f32_f16_sdwa v111, v66 dst_sel:DWORD dst_unused:UNUSED_PAD src0_sel:WORD_1
	v_cvt_f32_f16_e32 v110, v66
	ds_write_b128 v107, v[82:85]
	v_cvt_f32_f16_sdwa v77, v67 dst_sel:DWORD dst_unused:UNUSED_PAD src0_sel:WORD_1
	v_cvt_f32_f16_e32 v76, v67
	v_cvt_f32_f16_sdwa v67, v68 dst_sel:DWORD dst_unused:UNUSED_PAD src0_sel:WORD_1
	v_cvt_f32_f16_e32 v66, v68
	v_cvt_f32_f16_sdwa v83, v69 dst_sel:DWORD dst_unused:UNUSED_PAD src0_sel:WORD_1
	v_cvt_f32_f16_e32 v82, v69
	s_waitcnt lgkmcnt(1)
	v_pk_fma_f32 v[74:75], v[96:97], v[110:111], v[108:109] op_sel_hi:[0,1,0]
	v_pk_fma_f32 v[76:77], v[96:97], v[76:77], v[108:109] op_sel_hi:[0,1,0]
	v_pk_fma_f32 v[66:67], v[96:97], v[66:67], v[108:109] op_sel_hi:[0,1,0]
	s_and_b64 vcc, exec, s[0:1]
	v_pk_fma_f32 v[68:69], v[96:97], v[82:83], v[108:109] op_sel_hi:[0,1,0]
	s_cmp_lg_u32 s3, 2
	s_cbranch_scc1 .LBB5_20
	v_mov_b32_e32 v82, 0x400000
	v_lshl_or_b32 v82, v101, 14, v82
	v_mov_b32_e32 v83, 0
	v_lshl_add_u64 v[82:83], v[94:95], 0, v[82:83]
	global_store_dwordx4 v[82:83], v[74:77], off nt
	global_store_dwordx4 v[82:83], v[66:69], off offset:16 nt
.LBB5_20:
	s_nop 0
	v_cvt_pk_f16_f32 v74, v74, v75
	v_cvt_pk_f16_f32 v75, v76, v77
	v_cvt_pk_f16_f32 v76, v66, v67
	v_cvt_pk_f16_f32 v77, v68, v69
	ds_write_b128 v106, v[74:77]
	s_waitcnt lgkmcnt(0)
	s_barrier
	ds_read_b64_tr_b16 v[66:67], v87
	ds_read_b64_tr_b16 v[68:69], v87 offset:576
	ds_read_b64_tr_b16 v[76:77], v87 offset:640
	ds_read_b64_tr_b16 v[82:83], v87 offset:2304
	ds_read_b64_tr_b16 v[108:109], v87 offset:2368
	ds_read_b64_tr_b16 v[74:75], v87 offset:64
	ds_read_b32 v116, v103 offset:1280
	s_waitcnt vmcnt(9) lgkmcnt(5)
	v_mfma_f32_32x32x16_f16 v[2:17], v[62:65], v[66:69], v[2:17]
	ds_read_b64_tr_b16 v[84:85], v87 offset:2880
	v_add_co_u32_e32 v96, vcc, 0x6000, v88
	s_mov_b64 s[4:5], vcc
	s_waitcnt lgkmcnt(2)
	v_mfma_f32_32x32x16_f16 v[18:33], v[62:65], v[74:77], v[18:33]
	ds_read_b64_tr_b16 v[110:111], v87 offset:2944
	ds_read_b64_tr_b16 v[62:63], v87 offset:4608
	ds_read_b64_tr_b16 v[112:113], v87 offset:4672
	ds_read_b64_tr_b16 v[64:65], v87 offset:5184
	s_waitcnt vmcnt(8) lgkmcnt(4)
	v_mfma_f32_32x32x16_f16 v[2:17], v[50:53], v[82:85], v[2:17]
	v_add_co_u32_e32 v82, vcc, 0x300000, v92
	s_nop 1
	v_addc_co_u32_e32 v83, vcc, 0, v93, vcc
	v_add_co_u32_e32 v84, vcc, 0x300000, v90
	s_waitcnt lgkmcnt(3)
	v_mfma_f32_32x32x16_f16 v[18:33], v[50:53], v[108:111], v[18:33]
	v_addc_co_u32_e32 v85, vcc, 0, v91, vcc
	ds_read_b64_tr_b16 v[114:115], v87 offset:5248
	ds_read_b64_tr_b16 v[50:51], v87 offset:6912
	ds_read_b64_tr_b16 v[108:109], v87 offset:6976
	global_load_dwordx4 v[74:77], v[82:83], off
	global_load_dwordx4 v[66:69], v[84:85], off
	v_addc_co_u32_e64 v97, vcc, 0, v89, s[4:5]
	s_and_b64 vcc, exec, s[0:1]
	s_waitcnt vmcnt(9) lgkmcnt(3)
	v_mfma_f32_32x32x16_f16 v[2:17], v[46:49], v[62:65], v[2:17]
	ds_read_b32 v62, v102 offset:1280
	ds_read_b64_tr_b16 v[52:53], v87 offset:7488
	ds_read_b64_tr_b16 v[110:111], v87 offset:7552
	s_waitcnt vmcnt(7)
	v_cvt_f32_f16_sdwa v65, v80 dst_sel:DWORD dst_unused:UNUSED_PAD src0_sel:WORD_1
	v_cvt_f32_f16_e32 v64, v80
	s_waitcnt lgkmcnt(5)
	v_mfma_f32_32x32x16_f16 v[18:33], v[46:49], v[112:115], v[18:33]
	v_cvt_f32_f16_sdwa v47, v78 dst_sel:DWORD dst_unused:UNUSED_PAD src0_sel:WORD_1
	v_cvt_f32_f16_e32 v46, v78
	v_cvt_f32_f16_sdwa v49, v79 dst_sel:DWORD dst_unused:UNUSED_PAD src0_sel:WORD_1
	v_cvt_f32_f16_e32 v48, v79
	s_waitcnt lgkmcnt(2)
	v_pk_fma_f32 v[78:79], v[62:63], v[64:65], v[116:117] op_sel_hi:[0,1,0]
	v_pk_fma_f32 v[82:83], v[62:63], v[46:47], v[116:117] op_sel_hi:[0,1,0]
	v_cvt_f32_f16_sdwa v47, v81 dst_sel:DWORD dst_unused:UNUSED_PAD src0_sel:WORD_1
	s_waitcnt lgkmcnt(1)
	v_mfma_f32_32x32x16_f16 v[2:17], v[38:41], v[50:53], v[2:17]
	v_cvt_f32_f16_e32 v46, v81
	v_fma_f32 v84, v62, v48, v116
	v_fma_f32 v85, v62, v49, v116
	v_fma_f32 v80, v62, v46, v116
	v_fma_f32 v81, v62, v47, v116
	s_waitcnt lgkmcnt(0)
	v_mfma_f32_32x32x16_f16 v[18:33], v[38:41], v[108:111], v[18:33]
	s_cmp_lg_u32 s3, 2
	s_cbranch_scc1 .LBB5_22
	v_mov_b32_e32 v38, 0x500000
	v_lshl_or_b32 v38, v100, 14, v38
	v_mov_b32_e32 v39, 0
	v_lshl_add_u64 v[38:39], v[94:95], 0, v[38:39]
	global_store_dwordx4 v[38:39], v[82:85], off nt
	global_store_dwordx4 v[38:39], v[78:81], off offset:16 nt
.LBB5_22:
	global_load_dwordx4 v[62:65], v[96:97], off
	global_load_dwordx4 v[50:53], v[96:97], off offset:1024
	global_load_dwordx4 v[46:49], v[96:97], off offset:2048
	s_nop 0
	global_load_dwordx4 v[38:41], v[96:97], off offset:3072
	v_cvt_pk_f16_f32 v82, v82, v83
	v_cvt_pk_f16_f32 v83, v84, v85
	ds_read_b32 v96, v104 offset:1280
	ds_read_b32 v108, v105 offset:1280
	v_cvt_pk_f16_f32 v84, v78, v79
	v_cvt_pk_f16_f32 v85, v80, v81
	s_waitcnt vmcnt(10)
	v_cvt_f32_f16_sdwa v111, v70 dst_sel:DWORD dst_unused:UNUSED_PAD src0_sel:WORD_1
	v_cvt_f32_f16_e32 v110, v70
	ds_write_b128 v107, v[82:85] offset:9216
	v_cvt_f32_f16_sdwa v81, v71 dst_sel:DWORD dst_unused:UNUSED_PAD src0_sel:WORD_1
	v_cvt_f32_f16_e32 v80, v71
	v_cvt_f32_f16_sdwa v71, v72 dst_sel:DWORD dst_unused:UNUSED_PAD src0_sel:WORD_1
	v_cvt_f32_f16_e32 v70, v72
	v_cvt_f32_f16_sdwa v83, v73 dst_sel:DWORD dst_unused:UNUSED_PAD src0_sel:WORD_1
	v_cvt_f32_f16_e32 v82, v73
	s_waitcnt lgkmcnt(1)
	v_pk_fma_f32 v[78:79], v[96:97], v[110:111], v[108:109] op_sel_hi:[0,1,0]
	v_pk_fma_f32 v[80:81], v[96:97], v[80:81], v[108:109] op_sel_hi:[0,1,0]
	v_pk_fma_f32 v[70:71], v[96:97], v[70:71], v[108:109] op_sel_hi:[0,1,0]
	s_and_b64 vcc, exec, s[0:1]
	v_pk_fma_f32 v[72:73], v[96:97], v[82:83], v[108:109] op_sel_hi:[0,1,0]
	s_cmp_lg_u32 s3, 2
	s_cbranch_scc1 .LBB5_24
	v_mov_b32_e32 v82, 0x500000
	v_lshl_or_b32 v82, v101, 14, v82
	v_mov_b32_e32 v83, 0
	v_lshl_add_u64 v[82:83], v[94:95], 0, v[82:83]
	global_store_dwordx4 v[82:83], v[78:81], off nt
	global_store_dwordx4 v[82:83], v[70:73], off offset:16 nt
.LBB5_24:
	s_nop 0
	v_cvt_pk_f16_f32 v78, v78, v79
	v_cvt_pk_f16_f32 v79, v80, v81
	v_cvt_pk_f16_f32 v80, v70, v71
	v_cvt_pk_f16_f32 v81, v72, v73
	ds_write_b128 v106, v[78:81] offset:9216
	s_waitcnt lgkmcnt(0)
	s_barrier
	ds_read_b64_tr_b16 v[70:71], v87 offset:9216
	ds_read_b64_tr_b16 v[72:73], v87 offset:9792
	ds_read_b64_tr_b16 v[80:81], v87 offset:9856
	ds_read_b64_tr_b16 v[82:83], v87 offset:11520
	ds_read_b64_tr_b16 v[108:109], v87 offset:11584
	ds_read_b64_tr_b16 v[78:79], v87 offset:9280
	ds_read_b32 v96, v103 offset:1536
	s_waitcnt vmcnt(9) lgkmcnt(5)
	v_mfma_f32_32x32x16_f16 v[2:17], v[58:61], v[70:73], v[2:17]
	ds_read_b64_tr_b16 v[84:85], v87 offset:12096
	v_add_co_u32_e32 v88, vcc, 0x7000, v88
	s_mov_b64 s[4:5], vcc
	s_waitcnt lgkmcnt(2)
	v_mfma_f32_32x32x16_f16 v[18:33], v[58:61], v[78:81], v[18:33]
	ds_read_b64_tr_b16 v[110:111], v87 offset:12160
	ds_read_b64_tr_b16 v[58:59], v87 offset:13824
	ds_read_b64_tr_b16 v[112:113], v87 offset:13888
	ds_read_b64_tr_b16 v[60:61], v87 offset:14400
	s_waitcnt vmcnt(8) lgkmcnt(4)
	v_mfma_f32_32x32x16_f16 v[2:17], v[54:57], v[82:85], v[2:17]
	v_add_co_u32_e32 v82, vcc, 0x380000, v92
	s_nop 1
	v_addc_co_u32_e32 v83, vcc, 0, v93, vcc
	v_add_co_u32_e32 v84, vcc, 0x380000, v90
	s_waitcnt lgkmcnt(3)
	v_mfma_f32_32x32x16_f16 v[18:33], v[54:57], v[108:111], v[18:33]
	v_addc_co_u32_e32 v85, vcc, 0, v91, vcc
	ds_read_b64_tr_b16 v[114:115], v87 offset:14464
	ds_read_b64_tr_b16 v[54:55], v87 offset:16128
	ds_read_b64_tr_b16 v[90:91], v87 offset:16192
	global_load_dwordx4 v[78:81], v[82:83], off
	global_load_dwordx4 v[70:73], v[84:85], off
	v_addc_co_u32_e64 v89, vcc, 0, v89, s[4:5]
	s_and_b64 vcc, exec, s[0:1]
	s_waitcnt vmcnt(9) lgkmcnt(3)
	v_mfma_f32_32x32x16_f16 v[2:17], v[42:45], v[58:61], v[2:17]
	ds_read_b32 v58, v102 offset:1536
	ds_read_b64_tr_b16 v[56:57], v87 offset:16704
	ds_read_b64_tr_b16 v[92:93], v87 offset:16768
	s_waitcnt vmcnt(7)
	v_cvt_f32_f16_sdwa v61, v76 dst_sel:DWORD dst_unused:UNUSED_PAD src0_sel:WORD_1
	v_cvt_f32_f16_e32 v60, v76
	s_waitcnt lgkmcnt(5)
	v_mfma_f32_32x32x16_f16 v[18:33], v[42:45], v[112:115], v[18:33]
	v_cvt_f32_f16_sdwa v43, v74 dst_sel:DWORD dst_unused:UNUSED_PAD src0_sel:WORD_1
	v_cvt_f32_f16_e32 v42, v74
	v_cvt_f32_f16_sdwa v45, v75 dst_sel:DWORD dst_unused:UNUSED_PAD src0_sel:WORD_1
	v_cvt_f32_f16_e32 v44, v75
	s_waitcnt lgkmcnt(2)
	v_pk_fma_f32 v[74:75], v[58:59], v[60:61], v[96:97] op_sel_hi:[0,1,0]
	v_pk_fma_f32 v[82:83], v[58:59], v[42:43], v[96:97] op_sel_hi:[0,1,0]
	v_cvt_f32_f16_sdwa v43, v77 dst_sel:DWORD dst_unused:UNUSED_PAD src0_sel:WORD_1
	s_waitcnt lgkmcnt(1)
	v_mfma_f32_32x32x16_f16 v[2:17], v[34:37], v[54:57], v[2:17]
	v_cvt_f32_f16_e32 v42, v77
	v_fma_f32 v84, v58, v44, v96
	v_fma_f32 v85, v58, v45, v96
	v_fma_f32 v76, v58, v42, v96
	v_fma_f32 v77, v58, v43, v96
	s_waitcnt lgkmcnt(0)
	v_mfma_f32_32x32x16_f16 v[18:33], v[34:37], v[90:93], v[18:33]
	s_cmp_lg_u32 s3, 3
	s_cbranch_scc1 .LBB5_26
	v_mov_b32_e32 v34, 0x600000
	v_lshl_or_b32 v34, v100, 14, v34
	v_mov_b32_e32 v35, 0
	v_lshl_add_u64 v[34:35], v[94:95], 0, v[34:35]
	global_store_dwordx4 v[34:35], v[82:85], off nt
	global_store_dwordx4 v[34:35], v[74:77], off offset:16 nt
.LBB5_26:
	global_load_dwordx4 v[58:61], v[88:89], off
	global_load_dwordx4 v[54:57], v[88:89], off offset:1024
	global_load_dwordx4 v[42:45], v[88:89], off offset:2048
	s_nop 0
	global_load_dwordx4 v[34:37], v[88:89], off offset:3072
	v_cvt_pk_f16_f32 v82, v82, v83
	v_cvt_pk_f16_f32 v83, v84, v85
	ds_read_b32 v88, v104 offset:1536
	ds_read_b32 v90, v105 offset:1536
	v_cvt_pk_f16_f32 v84, v74, v75
	v_cvt_pk_f16_f32 v85, v76, v77
	s_waitcnt vmcnt(10)
	v_cvt_f32_f16_sdwa v93, v66 dst_sel:DWORD dst_unused:UNUSED_PAD src0_sel:WORD_1
	v_cvt_f32_f16_e32 v92, v66
	ds_write_b128 v107, v[82:85]
	v_cvt_f32_f16_sdwa v77, v67 dst_sel:DWORD dst_unused:UNUSED_PAD src0_sel:WORD_1
	v_cvt_f32_f16_e32 v76, v67
	v_cvt_f32_f16_sdwa v67, v68 dst_sel:DWORD dst_unused:UNUSED_PAD src0_sel:WORD_1
	v_cvt_f32_f16_e32 v66, v68
	v_cvt_f32_f16_sdwa v83, v69 dst_sel:DWORD dst_unused:UNUSED_PAD src0_sel:WORD_1
	v_cvt_f32_f16_e32 v82, v69
	s_waitcnt lgkmcnt(1)
	v_pk_fma_f32 v[74:75], v[88:89], v[92:93], v[90:91] op_sel_hi:[0,1,0]
	v_pk_fma_f32 v[76:77], v[88:89], v[76:77], v[90:91] op_sel_hi:[0,1,0]
	v_pk_fma_f32 v[66:67], v[88:89], v[66:67], v[90:91] op_sel_hi:[0,1,0]
	s_and_b64 vcc, exec, s[0:1]
	v_pk_fma_f32 v[68:69], v[88:89], v[82:83], v[90:91] op_sel_hi:[0,1,0]
	s_cmp_lg_u32 s3, 3
	s_cbranch_scc1 .LBB5_28
	v_mov_b32_e32 v82, 0x600000
	v_lshl_or_b32 v82, v101, 14, v82
	v_mov_b32_e32 v83, 0
	v_lshl_add_u64 v[82:83], v[94:95], 0, v[82:83]
	global_store_dwordx4 v[82:83], v[74:77], off nt
	global_store_dwordx4 v[82:83], v[66:69], off offset:16 nt
.LBB5_28:
	s_nop 0
	v_cvt_pk_f16_f32 v74, v74, v75
	v_cvt_pk_f16_f32 v75, v76, v77
	v_cvt_pk_f16_f32 v76, v66, v67
	v_cvt_pk_f16_f32 v77, v68, v69
	ds_write_b128 v106, v[74:77]
	s_waitcnt lgkmcnt(0)
	s_barrier
	ds_read_b64_tr_b16 v[66:67], v87
	ds_read_b64_tr_b16 v[68:69], v87 offset:576
	ds_read_b64_tr_b16 v[76:77], v87 offset:640
	ds_read_b64_tr_b16 v[82:83], v87 offset:2304
	ds_read_b64_tr_b16 v[88:89], v87 offset:2368
	ds_read_b64_tr_b16 v[74:75], v87 offset:64
	ds_read_b32 v92, v103 offset:1792
	s_waitcnt vmcnt(9) lgkmcnt(5)
	v_mfma_f32_32x32x16_f16 v[2:17], v[62:65], v[66:69], v[2:17]
	s_and_b64 vcc, exec, s[0:1]
	s_waitcnt lgkmcnt(1)
	v_mfma_f32_32x32x16_f16 v[18:33], v[62:65], v[74:77], v[18:33]
	ds_read_b64_tr_b16 v[84:85], v87 offset:2880
	ds_read_b64_tr_b16 v[90:91], v87 offset:2944
	ds_read_b64_tr_b16 v[62:63], v87 offset:4608
	ds_read_b64_tr_b16 v[66:67], v87 offset:4672
	s_waitcnt vmcnt(8) lgkmcnt(3)
	v_mfma_f32_32x32x16_f16 v[2:17], v[50:53], v[82:85], v[2:17]
	s_waitcnt lgkmcnt(2)
	v_mfma_f32_32x32x16_f16 v[18:33], v[50:53], v[88:91], v[18:33]
	ds_read_b64_tr_b16 v[64:65], v87 offset:5184
	ds_read_b64_tr_b16 v[68:69], v87 offset:5248
	ds_read_b64_tr_b16 v[50:51], v87 offset:6912
	ds_read_b64_tr_b16 v[74:75], v87 offset:6976
	s_waitcnt vmcnt(7) lgkmcnt(3)
	v_mfma_f32_32x32x16_f16 v[2:17], v[46:49], v[62:65], v[2:17]
	ds_read_b32 v62, v102 offset:1792
	ds_read_b64_tr_b16 v[52:53], v87 offset:7488
	ds_read_b64_tr_b16 v[76:77], v87 offset:7552
	s_waitcnt vmcnt(5)
	v_cvt_f32_f16_sdwa v65, v80 dst_sel:DWORD dst_unused:UNUSED_PAD src0_sel:WORD_1
	v_cvt_f32_f16_e32 v64, v80
	s_waitcnt lgkmcnt(5)
	v_mfma_f32_32x32x16_f16 v[18:33], v[46:49], v[66:69], v[18:33]
	v_cvt_f32_f16_sdwa v47, v78 dst_sel:DWORD dst_unused:UNUSED_PAD src0_sel:WORD_1
	v_cvt_f32_f16_e32 v46, v78
	v_cvt_f32_f16_sdwa v49, v79 dst_sel:DWORD dst_unused:UNUSED_PAD src0_sel:WORD_1
	v_cvt_f32_f16_e32 v48, v79
	v_cvt_f32_f16_sdwa v67, v81 dst_sel:DWORD dst_unused:UNUSED_PAD src0_sel:WORD_1
	v_cvt_f32_f16_e32 v66, v81
	s_waitcnt lgkmcnt(1)
	v_mfma_f32_32x32x16_f16 v[2:17], v[38:41], v[50:53], v[2:17]
	v_fma_f32 v50, v62, v46, v92
	v_fma_f32 v51, v62, v47, v92
	v_fma_f32 v52, v62, v48, v92
	v_fma_f32 v53, v62, v49, v92
	v_fma_f32 v46, v62, v64, v92
	v_fma_f32 v47, v62, v65, v92
	v_pk_fma_f32 v[48:49], v[62:63], v[66:67], v[92:93] op_sel_hi:[0,1,0]
	s_waitcnt lgkmcnt(0)
	v_mfma_f32_32x32x16_f16 v[18:33], v[38:41], v[74:77], v[18:33]
	s_cmp_lg_u32 s3, 3
	s_cbranch_scc1 .LBB5_30
	v_mov_b32_e32 v38, 0x700000
	v_lshl_or_b32 v38, v100, 14, v38
	v_mov_b32_e32 v39, 0
	v_lshl_add_u64 v[38:39], v[94:95], 0, v[38:39]
	global_store_dwordx4 v[38:39], v[50:53], off nt
	global_store_dwordx4 v[38:39], v[46:49], off offset:16 nt
.LBB5_30:
	v_cvt_pk_f16_f32 v38, v50, v51
	v_cvt_pk_f16_f32 v39, v52, v53
	ds_read_b32 v50, v104 offset:1792
	ds_read_b32 v52, v105 offset:1792
	v_cvt_pk_f16_f32 v40, v46, v47
	v_cvt_pk_f16_f32 v41, v48, v49
	s_waitcnt vmcnt(4)
	v_cvt_f32_f16_sdwa v63, v70 dst_sel:DWORD dst_unused:UNUSED_PAD src0_sel:WORD_1
	v_cvt_f32_f16_e32 v62, v70
	ds_write_b128 v107, v[38:41] offset:9216
	v_cvt_f32_f16_sdwa v41, v71 dst_sel:DWORD dst_unused:UNUSED_PAD src0_sel:WORD_1
	v_cvt_f32_f16_e32 v40, v71
	v_cvt_f32_f16_sdwa v47, v72 dst_sel:DWORD dst_unused:UNUSED_PAD src0_sel:WORD_1
	v_cvt_f32_f16_e32 v46, v72
	v_cvt_f32_f16_sdwa v49, v73 dst_sel:DWORD dst_unused:UNUSED_PAD src0_sel:WORD_1
	v_cvt_f32_f16_e32 v48, v73
	s_waitcnt lgkmcnt(1)
	v_pk_fma_f32 v[38:39], v[50:51], v[62:63], v[52:53] op_sel_hi:[0,1,0]
	v_pk_fma_f32 v[40:41], v[50:51], v[40:41], v[52:53] op_sel_hi:[0,1,0]
	v_pk_fma_f32 v[46:47], v[50:51], v[46:47], v[52:53] op_sel_hi:[0,1,0]
	s_and_b64 vcc, exec, s[0:1]
	v_pk_fma_f32 v[48:49], v[50:51], v[48:49], v[52:53] op_sel_hi:[0,1,0]
	s_cmp_lg_u32 s3, 3
	s_cbranch_scc1 .LBB5_32
	v_mov_b32_e32 v50, 0x700000
	v_lshl_or_b32 v50, v101, 14, v50
	v_mov_b32_e32 v51, 0
	v_lshl_add_u64 v[50:51], v[94:95], 0, v[50:51]
	global_store_dwordx4 v[50:51], v[38:41], off nt
	global_store_dwordx4 v[50:51], v[46:49], off offset:16 nt
.LBB5_32:
	s_nop 0
	v_cvt_pk_f16_f32 v38, v38, v39
	v_cvt_pk_f16_f32 v39, v40, v41
	v_cvt_pk_f16_f32 v40, v46, v47
	v_cvt_pk_f16_f32 v41, v48, v49
	ds_write_b128 v106, v[38:41] offset:9216
	s_waitcnt lgkmcnt(0)
	s_barrier
	ds_read_b64_tr_b16 v[38:39], v87 offset:9216
	ds_read_b64_tr_b16 v[40:41], v87 offset:9792
	ds_read_b64_tr_b16 v[48:49], v87 offset:9856
	ds_read_b64_tr_b16 v[46:47], v87 offset:9280
	s_waitcnt vmcnt(3) lgkmcnt(2)
	v_mfma_f32_32x32x16_f16 v[2:17], v[58:61], v[38:41], v[2:17]
	s_lshl_b32 s0, s3, 7
	s_movk_i32 s1, 0x110
	s_lshl_b64 s[4:5], s[16:17], 22
	s_add_u32 s3, s12, s4
	s_addc_u32 s4, s13, s5
	s_lshl_b32 s2, s2, 1
	s_add_u32 s2, s3, s2
	s_waitcnt lgkmcnt(0)
	v_mfma_f32_32x32x16_f16 v[18:33], v[58:61], v[46:49], v[18:33]
	ds_read_b64_tr_b16 v[38:39], v87 offset:11520
	ds_read_b64_tr_b16 v[40:41], v87 offset:12096
	ds_read_b64_tr_b16 v[48:49], v87 offset:12160
	ds_read_b64_tr_b16 v[46:47], v87 offset:11584
	s_addc_u32 s3, s4, 0
	v_lshrrev_b32_e32 v1, 4, v1
	s_waitcnt vmcnt(2) lgkmcnt(2)
	v_mfma_f32_32x32x16_f16 v[2:17], v[54:57], v[38:41], v[2:17]
	s_waitcnt lgkmcnt(0)
	v_mfma_f32_32x32x16_f16 v[18:33], v[54:57], v[46:49], v[18:33]
	ds_read_b64_tr_b16 v[38:39], v87 offset:13824
	ds_read_b64_tr_b16 v[40:41], v87 offset:14400
	ds_read_b64_tr_b16 v[48:49], v87 offset:14464
	ds_read_b64_tr_b16 v[46:47], v87 offset:13888
	s_waitcnt vmcnt(1) lgkmcnt(2)
	v_mfma_f32_32x32x16_f16 v[2:17], v[42:45], v[38:41], v[2:17]
	s_waitcnt lgkmcnt(0)
	v_mfma_f32_32x32x16_f16 v[18:33], v[42:45], v[46:49], v[18:33]
	ds_read_b64_tr_b16 v[38:39], v87 offset:16128
	ds_read_b64_tr_b16 v[40:41], v87 offset:16704
	ds_read_b64_tr_b16 v[44:45], v87 offset:16768
	ds_read_b64_tr_b16 v[42:43], v87 offset:16192
	s_waitcnt lgkmcnt(0)
	s_barrier
	s_waitcnt vmcnt(0)
	v_mfma_f32_32x32x16_f16 v[2:17], v[34:37], v[38:41], v[2:17]
	v_and_b32_e32 v38, 4, v100
	v_lshl_or_b32 v38, v99, 5, v38
	v_and_b32_e32 v39, 31, v0
	v_mul_u32_u24_e32 v38, 0x110, v38
	v_lshl_add_u32 v38, v39, 2, v38
	v_mfma_f32_32x32x16_f16 v[18:33], v[34:37], v[42:45], v[18:33]
	s_nop 11
	ds_write2_b32 v38, v2, v18 offset1:32
	ds_write2_b32 v38, v3, v19 offset0:68 offset1:100
	ds_write2_b32 v38, v4, v20 offset0:136 offset1:168
	ds_write2_b32 v38, v5, v21 offset0:204 offset1:236
	v_add_u32_e32 v2, 0x800, v38
	ds_write2_b32 v2, v6, v22 offset0:32 offset1:64
	ds_write2_b32 v2, v7, v23 offset0:100 offset1:132
	ds_write2_b32 v2, v8, v24 offset0:168 offset1:200
	v_add_u32_e32 v2, 0xa00, v38
	ds_write2_b32 v2, v9, v25 offset0:108 offset1:140
	v_add_u32_e32 v2, 0x1000, v38
	ds_write2_b32 v2, v10, v26 offset0:64 offset1:96
	ds_write2_b32 v2, v11, v27 offset0:132 offset1:164
	ds_write2_b32 v2, v12, v28 offset0:200 offset1:232
	v_add_u32_e32 v2, 0x1400, v38
	ds_write2_b32 v2, v13, v29 offset0:12 offset1:44
	v_add_u32_e32 v2, 0x1800, v38
	ds_write2_b32 v2, v14, v30 offset0:96 offset1:128
	ds_write2_b32 v2, v15, v31 offset0:164 offset1:196
	v_add_u32_e32 v2, 0x1a00, v38
	ds_write2_b32 v2, v16, v32 offset0:104 offset1:136
	v_add_u32_e32 v2, 0x1c00, v38
	v_lshrrev_b32_e32 v6, 4, v0
	ds_write2_b32 v2, v17, v33 offset0:44 offset1:76
	v_or_b32_e32 v2, s0, v6
	v_ashrrev_i32_e32 v3, 31, v2
	v_lshl_add_u64 v[4:5], v[2:3], 2, s[10:11]
	s_waitcnt lgkmcnt(0)
	s_barrier
	global_load_dword v8, v[4:5], off
	v_and_b32_e32 v4, 60, v86
	v_lshlrev_b32_e32 v18, 2, v4
	v_lshlrev_b32_e32 v10, 1, v4
	v_mad_u32_u24 v4, v6, s1, v18
	ds_read_b128 v[4:7], v4
	v_mov_b32_e32 v11, 0
	v_lshlrev_b64 v[14:15], 13, v[2:3]
	v_lshl_add_u64 v[2:3], s[2:3], 0, v[10:11]
	v_lshl_add_u64 v[10:11], v[2:3], 0, v[14:15]
	s_waitcnt lgkmcnt(0)
	v_mov_b32_e32 v14, v5
	v_mov_b32_e32 v15, v6
	v_lshrrev_b32_e32 v9, 4, v98
	v_or_b32_e32 v12, s0, v9
	v_ashrrev_i32_e32 v13, 31, v12
	v_lshl_add_u64 v[16:17], v[12:13], 2, s[10:11]
	v_lshlrev_b64 v[12:13], 13, v[12:13]
	v_lshl_add_u64 v[12:13], v[2:3], 0, v[12:13]
	s_waitcnt vmcnt(0)
	v_add_f32_e32 v4, v4, v8
	v_add_f32_e32 v5, v7, v8
	v_cvt_f16_f32_e32 v6, v4
	v_cvt_f16_f32_e32 v7, v5
	v_pk_add_f32 v[4:5], v[14:15], v[8:9] op_sel_hi:[1,0]
	s_nop 0
	v_cvt_pk_f16_f32 v5, v4, v5
	v_pack_b32_f16 v4, v6, v5
	v_alignbit_b32 v5, v7, v5, 16
	global_store_dwordx2 v[10:11], v[4:5], off
	global_load_dword v8, v[16:17], off
	v_or_b32_e32 v4, 0x200, v0
	v_lshrrev_b32_e32 v19, 4, v4
	v_mad_u32_u24 v4, v9, s1, v18
	ds_read_b128 v[4:7], v4
	v_or_b32_e32 v10, s0, v19
	v_ashrrev_i32_e32 v11, 31, v10
	v_lshl_add_u64 v[14:15], v[10:11], 2, s[10:11]
	v_lshlrev_b64 v[10:11], 13, v[10:11]
	s_waitcnt lgkmcnt(0)
	v_mov_b32_e32 v16, v5
	v_mov_b32_e32 v17, v6
	v_lshl_add_u64 v[10:11], v[2:3], 0, v[10:11]
	s_waitcnt vmcnt(0)
	v_add_f32_e32 v4, v4, v8
	v_add_f32_e32 v5, v7, v8
	v_cvt_f16_f32_e32 v6, v4
	v_cvt_f16_f32_e32 v7, v5
	v_pk_add_f32 v[4:5], v[16:17], v[8:9] op_sel_hi:[1,0]
	s_nop 0
	v_cvt_pk_f16_f32 v5, v4, v5
	v_pack_b32_f16 v4, v6, v5
	v_alignbit_b32 v5, v7, v5, 16
	global_store_dwordx2 v[12:13], v[4:5], off
	global_load_dword v8, v[14:15], off
	v_or_b32_e32 v4, 0x300, v0
	v_lshrrev_b32_e32 v9, 4, v4
	v_mad_u32_u24 v4, v19, s1, v18
	ds_read_b128 v[4:7], v4
	v_or_b32_e32 v12, s0, v9
	v_ashrrev_i32_e32 v13, 31, v12
	v_lshl_add_u64 v[14:15], v[12:13], 2, s[10:11]
	v_lshlrev_b64 v[12:13], 13, v[12:13]
	s_waitcnt lgkmcnt(0)
	v_mov_b32_e32 v16, v5
	v_mov_b32_e32 v17, v6
	v_lshl_add_u64 v[12:13], v[2:3], 0, v[12:13]
	s_waitcnt vmcnt(0)
	v_add_f32_e32 v4, v4, v8
	v_add_f32_e32 v5, v7, v8
	v_cvt_f16_f32_e32 v6, v4
	v_cvt_f16_f32_e32 v7, v5
	v_pk_add_f32 v[4:5], v[16:17], v[8:9] op_sel_hi:[1,0]
	s_nop 0
	v_cvt_pk_f16_f32 v5, v4, v5
	v_pack_b32_f16 v4, v6, v5
	v_alignbit_b32 v5, v7, v5, 16
	global_store_dwordx2 v[10:11], v[4:5], off
	global_load_dword v8, v[14:15], off
	v_mad_u32_u24 v4, v9, s1, v18
	ds_read_b128 v[4:7], v4
	v_or_b32_e32 v10, s0, v1
	v_ashrrev_i32_e32 v11, 31, v10
	v_lshl_add_u64 v[14:15], v[10:11], 2, s[10:11]
	v_mad_u32_u24 v1, v1, s1, v18
	s_waitcnt lgkmcnt(0)
	v_mov_b32_e32 v16, v5
	v_mov_b32_e32 v17, v6
	v_lshlrev_b64 v[10:11], 13, v[10:11]
	v_lshl_add_u64 v[10:11], v[2:3], 0, v[10:11]
	s_waitcnt vmcnt(0)
	v_add_f32_e32 v4, v4, v8
	v_add_f32_e32 v5, v7, v8
	v_cvt_f16_f32_e32 v6, v4
	v_cvt_f16_f32_e32 v7, v5
	v_pk_add_f32 v[4:5], v[16:17], v[8:9] op_sel_hi:[1,0]
	s_nop 0
	v_cvt_pk_f16_f32 v5, v4, v5
	v_pack_b32_f16 v4, v6, v5
	v_alignbit_b32 v5, v7, v5, 16
	global_store_dwordx2 v[12:13], v[4:5], off
	global_load_dword v8, v[14:15], off
	v_or_b32_e32 v4, 0x500, v0
	v_lshrrev_b32_e32 v9, 4, v4
	ds_read_b128 v[4:7], v1
	v_or_b32_e32 v12, s0, v9
	v_ashrrev_i32_e32 v13, 31, v12
	v_lshl_add_u64 v[14:15], v[12:13], 2, s[10:11]
	v_lshlrev_b64 v[12:13], 13, v[12:13]
	s_waitcnt lgkmcnt(0)
	v_mov_b32_e32 v17, v6
	v_mov_b32_e32 v16, v5
	v_lshl_add_u64 v[12:13], v[2:3], 0, v[12:13]
	s_waitcnt vmcnt(0)
	v_add_f32_e32 v1, v4, v8
	v_add_f32_e32 v4, v7, v8
	v_cvt_f16_f32_e32 v1, v1
	v_cvt_f16_f32_e32 v6, v4
	v_pk_add_f32 v[4:5], v[16:17], v[8:9] op_sel_hi:[1,0]
	s_nop 0
	v_cvt_pk_f16_f32 v5, v4, v5
	v_pack_b32_f16 v4, v1, v5
	v_alignbit_b32 v5, v6, v5, 16
	global_store_dwordx2 v[10:11], v[4:5], off
	global_load_dword v8, v[14:15], off
	v_mad_u32_u24 v4, v9, s1, v18
	ds_read_b128 v[4:7], v4
	v_or_b32_e32 v1, 0x600, v0
	v_lshrrev_b32_e32 v1, 4, v1
	v_or_b32_e32 v10, s0, v1
	v_ashrrev_i32_e32 v11, 31, v10
	s_waitcnt lgkmcnt(0)
	v_mov_b32_e32 v16, v5
	v_mov_b32_e32 v17, v6
	v_lshl_add_u64 v[14:15], v[10:11], 2, s[10:11]
	v_mad_u32_u24 v1, v1, s1, v18
	v_or_b32_e32 v0, 0x700, v0
	v_lshlrev_b64 v[10:11], 13, v[10:11]
	v_lshl_add_u64 v[10:11], v[2:3], 0, v[10:11]
	s_waitcnt vmcnt(0)
	v_add_f32_e32 v4, v4, v8
	v_add_f32_e32 v5, v7, v8
	v_cvt_f16_f32_e32 v6, v4
	v_cvt_f16_f32_e32 v7, v5
	v_pk_add_f32 v[4:5], v[16:17], v[8:9] op_sel_hi:[1,0]
	v_lshrrev_b32_e32 v9, 4, v0
	v_cvt_pk_f16_f32 v5, v4, v5
	v_pack_b32_f16 v4, v6, v5
	v_alignbit_b32 v5, v7, v5, 16
	global_store_dwordx2 v[12:13], v[4:5], off
	global_load_dword v8, v[14:15], off
	ds_read_b128 v[4:7], v1
	v_or_b32_e32 v0, s0, v9
	v_ashrrev_i32_e32 v1, 31, v0
	v_lshl_add_u64 v[12:13], v[0:1], 2, s[10:11]
	v_lshlrev_b64 v[0:1], 13, v[0:1]
	s_waitcnt lgkmcnt(0)
	v_mov_b32_e32 v14, v5
	v_mov_b32_e32 v15, v6
	v_lshl_add_u64 v[0:1], v[2:3], 0, v[0:1]
	s_waitcnt vmcnt(0)
	v_add_f32_e32 v4, v4, v8
	v_add_f32_e32 v5, v7, v8
	v_cvt_f16_f32_e32 v6, v4
	v_cvt_f16_f32_e32 v7, v5
	v_pk_add_f32 v[4:5], v[14:15], v[8:9] op_sel_hi:[1,0]
	s_nop 0
	v_cvt_pk_f16_f32 v5, v4, v5
	v_pack_b32_f16 v4, v6, v5
	v_alignbit_b32 v5, v7, v5, 16
	global_store_dwordx2 v[10:11], v[4:5], off
	global_load_dword v8, v[12:13], off
	v_mad_u32_u24 v4, v9, s1, v18
	ds_read_b128 v[4:7], v4
	s_waitcnt lgkmcnt(0)
	v_mov_b32_e32 v10, v5
	v_mov_b32_e32 v11, v6
	s_waitcnt vmcnt(0)
	v_add_f32_e32 v4, v4, v8
	v_add_f32_e32 v5, v7, v8
	v_cvt_f16_f32_e32 v6, v4
	v_cvt_f16_f32_e32 v7, v5
	v_pk_add_f32 v[4:5], v[10:11], v[8:9] op_sel_hi:[1,0]
	s_nop 0
	v_cvt_pk_f16_f32 v5, v4, v5
	v_pack_b32_f16 v4, v6, v5
	v_alignbit_b32 v5, v7, v5, 16
	global_store_dwordx2 v[0:1], v[4:5], off
	s_endpgm
	.p2alignl 8, 3212836864

_Z9k_gemm_tlILi3ELb0EEvPKDF16_6TlArgs:
	s_load_dwordx4 s[8:11], s[0:1], 0x0
	s_load_dwordx4 s[4:7], s[0:1], 0x30
	v_lshrrev_b32_e32 v43, 6, v0
	s_lshl_b32 s1, s2, 6
	v_lshl_or_b32 v34, s3, 2, v43
	v_mov_b32_e32 v35, 0
	s_lshr_b32 s0, s2, 6
	s_and_b32 s2, s1, 0xfc0
	s_mov_b32 s1, 0
	v_lshlrev_b64 v[2:3], 15, v[34:35]
	s_waitcnt lgkmcnt(0)
	v_lshl_add_u64 v[2:3], s[8:9], 0, v[2:3]
	s_lshl_b64 s[8:9], s[0:1], 22
	s_add_u32 s8, s10, s8
	v_lshlrev_b32_e32 v42, 4, v0
	s_addc_u32 s9, s11, s9
	s_lshl_b32 s10, s2, 1
	v_and_b32_e32 v34, 0x3f0, v42
	s_add_u32 s8, s8, s10
	v_lshl_add_u64 v[36:37], v[2:3], 0, v[34:35]
	v_lshrrev_b32_e32 v44, 3, v0
	s_addc_u32 s9, s9, 0
	v_and_b32_e32 v34, 0x70, v42
	v_or_b32_e32 v1, 0x100, v0
	v_lshl_add_u64 v[2:3], s[8:9], 0, v[34:35]
	v_lshrrev_b32_e32 v14, 3, v1
	v_lshlrev_b32_e32 v4, 13, v44
	v_mov_b32_e32 v5, v35
	v_lshl_add_u64 v[38:39], v[2:3], 0, v[4:5]
	v_lshlrev_b32_e32 v4, 13, v14
	v_lshl_add_u64 v[40:41], v[2:3], 0, v[4:5]
	global_load_dwordx4 v[2:5], v[38:39], off
	global_load_dwordx4 v[6:9], v[40:41], off
	global_load_dwordx4 v[18:21], v[36:37], off
	global_load_dwordx4 v[48:51], v[36:37], off offset:1024
	global_load_dwordx4 v[52:55], v[36:37], off offset:2048
	global_load_dwordx4 v[56:59], v[36:37], off offset:3072
	v_lshrrev_b32_e32 v11, 2, v0
	v_lshlrev_b32_e32 v10, 3, v0
	v_and_b32_e32 v12, 16, v0
	v_and_b32_e32 v11, 11, v11
	s_movk_i32 s8, 0x1000
	v_and_b32_e32 v10, 24, v10
	v_lshlrev_b32_e32 v12, 1, v12
	v_mul_u32_u24_e32 v11, 0x90, v11
	v_add3_u32 v45, v11, v10, v12
	v_add_co_u32_e32 v10, vcc, s8, v36
	s_mov_b32 s10, 0x80000
	s_nop 0
	v_addc_co_u32_e32 v11, vcc, 0, v37, vcc
	v_add_co_u32_e32 v12, vcc, s10, v38
	s_movk_i32 s9, 0x2000
	s_nop 0
	v_addc_co_u32_e32 v13, vcc, 0, v39, vcc
	global_load_dwordx4 v[60:63], v[12:13], off
	v_add_co_u32_e32 v12, vcc, s10, v40
	s_movk_i32 s11, 0x90
	s_nop 0
	v_addc_co_u32_e32 v13, vcc, 0, v41, vcc
	v_add_co_u32_e32 v104, vcc, s9, v36
	global_load_dwordx4 v[64:67], v[12:13], off
	s_nop 0
	v_addc_co_u32_e32 v105, vcc, 0, v37, vcc
	global_load_dwordx4 v[68:71], v[104:105], off offset:-4096
	global_load_dwordx4 v[72:75], v[10:11], off offset:1024
	global_load_dwordx4 v[76:79], v[10:11], off offset:2048
	global_load_dwordx4 v[80:83], v[10:11], off offset:3072
	v_mad_u32_u24 v46, v44, s11, v34
	v_mad_u32_u24 v34, v14, s11, v34
	s_mov_b32 s8, 0x100000
	v_add_co_u32_e32 v106, vcc, s8, v38
	s_mov_b32 s9, 0x180000
	s_nop 0
	v_addc_co_u32_e32 v107, vcc, 0, v39, vcc
	v_add_co_u32_e32 v108, vcc, s8, v40
	s_movk_i32 s8, 0x3000
	s_nop 0
	v_addc_co_u32_e32 v109, vcc, 0, v41, vcc
	s_lshl_b32 s3, s3, 7
	s_lshl_b64 s[0:1], s[0:1], 23
	s_add_u32 s0, s6, s0
	s_addc_u32 s1, s7, s1
	s_lshl_b32 s2, s2, 2
	s_add_u32 s0, s0, s2
	s_addc_u32 s1, s1, 0
	v_lshrrev_b32_e32 v1, 4, v1
	s_waitcnt vmcnt(11)
	ds_write_b128 v46, v[2:5]
	s_waitcnt vmcnt(10)
	ds_write_b128 v34, v[6:9]
	s_waitcnt lgkmcnt(0)
	s_barrier
	ds_read_b64_tr_b16 v[2:3], v45
	ds_read_b64_tr_b16 v[4:5], v45 offset:576
	ds_read_b64_tr_b16 v[24:25], v45 offset:640
	ds_read_b64_tr_b16 v[22:23], v45 offset:64
	s_waitcnt vmcnt(9) lgkmcnt(2)
	v_mfma_f32_32x32x16_f16 v[2:17], v[18:21], v[2:5], 0
	ds_read_b64_tr_b16 v[84:85], v45 offset:2304
	ds_read_b64_tr_b16 v[86:87], v45 offset:2880
	ds_read_b64_tr_b16 v[90:91], v45 offset:2944
	ds_read_b64_tr_b16 v[88:89], v45 offset:2368
	s_waitcnt lgkmcnt(4)
	v_mfma_f32_32x32x16_f16 v[18:33], v[18:21], v[22:25], 0
	s_waitcnt vmcnt(8) lgkmcnt(2)
	v_mfma_f32_32x32x16_f16 v[2:17], v[48:51], v[84:87], v[2:17]
	s_waitcnt lgkmcnt(0)
	v_mfma_f32_32x32x16_f16 v[18:33], v[48:51], v[88:91], v[18:33]
	ds_read_b64_tr_b16 v[48:49], v45 offset:4608
	ds_read_b64_tr_b16 v[50:51], v45 offset:5184
	ds_read_b64_tr_b16 v[86:87], v45 offset:5248
	ds_read_b64_tr_b16 v[84:85], v45 offset:4672
	s_waitcnt vmcnt(7) lgkmcnt(2)
	v_mfma_f32_32x32x16_f16 v[2:17], v[52:55], v[48:51], v[2:17]
	ds_read_b64_tr_b16 v[48:49], v45 offset:6912
	ds_read_b64_tr_b16 v[50:51], v45 offset:7488
	s_waitcnt lgkmcnt(2)
	v_mfma_f32_32x32x16_f16 v[18:33], v[52:55], v[84:87], v[18:33]
	ds_read_b64_tr_b16 v[54:55], v45 offset:7552
	ds_read_b64_tr_b16 v[52:53], v45 offset:6976
	s_waitcnt vmcnt(6) lgkmcnt(2)
	v_mfma_f32_32x32x16_f16 v[2:17], v[56:59], v[48:51], v[2:17]
	global_load_dwordx4 v[48:51], v[104:105], off
	global_load_dwordx4 v[84:87], v[104:105], off offset:1024
	global_load_dwordx4 v[88:91], v[106:107], off
	global_load_dwordx4 v[92:95], v[108:109], off
	global_load_dwordx4 v[96:99], v[104:105], off offset:2048
	global_load_dwordx4 v[100:103], v[104:105], off offset:3072
	s_waitcnt vmcnt(11)
	ds_write_b128 v46, v[60:63] offset:9216
	s_waitcnt vmcnt(10)
	ds_write_b128 v34, v[64:67] offset:9216
	s_waitcnt lgkmcnt(0)
	s_barrier
	v_add_co_u32_e32 v104, vcc, s8, v36
	v_mfma_f32_32x32x16_f16 v[18:33], v[56:59], v[52:55], v[18:33]
	ds_read_b64_tr_b16 v[52:53], v45 offset:9216
	ds_read_b64_tr_b16 v[54:55], v45 offset:9792
	ds_read_b64_tr_b16 v[58:59], v45 offset:9856
	ds_read_b64_tr_b16 v[56:57], v45 offset:9280
	v_addc_co_u32_e32 v105, vcc, 0, v37, vcc
	v_add_co_u32_e32 v64, vcc, s9, v38
	s_movk_i32 s8, 0x4000
	s_nop 0
	v_addc_co_u32_e32 v65, vcc, 0, v39, vcc
	s_waitcnt vmcnt(9) lgkmcnt(2)
	v_mfma_f32_32x32x16_f16 v[2:17], v[68:71], v[52:55], v[2:17]
	v_add_co_u32_e32 v66, vcc, s9, v40
	s_mov_b32 s9, 0x280000
	s_nop 0
	v_addc_co_u32_e32 v67, vcc, 0, v41, vcc
	v_add_co_u32_e32 v106, vcc, s8, v36
	s_waitcnt lgkmcnt(0)
	v_mfma_f32_32x32x16_f16 v[18:33], v[68:71], v[56:59], v[18:33]
	ds_read_b64_tr_b16 v[52:53], v45 offset:11520
	ds_read_b64_tr_b16 v[54:55], v45 offset:12096
	ds_read_b64_tr_b16 v[58:59], v45 offset:12160
	ds_read_b64_tr_b16 v[56:57], v45 offset:11584
	v_addc_co_u32_e32 v107, vcc, 0, v37, vcc
	s_mov_b32 s8, 0x200000
	s_waitcnt vmcnt(8) lgkmcnt(2)
	v_mfma_f32_32x32x16_f16 v[2:17], v[72:75], v[52:55], v[2:17]
	ds_read_b64_tr_b16 v[52:53], v45 offset:13824
	ds_read_b64_tr_b16 v[54:55], v45 offset:14400
	s_waitcnt lgkmcnt(2)
	v_mfma_f32_32x32x16_f16 v[18:33], v[72:75], v[56:59], v[18:33]
	ds_read_b64_tr_b16 v[58:59], v45 offset:14464
	ds_read_b64_tr_b16 v[56:57], v45 offset:13888
	s_waitcnt vmcnt(7) lgkmcnt(2)
	v_mfma_f32_32x32x16_f16 v[2:17], v[76:79], v[52:55], v[2:17]
	ds_read_b64_tr_b16 v[52:53], v45 offset:16128
	ds_read_b64_tr_b16 v[54:55], v45 offset:16704
	s_waitcnt lgkmcnt(2)
	v_mfma_f32_32x32x16_f16 v[18:33], v[76:79], v[56:59], v[18:33]
	global_load_dwordx4 v[56:59], v[64:65], off
	global_load_dwordx4 v[60:63], v[66:67], off
	ds_read_b64_tr_b16 v[66:67], v45 offset:16768
	ds_read_b64_tr_b16 v[64:65], v45 offset:16192
	s_waitcnt vmcnt(8) lgkmcnt(2)
	v_mfma_f32_32x32x16_f16 v[2:17], v[80:83], v[52:55], v[2:17]
	global_load_dwordx4 v[52:55], v[106:107], off offset:-4096
	global_load_dwordx4 v[68:71], v[104:105], off offset:1024
	global_load_dwordx4 v[72:75], v[104:105], off offset:2048
	global_load_dwordx4 v[76:79], v[104:105], off offset:3072
	s_waitcnt vmcnt(9)
	ds_write_b128 v46, v[88:91]
	s_waitcnt vmcnt(8)
	ds_write_b128 v34, v[92:95]
	s_waitcnt lgkmcnt(2)
	v_mfma_f32_32x32x16_f16 v[18:33], v[80:83], v[64:67], v[18:33]
	s_waitcnt lgkmcnt(0)
	s_barrier
	ds_read_b64_tr_b16 v[64:65], v45
	ds_read_b64_tr_b16 v[66:67], v45 offset:576
	ds_read_b64_tr_b16 v[82:83], v45 offset:640
	ds_read_b64_tr_b16 v[80:81], v45 offset:64
	v_add_co_u32_e32 v104, vcc, s8, v38
	s_waitcnt lgkmcnt(2)
	v_mfma_f32_32x32x16_f16 v[2:17], v[48:51], v[64:67], v[2:17]
	v_addc_co_u32_e32 v105, vcc, 0, v39, vcc
	v_add_co_u32_e32 v108, vcc, s8, v40
	s_movk_i32 s8, 0x5000
	s_nop 0
	v_addc_co_u32_e32 v109, vcc, 0, v41, vcc
	s_waitcnt lgkmcnt(0)
	v_mfma_f32_32x32x16_f16 v[18:33], v[48:51], v[80:83], v[18:33]
	ds_read_b64_tr_b16 v[48:49], v45 offset:2304
	ds_read_b64_tr_b16 v[50:51], v45 offset:2880
	ds_read_b64_tr_b16 v[66:67], v45 offset:2944
	ds_read_b64_tr_b16 v[64:65], v45 offset:2368
	s_waitcnt lgkmcnt(2)
	v_mfma_f32_32x32x16_f16 v[2:17], v[84:87], v[48:51], v[2:17]
	s_waitcnt lgkmcnt(0)
	v_mfma_f32_32x32x16_f16 v[18:33], v[84:87], v[64:67], v[18:33]
	ds_read_b64_tr_b16 v[48:49], v45 offset:4608
	ds_read_b64_tr_b16 v[50:51], v45 offset:5184
	ds_read_b64_tr_b16 v[66:67], v45 offset:5248
	ds_read_b64_tr_b16 v[64:65], v45 offset:4672
	s_waitcnt vmcnt(7) lgkmcnt(2)
	v_mfma_f32_32x32x16_f16 v[2:17], v[96:99], v[48:51], v[2:17]
	global_load_dwordx4 v[48:51], v[106:107], off
	global_load_dwordx4 v[80:83], v[106:107], off offset:1024
	s_waitcnt lgkmcnt(0)
	v_mfma_f32_32x32x16_f16 v[18:33], v[96:99], v[64:67], v[18:33]
	ds_read_b64_tr_b16 v[64:65], v45 offset:6912
	ds_read_b64_tr_b16 v[66:67], v45 offset:7488
	ds_read_b64_tr_b16 v[86:87], v45 offset:7552
	ds_read_b64_tr_b16 v[84:85], v45 offset:6976
	s_waitcnt vmcnt(8) lgkmcnt(2)
	v_mfma_f32_32x32x16_f16 v[2:17], v[100:103], v[64:67], v[2:17]
	global_load_dwordx4 v[64:67], v[104:105], off
	global_load_dwordx4 v[88:91], v[108:109], off
	global_load_dwordx4 v[92:95], v[106:107], off offset:2048
	global_load_dwordx4 v[96:99], v[106:107], off offset:3072
	s_waitcnt vmcnt(11)
	ds_write_b128 v46, v[56:59] offset:9216
	s_waitcnt vmcnt(10)
	ds_write_b128 v34, v[60:63] offset:9216
	s_waitcnt lgkmcnt(0)
	s_barrier
	ds_read_b64_tr_b16 v[56:57], v45 offset:9216
	ds_read_b64_tr_b16 v[58:59], v45 offset:9792
	ds_read_b64_tr_b16 v[62:63], v45 offset:9856
	ds_read_b64_tr_b16 v[60:61], v45 offset:9280
	v_mfma_f32_32x32x16_f16 v[18:33], v[100:103], v[84:87], v[18:33]
	v_add_co_u32_e32 v104, vcc, s8, v36
	s_movk_i32 s8, 0x6000
	s_nop 0
	v_addc_co_u32_e32 v105, vcc, 0, v37, vcc
	s_waitcnt vmcnt(9) lgkmcnt(2)
	v_mfma_f32_32x32x16_f16 v[2:17], v[52:55], v[56:59], v[2:17]
	s_waitcnt lgkmcnt(0)
	v_mfma_f32_32x32x16_f16 v[18:33], v[52:55], v[60:63], v[18:33]
	ds_read_b64_tr_b16 v[52:53], v45 offset:11520
	ds_read_b64_tr_b16 v[54:55], v45 offset:12096
	ds_read_b64_tr_b16 v[58:59], v45 offset:12160
	ds_read_b64_tr_b16 v[56:57], v45 offset:11584
	s_waitcnt vmcnt(8) lgkmcnt(2)
	v_mfma_f32_32x32x16_f16 v[2:17], v[68:71], v[52:55], v[2:17]
	ds_read_b64_tr_b16 v[52:53], v45 offset:13824
	ds_read_b64_tr_b16 v[54:55], v45 offset:14400
	s_waitcnt lgkmcnt(2)
	v_mfma_f32_32x32x16_f16 v[18:33], v[68:71], v[56:59], v[18:33]
	ds_read_b64_tr_b16 v[58:59], v45 offset:14464
	ds_read_b64_tr_b16 v[56:57], v45 offset:13888
	v_add_co_u32_e32 v68, vcc, s9, v38
	s_nop 1
	v_addc_co_u32_e32 v69, vcc, 0, v39, vcc
	v_add_co_u32_e32 v70, vcc, s9, v40
	s_waitcnt vmcnt(7) lgkmcnt(2)
	v_mfma_f32_32x32x16_f16 v[2:17], v[72:75], v[52:55], v[2:17]
	v_addc_co_u32_e32 v71, vcc, 0, v41, vcc
	ds_read_b64_tr_b16 v[52:53], v45 offset:16128
	ds_read_b64_tr_b16 v[54:55], v45 offset:16704
	v_add_co_u32_e32 v106, vcc, s8, v36
	s_mov_b32 s8, 0x300000
	s_nop 0
	v_addc_co_u32_e32 v107, vcc, 0, v37, vcc
	s_waitcnt lgkmcnt(2)
	v_mfma_f32_32x32x16_f16 v[18:33], v[72:75], v[56:59], v[18:33]
	global_load_dwordx4 v[56:59], v[68:69], off
	global_load_dwordx4 v[60:63], v[70:71], off
	ds_read_b64_tr_b16 v[70:71], v45 offset:16768
	ds_read_b64_tr_b16 v[68:69], v45 offset:16192
	s_mov_b32 s9, 0x380000
	s_waitcnt vmcnt(8) lgkmcnt(2)
	v_mfma_f32_32x32x16_f16 v[2:17], v[76:79], v[52:55], v[2:17]
	global_load_dwordx4 v[52:55], v[106:107], off offset:-4096
	global_load_dwordx4 v[72:75], v[104:105], off offset:1024
	global_load_dwordx4 v[84:87], v[104:105], off offset:2048
	global_load_dwordx4 v[100:103], v[104:105], off offset:3072
	s_waitcnt vmcnt(9)
	ds_write_b128 v46, v[64:67]
	s_waitcnt vmcnt(8)
	ds_write_b128 v34, v[88:91]
	s_waitcnt lgkmcnt(2)
	v_mfma_f32_32x32x16_f16 v[18:33], v[76:79], v[68:71], v[18:33]
	s_waitcnt lgkmcnt(0)
	s_barrier
	ds_read_b64_tr_b16 v[64:65], v45
	ds_read_b64_tr_b16 v[66:67], v45 offset:576
	ds_read_b64_tr_b16 v[70:71], v45 offset:640
	ds_read_b64_tr_b16 v[68:69], v45 offset:64
	v_add_co_u32_e32 v104, vcc, s8, v38
	s_waitcnt lgkmcnt(2)
	v_mfma_f32_32x32x16_f16 v[2:17], v[48:51], v[64:67], v[2:17]
	v_addc_co_u32_e32 v105, vcc, 0, v39, vcc
	v_add_co_u32_e32 v108, vcc, s8, v40
	s_movk_i32 s8, 0x7000
	s_nop 0
	v_addc_co_u32_e32 v109, vcc, 0, v41, vcc
	s_waitcnt lgkmcnt(0)
	v_mfma_f32_32x32x16_f16 v[18:33], v[48:51], v[68:71], v[18:33]
	ds_read_b64_tr_b16 v[48:49], v45 offset:2304
	ds_read_b64_tr_b16 v[50:51], v45 offset:2880
	ds_read_b64_tr_b16 v[66:67], v45 offset:2944
	ds_read_b64_tr_b16 v[64:65], v45 offset:2368
	s_waitcnt lgkmcnt(2)
	v_mfma_f32_32x32x16_f16 v[2:17], v[80:83], v[48:51], v[2:17]
	s_waitcnt lgkmcnt(0)
	v_mfma_f32_32x32x16_f16 v[18:33], v[80:83], v[64:67], v[18:33]
	ds_read_b64_tr_b16 v[48:49], v45 offset:4608
	ds_read_b64_tr_b16 v[50:51], v45 offset:5184
	ds_read_b64_tr_b16 v[66:67], v45 offset:5248
	ds_read_b64_tr_b16 v[64:65], v45 offset:4672
	s_waitcnt vmcnt(7) lgkmcnt(2)
	v_mfma_f32_32x32x16_f16 v[2:17], v[92:95], v[48:51], v[2:17]
	ds_read_b64_tr_b16 v[48:49], v45 offset:6912
	ds_read_b64_tr_b16 v[50:51], v45 offset:7488
	s_waitcnt lgkmcnt(2)
	v_mfma_f32_32x32x16_f16 v[18:33], v[92:95], v[64:67], v[18:33]
	ds_read_b64_tr_b16 v[66:67], v45 offset:7552
	ds_read_b64_tr_b16 v[64:65], v45 offset:6976
	s_waitcnt vmcnt(6) lgkmcnt(2)
	v_mfma_f32_32x32x16_f16 v[2:17], v[96:99], v[48:51], v[2:17]
	global_load_dwordx4 v[48:51], v[104:105], off
	global_load_dwordx4 v[68:71], v[108:109], off
	global_load_dwordx4 v[76:79], v[106:107], off
	global_load_dwordx4 v[80:83], v[106:107], off offset:1024
	global_load_dwordx4 v[88:91], v[106:107], off offset:2048
	global_load_dwordx4 v[92:95], v[106:107], off offset:3072
	s_waitcnt vmcnt(11)
	ds_write_b128 v46, v[56:59] offset:9216
	s_waitcnt vmcnt(10)
	ds_write_b128 v34, v[60:63] offset:9216
	s_waitcnt lgkmcnt(0)
	s_barrier
	ds_read_b64_tr_b16 v[56:57], v45 offset:9216
	ds_read_b64_tr_b16 v[58:59], v45 offset:9792
	ds_read_b64_tr_b16 v[62:63], v45 offset:9856
	ds_read_b64_tr_b16 v[60:61], v45 offset:9280
	v_mfma_f32_32x32x16_f16 v[18:33], v[96:99], v[64:67], v[18:33]
	s_waitcnt vmcnt(9) lgkmcnt(2)
	v_mfma_f32_32x32x16_f16 v[2:17], v[52:55], v[56:59], v[2:17]
	s_waitcnt lgkmcnt(0)
	v_mfma_f32_32x32x16_f16 v[18:33], v[52:55], v[60:63], v[18:33]
	ds_read_b64_tr_b16 v[52:53], v45 offset:11520
	ds_read_b64_tr_b16 v[54:55], v45 offset:12096
	ds_read_b64_tr_b16 v[58:59], v45 offset:12160
	ds_read_b64_tr_b16 v[56:57], v45 offset:11584
	v_add_co_u32_e32 v60, vcc, s9, v38
	s_nop 1
	v_addc_co_u32_e32 v61, vcc, 0, v39, vcc
	v_add_co_u32_e32 v62, vcc, s9, v40
	s_waitcnt vmcnt(8) lgkmcnt(2)
	v_mfma_f32_32x32x16_f16 v[2:17], v[72:75], v[52:55], v[2:17]
	ds_read_b64_tr_b16 v[52:53], v45 offset:13824
	ds_read_b64_tr_b16 v[54:55], v45 offset:14400
	v_addc_co_u32_e32 v63, vcc, 0, v41, vcc
	v_add_co_u32_e32 v36, vcc, s8, v36
	s_movk_i32 s8, 0x110
	s_nop 0
	v_addc_co_u32_e32 v37, vcc, 0, v37, vcc
	s_waitcnt lgkmcnt(2)
	v_mfma_f32_32x32x16_f16 v[18:33], v[72:75], v[56:59], v[18:33]
	ds_read_b64_tr_b16 v[58:59], v45 offset:14464
	ds_read_b64_tr_b16 v[56:57], v45 offset:13888
	s_waitcnt vmcnt(7) lgkmcnt(2)
	v_mfma_f32_32x32x16_f16 v[2:17], v[84:87], v[52:55], v[2:17]
	global_load_dwordx4 v[38:41], v[60:61], off
	global_load_dwordx4 v[52:55], v[62:63], off
	s_waitcnt lgkmcnt(0)
	v_mfma_f32_32x32x16_f16 v[18:33], v[84:87], v[56:59], v[18:33]
	ds_read_b64_tr_b16 v[56:57], v45 offset:16128
	ds_read_b64_tr_b16 v[58:59], v45 offset:16704
	global_load_dwordx4 v[60:63], v[36:37], off
	ds_read_b64_tr_b16 v[66:67], v45 offset:16768
	ds_read_b64_tr_b16 v[64:65], v45 offset:16192
	s_waitcnt vmcnt(9) lgkmcnt(2)
	v_mfma_f32_32x32x16_f16 v[2:17], v[100:103], v[56:59], v[2:17]
	global_load_dwordx4 v[56:59], v[36:37], off offset:1024
	global_load_dwordx4 v[72:75], v[36:37], off offset:2048
	global_load_dwordx4 v[84:87], v[36:37], off offset:3072
	s_waitcnt vmcnt(11)
	ds_write_b128 v46, v[48:51]
	s_waitcnt vmcnt(10)
	ds_write_b128 v34, v[68:71]
	s_waitcnt lgkmcnt(2)
	v_mfma_f32_32x32x16_f16 v[18:33], v[100:103], v[64:67], v[18:33]
	s_waitcnt lgkmcnt(0)
	s_barrier
	ds_read_b64_tr_b16 v[48:49], v45
	ds_read_b64_tr_b16 v[50:51], v45 offset:576
	ds_read_b64_tr_b16 v[66:67], v45 offset:640
	ds_read_b64_tr_b16 v[64:65], v45 offset:64
	s_waitcnt vmcnt(9) lgkmcnt(2)
	v_mfma_f32_32x32x16_f16 v[2:17], v[76:79], v[48:51], v[2:17]
	s_waitcnt lgkmcnt(0)
	v_mfma_f32_32x32x16_f16 v[18:33], v[76:79], v[64:67], v[18:33]
	ds_read_b64_tr_b16 v[48:49], v45 offset:2304
	ds_read_b64_tr_b16 v[50:51], v45 offset:2880
	ds_read_b64_tr_b16 v[66:67], v45 offset:2944
	ds_read_b64_tr_b16 v[64:65], v45 offset:2368
	s_waitcnt vmcnt(8) lgkmcnt(2)
	v_mfma_f32_32x32x16_f16 v[2:17], v[80:83], v[48:51], v[2:17]
	s_waitcnt lgkmcnt(0)
	v_mfma_f32_32x32x16_f16 v[18:33], v[80:83], v[64:67], v[18:33]
	ds_read_b64_tr_b16 v[48:49], v45 offset:4608
	ds_read_b64_tr_b16 v[50:51], v45 offset:5184
	ds_read_b64_tr_b16 v[66:67], v45 offset:5248
	ds_read_b64_tr_b16 v[64:65], v45 offset:4672
	s_waitcnt vmcnt(7) lgkmcnt(2)
	v_mfma_f32_32x32x16_f16 v[2:17], v[88:91], v[48:51], v[2:17]
	s_waitcnt lgkmcnt(0)
	v_mfma_f32_32x32x16_f16 v[18:33], v[88:91], v[64:67], v[18:33]
	ds_read_b64_tr_b16 v[48:49], v45 offset:6912
	ds_read_b64_tr_b16 v[50:51], v45 offset:7488
	ds_read_b64_tr_b16 v[66:67], v45 offset:7552
	ds_read_b64_tr_b16 v[64:65], v45 offset:6976
	s_waitcnt vmcnt(5)
	ds_write_b128 v46, v[38:41] offset:9216
	s_waitcnt vmcnt(4)
	ds_write_b128 v34, v[52:55] offset:9216
	s_waitcnt lgkmcnt(0)
	s_barrier
	v_mfma_f32_32x32x16_f16 v[2:17], v[92:95], v[48:51], v[2:17]
	ds_read_b64_tr_b16 v[36:37], v45 offset:9216
	ds_read_b64_tr_b16 v[38:39], v45 offset:9792
	ds_read_b64_tr_b16 v[48:49], v45 offset:9856
	ds_read_b64_tr_b16 v[46:47], v45 offset:9280
	v_and_b32_e32 v34, 4, v44
	v_lshl_or_b32 v34, v43, 5, v34
	v_mul_u32_u24_e32 v34, 0x110, v34
	v_mfma_f32_32x32x16_f16 v[18:33], v[92:95], v[64:67], v[18:33]
	s_waitcnt vmcnt(3) lgkmcnt(2)
	v_mfma_f32_32x32x16_f16 v[2:17], v[60:63], v[36:39], v[2:17]
	s_waitcnt lgkmcnt(0)
	v_mfma_f32_32x32x16_f16 v[18:33], v[60:63], v[46:49], v[18:33]
	ds_read_b64_tr_b16 v[36:37], v45 offset:11520
	ds_read_b64_tr_b16 v[38:39], v45 offset:12096
	ds_read_b64_tr_b16 v[48:49], v45 offset:12160
	ds_read_b64_tr_b16 v[46:47], v45 offset:11584
	s_waitcnt vmcnt(2) lgkmcnt(2)
	v_mfma_f32_32x32x16_f16 v[2:17], v[56:59], v[36:39], v[2:17]
	s_waitcnt lgkmcnt(0)
	v_mfma_f32_32x32x16_f16 v[18:33], v[56:59], v[46:49], v[18:33]
	ds_read_b64_tr_b16 v[36:37], v45 offset:13824
	ds_read_b64_tr_b16 v[38:39], v45 offset:14400
	ds_read_b64_tr_b16 v[48:49], v45 offset:14464
	ds_read_b64_tr_b16 v[46:47], v45 offset:13888
	s_waitcnt vmcnt(1) lgkmcnt(2)
	v_mfma_f32_32x32x16_f16 v[2:17], v[72:75], v[36:39], v[2:17]
	s_waitcnt lgkmcnt(0)
	v_mfma_f32_32x32x16_f16 v[18:33], v[72:75], v[46:49], v[18:33]
	ds_read_b64_tr_b16 v[36:37], v45 offset:16128
	ds_read_b64_tr_b16 v[38:39], v45 offset:16704
	ds_read_b64_tr_b16 v[48:49], v45 offset:16768
	ds_read_b64_tr_b16 v[46:47], v45 offset:16192
	s_waitcnt lgkmcnt(0)
	s_barrier
	s_waitcnt vmcnt(0)
	v_mfma_f32_32x32x16_f16 v[2:17], v[84:87], v[36:39], v[2:17]
	v_and_b32_e32 v36, 31, v0
	v_lshl_add_u32 v34, v36, 2, v34
	v_mfma_f32_32x32x16_f16 v[18:33], v[84:87], v[46:49], v[18:33]
	s_nop 11
	ds_write2_b32 v34, v2, v18 offset1:32
	ds_write2_b32 v34, v3, v19 offset0:68 offset1:100
	ds_write2_b32 v34, v4, v20 offset0:136 offset1:168
	ds_write2_b32 v34, v5, v21 offset0:204 offset1:236
	v_add_u32_e32 v2, 0x800, v34
	ds_write2_b32 v2, v6, v22 offset0:32 offset1:64
	ds_write2_b32 v2, v7, v23 offset0:100 offset1:132
	ds_write2_b32 v2, v8, v24 offset0:168 offset1:200
	v_add_u32_e32 v2, 0xa00, v34
	ds_write2_b32 v2, v9, v25 offset0:108 offset1:140
	v_add_u32_e32 v2, 0x1000, v34
	ds_write2_b32 v2, v10, v26 offset0:64 offset1:96
	ds_write2_b32 v2, v11, v27 offset0:132 offset1:164
	ds_write2_b32 v2, v12, v28 offset0:200 offset1:232
	v_add_u32_e32 v2, 0x1400, v34
	ds_write2_b32 v2, v13, v29 offset0:12 offset1:44
	v_add_u32_e32 v2, 0x1800, v34
	v_lshrrev_b32_e32 v4, 4, v0
	ds_write2_b32 v2, v14, v30 offset0:96 offset1:128
	ds_write2_b32 v2, v15, v31 offset0:164 offset1:196
	v_add_u32_e32 v2, 0x1a00, v34
	v_or_b32_e32 v10, s3, v4
	ds_write2_b32 v2, v16, v32 offset0:104 offset1:136
	v_add_u32_e32 v2, 0x1c00, v34
	v_ashrrev_i32_e32 v11, 31, v10
	ds_write2_b32 v2, v17, v33 offset0:44 offset1:76
	v_lshl_add_u64 v[2:3], v[10:11], 2, s[4:5]
	s_waitcnt lgkmcnt(0)
	s_barrier
	global_load_dword v12, v[2:3], off
	v_and_b32_e32 v34, 0xf0, v42
	v_mad_u32_u24 v6, v4, s8, v34
	ds_read_b128 v[2:5], v6
	v_lshl_add_u64 v[14:15], s[0:1], 0, v[34:35]
	ds_read_b128 v[6:9], v6 offset:17408
	s_ashr_i32 s0, s3, 31
	s_waitcnt vmcnt(0) lgkmcnt(1)
	v_pk_add_f32 v[4:5], v[4:5], v[12:13] op_sel_hi:[1,0]
	v_pk_add_f32 v[2:3], v[2:3], v[12:13] op_sel_hi:[1,0]
	v_lshlrev_b64 v[12:13], 14, v[10:11]
	v_lshl_add_u64 v[12:13], v[14:15], 0, v[12:13]
	global_store_dwordx4 v[12:13], v[2:5], off nt
	v_or_b32_e32 v12, s3, v1
	v_ashrrev_i32_e32 v13, 31, v12
	v_lshl_add_u64 v[2:3], v[12:13], 2, s[4:5]
	global_load_dword v16, v[2:3], off
	v_or_b32_e32 v2, 0x200, v0
	v_mad_u32_u24 v1, v1, s8, v34
	v_lshrrev_b32_e32 v11, 4, v2
	ds_read_b128 v[2:5], v1
	v_or_b32_e32 v18, s3, v11
	v_lshlrev_b64 v[12:13], 14, v[12:13]
	v_ashrrev_i32_e32 v19, 31, v18
	v_lshl_add_u64 v[12:13], v[14:15], 0, v[12:13]
	v_lshl_add_u64 v[20:21], v[18:19], 2, s[4:5]
	v_or_b32_e32 v1, 0x300, v0
	v_lshrrev_b32_e32 v1, 4, v1
	v_lshlrev_b64 v[18:19], 14, v[18:19]
	v_lshl_add_u64 v[18:19], v[14:15], 0, v[18:19]
	s_waitcnt vmcnt(0) lgkmcnt(0)
	v_pk_add_f32 v[4:5], v[4:5], v[16:17] op_sel_hi:[1,0]
	v_pk_add_f32 v[2:3], v[2:3], v[16:17] op_sel_hi:[1,0]
	global_store_dwordx4 v[12:13], v[2:5], off nt
	global_load_dword v12, v[20:21], off
	v_or_b32_e32 v16, s3, v1
	v_mad_u32_u24 v2, v11, s8, v34
	ds_read_b128 v[2:5], v2
	v_ashrrev_i32_e32 v17, 31, v16
	v_lshl_add_u64 v[20:21], v[16:17], 2, s[4:5]
	v_mad_u32_u24 v1, v1, s8, v34
	v_lshlrev_b64 v[16:17], 14, v[16:17]
	v_mov_b32_e32 v11, s0
	v_lshl_add_u64 v[16:17], v[14:15], 0, v[16:17]
	s_waitcnt vmcnt(0) lgkmcnt(0)
	v_pk_add_f32 v[4:5], v[4:5], v[12:13] op_sel_hi:[1,0]
	v_pk_add_f32 v[2:3], v[2:3], v[12:13] op_sel_hi:[1,0]
	global_store_dwordx4 v[18:19], v[2:5], off nt
	global_load_dword v12, v[20:21], off
	ds_read_b128 v[2:5], v1
	v_lshl_add_u64 v[18:19], v[10:11], 2, s[4:5]
	v_or_b32_e32 v1, 0x500, v0
	v_lshrrev_b32_e32 v1, 4, v1
	s_waitcnt vmcnt(0) lgkmcnt(0)
	v_pk_add_f32 v[4:5], v[4:5], v[12:13] op_sel_hi:[1,0]
	v_pk_add_f32 v[2:3], v[2:3], v[12:13] op_sel_hi:[1,0]
	global_store_dwordx4 v[16:17], v[2:5], off nt
	global_load_dword v2, v[18:19], off offset:256
	v_or_b32_e32 v12, s3, v1
	v_or_b32_e32 v4, 64, v10
	v_ashrrev_i32_e32 v5, 31, v4
	v_lshlrev_b64 v[4:5], 14, v[4:5]
	v_ashrrev_i32_e32 v13, 31, v12
	v_lshl_add_u64 v[16:17], v[14:15], 0, v[4:5]
	v_lshl_add_u64 v[10:11], v[12:13], 2, s[4:5]
	v_mad_u32_u24 v1, v1, s8, v34
	s_waitcnt vmcnt(0)
	v_pk_add_f32 v[4:5], v[8:9], v[2:3] op_sel_hi:[1,0]
	v_pk_add_f32 v[2:3], v[6:7], v[2:3] op_sel_hi:[1,0]
	global_store_dwordx4 v[16:17], v[2:5], off nt
	global_load_dword v6, v[10:11], off
	v_lshlrev_b64 v[10:11], 14, v[12:13]
	v_or_b32_e32 v2, 0x600, v0
	v_lshrrev_b32_e32 v7, 4, v2
	ds_read_b128 v[2:5], v1
	v_or_b32_e32 v8, s3, v7
	v_ashrrev_i32_e32 v9, 31, v8
	v_lshl_add_u64 v[10:11], v[14:15], 0, v[10:11]
	v_lshl_add_u64 v[12:13], v[8:9], 2, s[4:5]
	v_or_b32_e32 v0, 0x700, v0
	v_lshlrev_b64 v[8:9], 14, v[8:9]
	v_lshl_add_u64 v[8:9], v[14:15], 0, v[8:9]
	s_waitcnt vmcnt(0) lgkmcnt(0)
	v_pk_add_f32 v[4:5], v[4:5], v[6:7] op_sel_hi:[1,0]
	v_pk_add_f32 v[2:3], v[2:3], v[6:7] op_sel_hi:[1,0]
	global_store_dwordx4 v[10:11], v[2:5], off nt
	global_load_dword v4, v[12:13], off
	s_nop 0
	v_lshrrev_b32_e32 v5, 4, v0
	v_mad_u32_u24 v0, v7, s8, v34
	ds_read_b128 v[0:3], v0
	v_or_b32_e32 v6, s3, v5
	v_ashrrev_i32_e32 v7, 31, v6
	v_lshl_add_u64 v[10:11], v[6:7], 2, s[4:5]
	v_lshlrev_b64 v[6:7], 14, v[6:7]
	s_waitcnt vmcnt(0) lgkmcnt(0)
	v_pk_add_f32 v[2:3], v[2:3], v[4:5] op_sel_hi:[1,0]
	v_pk_add_f32 v[0:1], v[0:1], v[4:5] op_sel_hi:[1,0]
	global_store_dwordx4 v[8:9], v[0:3], off nt
	global_load_dword v4, v[10:11], off
	s_nop 0
	v_mad_u32_u24 v0, v5, s8, v34
	ds_read_b128 v[0:3], v0
	s_waitcnt vmcnt(0) lgkmcnt(0)
	v_pk_add_f32 v[2:3], v[2:3], v[4:5] op_sel_hi:[1,0]
	v_pk_add_f32 v[0:1], v[0:1], v[4:5] op_sel_hi:[1,0]
	v_lshl_add_u64 v[4:5], v[14:15], 0, v[6:7]
	global_store_dwordx4 v[4:5], v[0:3], off nt
	s_endpgm
	.p2alignl 8, 3212836864

amdhsa.kernels:
  - .agpr_count:     0
    .args:
      - .actual_access:  read_only
        .address_space:  global
        .offset:         0
        .size:           8
        .value_kind:     global_buffer
      - .actual_access:  read_only
        .address_space:  global
        .offset:         8
        .size:           8
        .value_kind:     global_buffer
      - .actual_access:  read_only
        .address_space:  global
        .offset:         16
        .size:           8
        .value_kind:     global_buffer
      - .actual_access:  write_only
        .address_space:  global
        .offset:         24
        .size:           8
        .value_kind:     global_buffer
      - .actual_access:  write_only
        .address_space:  global
        .offset:         32
        .size:           8
        .value_kind:     global_buffer
      - .actual_access:  write_only
        .address_space:  global
        .offset:         40
        .size:           8
        .value_kind:     global_buffer
      - .offset:         48
        .size:           104
        .value_kind:     by_value
    .group_segment_fixed_size: 37248
    .kernarg_segment_align: 8
    .kernarg_segment_size: 152
    .language:       OpenCL C
    .language_version:
      - 2
      - 0
    .max_flat_workgroup_size: 512
    .name:           _Z4k_lnPKfS0_S0_PDF16_PfS2_7CvtArgs
    .private_segment_fixed_size: 0
    .sgpr_count:     40
    .sgpr_spill_count: 0
    .symbol:         _Z4k_lnPKfS0_S0_PDF16_PfS2_7CvtArgs.kd
    .uniform_work_group_size: 1
    .uses_dynamic_stack: false
    .vgpr_count:     66
    .vgpr_spill_count: 0
    .wavefront_size: 64
  - .agpr_count:     36
    .args:
      - .actual_access:  read_only
        .address_space:  global
        .offset:         0
        .size:           8
        .value_kind:     global_buffer
      - .actual_access:  read_only
        .address_space:  global
        .offset:         8
        .size:           8
        .value_kind:     global_buffer
      - .actual_access:  read_only
        .address_space:  global
        .offset:         16
        .size:           8
        .value_kind:     global_buffer
      - .actual_access:  read_only
        .address_space:  global
        .offset:         24
        .size:           8
        .value_kind:     global_buffer
      - .actual_access:  read_only
        .address_space:  global
        .offset:         32
        .size:           8
        .value_kind:     global_buffer
      - .actual_access:  read_only
        .address_space:  global
        .offset:         40
        .size:           8
        .value_kind:     global_buffer
      - .actual_access:  read_only
        .address_space:  global
        .offset:         48
        .size:           8
        .value_kind:     global_buffer
      - .actual_access:  read_only
        .address_space:  global
        .offset:         56
        .size:           8
        .value_kind:     global_buffer
      - .actual_access:  write_only
        .address_space:  global
        .offset:         64
        .size:           8
        .value_kind:     global_buffer
      - .actual_access:  write_only
        .address_space:  global
        .offset:         72
        .size:           8
        .value_kind:     global_buffer
      - .actual_access:  write_only
        .address_space:  global
        .offset:         80
        .size:           8
        .value_kind:     global_buffer
      - .actual_access:  write_only
        .address_space:  global
        .offset:         88
        .size:           8
        .value_kind:     global_buffer
      - .actual_access:  write_only
        .address_space:  global
        .offset:         96
        .size:           8
        .value_kind:     global_buffer
    .group_segment_fixed_size: 77312
    .kernarg_segment_align: 8
    .kernarg_segment_size: 104
    .language:       OpenCL C
    .language_version:
      - 2
      - 0
    .max_flat_workgroup_size: 256
    .name:           _Z7k_frontPKDF16_S0_PKfS2_S0_S2_S2_S2_PjPfS4_S4_S4_
    .private_segment_fixed_size: 0
    .sgpr_count:     25
    .sgpr_spill_count: 0
    .symbol:         _Z7k_frontPKDF16_S0_PKfS2_S0_S2_S2_S2_PjPfS4_S4_S4_.kd
    .uniform_work_group_size: 1
    .uses_dynamic_stack: false
    .vgpr_count:     204
    .vgpr_spill_count: 0
    .wavefront_size: 64
  - .agpr_count:     0
    .args:
      - .actual_access:  read_only
        .address_space:  global
        .offset:         0
        .size:           8
        .value_kind:     global_buffer
      - .address_space:  global
        .offset:         8
        .size:           8
        .value_kind:     global_buffer
      - .actual_access:  read_only
        .address_space:  global
        .offset:         16
        .size:           8
        .value_kind:     global_buffer
    .group_segment_fixed_size: 0
    .kernarg_segment_align: 8
    .kernarg_segment_size: 24
    .language:       OpenCL C
    .language_version:
      - 2
      - 0
    .max_flat_workgroup_size: 64
    .name:           _Z7k_scan2PKfPfS0_
    .private_segment_fixed_size: 0
    .sgpr_count:     48
    .sgpr_spill_count: 0
    .symbol:         _Z7k_scan2PKfPfS0_.kd
    .uniform_work_group_size: 1
    .uses_dynamic_stack: false
    .vgpr_count:     150
    .vgpr_spill_count: 0
    .wavefront_size: 64
  - .agpr_count:     0
    .args:
      - .actual_access:  read_only
        .address_space:  global
        .offset:         0
        .size:           8
        .value_kind:     global_buffer
      - .actual_access:  read_only
        .address_space:  global
        .offset:         8
        .size:           8
        .value_kind:     global_buffer
      - .actual_access:  read_only
        .address_space:  global
        .offset:         16
        .size:           8
        .value_kind:     global_buffer
      - .actual_access:  read_only
        .address_space:  global
        .offset:         24
        .size:           8
        .value_kind:     global_buffer
      - .actual_access:  read_only
        .address_space:  global
        .offset:         32
        .size:           8
        .value_kind:     global_buffer
      - .actual_access:  read_only
        .address_space:  global
        .offset:         40
        .size:           8
        .value_kind:     global_buffer
      - .actual_access:  read_only
        .address_space:  global
        .offset:         48
        .size:           8
        .value_kind:     global_buffer
      - .actual_access:  read_only
        .address_space:  global
        .offset:         56
        .size:           8
        .value_kind:     global_buffer
      - .actual_access:  read_only
        .address_space:  global
        .offset:         64
        .size:           8
        .value_kind:     global_buffer
      - .offset:         72
        .size:           72
        .value_kind:     by_value
    .group_segment_fixed_size: 60416
    .kernarg_segment_align: 8
    .kernarg_segment_size: 144
    .language:       OpenCL C
    .language_version:
      - 2
      - 0
    .max_flat_workgroup_size: 256
    .name:           _Z7k_scan3PKjPKfS2_S2_S2_S2_PKDF16_S4_S4_7EpiArgs
    .private_segment_fixed_size: 0
    .sgpr_count:     34
    .sgpr_spill_count: 0
    .symbol:         _Z7k_scan3PKjPKfS2_S2_S2_S2_PKDF16_S4_S4_7EpiArgs.kd
    .uniform_work_group_size: 1
    .uses_dynamic_stack: false
    .vgpr_count:     236
    .vgpr_spill_count: 0
    .wavefront_size: 64
  - .agpr_count:     0
    .args:
      - .actual_access:  read_only
        .address_space:  global
        .offset:         0
        .size:           8
        .value_kind:     global_buffer
      - .actual_access:  read_only
        .address_space:  global
        .offset:         8
        .size:           8
        .value_kind:     global_buffer
      - .actual_access:  read_only
        .address_space:  global
        .offset:         16
        .size:           8
        .value_kind:     global_buffer
      - .actual_access:  write_only
        .address_space:  global
        .offset:         24
        .size:           8
        .value_kind:     global_buffer
    .group_segment_fixed_size: 20160
    .kernarg_segment_align: 8
    .kernarg_segment_size: 32
    .language:       OpenCL C
    .language_version:
      - 2
      - 0
    .max_flat_workgroup_size: 256
    .name:           _Z8k_dwconvPKDF16_PKfS2_PDF16_
    .private_segment_fixed_size: 0
    .sgpr_count:     86
    .sgpr_spill_count: 0
    .symbol:         _Z8k_dwconvPKDF16_PKfS2_PDF16_.kd
    .uniform_work_group_size: 1
    .uses_dynamic_stack: false
    .vgpr_count:     65
    .vgpr_spill_count: 0
    .wavefront_size: 64
  - .agpr_count:     0
    .args:
      - .actual_access:  read_only
        .address_space:  global
        .offset:         0
        .size:           8
        .value_kind:     global_buffer
      - .offset:         8
        .size:           72
        .value_kind:     by_value
    .group_segment_fixed_size: 38912
    .kernarg_segment_align: 8
    .kernarg_segment_size: 80
    .language:       OpenCL C
    .language_version:
      - 2
      - 0
    .max_flat_workgroup_size: 256
    .name:           _Z9k_gemm_tlILi2ELb1EEvPKDF16_6TlArgs
    .private_segment_fixed_size: 0
    .sgpr_count:     27
    .sgpr_spill_count: 0
    .symbol:         _Z9k_gemm_tlILi2ELb1EEvPKDF16_6TlArgs.kd
    .uniform_work_group_size: 1
    .uses_dynamic_stack: false
    .vgpr_count:     124
    .vgpr_spill_count: 0
    .wavefront_size: 64
  - .agpr_count:     0
    .args:
      - .actual_access:  read_only
        .address_space:  global
        .offset:         0
        .size:           8
        .value_kind:     global_buffer
      - .offset:         8
        .size:           72
        .value_kind:     by_value
    .group_segment_fixed_size: 34816
    .kernarg_segment_align: 8
    .kernarg_segment_size: 80
    .language:       OpenCL C
    .language_version:
      - 2
      - 0
    .max_flat_workgroup_size: 256
    .name:           _Z9k_gemm_tlILi3ELb0EEvPKDF16_6TlArgs
    .private_segment_fixed_size: 0
    .sgpr_count:     18
    .sgpr_spill_count: 0
    .symbol:         _Z9k_gemm_tlILi3ELb0EEvPKDF16_6TlArgs.kd
    .uniform_work_group_size: 1
    .uses_dynamic_stack: false
    .vgpr_count:     110
    .vgpr_spill_count: 0
    .wavefront_size: 64
